# attention: lane^32 exchange of the row max / row sum by v_permlane32_swap instead of ds_bpermute (counted lgkmcnt waits re-derived)
# speedup vs baseline: 1.0017x; 1.0017x over previous
; __device__ __forceinline__ unsigned cvt_pk_bf16(float lo, float hi) { unsigned r; asm volatile("v_cvt_pk_bf16_f32 %0, %1, %2" : "=v"(r) : "v"(lo), "v"(hi)); return r; }
; #define LAS __attribute__((address_space(3)))
; template <int STAGE, int OFF> __device__ __forceinline__ void attn32_unit(const bf16* base, bf16* yrow0, int blk0, int u, LAS unsigned char* xtab, LAS unsigned char* kbuf, LAS unsigned char* vbuf, int lane, ...
;     ...
;         for (int rg = 0; rg < 16; ++rg) { sc[rg] = __builtin_amdgcn_exp2f(sc[rg] - m); ps += sc[rg]; }
;         l += ps;
;         bf16x8 pb[2];
; #pragma unroll
;         for (int s2 = 0; s2 < 2; ++s2) { v4u w; w.x = pg8::cvt_pk_bf16(sc[8 * s2], sc[8 * s2 + 1]); w.y = pg8::cvt_pk_bf16(sc[8 * s2 + 2], sc[8 * s2 + 3]); w.z = pg8::cvt_pk_bf16(sc[8 * s2 + 4], sc[8 * s2 + 5]); w.w = pg8::cvt_pk_bf16(sc[8 * s2 + 6], sc[8 * s2 + 7]); pb[s2] = __builtin_bit_cast(bf16x8, w); }
; #pragma unroll
;         for (int mb = 0; mb < 2; ++mb)
; #pragma unroll
;             for (int s2 = 0; s2 < 2; ++s2) {
;                 LAS unsigned char* vp = vbuf + tr_off + (16 * s2) * 160 + 64 * mb;
;                 const v4i16 a0 = __builtin_amdgcn_ds_read_tr16_b64_v4i16((LAS v4i16*)vp), a1 = __builtin_amdgcn_ds_read_tr16_b64_v4i16((LAS v4i16*)(vp + 8 * 160));
;                 const bf16x8 va = __builtin_shufflevector(a0, a1, 0, 1, 2, 3, 4, 5, 6, 7);
;                 o[mb] = MFMA32(va, pb[s2], o[mb]);
;             }
;         asm volatile("" ::: "memory");
;     }
;     l += __shfl_xor(l, 32);
;     if (STAGE < 2) {
; #pragma unroll
;         for (int mb = 0; mb < 2; ++mb)
; #pragma unroll
;             for (int gq = 0; gq < 4; ++gq) { v2u w; w.x = pk2(o[mb][4 * gq], o[mb][4 * gq + 1]); w.y = pk2(o[mb][4 * gq + 2], o[mb][4 * gq + 3]); *(LAS v2u*)(xrow + 2 * (32 * mb + 8 * gq + 4 * h)) = w; }
;         if (h == 0) { *(LAS float*)(xrow + 128) = m; *(LAS float*)(xrow + 132) = l; }
;     } else {
;         const float inv = __builtin_amdgcn_rcpf(l);
;         bf16* yo = yrow0 + (size_t)tq * 1024 + 4 * h;
; #pragma unroll
;         for (int mb = 0; mb < 2; ++mb)
; #pragma unroll
;             for (int gq = 0; gq < 4; ++gq) { uint2 w; w.x = pk2(o[mb][4 * gq] * inv, o[mb][4 * gq + 1] * inv); w.y = pk2(o[mb][4 * gq + 2] * inv, o[mb][4 * gq + 3] * inv); *(uint2*)(yo + 32 * mb + 8 * gq) = w; }
.LBB0_355:
	v_sub_f32_e32 v36, v36, v139
	v_exp_f32_e32 v142, v36
	v_sub_f32_e32 v36, v37, v139
	v_exp_f32_e32 v143, v36
	v_sub_f32_e32 v36, v38, v139
	v_exp_f32_e32 v144, v36
	v_sub_f32_e32 v36, v39, v139
	v_exp_f32_e32 v145, v36
	v_sub_f32_e32 v36, v40, v139
	v_exp_f32_e32 v146, v36
	v_sub_f32_e32 v36, v41, v139
	v_exp_f32_e32 v147, v36
	v_sub_f32_e32 v36, v42, v139
	v_exp_f32_e32 v148, v36
	v_sub_f32_e32 v36, v43, v139
	v_exp_f32_e32 v149, v36
	v_sub_f32_e32 v36, v44, v139
	v_sub_f32_e32 v51, v70, v139
	v_exp_f32_e32 v150, v36
	v_sub_f32_e32 v36, v45, v139
	v_exp_f32_e32 v51, v51
	v_sub_f32_e32 v35, v35, v139
	v_exp_f32_e32 v151, v36
	v_sub_f32_e32 v36, v46, v139
	v_exp_f32_e32 v35, v35
	v_exp_f32_e32 v152, v36
	v_sub_f32_e32 v36, v47, v139
	v_exp_f32_e32 v153, v36
	v_sub_f32_e32 v36, v48, v139
	v_exp_f32_e32 v48, v36
	v_sub_f32_e32 v36, v49, v139
	v_exp_f32_e32 v49, v36
	v_cvt_pk_bf16_f32 v36, v51, v35
	v_add_f32_e32 v51, 0, v51
	v_add_f32_e32 v35, v35, v51
	v_add_f32_e32 v35, v142, v35
	v_add_f32_e32 v35, v143, v35
	v_add_f32_e32 v35, v144, v35
	v_cvt_pk_bf16_f32 v37, v142, v143
	v_cvt_pk_bf16_f32 v38, v144, v145
	v_cvt_pk_bf16_f32 v39, v146, v147
	v_cvt_pk_bf16_f32 v40, v148, v149
	v_cvt_pk_bf16_f32 v41, v150, v151
	v_cvt_pk_bf16_f32 v42, v152, v153
	v_cvt_pk_bf16_f32 v43, v48, v49
	ds_read_b64_tr_b16 v[44:45], v181 offset:4608
	ds_read_b64_tr_b16 v[46:47], v181 offset:5888
	v_add_f32_e32 v35, v145, v35
	v_add_f32_e32 v35, v146, v35
	v_add_f32_e32 v35, v147, v35
	v_add_f32_e32 v35, v148, v35
	v_add_f32_e32 v35, v149, v35
	s_waitcnt lgkmcnt(0)
	v_mfma_f32_32x32x16_bf16 v[18:33], v[44:47], v[36:39], v[18:33]
	v_add_f32_e32 v35, v150, v35
	v_add_f32_e32 v35, v151, v35
	v_add_f32_e32 v35, v152, v35
	v_add_f32_e32 v35, v153, v35
	v_add_f32_e32 v35, v48, v35
	ds_read_b64_tr_b16 v[70:71], v181 offset:7168
	ds_read_b64_tr_b16 v[72:73], v181 offset:8448
	ds_read_b64_tr_b16 v[140:141], v181 offset:5952
	ds_read_b64_tr_b16 v[138:139], v181 offset:4672
	v_add_f32_e32 v35, v49, v35
	v_add_f32_e32 v34, v34, v35
	v_mov_b32_e32 v35, v34
	s_nop 1
	v_permlane32_swap_b32_e32 v35, v34
	s_waitcnt lgkmcnt(2)
	v_mfma_f32_32x32x16_bf16 v[18:33], v[70:73], v[40:43], v[18:33]
	v_mov_b32_e32 v51, v169
	v_mov_b32_e32 v171, v169
	ds_read_b64_tr_b16 v[46:47], v181 offset:8512
	ds_read_b64_tr_b16 v[44:45], v181 offset:7232
	s_waitcnt lgkmcnt(2)
	v_add_f32_e32 v34, v34, v35
	v_rcp_f32_e32 v34, v34
	s_add_i32 s26, s26, s27
	v_mfma_f32_32x32x16_bf16 v[2:17], v[138:141], v[36:39], v[2:17]
	s_nop 2
	v_mov_b32_e32 v38, v18
	v_mov_b32_e32 v39, v20
	v_mul_f32_e64 v38, v38, v34
	v_mul_f32_e64 v39, v39, v34
	v_mov_b32_e32 v20, v19
	v_pk_mul_f32 v[18:19], v[20:21], v[34:35] op_sel_hi:[1,0]
	v_and_b32_sdwa v21, v38, v236 dst_sel:DWORD dst_unused:UNUSED_PAD src0_sel:WORD_1 src1_sel:DWORD
	v_add3_u32 v21, v38, v21, s35
	v_and_b32_sdwa v35, v19, v236 dst_sel:DWORD dst_unused:UNUSED_PAD src0_sel:WORD_1 src1_sel:DWORD
	v_and_b32_sdwa v38, v18, v236 dst_sel:DWORD dst_unused:UNUSED_PAD src0_sel:WORD_1 src1_sel:DWORD
	v_lshlrev_b64 v[36:37], 11, v[50:51]
	v_and_b32_sdwa v20, v39, v236 dst_sel:DWORD dst_unused:UNUSED_PAD src0_sel:WORD_1 src1_sel:DWORD
	v_add3_u32 v19, v19, v35, s35
	v_add3_u32 v18, v18, v38, s35
	v_lshl_add_u64 v[36:37], s[12:13], 0, v[36:37]
	v_add3_u32 v20, v39, v20, s35
	v_and_b32_e32 v19, 0xffff0000, v19
	v_and_b32_e32 v18, 0xffff0000, v18
	v_lshl_add_u64 v[36:37], v[36:37], 0, v[170:171]
	v_or_b32_sdwa v19, v19, v20 dst_sel:DWORD dst_unused:UNUSED_PAD src0_sel:DWORD src1_sel:WORD_1
	v_or_b32_sdwa v18, v18, v21 dst_sel:DWORD dst_unused:UNUSED_PAD src0_sel:DWORD src1_sel:WORD_1
	global_store_dwordx2 v[36:37], v[18:19], off
	v_mov_b32_e32 v18, v22
	v_mov_b32_e32 v19, v24
	v_pk_mul_f32 v[18:19], v[18:19], v[34:35] op_sel_hi:[1,0]
	v_mov_b32_e32 v24, v23
	v_pk_mul_f32 v[20:21], v[24:25], v[34:35] op_sel_hi:[1,0]
	v_and_b32_sdwa v22, v19, v236 dst_sel:DWORD dst_unused:UNUSED_PAD src0_sel:WORD_1 src1_sel:DWORD
	v_and_b32_sdwa v23, v18, v236 dst_sel:DWORD dst_unused:UNUSED_PAD src0_sel:WORD_1 src1_sel:DWORD
	v_add3_u32 v18, v18, v23, s35
	v_add3_u32 v19, v19, v22, s35
	v_and_b32_sdwa v22, v21, v236 dst_sel:DWORD dst_unused:UNUSED_PAD src0_sel:WORD_1 src1_sel:DWORD
	v_and_b32_sdwa v23, v20, v236 dst_sel:DWORD dst_unused:UNUSED_PAD src0_sel:WORD_1 src1_sel:DWORD
	v_add3_u32 v21, v21, v22, s35
	v_add3_u32 v20, v20, v23, s35
	v_and_b32_e32 v21, 0xffff0000, v21
	v_and_b32_e32 v20, 0xffff0000, v20
	v_or_b32_sdwa v19, v21, v19 dst_sel:DWORD dst_unused:UNUSED_PAD src0_sel:DWORD src1_sel:WORD_1
	v_or_b32_sdwa v18, v20, v18 dst_sel:DWORD dst_unused:UNUSED_PAD src0_sel:DWORD src1_sel:WORD_1
	global_store_dwordx2 v[36:37], v[18:19], off offset:16
	v_mov_b32_e32 v18, v26
	v_mov_b32_e32 v19, v28
	v_pk_mul_f32 v[18:19], v[18:19], v[34:35] op_sel_hi:[1,0]
	v_mov_b32_e32 v28, v27
	v_pk_mul_f32 v[20:21], v[28:29], v[34:35] op_sel_hi:[1,0]
	v_and_b32_sdwa v22, v19, v236 dst_sel:DWORD dst_unused:UNUSED_PAD src0_sel:WORD_1 src1_sel:DWORD
	v_and_b32_sdwa v23, v18, v236 dst_sel:DWORD dst_unused:UNUSED_PAD src0_sel:WORD_1 src1_sel:DWORD
	v_add3_u32 v18, v18, v23, s35
	v_add3_u32 v19, v19, v22, s35
	v_and_b32_sdwa v22, v21, v236 dst_sel:DWORD dst_unused:UNUSED_PAD src0_sel:WORD_1 src1_sel:DWORD
	v_and_b32_sdwa v23, v20, v236 dst_sel:DWORD dst_unused:UNUSED_PAD src0_sel:WORD_1 src1_sel:DWORD
	v_add3_u32 v21, v21, v22, s35
	v_add3_u32 v20, v20, v23, s35
	v_and_b32_e32 v21, 0xffff0000, v21
	v_and_b32_e32 v20, 0xffff0000, v20
	s_waitcnt lgkmcnt(0)
; __device__ __forceinline__ unsigned pk2(float lo, float hi) { return f2bf(lo) | (f2bf(hi) << 16); }
; template <int STAGE, int OFF> __device__ __forceinline__ void attn32_unit(const bf16* base, bf16* yrow0, int blk0, int u, LAS unsigned char* xtab, LAS unsigned char* kbuf, LAS unsigned char* vbuf, int lane, ...
;     ...
;         const float inv = __builtin_amdgcn_rcpf(l);
;         bf16* yo = yrow0 + (size_t)tq * 1024 + 4 * h;
; #pragma unroll
;         for (int mb = 0; mb < 2; ++mb)
; #pragma unroll
;             for (int gq = 0; gq < 4; ++gq) { uint2 w; w.x = pk2(o[mb][4 * gq] * inv, o[mb][4 * gq + 1] * inv); w.y = pk2(o[mb][4 * gq + 2] * inv, o[mb][4 * gq + 3] * inv); *(uint2*)(yo + 32 * mb + 8 * gq) = w; }
; __device__ __forceinline__ void p2_attention(const Params& P, LAS unsigned char* lds, int lane, int wave, int vb) {
;     ...
;         __syncthreads();
;     }
	v_mfma_f32_32x32x16_bf16 v[2:17], v[44:47], v[40:43], v[2:17]
	v_or_b32_sdwa v19, v21, v19 dst_sel:DWORD dst_unused:UNUSED_PAD src0_sel:DWORD src1_sel:WORD_1
	v_or_b32_sdwa v18, v20, v18 dst_sel:DWORD dst_unused:UNUSED_PAD src0_sel:DWORD src1_sel:WORD_1
	global_store_dwordx2 v[36:37], v[18:19], off offset:32
	v_mov_b32_e32 v18, v30
	v_mov_b32_e32 v19, v32
	v_pk_mul_f32 v[18:19], v[18:19], v[34:35] op_sel_hi:[1,0]
	v_mov_b32_e32 v32, v31
	v_pk_mul_f32 v[20:21], v[32:33], v[34:35] op_sel_hi:[1,0]
	v_and_b32_sdwa v22, v19, v236 dst_sel:DWORD dst_unused:UNUSED_PAD src0_sel:WORD_1 src1_sel:DWORD
	v_and_b32_sdwa v23, v18, v236 dst_sel:DWORD dst_unused:UNUSED_PAD src0_sel:WORD_1 src1_sel:DWORD
	v_add3_u32 v18, v18, v23, s35
	v_add3_u32 v19, v19, v22, s35
	v_and_b32_sdwa v22, v21, v236 dst_sel:DWORD dst_unused:UNUSED_PAD src0_sel:WORD_1 src1_sel:DWORD
	v_and_b32_sdwa v23, v20, v236 dst_sel:DWORD dst_unused:UNUSED_PAD src0_sel:WORD_1 src1_sel:DWORD
	v_add3_u32 v21, v21, v22, s35
	v_add3_u32 v20, v20, v23, s35
	v_and_b32_e32 v21, 0xffff0000, v21
	v_and_b32_e32 v20, 0xffff0000, v20
	v_or_b32_sdwa v19, v21, v19 dst_sel:DWORD dst_unused:UNUSED_PAD src0_sel:DWORD src1_sel:WORD_1
	v_or_b32_sdwa v18, v20, v18 dst_sel:DWORD dst_unused:UNUSED_PAD src0_sel:DWORD src1_sel:WORD_1
	global_store_dwordx2 v[36:37], v[18:19], off offset:48
	v_mov_b32_e32 v18, v2
	v_mov_b32_e32 v19, v4
	v_pk_mul_f32 v[18:19], v[18:19], v[34:35] op_sel_hi:[1,0]
	v_mov_b32_e32 v4, v3
	v_pk_mul_f32 v[2:3], v[4:5], v[34:35] op_sel_hi:[1,0]
	v_and_b32_sdwa v4, v19, v236 dst_sel:DWORD dst_unused:UNUSED_PAD src0_sel:WORD_1 src1_sel:DWORD
	v_and_b32_sdwa v5, v18, v236 dst_sel:DWORD dst_unused:UNUSED_PAD src0_sel:WORD_1 src1_sel:DWORD
	v_add3_u32 v5, v18, v5, s35
	v_add3_u32 v4, v19, v4, s35
	v_and_b32_sdwa v18, v3, v236 dst_sel:DWORD dst_unused:UNUSED_PAD src0_sel:WORD_1 src1_sel:DWORD
	v_and_b32_sdwa v19, v2, v236 dst_sel:DWORD dst_unused:UNUSED_PAD src0_sel:WORD_1 src1_sel:DWORD
	v_add3_u32 v3, v3, v18, s35
	v_add3_u32 v2, v2, v19, s35
	v_and_b32_e32 v3, 0xffff0000, v3
	v_and_b32_e32 v2, 0xffff0000, v2
	v_or_b32_sdwa v3, v3, v4 dst_sel:DWORD dst_unused:UNUSED_PAD src0_sel:DWORD src1_sel:WORD_1
	v_or_b32_sdwa v2, v2, v5 dst_sel:DWORD dst_unused:UNUSED_PAD src0_sel:DWORD src1_sel:WORD_1
	global_store_dwordx2 v[36:37], v[2:3], off offset:64
	v_mov_b32_e32 v2, v6
	v_mov_b32_e32 v3, v8
	v_pk_mul_f32 v[2:3], v[2:3], v[34:35] op_sel_hi:[1,0]
	v_mov_b32_e32 v8, v7
	v_pk_mul_f32 v[4:5], v[8:9], v[34:35] op_sel_hi:[1,0]
	v_and_b32_sdwa v6, v3, v236 dst_sel:DWORD dst_unused:UNUSED_PAD src0_sel:WORD_1 src1_sel:DWORD
	v_and_b32_sdwa v7, v2, v236 dst_sel:DWORD dst_unused:UNUSED_PAD src0_sel:WORD_1 src1_sel:DWORD
	v_add3_u32 v2, v2, v7, s35
	v_add3_u32 v3, v3, v6, s35
	v_and_b32_sdwa v6, v5, v236 dst_sel:DWORD dst_unused:UNUSED_PAD src0_sel:WORD_1 src1_sel:DWORD
	v_and_b32_sdwa v7, v4, v236 dst_sel:DWORD dst_unused:UNUSED_PAD src0_sel:WORD_1 src1_sel:DWORD
	v_add3_u32 v5, v5, v6, s35
	v_add3_u32 v4, v4, v7, s35
	v_and_b32_e32 v5, 0xffff0000, v5
	v_and_b32_e32 v4, 0xffff0000, v4
	v_or_b32_sdwa v3, v5, v3 dst_sel:DWORD dst_unused:UNUSED_PAD src0_sel:DWORD src1_sel:WORD_1
	v_or_b32_sdwa v2, v4, v2 dst_sel:DWORD dst_unused:UNUSED_PAD src0_sel:DWORD src1_sel:WORD_1
	global_store_dwordx2 v[36:37], v[2:3], off offset:80
	v_mov_b32_e32 v2, v10
	v_mov_b32_e32 v3, v12
	v_pk_mul_f32 v[2:3], v[2:3], v[34:35] op_sel_hi:[1,0]
	v_mov_b32_e32 v12, v11
	v_pk_mul_f32 v[4:5], v[12:13], v[34:35] op_sel_hi:[1,0]
	v_and_b32_sdwa v6, v3, v236 dst_sel:DWORD dst_unused:UNUSED_PAD src0_sel:WORD_1 src1_sel:DWORD
	v_and_b32_sdwa v7, v2, v236 dst_sel:DWORD dst_unused:UNUSED_PAD src0_sel:WORD_1 src1_sel:DWORD
	v_add3_u32 v2, v2, v7, s35
	v_add3_u32 v3, v3, v6, s35
	v_and_b32_sdwa v6, v5, v236 dst_sel:DWORD dst_unused:UNUSED_PAD src0_sel:WORD_1 src1_sel:DWORD
	v_and_b32_sdwa v7, v4, v236 dst_sel:DWORD dst_unused:UNUSED_PAD src0_sel:WORD_1 src1_sel:DWORD
	v_add3_u32 v5, v5, v6, s35
	v_add3_u32 v4, v4, v7, s35
	v_and_b32_e32 v5, 0xffff0000, v5
	v_and_b32_e32 v4, 0xffff0000, v4
	v_or_b32_sdwa v3, v5, v3 dst_sel:DWORD dst_unused:UNUSED_PAD src0_sel:DWORD src1_sel:WORD_1
	v_or_b32_sdwa v2, v4, v2 dst_sel:DWORD dst_unused:UNUSED_PAD src0_sel:DWORD src1_sel:WORD_1
	global_store_dwordx2 v[36:37], v[2:3], off offset:96
	v_mov_b32_e32 v2, v14
	v_mov_b32_e32 v3, v16
	v_pk_mul_f32 v[2:3], v[2:3], v[34:35] op_sel_hi:[1,0]
	v_mov_b32_e32 v16, v15
	v_pk_mul_f32 v[4:5], v[16:17], v[34:35] op_sel_hi:[1,0]
	v_and_b32_sdwa v6, v3, v236 dst_sel:DWORD dst_unused:UNUSED_PAD src0_sel:WORD_1 src1_sel:DWORD
	v_and_b32_sdwa v7, v2, v236 dst_sel:DWORD dst_unused:UNUSED_PAD src0_sel:WORD_1 src1_sel:DWORD
	v_add3_u32 v2, v2, v7, s35
	v_add3_u32 v3, v3, v6, s35
	v_and_b32_sdwa v6, v5, v236 dst_sel:DWORD dst_unused:UNUSED_PAD src0_sel:WORD_1 src1_sel:DWORD
	v_and_b32_sdwa v7, v4, v236 dst_sel:DWORD dst_unused:UNUSED_PAD src0_sel:WORD_1 src1_sel:DWORD
	v_add3_u32 v5, v5, v6, s35
	v_add3_u32 v4, v4, v7, s35
	v_and_b32_e32 v5, 0xffff0000, v5
	v_and_b32_e32 v4, 0xffff0000, v4
	v_or_b32_sdwa v3, v5, v3 dst_sel:DWORD dst_unused:UNUSED_PAD src0_sel:DWORD src1_sel:WORD_1
	v_or_b32_sdwa v2, v4, v2 dst_sel:DWORD dst_unused:UNUSED_PAD src0_sel:DWORD src1_sel:WORD_1
	s_cmpk_lt_i32 s37, 0x200
	s_mov_b32 s8, s37
	global_store_dwordx2 v[36:37], v[2:3], off offset:112
	s_barrier
	s_cbranch_scc0 .LBB0_432

; #define LAS __attribute__((address_space(3)))
; #define MFMA32(a, b, c) __builtin_amdgcn_mfma_f32_32x32x16_bf16((a), (b), (c), 0, 0, 0)
; template <int STAGE, int OFF> __device__ __forceinline__ void attn32_unit(const bf16* base, bf16* yrow0, int blk0, int u, LAS unsigned char* xtab, LAS unsigned char* kbuf, LAS unsigned char* vbuf, int lane, ...
;     ...
;     for (int pp = 0; pp < 5; ++pp) {
;         constexpr int dummy = 0; (void)dummy;
;         const int set = (pp + OFF) % 2, n0 = -128 + 32 * pp;
; #pragma unroll
;         for (int c = 0; c < 4; ++c) { *(LAS v4u*)(kbuf + (8 * c + lrow) * 144 + lch * 16) = kr[set][c]; *(LAS v4u*)(vbuf + (8 * c + lrow) * 160 + lch * 16) = vr[set][c]; }
;         if (pp + 2 < 5) { ATT32_LOAD(set, pp + 2, t0, SH); }
;         else { const bf16* base_ = base; { const bf16* base = nbase; ATT32_LOAD(set, pp + 2 - 5, nt0, nsh); } (void)base_; }
;         f32x16 sc;
; #pragma unroll
;         for (int i = 0; i < 16; ++i) sc[i] = 0.f;
; #pragma unroll
;         for (int ks = 0; ks < 4; ++ks) { const bf16x8 ka = *(const LAS bf16x8*)(kbuf + qi * 144 + 32 * ks + 16 * h); sc = MFMA32(ka, qb[ks], sc); }
;         if (pp == 4) {
; #pragma unroll
;             for (int ks = 0; ks < 4; ++ks) qb[ks] = *(const bf16x8*)(nbase + (size_t)min(nt0 + (qi << nsh), SEQ - 1) * 1536 + 16 * ks + 8 * h);
;         }
;         const int mbase = n0 + 4 * h - lo; float mx = -INFINITY;
; #pragma unroll
;         for (int rg = 0; rg < 16; ++rg) { sc[rg] = ((unsigned)(mbase + (rg & 3) + 8 * (rg >> 2)) <= mspan) ? sc[rg] : -INFINITY; mx = fmaxf(mx, sc[rg]); }
;         mx = fmaxf(mx, __shfl_xor(mx, 32));
;         if (__any(mx > m)) {
;             const float mn = fmaxf(m, mx), alpha = __builtin_amdgcn_exp2f(m - mn); m = mn; l *= alpha;
; #pragma unroll
;             for (int i = 0; i < 16; ++i) { o[0][i] *= alpha; o[1][i] *= alpha; }
;         }
;         float ps = 0.f;
; #pragma unroll
;         for (int rg = 0; rg < 16; ++rg) { sc[rg] = __builtin_amdgcn_exp2f(sc[rg] - m); ps += sc[rg]; }
;         l += ps;
;         bf16x8 pb[2];
; #pragma unroll
;         for (int s2 = 0; s2 < 2; ++s2) { v4u w; w.x = pg8::cvt_pk_bf16(sc[8 * s2], sc[8 * s2 + 1]); w.y = pg8::cvt_pk_bf16(sc[8 * s2 + 2], sc[8 * s2 + 3]); w.z = pg8::cvt_pk_bf16(sc[8 * s2 + 4], sc[8 * s2 + 5]); w.w = pg8::cvt_pk_bf16(sc[8 * s2 + 6], sc[8 * s2 + 7]); pb[s2] = __builtin_bit_cast(bf16x8, w); }
.LBB0_360:
	s_waitcnt vmcnt(0)
	ds_write_b128 v231, v[74:77]
	ds_write_b128 v232, v[82:85] offset:4608
	ds_write_b128 v231, v[78:81] offset:1152
	ds_write_b128 v232, v[94:97] offset:5888
	ds_write_b128 v231, v[86:89] offset:2304
	ds_write_b128 v232, v[98:101] offset:7168
	ds_write_b128 v231, v[90:93] offset:3456
	ds_write_b128 v232, v[102:105] offset:8448
	ds_read_b128 v[2:5], v177
	ds_read_b128 v[18:21], v177 offset:32
	s_ashr_i32 s12, s9, 8
	s_lshl_b32 s0, s9, 9
	s_and_b32 s13, s0, 0x3e00
	s_mul_i32 s1, s12, 0x3000000
	s_mul_hi_i32 s0, s12, 0x3000000
	s_add_u32 s1, s16, s1
	s_addc_u32 s0, s17, s0
	s_waitcnt lgkmcnt(0)
	v_mfma_f32_32x32x16_bf16 v[2:17], v[2:5], v[66:69], 0
	s_lshl_b32 s8, s9, 1
	s_and_b32 s8, s8, 0x1c0
	s_lshl_b32 s39, s8, 1
	s_add_u32 s8, s1, s39
	s_addc_u32 s9, s0, 0
	s_add_i32 s10, s13, s23
	s_sub_i32 s0, 0, s10
	v_mfma_f32_32x32x16_bf16 v[2:17], v[18:21], v[62:65], v[2:17]
	v_max_i32_e32 v22, s0, v175
	v_add_u32_e32 v168, s10, v174
	v_sub_u32_e32 v171, v1, v22
	v_sub_u32_e32 v173, v178, v22
	v_med3_i32 v22, v168, 0, v233
	v_mul_u32_u24_e32 v30, 0xc00, v22
	ds_read_b128 v[22:25], v177 offset:96
	ds_read_b128 v[26:29], v177 offset:64
	s_waitcnt lgkmcnt(0)
	v_mfma_f32_32x32x16_bf16 v[2:17], v[26:29], v[58:61], v[2:17]
	v_or_b32_e32 v18, v30, v176
	global_load_dwordx4 v[70:73], v18, s[8:9] offset:1024
	global_load_dwordx4 v[138:141], v18, s[8:9] offset:2048
	v_or_b32_e32 v18, 8, v168
	v_med3_i32 v18, v18, 0, v233
	v_mul_u32_u24_e32 v18, 0xc00, v18
	v_or_b32_e32 v18, v18, v176
	global_load_dwordx4 v[142:145], v18, s[8:9] offset:1024
	global_load_dwordx4 v[146:149], v18, s[8:9] offset:2048
	v_mfma_f32_32x32x16_bf16 v[2:17], v[22:25], v[54:57], v[2:17]
	v_or_b32_e32 v18, 16, v168
	v_med3_i32 v18, v18, 0, v233
	v_mul_u32_u24_e32 v18, 0xc00, v18
	v_or_b32_e32 v18, v18, v176
	global_load_dwordx4 v[150:153], v18, s[8:9] offset:1024
	global_load_dwordx4 v[154:157], v18, s[8:9] offset:2048
	v_cmp_le_u32_e32 vcc, v173, v171
	v_add_u32_e32 v18, 1, v173
	v_add_u32_e32 v19, 2, v173
	s_nop 2
	v_cndmask_b32_e32 v2, v234, v2, vcc
	v_cmp_le_u32_e32 vcc, v18, v171
	v_or_b32_e32 v20, 24, v168
	v_med3_i32 v20, v20, 0, v233
	v_cndmask_b32_e32 v3, v234, v3, vcc
	v_cmp_le_u32_e32 vcc, v19, v171
	v_add_u32_e32 v19, 3, v173
	v_max3_f32 v18, v2, s31, v3
	v_cndmask_b32_e32 v4, v234, v4, vcc
	v_cmp_le_u32_e32 vcc, v19, v171
	v_add_u32_e32 v19, 8, v173
	v_mul_u32_u24_e32 v20, 0xc00, v20
	v_cndmask_b32_e32 v5, v234, v5, vcc
	v_cmp_le_u32_e32 vcc, v19, v171
	v_add_u32_e32 v19, 9, v173
	v_max3_f32 v18, v18, v4, v5
	v_cndmask_b32_e32 v6, v234, v6, vcc
	v_cmp_le_u32_e32 vcc, v19, v171
	v_add_u32_e32 v19, 10, v173
	v_or_b32_e32 v20, v20, v176
	v_cndmask_b32_e32 v7, v234, v7, vcc
	v_cmp_le_u32_e32 vcc, v19, v171
	v_add_u32_e32 v19, 11, v173
	v_max3_f32 v18, v18, v6, v7
	v_cndmask_b32_e32 v8, v234, v8, vcc
	v_cmp_le_u32_e32 vcc, v19, v171
	v_add_u32_e32 v19, 16, v173
	global_load_dwordx4 v[158:161], v20, s[8:9] offset:1024
	global_load_dwordx4 v[162:165], v20, s[8:9] offset:2048
	v_cndmask_b32_e32 v9, v234, v9, vcc
	v_cmp_le_u32_e32 vcc, v19, v171
	v_add_u32_e32 v19, 17, v173
	v_max3_f32 v18, v18, v8, v9
	v_cndmask_b32_e32 v10, v234, v10, vcc
	v_cmp_le_u32_e32 vcc, v19, v171
	v_add_u32_e32 v19, 18, v173
	s_nop 0
	v_cndmask_b32_e32 v11, v234, v11, vcc
	v_cmp_le_u32_e32 vcc, v19, v171
	v_add_u32_e32 v19, 19, v173
	v_max3_f32 v18, v18, v10, v11
	v_cndmask_b32_e32 v12, v234, v12, vcc
	v_cmp_le_u32_e32 vcc, v19, v171
	v_add_u32_e32 v19, 24, v173
	s_nop 0
	v_cndmask_b32_e32 v13, v234, v13, vcc
	v_cmp_le_u32_e32 vcc, v19, v171
	v_add_u32_e32 v19, 25, v173
	v_max3_f32 v18, v18, v12, v13
	v_cndmask_b32_e32 v14, v234, v14, vcc
	v_cmp_le_u32_e32 vcc, v19, v171
	v_add_u32_e32 v19, 26, v173
	s_nop 0
	v_cndmask_b32_e32 v15, v234, v15, vcc
	v_cmp_le_u32_e32 vcc, v19, v171
	v_add_u32_e32 v19, 27, v173
	v_max3_f32 v18, v18, v14, v15
	v_cndmask_b32_e32 v16, v234, v16, vcc
	v_cmp_le_u32_e32 vcc, v19, v171
	s_nop 1
	v_cndmask_b32_e32 v17, v234, v17, vcc
	v_max3_f32 v18, v18, v16, v17
	v_mov_b32_e32 v19, v18
	s_nop 1
	v_permlane32_swap_b32_e32 v19, v18
	s_waitcnt lgkmcnt(0)
	v_max_f32_e32 v19, v19, v19
	v_max_f32_e32 v18, v18, v19
	v_cmp_lt_f32_e32 vcc, s34, v18
	s_cmp_eq_u64 vcc, 0
	v_max_f32_e32 v19, 0xf149f2ca, v18
	s_cselect_b64 vcc, -1, 0
	v_cndmask_b32_e32 v172, v19, v235, vcc
	v_sub_f32_e32 v2, v2, v172
	v_exp_f32_e32 v50, v2
	v_sub_f32_e32 v2, v3, v172
	v_exp_f32_e32 v51, v2
	v_sub_f32_e32 v2, v4, v172
	v_exp_f32_e32 v82, v2
	v_sub_f32_e32 v2, v5, v172
	v_exp_f32_e32 v83, v2
	v_sub_f32_e32 v2, v6, v172
	v_exp_f32_e32 v6, v2
	v_sub_f32_e32 v2, v7, v172
	v_exp_f32_e32 v7, v2
	v_sub_f32_e32 v2, v8, v172
	v_exp_f32_e32 v8, v2
	v_sub_f32_e32 v2, v9, v172
	v_exp_f32_e32 v9, v2
	v_sub_f32_e32 v2, v10, v172
	v_exp_f32_e32 v237, v2
	v_sub_f32_e32 v2, v11, v172
	v_exp_f32_e32 v246, v2
	v_sub_f32_e32 v2, v12, v172
	v_exp_f32_e32 v247, v2
	v_sub_f32_e32 v2, v13, v172
	v_exp_f32_e32 v248, v2
	v_sub_f32_e32 v2, v14, v172
	v_sub_f32_e32 v21, 0xf149f2ca, v19
	v_exp_f32_e32 v249, v2
	v_sub_f32_e32 v2, v15, v172
	v_exp_f32_e32 v21, v21
	v_exp_f32_e32 v250, v2
	v_sub_f32_e32 v2, v16, v172
	v_exp_f32_e32 v251, v2
	v_sub_f32_e32 v2, v17, v172
	v_exp_f32_e32 v252, v2
	v_cvt_pk_bf16_f32 v74, v50, v51
	v_cvt_pk_bf16_f32 v75, v82, v83
	v_cvt_pk_bf16_f32 v76, v6, v7
	v_cvt_pk_bf16_f32 v77, v8, v9
	v_cvt_pk_bf16_f32 v238, v237, v246
	v_cvt_pk_bf16_f32 v239, v247, v248
	v_cvt_pk_bf16_f32 v240, v249, v250
	v_cvt_pk_bf16_f32 v241, v251, v252
	ds_read_b64_tr_b16 v[2:3], v181 offset:4608
	ds_read_b64_tr_b16 v[4:5], v181 offset:5888
	v_mul_f32_e32 v18, 0, v21
	v_cndmask_b32_e64 v34, v18, 0, vcc
	v_mov_b32_e32 v35, v34
	v_mov_b32_e32 v36, v34
	v_mov_b32_e32 v37, v34
	v_mov_b32_e32 v38, v34
	v_mov_b32_e32 v39, v34
	v_mov_b32_e32 v40, v34
	v_mov_b32_e32 v41, v34
	v_mov_b32_e32 v42, v34
	v_mov_b32_e32 v43, v34
	v_mov_b32_e32 v44, v34
	v_mov_b32_e32 v45, v34
	v_mov_b32_e32 v46, v34
	v_mov_b32_e32 v47, v34
	v_mov_b32_e32 v48, v34
	v_mov_b32_e32 v49, v34
	ds_read_b64_tr_b16 v[80:81], v181 offset:5952
	ds_read_b64_tr_b16 v[78:79], v181 offset:4672
	s_waitcnt lgkmcnt(2)
; template <int STAGE, int OFF> __device__ __forceinline__ void attn32_unit(const bf16* base, bf16* yrow0, int blk0, int u, LAS unsigned char* xtab, LAS unsigned char* kbuf, LAS unsigned char* vbuf, int lane, ...
;     ...
;         const int set = (pp + OFF) % 2, n0 = -128 + 32 * pp;
; #pragma unroll
;         for (int c = 0; c < 4; ++c) { *(LAS v4u*)(kbuf + (8 * c + lrow) * 144 + lch * 16) = kr[set][c]; *(LAS v4u*)(vbuf + (8 * c + lrow) * 160 + lch * 16) = vr[set][c]; }
;         if (pp + 2 < 5) { ATT32_LOAD(set, pp + 2, t0, SH); }
;         else { const bf16* base_ = base; { const bf16* base = nbase; ATT32_LOAD(set, pp + 2 - 5, nt0, nsh); } (void)base_; }
;         f32x16 sc;
; #pragma unroll
;         for (int i = 0; i < 16; ++i) sc[i] = 0.f;
; #pragma unroll
;         for (int ks = 0; ks < 4; ++ks) { const bf16x8 ka = *(const LAS bf16x8*)(kbuf + qi * 144 + 32 * ks + 16 * h); sc = MFMA32(ka, qb[ks], sc); }
;         if (pp == 4) {
; #pragma unroll
;             for (int ks = 0; ks < 4; ++ks) qb[ks] = *(const bf16x8*)(nbase + (size_t)min(nt0 + (qi << nsh), SEQ - 1) * 1536 + 16 * ks + 8 * h);
;         }
;         const int mbase = n0 + 4 * h - lo; float mx = -INFINITY;
; #pragma unroll
;         for (int rg = 0; rg < 16; ++rg) { sc[rg] = ((unsigned)(mbase + (rg & 3) + 8 * (rg >> 2)) <= mspan) ? sc[rg] : -INFINITY; mx = fmaxf(mx, sc[rg]); }
;         mx = fmaxf(mx, __shfl_xor(mx, 32));
;         if (__any(mx > m)) {
;             const float mn = fmaxf(m, mx), alpha = __builtin_amdgcn_exp2f(m - mn); m = mn; l *= alpha;
; #pragma unroll
;             for (int i = 0; i < 16; ++i) { o[0][i] *= alpha; o[1][i] *= alpha; }
;         }
;         float ps = 0.f;
; #pragma unroll
;         for (int rg = 0; rg < 16; ++rg) { sc[rg] = __builtin_amdgcn_exp2f(sc[rg] - m); ps += sc[rg]; }
;         l += ps;
;         bf16x8 pb[2];
; #pragma unroll
;         for (int s2 = 0; s2 < 2; ++s2) { v4u w; w.x = pg8::cvt_pk_bf16(sc[8 * s2], sc[8 * s2 + 1]); w.y = pg8::cvt_pk_bf16(sc[8 * s2 + 2], sc[8 * s2 + 3]); w.z = pg8::cvt_pk_bf16(sc[8 * s2 + 4], sc[8 * s2 + 5]); w.w = pg8::cvt_pk_bf16(sc[8 * s2 + 6], sc[8 * s2 + 7]); pb[s2] = __builtin_bit_cast(bf16x8, w); }
; #pragma unroll
;         for (int mb = 0; mb < 2; ++mb)
; #pragma unroll
;             for (int s2 = 0; s2 < 2; ++s2) {
;                 LAS unsigned char* vp = vbuf + tr_off + (16 * s2) * 160 + 64 * mb;
	v_mfma_f32_32x32x16_bf16 v[18:33], v[2:5], v[74:77], v[34:49]
	ds_read_b64_tr_b16 v[2:3], v181 offset:7168
	ds_read_b64_tr_b16 v[4:5], v181 offset:8448
	v_add_f32_e32 v10, 0, v50
	v_add_f32_e32 v10, v51, v10
	ds_read_b64_tr_b16 v[244:245], v181 offset:8512
	ds_read_b64_tr_b16 v[242:243], v181 offset:7232
	ds_write_b128 v231, v[106:109]
	ds_write_b128 v232, v[122:125] offset:4608
	ds_write_b128 v231, v[110:113] offset:1152
	ds_write_b128 v232, v[126:129] offset:5888
	ds_write_b128 v231, v[114:117] offset:2304
	ds_write_b128 v232, v[130:133] offset:7168
	ds_write_b128 v231, v[118:121] offset:3456
	ds_write_b128 v232, v[134:137] offset:8448
	s_waitcnt lgkmcnt(10)
	v_mfma_f32_32x32x16_bf16 v[18:33], v[2:5], v[238:241], v[18:33]
	v_add_f32_e32 v2, v82, v10
	v_add_f32_e32 v2, v83, v2
	v_add_f32_e32 v2, v6, v2
	v_add_f32_e32 v2, v7, v2
	v_add_f32_e32 v2, v8, v2
	v_add_f32_e32 v253, v9, v2
	v_mov_b64_e32 v[2:3], v[34:35]
	v_mov_b64_e32 v[4:5], v[36:37]
	v_mov_b64_e32 v[6:7], v[38:39]
	v_mov_b64_e32 v[8:9], v[40:41]
	v_mov_b64_e32 v[10:11], v[42:43]
	v_mov_b64_e32 v[12:13], v[44:45]
	v_mov_b64_e32 v[14:15], v[46:47]
	v_mov_b64_e32 v[16:17], v[48:49]
	ds_read_b128 v[36:39], v177
	v_or_b32_e32 v35, 32, v168
	v_med3_i32 v35, v35, 0, v233
	v_mul_u32_u24_e32 v35, 0xc00, v35
	v_or_b32_e32 v35, v35, v176
	v_mfma_f32_32x32x16_bf16 v[2:17], v[78:81], v[74:77], v[2:17]
	global_load_dwordx4 v[74:77], v35, s[8:9] offset:1024
	global_load_dwordx4 v[78:81], v35, s[8:9] offset:2048
	ds_read_b128 v[90:93], v177 offset:32
	v_or_b32_e32 v35, 40, v168
	v_med3_i32 v35, v35, 0, v233
	v_mul_u32_u24_e32 v35, 0xc00, v35
	v_or_b32_e32 v35, v35, v176
	global_load_dwordx4 v[82:85], v35, s[8:9] offset:1024
	global_load_dwordx4 v[86:89], v35, s[8:9] offset:2048
	s_waitcnt lgkmcnt(1)
	v_mfma_f32_32x32x16_bf16 v[36:51], v[36:39], v[66:69], 0
	v_or_b32_e32 v35, 48, v168
	v_med3_i32 v35, v35, 0, v233
	v_mul_u32_u24_e32 v35, 0xc00, v35
	v_or_b32_e32 v35, v35, v176
	ds_read_b128 v[106:109], v177 offset:96
	ds_read_b128 v[110:113], v177 offset:64
	s_waitcnt lgkmcnt(2)
	v_mfma_f32_32x32x16_bf16 v[36:51], v[90:93], v[62:65], v[36:51]
	global_load_dwordx4 v[90:93], v35, s[8:9] offset:1024
	global_load_dwordx4 v[94:97], v35, s[8:9] offset:2048
	v_or_b32_e32 v35, 56, v168
	v_med3_i32 v35, v35, 0, v233
	v_mul_u32_u24_e32 v35, 0xc00, v35
	v_or_b32_e32 v35, v35, v176
	global_load_dwordx4 v[98:101], v35, s[8:9] offset:1024
	global_load_dwordx4 v[102:105], v35, s[8:9] offset:2048
	v_add_f32_e32 v35, v237, v253
	s_waitcnt lgkmcnt(0)
	v_mfma_f32_32x32x16_bf16 v[36:51], v[110:113], v[58:61], v[36:51]
	v_add_f32_e32 v35, v246, v35
	v_add_f32_e32 v35, v247, v35
	v_add_f32_e32 v35, v248, v35
	v_add_f32_e32 v35, v249, v35
	v_add_f32_e32 v35, v250, v35
	v_add_f32_e32 v110, v251, v35
	v_add_u32_e32 v35, 32, v173
	v_mfma_f32_32x32x16_bf16 v[36:51], v[106:109], v[54:57], v[36:51]
	v_cmp_le_u32_e32 vcc, v35, v171
	v_mfma_f32_32x32x16_bf16 v[2:17], v[242:245], v[238:241], v[2:17]
	s_nop 9
	v_cndmask_b32_e32 v35, v234, v36, vcc
	v_add_u32_e32 v36, 33, v173
	v_cmp_le_u32_e32 vcc, v36, v171
	s_nop 1
	v_cndmask_b32_e32 v36, v234, v37, vcc
	v_add_u32_e32 v37, 34, v173
	v_cmp_le_u32_e32 vcc, v37, v171
	v_max3_f32 v106, v35, s31, v36
	s_nop 0
	v_cndmask_b32_e32 v37, v234, v38, vcc
	v_add_u32_e32 v38, 35, v173
	v_cmp_le_u32_e32 vcc, v38, v171
	s_nop 1
	v_cndmask_b32_e32 v38, v234, v39, vcc
	v_add_u32_e32 v39, 40, v173
	v_cmp_le_u32_e32 vcc, v39, v171
	v_max3_f32 v106, v106, v37, v38
	s_nop 0
	v_cndmask_b32_e32 v39, v234, v40, vcc
	v_add_u32_e32 v40, 41, v173
	v_cmp_le_u32_e32 vcc, v40, v171
	s_nop 1
	v_cndmask_b32_e32 v40, v234, v41, vcc
	v_add_u32_e32 v41, 42, v173
	v_cmp_le_u32_e32 vcc, v41, v171
	v_max3_f32 v106, v106, v39, v40
	s_nop 0
	v_cndmask_b32_e32 v41, v234, v42, vcc
	v_add_u32_e32 v42, 43, v173
	v_cmp_le_u32_e32 vcc, v42, v171
	s_nop 1
	v_cndmask_b32_e32 v42, v234, v43, vcc
	v_add_u32_e32 v43, 48, v173
	v_cmp_le_u32_e32 vcc, v43, v171
	v_max3_f32 v106, v106, v41, v42
	s_nop 0
	v_cndmask_b32_e32 v43, v234, v44, vcc
	v_add_u32_e32 v44, 49, v173
	v_cmp_le_u32_e32 vcc, v44, v171
	s_nop 1
	v_cndmask_b32_e32 v44, v234, v45, vcc
	v_add_u32_e32 v45, 50, v173
	v_cmp_le_u32_e32 vcc, v45, v171
	v_max3_f32 v106, v106, v43, v44
	s_nop 0
	v_cndmask_b32_e32 v45, v234, v46, vcc
	v_add_u32_e32 v46, 51, v173
	v_cmp_le_u32_e32 vcc, v46, v171
	s_nop 1
	v_cndmask_b32_e32 v46, v234, v47, vcc
	v_add_u32_e32 v47, 56, v173
	v_cmp_le_u32_e32 vcc, v47, v171
	v_max3_f32 v106, v106, v45, v46
	s_nop 0
	v_cndmask_b32_e32 v47, v234, v48, vcc
	v_add_u32_e32 v48, 57, v173
	v_cmp_le_u32_e32 vcc, v48, v171
	s_nop 1
	v_cndmask_b32_e32 v48, v234, v49, vcc
	v_add_u32_e32 v49, 58, v173
	v_cmp_le_u32_e32 vcc, v49, v171
	v_max3_f32 v106, v106, v47, v48
	s_nop 0
	v_cndmask_b32_e32 v49, v234, v50, vcc
	v_add_u32_e32 v50, 59, v173
	v_cmp_le_u32_e32 vcc, v50, v171
	v_add_f32_e32 v50, v252, v110
	v_add_f32_e32 v50, v34, v50
	v_cndmask_b32_e32 v51, v234, v51, vcc
	v_max3_f32 v106, v106, v49, v51
	v_mov_b32_e32 v107, v106
	s_nop 1
	v_permlane32_swap_b32_e32 v107, v106
	s_waitcnt lgkmcnt(0)
	v_max_f32_e32 v34, v107, v107
	v_max_f32_e32 v34, v106, v34
	v_cmp_gt_f32_e32 vcc, v34, v172
	s_cbranch_vccz .LBB0_362
	v_max_f32_e32 v34, v34, v34
	v_max_f32_e32 v106, v172, v172
	v_max_f32_e32 v106, v106, v34
	v_sub_f32_e32 v34, v172, v106
	v_exp_f32_e32 v34, v34
	v_mov_b32_e32 v172, v106
	v_pk_mul_f32 v[32:33], v[32:33], v[34:35] op_sel_hi:[1,0]
	v_pk_mul_f32 v[30:31], v[30:31], v[34:35] op_sel_hi:[1,0]
	v_pk_mul_f32 v[28:29], v[28:29], v[34:35] op_sel_hi:[1,0]
	v_pk_mul_f32 v[26:27], v[26:27], v[34:35] op_sel_hi:[1,0]
	v_pk_mul_f32 v[24:25], v[24:25], v[34:35] op_sel_hi:[1,0]
	v_pk_mul_f32 v[22:23], v[22:23], v[34:35] op_sel_hi:[1,0]
	v_pk_mul_f32 v[20:21], v[20:21], v[34:35] op_sel_hi:[1,0]
	v_pk_mul_f32 v[18:19], v[18:19], v[34:35] op_sel_hi:[1,0]
	v_pk_mul_f32 v[16:17], v[16:17], v[34:35] op_sel_hi:[1,0]
	v_pk_mul_f32 v[14:15], v[14:15], v[34:35] op_sel_hi:[1,0]
	v_pk_mul_f32 v[12:13], v[12:13], v[34:35] op_sel_hi:[1,0]
	v_pk_mul_f32 v[10:11], v[10:11], v[34:35] op_sel_hi:[1,0]
	v_pk_mul_f32 v[8:9], v[8:9], v[34:35] op_sel_hi:[1,0]
	v_pk_mul_f32 v[6:7], v[6:7], v[34:35] op_sel_hi:[1,0]
	v_pk_mul_f32 v[4:5], v[4:5], v[34:35] op_sel_hi:[1,0]
	v_pk_mul_f32 v[2:3], v[2:3], v[34:35] op_sel_hi:[1,0]
	v_mul_f32_e32 v50, v50, v34
; template <int STAGE, int OFF> __device__ __forceinline__ void attn32_unit(const bf16* base, bf16* yrow0, int blk0, int u, LAS unsigned char* xtab, LAS unsigned char* kbuf, LAS unsigned char* vbuf, int lane, ...
;     ...
;     for (int pp = 0; pp < 5; ++pp) {
;         constexpr int dummy = 0; (void)dummy;
;         const int set = (pp + OFF) % 2, n0 = -128 + 32 * pp;
; #pragma unroll
;         for (int c = 0; c < 4; ++c) { *(LAS v4u*)(kbuf + (8 * c + lrow) * 144 + lch * 16) = kr[set][c]; *(LAS v4u*)(vbuf + (8 * c + lrow) * 160 + lch * 16) = vr[set][c]; }
;         if (pp + 2 < 5) { ATT32_LOAD(set, pp + 2, t0, SH); }
;         else { const bf16* base_ = base; { const bf16* base = nbase; ATT32_LOAD(set, pp + 2 - 5, nt0, nsh); } (void)base_; }
;         f32x16 sc;
; #pragma unroll
;         for (int i = 0; i < 16; ++i) sc[i] = 0.f;
; #pragma unroll
;         for (int ks = 0; ks < 4; ++ks) { const bf16x8 ka = *(const LAS bf16x8*)(kbuf + qi * 144 + 32 * ks + 16 * h); sc = MFMA32(ka, qb[ks], sc); }
;         if (pp == 4) {
; #pragma unroll
;             for (int ks = 0; ks < 4; ++ks) qb[ks] = *(const bf16x8*)(nbase + (size_t)min(nt0 + (qi << nsh), SEQ - 1) * 1536 + 16 * ks + 8 * h);
;         }
;         const int mbase = n0 + 4 * h - lo; float mx = -INFINITY;
; #pragma unroll
;         for (int rg = 0; rg < 16; ++rg) { sc[rg] = ((unsigned)(mbase + (rg & 3) + 8 * (rg >> 2)) <= mspan) ? sc[rg] : -INFINITY; mx = fmaxf(mx, sc[rg]); }
;         mx = fmaxf(mx, __shfl_xor(mx, 32));
;         if (__any(mx > m)) {
;             const float mn = fmaxf(m, mx), alpha = __builtin_amdgcn_exp2f(m - mn); m = mn; l *= alpha;
; #pragma unroll
;             for (int i = 0; i < 16; ++i) { o[0][i] *= alpha; o[1][i] *= alpha; }
;         }
;         float ps = 0.f;
; #pragma unroll
;         for (int rg = 0; rg < 16; ++rg) { sc[rg] = __builtin_amdgcn_exp2f(sc[rg] - m); ps += sc[rg]; }
;         l += ps;
;         bf16x8 pb[2];
; #pragma unroll
;         for (int s2 = 0; s2 < 2; ++s2) { v4u w; w.x = pg8::cvt_pk_bf16(sc[8 * s2], sc[8 * s2 + 1]); w.y = pg8::cvt_pk_bf16(sc[8 * s2 + 2], sc[8 * s2 + 3]); w.z = pg8::cvt_pk_bf16(sc[8 * s2 + 4], sc[8 * s2 + 5]); w.w = pg8::cvt_pk_bf16(sc[8 * s2 + 6], sc[8 * s2 + 7]); pb[s2] = __builtin_bit_cast(bf16x8, w); }
; #pragma unroll
;         for (int mb = 0; mb < 2; ++mb)
; #pragma unroll
;             for (int s2 = 0; s2 < 2; ++s2) {
.LBB0_362:
	v_sub_f32_e32 v34, v35, v172
	v_exp_f32_e32 v106, v34
	v_sub_f32_e32 v34, v36, v172
	v_exp_f32_e32 v107, v34
	v_sub_f32_e32 v34, v37, v172
	v_exp_f32_e32 v108, v34
	v_sub_f32_e32 v34, v38, v172
	v_exp_f32_e32 v109, v34
	v_sub_f32_e32 v34, v39, v172
	v_exp_f32_e32 v110, v34
	v_sub_f32_e32 v34, v40, v172
	v_exp_f32_e32 v111, v34
	v_sub_f32_e32 v34, v41, v172
	v_exp_f32_e32 v112, v34
	v_sub_f32_e32 v34, v42, v172
	v_exp_f32_e32 v113, v34
	v_sub_f32_e32 v34, v43, v172
	v_exp_f32_e32 v237, v34
	v_sub_f32_e32 v34, v44, v172
	v_exp_f32_e32 v242, v34
	v_sub_f32_e32 v34, v45, v172
	v_exp_f32_e32 v243, v34
	v_sub_f32_e32 v34, v46, v172
	v_exp_f32_e32 v244, v34
	v_sub_f32_e32 v34, v47, v172
	v_exp_f32_e32 v245, v34
	v_sub_f32_e32 v34, v48, v172
	v_exp_f32_e32 v246, v34
	v_sub_f32_e32 v34, v49, v172
	v_exp_f32_e32 v247, v34
	v_sub_f32_e32 v34, v51, v172
	v_exp_f32_e32 v51, v34
	v_cvt_pk_bf16_f32 v34, v106, v107
	v_cvt_pk_bf16_f32 v35, v108, v109
	v_cvt_pk_bf16_f32 v36, v110, v111
	v_cvt_pk_bf16_f32 v37, v112, v113
	v_cvt_pk_bf16_f32 v134, v237, v242
	v_cvt_pk_bf16_f32 v135, v243, v244
	v_cvt_pk_bf16_f32 v136, v245, v246
	v_cvt_pk_bf16_f32 v137, v247, v51
	ds_read_b64_tr_b16 v[38:39], v181 offset:4608
	ds_read_b64_tr_b16 v[40:41], v181 offset:5888
	ds_read_b64_tr_b16 v[44:45], v181 offset:5952
	ds_read_b64_tr_b16 v[42:43], v181 offset:4672
	s_waitcnt lgkmcnt(2)
	v_mfma_f32_32x32x16_bf16 v[18:33], v[38:41], v[34:37], v[18:33]
	ds_read_b64_tr_b16 v[38:39], v181 offset:7168
	ds_read_b64_tr_b16 v[40:41], v181 offset:8448
	v_add_f32_e32 v46, 0, v106
	ds_read_b64_tr_b16 v[240:241], v181 offset:8512
	ds_read_b64_tr_b16 v[238:239], v181 offset:7232
	s_waitcnt vmcnt(15)
	ds_write_b128 v231, v[70:73]
	s_waitcnt vmcnt(14)
	ds_write_b128 v232, v[138:141] offset:4608
	s_waitcnt vmcnt(13)
	ds_write_b128 v231, v[142:145] offset:1152
	s_waitcnt vmcnt(12)
	ds_write_b128 v232, v[146:149] offset:5888
	s_waitcnt vmcnt(11)
	ds_write_b128 v231, v[150:153] offset:2304
	s_waitcnt vmcnt(10)
	ds_write_b128 v232, v[154:157] offset:7168
	s_waitcnt vmcnt(9)
	ds_write_b128 v231, v[158:161] offset:3456
	s_waitcnt vmcnt(8)
	ds_write_b128 v232, v[162:165] offset:8448
	v_add_u32_e32 v122, 0x50, v168
	v_add_u32_e32 v126, 0x58, v168
	s_waitcnt lgkmcnt(10)
	v_mfma_f32_32x32x16_bf16 v[18:33], v[38:41], v[134:137], v[18:33]
	v_add_f32_e32 v38, v107, v46
	v_add_f32_e32 v38, v108, v38
	v_add_f32_e32 v38, v109, v38
	v_add_f32_e32 v38, v110, v38
	v_add_f32_e32 v38, v111, v38
	v_add_f32_e32 v38, v112, v38
	v_add_f32_e32 v248, v113, v38
	v_mfma_f32_32x32x16_bf16 v[2:17], v[42:45], v[34:37], v[2:17]
	v_or_b32_e32 v34, s10, v53
	v_min_u32_e32 v34, 0x3fff, v34
	v_mul_u32_u24_e32 v38, 0xc00, v34
	ds_read_b128 v[34:37], v177
	v_or_b32_e32 v38, v38, v176
	global_load_dwordx4 v[70:73], v38, s[8:9] offset:1024
	global_load_dwordx4 v[106:109], v38, s[8:9] offset:2048
	v_add_u32_e32 v38, 0x48, v168
	v_med3_i32 v38, v38, 0, v233
	v_mul_u32_u24_e32 v38, 0xc00, v38
	ds_read_b128 v[118:121], v177 offset:32
	v_or_b32_e32 v114, v38, v176
	s_waitcnt lgkmcnt(1)
	v_mfma_f32_32x32x16_bf16 v[34:49], v[34:37], v[66:69], 0
	v_med3_i32 v122, v122, 0, v233
	v_med3_i32 v126, v126, 0, v233
	v_mul_u32_u24_e32 v122, 0xc00, v122
	v_mul_u32_u24_e32 v126, 0xc00, v126
	v_or_b32_e32 v122, v122, v176
	v_or_b32_e32 v130, v126, v176
	global_load_dwordx4 v[110:113], v114, s[8:9] offset:1024
	s_nop 0
	global_load_dwordx4 v[114:117], v114, s[8:9] offset:2048
	ds_read_b128 v[138:141], v177 offset:96
	ds_read_b128 v[142:145], v177 offset:64
	s_waitcnt lgkmcnt(2)
	v_mfma_f32_32x32x16_bf16 v[34:49], v[118:121], v[62:65], v[34:49]
	global_load_dwordx4 v[118:121], v122, s[8:9] offset:1024
	s_nop 0
	global_load_dwordx4 v[122:125], v122, s[8:9] offset:2048
	s_nop 0
	global_load_dwordx4 v[126:129], v130, s[8:9] offset:1024
	s_nop 0
	global_load_dwordx4 v[130:133], v130, s[8:9] offset:2048
	s_waitcnt lgkmcnt(0)
	v_mfma_f32_32x32x16_bf16 v[34:49], v[142:145], v[58:61], v[34:49]
	v_add_f32_e32 v142, v237, v248
	v_add_f32_e32 v142, v242, v142
	v_add_f32_e32 v142, v243, v142
	v_add_f32_e32 v142, v244, v142
	v_add_f32_e32 v142, v245, v142
	v_add_f32_e32 v142, v246, v142
	v_add_f32_e32 v142, v247, v142
	v_mfma_f32_32x32x16_bf16 v[34:49], v[138:141], v[54:57], v[34:49]
	v_add_u32_e32 v138, 64, v173
	v_cmp_le_u32_e32 vcc, v138, v171
	v_add_u32_e32 v138, 0x41, v173
	v_add_u32_e32 v139, 0x42, v173
	v_add_f32_e32 v51, v51, v142
	v_add_f32_e32 v51, v50, v51
	s_nop 5
	v_cndmask_b32_e32 v34, v234, v34, vcc
	v_cmp_le_u32_e32 vcc, v138, v171
	v_mfma_f32_32x32x16_bf16 v[2:17], v[238:241], v[134:137], v[2:17]
	s_nop 0
	v_cndmask_b32_e32 v35, v234, v35, vcc
	v_cmp_le_u32_e32 vcc, v139, v171
	v_add_u32_e32 v139, 0x43, v173
	v_max3_f32 v138, v34, s31, v35
	v_cndmask_b32_e32 v36, v234, v36, vcc
	v_cmp_le_u32_e32 vcc, v139, v171
	v_add_u32_e32 v139, 0x48, v173
	s_nop 0
	v_cndmask_b32_e32 v37, v234, v37, vcc
	v_cmp_le_u32_e32 vcc, v139, v171
	v_add_u32_e32 v139, 0x49, v173
	v_max3_f32 v138, v138, v36, v37
	v_cndmask_b32_e32 v38, v234, v38, vcc
	v_cmp_le_u32_e32 vcc, v139, v171
	v_add_u32_e32 v139, 0x4a, v173
	s_nop 0
	v_cndmask_b32_e32 v39, v234, v39, vcc
	v_cmp_le_u32_e32 vcc, v139, v171
	v_add_u32_e32 v139, 0x4b, v173
	v_max3_f32 v138, v138, v38, v39
	v_cndmask_b32_e32 v40, v234, v40, vcc
	v_cmp_le_u32_e32 vcc, v139, v171
	v_add_u32_e32 v139, 0x50, v173
	s_nop 0
	v_cndmask_b32_e32 v41, v234, v41, vcc
	v_cmp_le_u32_e32 vcc, v139, v171
	v_add_u32_e32 v139, 0x51, v173
	v_max3_f32 v138, v138, v40, v41
	v_cndmask_b32_e32 v42, v234, v42, vcc
	v_cmp_le_u32_e32 vcc, v139, v171
	v_add_u32_e32 v139, 0x52, v173
	s_nop 0
	v_cndmask_b32_e32 v43, v234, v43, vcc
	v_cmp_le_u32_e32 vcc, v139, v171
	v_add_u32_e32 v139, 0x53, v173
	v_max3_f32 v138, v138, v42, v43
	v_cndmask_b32_e32 v44, v234, v44, vcc
	v_cmp_le_u32_e32 vcc, v139, v171
	v_add_u32_e32 v139, 0x58, v173
	s_nop 0
	v_cndmask_b32_e32 v45, v234, v45, vcc
	v_cmp_le_u32_e32 vcc, v139, v171
	v_add_u32_e32 v139, 0x59, v173
	v_max3_f32 v138, v138, v44, v45
	v_cndmask_b32_e32 v46, v234, v46, vcc
	v_cmp_le_u32_e32 vcc, v139, v171
	v_add_u32_e32 v139, 0x5a, v173
	s_nop 0
	v_cndmask_b32_e32 v47, v234, v47, vcc
	v_cmp_le_u32_e32 vcc, v139, v171
	v_add_u32_e32 v139, 0x5b, v173
	v_max3_f32 v138, v138, v46, v47
	v_cndmask_b32_e32 v48, v234, v48, vcc
	v_cmp_le_u32_e32 vcc, v139, v171
	s_nop 1
	v_cndmask_b32_e32 v49, v234, v49, vcc
	v_max3_f32 v138, v138, v48, v49
	v_mov_b32_e32 v139, v138
	s_nop 1
	v_permlane32_swap_b32_e32 v139, v138
	s_waitcnt lgkmcnt(0)
	v_max_f32_e32 v50, v139, v139
	v_max_f32_e32 v50, v138, v50
	v_cmp_gt_f32_e32 vcc, v50, v172
	s_cbranch_vccz .LBB0_364
; __device__ __forceinline__ unsigned cvt_pk_bf16(float lo, float hi) { unsigned r; asm volatile("v_cvt_pk_bf16_f32 %0, %1, %2" : "=v"(r) : "v"(lo), "v"(hi)); return r; }
; #define LAS __attribute__((address_space(3)))
; #define MFMA32(a, b, c) __builtin_amdgcn_mfma_f32_32x32x16_bf16((a), (b), (c), 0, 0, 0)
; template <int STAGE, int OFF> __device__ __forceinline__ void attn32_unit(const bf16* base, bf16* yrow0, int blk0, int u, LAS unsigned char* xtab, LAS unsigned char* kbuf, LAS unsigned char* vbuf, int lane, ...
;     ...
;         if (__any(mx > m)) {
;             const float mn = fmaxf(m, mx), alpha = __builtin_amdgcn_exp2f(m - mn); m = mn; l *= alpha;
; #pragma unroll
;             for (int i = 0; i < 16; ++i) { o[0][i] *= alpha; o[1][i] *= alpha; }
;         }
;         float ps = 0.f;
; #pragma unroll
;         for (int rg = 0; rg < 16; ++rg) { sc[rg] = __builtin_amdgcn_exp2f(sc[rg] - m); ps += sc[rg]; }
;         l += ps;
;         bf16x8 pb[2];
; #pragma unroll
;         for (int s2 = 0; s2 < 2; ++s2) { v4u w; w.x = pg8::cvt_pk_bf16(sc[8 * s2], sc[8 * s2 + 1]); w.y = pg8::cvt_pk_bf16(sc[8 * s2 + 2], sc[8 * s2 + 3]); w.z = pg8::cvt_pk_bf16(sc[8 * s2 + 4], sc[8 * s2 + 5]); w.w = pg8::cvt_pk_bf16(sc[8 * s2 + 6], sc[8 * s2 + 7]); pb[s2] = __builtin_bit_cast(bf16x8, w); }
; #pragma unroll
;         for (int mb = 0; mb < 2; ++mb)
; #pragma unroll
;             for (int s2 = 0; s2 < 2; ++s2) {
;                 LAS unsigned char* vp = vbuf + tr_off + (16 * s2) * 160 + 64 * mb;
;                 const v4i16 a0 = __builtin_amdgcn_ds_read_tr16_b64_v4i16((LAS v4i16*)vp), a1 = __builtin_amdgcn_ds_read_tr16_b64_v4i16((LAS v4i16*)(vp + 8 * 160));
;                 const bf16x8 va = __builtin_shufflevector(a0, a1, 0, 1, 2, 3, 4, 5, 6, 7);
;                 o[mb] = MFMA32(va, pb[s2], o[mb]);
;             }
	v_max_f32_e32 v50, v50, v50
	v_max_f32_e32 v134, v172, v172
	v_max_f32_e32 v134, v134, v50
	v_sub_f32_e32 v50, v172, v134
	v_exp_f32_e32 v50, v50
	v_mov_b32_e32 v172, v134
	v_pk_mul_f32 v[32:33], v[32:33], v[50:51] op_sel_hi:[1,0]
	v_pk_mul_f32 v[30:31], v[30:31], v[50:51] op_sel_hi:[1,0]
	v_pk_mul_f32 v[28:29], v[28:29], v[50:51] op_sel_hi:[1,0]
	v_pk_mul_f32 v[26:27], v[26:27], v[50:51] op_sel_hi:[1,0]
	v_pk_mul_f32 v[24:25], v[24:25], v[50:51] op_sel_hi:[1,0]
	v_pk_mul_f32 v[22:23], v[22:23], v[50:51] op_sel_hi:[1,0]
	v_pk_mul_f32 v[20:21], v[20:21], v[50:51] op_sel_hi:[1,0]
	v_pk_mul_f32 v[18:19], v[18:19], v[50:51] op_sel_hi:[1,0]
	v_pk_mul_f32 v[16:17], v[16:17], v[50:51] op_sel_hi:[1,0]
	v_pk_mul_f32 v[14:15], v[14:15], v[50:51] op_sel_hi:[1,0]
	v_pk_mul_f32 v[12:13], v[12:13], v[50:51] op_sel_hi:[1,0]
	v_pk_mul_f32 v[10:11], v[10:11], v[50:51] op_sel_hi:[1,0]
	v_pk_mul_f32 v[8:9], v[8:9], v[50:51] op_sel_hi:[1,0]
	v_pk_mul_f32 v[6:7], v[6:7], v[50:51] op_sel_hi:[1,0]
	v_pk_mul_f32 v[4:5], v[4:5], v[50:51] op_sel_hi:[1,0]
	v_pk_mul_f32 v[2:3], v[2:3], v[50:51] op_sel_hi:[1,0]
	v_mul_f32_e32 v51, v51, v50
.LBB0_364:
	v_sub_f32_e32 v34, v34, v172
	v_exp_f32_e32 v138, v34
	v_sub_f32_e32 v34, v35, v172
	v_exp_f32_e32 v142, v34
	v_sub_f32_e32 v34, v36, v172
	v_exp_f32_e32 v143, v34
	v_sub_f32_e32 v34, v37, v172
	v_exp_f32_e32 v144, v34
	v_sub_f32_e32 v34, v38, v172
	v_exp_f32_e32 v145, v34
	v_sub_f32_e32 v34, v39, v172
	v_exp_f32_e32 v146, v34
	v_sub_f32_e32 v34, v40, v172
	v_exp_f32_e32 v147, v34
	v_sub_f32_e32 v34, v41, v172
	v_exp_f32_e32 v148, v34
	v_sub_f32_e32 v34, v42, v172
	v_exp_f32_e32 v150, v34
	v_sub_f32_e32 v34, v43, v172
	v_exp_f32_e32 v151, v34
	v_sub_f32_e32 v34, v44, v172
	v_exp_f32_e32 v152, v34
	v_sub_f32_e32 v34, v45, v172
	v_exp_f32_e32 v153, v34
	v_sub_f32_e32 v34, v46, v172
	v_exp_f32_e32 v154, v34
	v_sub_f32_e32 v34, v47, v172
	v_exp_f32_e32 v155, v34
	v_sub_f32_e32 v34, v48, v172
	v_exp_f32_e32 v156, v34
	v_sub_f32_e32 v34, v49, v172
	v_exp_f32_e32 v157, v34
	v_cvt_pk_bf16_f32 v34, v138, v142
	v_cvt_pk_bf16_f32 v35, v143, v144
	v_cvt_pk_bf16_f32 v36, v145, v146
	v_cvt_pk_bf16_f32 v37, v147, v148
	v_cvt_pk_bf16_f32 v134, v150, v151
	v_cvt_pk_bf16_f32 v135, v152, v153
	v_cvt_pk_bf16_f32 v136, v154, v155
	v_cvt_pk_bf16_f32 v137, v156, v157
	ds_read_b64_tr_b16 v[38:39], v181 offset:4608
	ds_read_b64_tr_b16 v[40:41], v181 offset:5888
	ds_read_b64_tr_b16 v[44:45], v181 offset:5952
	ds_read_b64_tr_b16 v[42:43], v181 offset:4672
	s_waitcnt lgkmcnt(2)
	v_mfma_f32_32x32x16_bf16 v[18:33], v[38:41], v[34:37], v[18:33]
	ds_read_b64_tr_b16 v[38:39], v181 offset:7168
	ds_read_b64_tr_b16 v[40:41], v181 offset:8448
	s_add_i32 s10, s13, s22
	v_add_u32_e32 v50, s10, v180
	v_add_f32_e32 v46, 0, v138
	ds_read_b64_tr_b16 v[140:141], v181 offset:8512
	ds_read_b64_tr_b16 v[138:139], v181 offset:7232
	s_waitcnt vmcnt(15)
	ds_write_b128 v231, v[74:77]
	s_waitcnt vmcnt(14)
	ds_write_b128 v232, v[78:81] offset:4608
	s_waitcnt vmcnt(13)
	ds_write_b128 v231, v[82:85] offset:1152
	s_waitcnt vmcnt(12)
	ds_write_b128 v232, v[86:89] offset:5888
	s_waitcnt vmcnt(11)
	ds_write_b128 v231, v[90:93] offset:2304
	s_waitcnt vmcnt(10)
	ds_write_b128 v232, v[94:97] offset:7168
	s_waitcnt vmcnt(9)
	ds_write_b128 v231, v[98:101] offset:3456
	s_waitcnt vmcnt(8)
	ds_write_b128 v232, v[102:105] offset:8448
	s_waitcnt lgkmcnt(10)
	v_mfma_f32_32x32x16_bf16 v[18:33], v[38:41], v[134:137], v[18:33]
	v_add_f32_e32 v38, v142, v46
	v_add_f32_e32 v38, v143, v38
	v_add_f32_e32 v38, v144, v38
	v_add_f32_e32 v38, v145, v38
	v_add_f32_e32 v38, v146, v38
	v_add_f32_e32 v38, v147, v38
	v_add_f32_e32 v158, v148, v38
	v_mfma_f32_32x32x16_bf16 v[2:17], v[42:45], v[34:37], v[2:17]
	v_max_i32_e32 v34, 0xffffffa0, v50
	v_add_u32_e32 v34, 0x60, v34
	v_min_u32_e32 v34, 0x3fff, v34
	v_mul_u32_u24_e32 v34, 0xc00, v34
	v_or_b32_e32 v34, v34, v176
	global_load_dwordx4 v[74:77], v34, s[8:9] offset:1024
	global_load_dwordx4 v[78:81], v34, s[8:9] offset:2048
	v_max_i32_e32 v34, 0xffffff98, v50
	v_add_u32_e32 v38, 0x68, v34
	ds_read_b128 v[34:37], v177
	v_min_u32_e32 v38, 0x3fff, v38
	v_mul_u32_u24_e32 v38, 0xc00, v38
	v_or_b32_e32 v38, v38, v176
	global_load_dwordx4 v[82:85], v38, s[8:9] offset:1024
	global_load_dwordx4 v[86:89], v38, s[8:9] offset:2048
	v_max_i32_e32 v38, 0xffffff90, v50
	ds_read_b128 v[98:101], v177 offset:32
	v_add_u32_e32 v90, 0x70, v38
	s_waitcnt lgkmcnt(1)
	v_mfma_f32_32x32x16_bf16 v[34:49], v[34:37], v[66:69], 0
	v_min_u32_e32 v90, 0x3fff, v90
	v_mul_u32_u24_e32 v90, 0xc00, v90
	v_or_b32_e32 v94, v90, v176
	global_load_dwordx4 v[90:93], v94, s[8:9] offset:1024
	s_nop 0
	global_load_dwordx4 v[94:97], v94, s[8:9] offset:2048
	ds_read_b128 v[142:145], v177 offset:96
	ds_read_b128 v[146:149], v177 offset:64
	s_waitcnt lgkmcnt(2)
	v_mfma_f32_32x32x16_bf16 v[34:49], v[98:101], v[62:65], v[34:49]
	v_max_i32_e32 v98, 0xffffff88, v50
	v_add_u32_e32 v98, 0x78, v98
	v_min_u32_e32 v98, 0x3fff, v98
	v_mul_u32_u24_e32 v98, 0xc00, v98
	v_or_b32_e32 v102, v98, v176
	global_load_dwordx4 v[98:101], v102, s[8:9] offset:1024
	s_nop 0
	global_load_dwordx4 v[102:105], v102, s[8:9] offset:2048
	s_waitcnt lgkmcnt(0)
; __device__ __forceinline__ unsigned cvt_pk_bf16(float lo, float hi) { unsigned r; asm volatile("v_cvt_pk_bf16_f32 %0, %1, %2" : "=v"(r) : "v"(lo), "v"(hi)); return r; }
; #define LAS __attribute__((address_space(3)))
; template <int STAGE, int OFF> __device__ __forceinline__ void attn32_unit(const bf16* base, bf16* yrow0, int blk0, int u, LAS unsigned char* xtab, LAS unsigned char* kbuf, LAS unsigned char* vbuf, int lane, ...
;     ...
; #pragma unroll
;         for (int ks = 0; ks < 4; ++ks) { const bf16x8 ka = *(const LAS bf16x8*)(kbuf + qi * 144 + 32 * ks + 16 * h); sc = MFMA32(ka, qb[ks], sc); }
;         if (pp == 4) {
; #pragma unroll
;             for (int ks = 0; ks < 4; ++ks) qb[ks] = *(const bf16x8*)(nbase + (size_t)min(nt0 + (qi << nsh), SEQ - 1) * 1536 + 16 * ks + 8 * h);
;         }
;         const int mbase = n0 + 4 * h - lo; float mx = -INFINITY;
; #pragma unroll
;         for (int rg = 0; rg < 16; ++rg) { sc[rg] = ((unsigned)(mbase + (rg & 3) + 8 * (rg >> 2)) <= mspan) ? sc[rg] : -INFINITY; mx = fmaxf(mx, sc[rg]); }
;         mx = fmaxf(mx, __shfl_xor(mx, 32));
;         if (__any(mx > m)) {
;             const float mn = fmaxf(m, mx), alpha = __builtin_amdgcn_exp2f(m - mn); m = mn; l *= alpha;
; #pragma unroll
;             for (int i = 0; i < 16; ++i) { o[0][i] *= alpha; o[1][i] *= alpha; }
;         }
;         float ps = 0.f;
; #pragma unroll
;         for (int rg = 0; rg < 16; ++rg) { sc[rg] = __builtin_amdgcn_exp2f(sc[rg] - m); ps += sc[rg]; }
;         l += ps;
;         bf16x8 pb[2];
; #pragma unroll
;         for (int s2 = 0; s2 < 2; ++s2) { v4u w; w.x = pg8::cvt_pk_bf16(sc[8 * s2], sc[8 * s2 + 1]); w.y = pg8::cvt_pk_bf16(sc[8 * s2 + 2], sc[8 * s2 + 3]); w.z = pg8::cvt_pk_bf16(sc[8 * s2 + 4], sc[8 * s2 + 5]); w.w = pg8::cvt_pk_bf16(sc[8 * s2 + 6], sc[8 * s2 + 7]); pb[s2] = __builtin_bit_cast(bf16x8, w); }
; #pragma unroll
;         for (int mb = 0; mb < 2; ++mb)
; #pragma unroll
;             for (int s2 = 0; s2 < 2; ++s2) {
;                 LAS unsigned char* vp = vbuf + tr_off + (16 * s2) * 160 + 64 * mb;
;                 const v4i16 a0 = __builtin_amdgcn_ds_read_tr16_b64_v4i16((LAS v4i16*)vp), a1 = __builtin_amdgcn_ds_read_tr16_b64_v4i16((LAS v4i16*)(vp + 8 * 160));
;                 const bf16x8 va = __builtin_shufflevector(a0, a1, 0, 1, 2, 3, 4, 5, 6, 7);
;                 o[mb] = MFMA32(va, pb[s2], o[mb]);
;             }
	v_mfma_f32_32x32x16_bf16 v[34:49], v[146:149], v[58:61], v[34:49]
	v_add_f32_e32 v146, v150, v158
	v_add_f32_e32 v146, v151, v146
	v_add_f32_e32 v146, v152, v146
	v_add_f32_e32 v146, v153, v146
	v_add_f32_e32 v146, v154, v146
	v_add_f32_e32 v146, v155, v146
	v_add_f32_e32 v146, v156, v146
	v_mfma_f32_32x32x16_bf16 v[34:49], v[142:145], v[54:57], v[34:49]
	v_add_u32_e32 v142, 0x60, v173
	v_cmp_le_u32_e32 vcc, v142, v171
	v_add_u32_e32 v142, 0x61, v173
	v_add_u32_e32 v143, 0x62, v173
	v_add_f32_e32 v144, v157, v146
	v_add_f32_e32 v51, v51, v144
	s_nop 5
	v_cndmask_b32_e32 v34, v234, v34, vcc
	v_cmp_le_u32_e32 vcc, v142, v171
	v_mfma_f32_32x32x16_bf16 v[2:17], v[138:141], v[134:137], v[2:17]
	s_nop 0
	v_cndmask_b32_e32 v35, v234, v35, vcc
	v_cmp_le_u32_e32 vcc, v143, v171
	v_add_u32_e32 v143, 0x63, v173
	v_max3_f32 v142, v34, s31, v35
	v_cndmask_b32_e32 v36, v234, v36, vcc
	v_cmp_le_u32_e32 vcc, v143, v171
	v_add_u32_e32 v143, 0x68, v173
	s_nop 0
	v_cndmask_b32_e32 v37, v234, v37, vcc
	v_cmp_le_u32_e32 vcc, v143, v171
	v_add_u32_e32 v143, 0x69, v173
	v_max3_f32 v142, v142, v36, v37
	v_cndmask_b32_e32 v38, v234, v38, vcc
	v_cmp_le_u32_e32 vcc, v143, v171
	v_add_u32_e32 v143, 0x6a, v173
	s_nop 0
	v_cndmask_b32_e32 v39, v234, v39, vcc
	v_cmp_le_u32_e32 vcc, v143, v171
	v_add_u32_e32 v143, 0x6b, v173
	v_max3_f32 v142, v142, v38, v39
	v_cndmask_b32_e32 v40, v234, v40, vcc
	v_cmp_le_u32_e32 vcc, v143, v171
	v_add_u32_e32 v143, 0x70, v173
	s_nop 0
	v_cndmask_b32_e32 v41, v234, v41, vcc
	v_cmp_le_u32_e32 vcc, v143, v171
	v_add_u32_e32 v143, 0x71, v173
	v_max3_f32 v142, v142, v40, v41
	v_cndmask_b32_e32 v42, v234, v42, vcc
	v_cmp_le_u32_e32 vcc, v143, v171
	v_add_u32_e32 v143, 0x72, v173
	s_nop 0
	v_cndmask_b32_e32 v43, v234, v43, vcc
	v_cmp_le_u32_e32 vcc, v143, v171
	v_add_u32_e32 v143, 0x73, v173
	v_max3_f32 v142, v142, v42, v43
	v_cndmask_b32_e32 v44, v234, v44, vcc
	v_cmp_le_u32_e32 vcc, v143, v171
	v_add_u32_e32 v143, 0x78, v173
	s_nop 0
	v_cndmask_b32_e32 v45, v234, v45, vcc
	v_cmp_le_u32_e32 vcc, v143, v171
	v_add_u32_e32 v143, 0x79, v173
	v_max3_f32 v142, v142, v44, v45
	v_cndmask_b32_e32 v46, v234, v46, vcc
	v_cmp_le_u32_e32 vcc, v143, v171
	v_add_u32_e32 v143, 0x7a, v173
	s_nop 0
	v_cndmask_b32_e32 v47, v234, v47, vcc
	v_cmp_le_u32_e32 vcc, v143, v171
	v_add_u32_e32 v143, 0x7b, v173
	v_max3_f32 v142, v142, v46, v47
	v_cndmask_b32_e32 v48, v234, v48, vcc
	v_cmp_le_u32_e32 vcc, v143, v171
	s_nop 1
	v_cndmask_b32_e32 v49, v234, v49, vcc
	v_max3_f32 v142, v142, v48, v49
	v_mov_b32_e32 v143, v142
	s_nop 1
	v_permlane32_swap_b32_e32 v143, v142
	s_waitcnt lgkmcnt(0)
	v_max_f32_e32 v134, v143, v143
	v_max_f32_e32 v134, v142, v134
	v_cmp_gt_f32_e32 vcc, v134, v172
	s_cbranch_vccz .LBB0_366
	v_max_f32_e32 v134, v134, v134
	v_max_f32_e32 v135, v172, v172
	v_max_f32_e32 v135, v135, v134
	v_sub_f32_e32 v134, v172, v135
	v_exp_f32_e32 v134, v134
	v_mov_b32_e32 v172, v135
	v_pk_mul_f32 v[32:33], v[32:33], v[134:135] op_sel_hi:[1,0]
	v_pk_mul_f32 v[30:31], v[30:31], v[134:135] op_sel_hi:[1,0]
	v_pk_mul_f32 v[28:29], v[28:29], v[134:135] op_sel_hi:[1,0]
	v_pk_mul_f32 v[26:27], v[26:27], v[134:135] op_sel_hi:[1,0]
	v_pk_mul_f32 v[24:25], v[24:25], v[134:135] op_sel_hi:[1,0]
	v_pk_mul_f32 v[22:23], v[22:23], v[134:135] op_sel_hi:[1,0]
	v_pk_mul_f32 v[20:21], v[20:21], v[134:135] op_sel_hi:[1,0]
	v_pk_mul_f32 v[18:19], v[18:19], v[134:135] op_sel_hi:[1,0]
	v_pk_mul_f32 v[16:17], v[16:17], v[134:135] op_sel_hi:[1,0]
	v_pk_mul_f32 v[14:15], v[14:15], v[134:135] op_sel_hi:[1,0]
	v_pk_mul_f32 v[12:13], v[12:13], v[134:135] op_sel_hi:[1,0]
	v_pk_mul_f32 v[10:11], v[10:11], v[134:135] op_sel_hi:[1,0]
	v_pk_mul_f32 v[8:9], v[8:9], v[134:135] op_sel_hi:[1,0]
	v_pk_mul_f32 v[6:7], v[6:7], v[134:135] op_sel_hi:[1,0]
	v_pk_mul_f32 v[4:5], v[4:5], v[134:135] op_sel_hi:[1,0]
	v_pk_mul_f32 v[2:3], v[2:3], v[134:135] op_sel_hi:[1,0]
	v_mul_f32_e32 v51, v51, v134
.LBB0_366:
	v_sub_f32_e32 v34, v34, v172
	v_exp_f32_e32 v134, v34
	v_sub_f32_e32 v34, v35, v172
	v_exp_f32_e32 v135, v34
	v_sub_f32_e32 v34, v36, v172
	v_exp_f32_e32 v136, v34
	v_sub_f32_e32 v34, v37, v172
	v_exp_f32_e32 v137, v34
	v_sub_f32_e32 v34, v38, v172
	v_exp_f32_e32 v146, v34
	v_sub_f32_e32 v34, v39, v172
	v_exp_f32_e32 v147, v34
	v_sub_f32_e32 v34, v40, v172
	v_exp_f32_e32 v148, v34
	v_sub_f32_e32 v34, v41, v172
	v_exp_f32_e32 v149, v34
	v_sub_f32_e32 v34, v42, v172
	v_exp_f32_e32 v152, v34
	v_sub_f32_e32 v34, v43, v172
	v_exp_f32_e32 v153, v34
	v_sub_f32_e32 v34, v44, v172
	v_exp_f32_e32 v154, v34
	v_sub_f32_e32 v34, v45, v172
	v_exp_f32_e32 v155, v34
	v_sub_f32_e32 v34, v46, v172
	v_exp_f32_e32 v156, v34
	v_sub_f32_e32 v34, v47, v172
	v_exp_f32_e32 v157, v34
	v_sub_f32_e32 v34, v48, v172
	v_exp_f32_e32 v158, v34
	v_sub_f32_e32 v34, v49, v172
	v_exp_f32_e32 v159, v34
	v_cvt_pk_bf16_f32 v34, v134, v135
	v_cvt_pk_bf16_f32 v35, v136, v137
	v_cvt_pk_bf16_f32 v36, v146, v147
	v_cvt_pk_bf16_f32 v37, v148, v149
	v_cvt_pk_bf16_f32 v138, v152, v153
	v_cvt_pk_bf16_f32 v139, v154, v155
	v_cvt_pk_bf16_f32 v140, v156, v157
	v_cvt_pk_bf16_f32 v141, v158, v159
	ds_read_b64_tr_b16 v[38:39], v181 offset:4608
	ds_read_b64_tr_b16 v[40:41], v181 offset:5888
	v_or_b32_e32 v42, s10, v1
	v_min_i32_e32 v142, 0x3fff, v42
	ds_read_b64_tr_b16 v[42:43], v181 offset:7168
	ds_read_b64_tr_b16 v[44:45], v181 offset:8448
	ds_read_b64_tr_b16 v[48:49], v181 offset:5952
	ds_read_b64_tr_b16 v[46:47], v181 offset:4672
	v_mul_u32_u24_e32 v168, 0xc00, v142
	s_waitcnt lgkmcnt(4)
; __device__ __forceinline__ unsigned cvt_pk_bf16(float lo, float hi) { unsigned r; asm volatile("v_cvt_pk_bf16_f32 %0, %1, %2" : "=v"(r) : "v"(lo), "v"(hi)); return r; }
; #define LAS __attribute__((address_space(3)))
; template <int STAGE, int OFF> __device__ __forceinline__ void attn32_unit(const bf16* base, bf16* yrow0, int blk0, int u, LAS unsigned char* xtab, LAS unsigned char* kbuf, LAS unsigned char* vbuf, int lane, ...
;     ...
; #pragma unroll
;         for (int ks = 0; ks < 4; ++ks) { const bf16x8 ka = *(const LAS bf16x8*)(kbuf + qi * 144 + 32 * ks + 16 * h); sc = MFMA32(ka, qb[ks], sc); }
;         if (pp == 4) {
; #pragma unroll
;             for (int ks = 0; ks < 4; ++ks) qb[ks] = *(const bf16x8*)(nbase + (size_t)min(nt0 + (qi << nsh), SEQ - 1) * 1536 + 16 * ks + 8 * h);
;         }
;         const int mbase = n0 + 4 * h - lo; float mx = -INFINITY;
; #pragma unroll
;         for (int rg = 0; rg < 16; ++rg) { sc[rg] = ((unsigned)(mbase + (rg & 3) + 8 * (rg >> 2)) <= mspan) ? sc[rg] : -INFINITY; mx = fmaxf(mx, sc[rg]); }
;         mx = fmaxf(mx, __shfl_xor(mx, 32));
;         if (__any(mx > m)) {
;             const float mn = fmaxf(m, mx), alpha = __builtin_amdgcn_exp2f(m - mn); m = mn; l *= alpha;
; #pragma unroll
;             for (int i = 0; i < 16; ++i) { o[0][i] *= alpha; o[1][i] *= alpha; }
;         }
;         float ps = 0.f;
; #pragma unroll
;         for (int rg = 0; rg < 16; ++rg) { sc[rg] = __builtin_amdgcn_exp2f(sc[rg] - m); ps += sc[rg]; }
;         l += ps;
;         bf16x8 pb[2];
; #pragma unroll
;         for (int s2 = 0; s2 < 2; ++s2) { v4u w; w.x = pg8::cvt_pk_bf16(sc[8 * s2], sc[8 * s2 + 1]); w.y = pg8::cvt_pk_bf16(sc[8 * s2 + 2], sc[8 * s2 + 3]); w.z = pg8::cvt_pk_bf16(sc[8 * s2 + 4], sc[8 * s2 + 5]); w.w = pg8::cvt_pk_bf16(sc[8 * s2 + 6], sc[8 * s2 + 7]); pb[s2] = __builtin_bit_cast(bf16x8, w); }
; #pragma unroll
;         for (int mb = 0; mb < 2; ++mb)
; #pragma unroll
;             for (int s2 = 0; s2 < 2; ++s2) {
;                 LAS unsigned char* vp = vbuf + tr_off + (16 * s2) * 160 + 64 * mb;
;                 const v4i16 a0 = __builtin_amdgcn_ds_read_tr16_b64_v4i16((LAS v4i16*)vp), a1 = __builtin_amdgcn_ds_read_tr16_b64_v4i16((LAS v4i16*)(vp + 8 * 160));
;                 const bf16x8 va = __builtin_shufflevector(a0, a1, 0, 1, 2, 3, 4, 5, 6, 7);
;                 o[mb] = MFMA32(va, pb[s2], o[mb]);
;             }
	v_mfma_f32_32x32x16_bf16 v[18:33], v[38:41], v[34:37], v[18:33]
	v_lshl_add_u64 v[38:39], s[8:9], 0, v[168:169]
	v_lshlrev_b32_e32 v168, 1, v166
	v_lshl_add_u64 v[150:151], v[38:39], 0, v[168:169]
	v_add_f32_e32 v38, 0, v134
	v_add_f32_e32 v38, v135, v38
	v_add_f32_e32 v38, v136, v38
	v_add_f32_e32 v38, v137, v38
	s_waitcnt lgkmcnt(0)
	v_mfma_f32_32x32x16_bf16 v[2:17], v[46:49], v[34:37], v[2:17]
	v_max_i32_e32 v34, 0xffffff80, v50
	v_add_u32_e32 v34, 0x80, v34
	v_min_u32_e32 v34, 0x3fff, v34
	v_add_f32_e32 v38, v146, v38
	v_mul_u32_u24_e32 v34, 0xc00, v34
	ds_read_b64_tr_b16 v[144:145], v181 offset:8512
	ds_read_b64_tr_b16 v[142:143], v181 offset:7232
	v_add_f32_e32 v38, v147, v38
	s_waitcnt vmcnt(15)
	ds_write_b128 v231, v[70:73]
	s_waitcnt vmcnt(14)
	ds_write_b128 v232, v[106:109] offset:4608
	s_waitcnt vmcnt(13)
	ds_write_b128 v231, v[110:113] offset:1152
	s_waitcnt vmcnt(12)
	ds_write_b128 v232, v[114:117] offset:5888
	s_waitcnt vmcnt(11)
	ds_write_b128 v231, v[118:121] offset:2304
	s_waitcnt vmcnt(10)
	ds_write_b128 v232, v[122:125] offset:7168
	s_waitcnt vmcnt(9)
	ds_write_b128 v231, v[126:129] offset:3456
	s_waitcnt vmcnt(8)
	ds_write_b128 v232, v[130:133] offset:8448
	v_or_b32_e32 v34, v34, v176
	v_add_f32_e32 v38, v148, v38
	global_load_dwordx4 v[106:109], v34, s[8:9] offset:1024
	global_load_dwordx4 v[110:113], v34, s[8:9] offset:2048
	v_max_i32_e32 v34, 0xffffff78, v50
	v_add_f32_e32 v160, v149, v38
	v_add_u32_e32 v38, 0x88, v34
	ds_read_b128 v[34:37], v177
	v_min_u32_e32 v38, 0x3fff, v38
	v_mul_u32_u24_e32 v38, 0xc00, v38
	v_or_b32_e32 v38, v38, v176
	global_load_dwordx4 v[114:117], v38, s[8:9] offset:1024
	global_load_dwordx4 v[118:121], v38, s[8:9] offset:2048
	v_max_i32_e32 v38, 0xffffff70, v50
	ds_read_b128 v[70:73], v177 offset:32
	v_mfma_f32_32x32x16_bf16 v[18:33], v[42:45], v[138:141], v[18:33]
	v_add_u32_e32 v122, 0x90, v38
	v_max_i32_e32 v50, 0xffffff68, v50
	v_add_u32_e32 v50, 0x98, v50
	v_min_u32_e32 v50, 0x3fff, v50
	v_mul_u32_u24_e32 v50, 0xc00, v50
	v_or_b32_e32 v50, v50, v176
	s_waitcnt lgkmcnt(1)
	v_mfma_f32_32x32x16_bf16 v[34:49], v[34:37], v[66:69], 0
	v_min_u32_e32 v66, 0x3fff, v122
	v_mul_u32_u24_e32 v66, 0xc00, v66
	v_or_b32_e32 v66, v66, v176
	global_load_dwordx4 v[122:125], v66, s[8:9] offset:1024
	global_load_dwordx4 v[126:129], v66, s[8:9] offset:2048
	ds_read_b128 v[146:149], v177 offset:96
	ds_read_b128 v[66:69], v177 offset:64
	global_load_dwordx4 v[130:133], v50, s[8:9] offset:1024
	global_load_dwordx4 v[134:137], v50, s[8:9] offset:2048
	v_add_f32_e32 v50, v152, v160
	s_waitcnt lgkmcnt(2)
	v_mfma_f32_32x32x16_bf16 v[34:49], v[70:73], v[62:65], v[34:49]
	v_add_f32_e32 v50, v153, v50
	v_add_f32_e32 v50, v154, v50
	v_add_f32_e32 v50, v155, v50
	v_add_f32_e32 v50, v156, v50
	v_add_f32_e32 v50, v157, v50
	s_waitcnt lgkmcnt(0)
	v_mfma_f32_32x32x16_bf16 v[34:49], v[66:69], v[58:61], v[34:49]
	global_load_dwordx4 v[66:69], v[150:151], off
	global_load_dwordx4 v[62:65], v[150:151], off offset:32
	global_load_dwordx4 v[58:61], v[150:151], off offset:64
	global_load_dwordx4 v[70:73], v[150:151], off offset:96
	v_add_f32_e32 v150, v158, v50
	v_add_u32_e32 v50, 0x80, v173
	v_cmp_le_u32_e32 vcc, v50, v171
	v_mfma_f32_32x32x16_bf16 v[34:49], v[146:149], v[54:57], v[34:49]
	v_add_u32_e32 v54, 0x82, v173
	v_mfma_f32_32x32x16_bf16 v[2:17], v[142:145], v[138:141], v[2:17]
	s_nop 9
	v_cndmask_b32_e32 v50, v234, v34, vcc
	v_add_u32_e32 v34, 0x81, v173
	v_cmp_le_u32_e32 vcc, v34, v171
	s_nop 1
	v_cndmask_b32_e32 v35, v234, v35, vcc
	v_cmp_le_u32_e32 vcc, v54, v171
	v_add_u32_e32 v54, 0x83, v173
	v_max3_f32 v34, v50, s31, v35
	v_cndmask_b32_e32 v36, v234, v36, vcc
	v_cmp_le_u32_e32 vcc, v54, v171
	v_add_u32_e32 v54, 0x88, v173
	s_nop 0
	v_cndmask_b32_e32 v37, v234, v37, vcc
	v_cmp_le_u32_e32 vcc, v54, v171
	v_add_u32_e32 v54, 0x89, v173
	v_max3_f32 v34, v34, v36, v37
	v_cndmask_b32_e32 v38, v234, v38, vcc
	v_cmp_le_u32_e32 vcc, v54, v171
	v_add_u32_e32 v54, 0x8a, v173
	s_nop 0
	v_cndmask_b32_e32 v39, v234, v39, vcc
	v_cmp_le_u32_e32 vcc, v54, v171
	v_add_u32_e32 v54, 0x8b, v173
	v_max3_f32 v34, v34, v38, v39
	v_cndmask_b32_e32 v40, v234, v40, vcc
	v_cmp_le_u32_e32 vcc, v54, v171
	v_add_u32_e32 v54, 0x90, v173
	s_nop 0
	v_cndmask_b32_e32 v41, v234, v41, vcc
	v_cmp_le_u32_e32 vcc, v54, v171
	v_add_u32_e32 v54, 0x91, v173
	v_max3_f32 v34, v34, v40, v41
	v_cndmask_b32_e32 v42, v234, v42, vcc
	v_cmp_le_u32_e32 vcc, v54, v171
	v_add_u32_e32 v54, 0x92, v173
	s_nop 0
	v_cndmask_b32_e32 v43, v234, v43, vcc
	v_cmp_le_u32_e32 vcc, v54, v171
	v_add_u32_e32 v54, 0x93, v173
	v_max3_f32 v34, v34, v42, v43
	v_cndmask_b32_e32 v44, v234, v44, vcc
	v_cmp_le_u32_e32 vcc, v54, v171
	v_add_u32_e32 v54, 0x98, v173
	s_nop 0
	v_cndmask_b32_e32 v45, v234, v45, vcc
	v_cmp_le_u32_e32 vcc, v54, v171
	v_add_u32_e32 v54, 0x99, v173
	v_max3_f32 v34, v34, v44, v45
	v_cndmask_b32_e32 v46, v234, v46, vcc
	v_cmp_le_u32_e32 vcc, v54, v171
	v_add_u32_e32 v54, 0x9a, v173
	s_nop 0
	v_cndmask_b32_e32 v47, v234, v47, vcc
	v_cmp_le_u32_e32 vcc, v54, v171
	v_add_u32_e32 v54, 0x9b, v173
	v_max3_f32 v34, v34, v46, v47
	v_cndmask_b32_e32 v48, v234, v48, vcc
	v_cmp_le_u32_e32 vcc, v54, v171
	s_nop 1
	v_cndmask_b32_e32 v49, v234, v49, vcc
	v_max3_f32 v54, v34, v48, v49
	v_mov_b32_e32 v55, v54
	s_nop 1
	v_permlane32_swap_b32_e32 v55, v54
	v_add_f32_e32 v34, v159, v150
	v_add_f32_e32 v34, v51, v34
	s_waitcnt lgkmcnt(0)
	v_max_f32_e32 v51, v55, v55
	v_max_f32_e32 v51, v54, v51
	v_cmp_gt_f32_e32 vcc, v51, v172
	s_cbranch_vccz .LBB0_368
	v_max_f32_e32 v51, v51, v51
	v_max_f32_e32 v54, v172, v172
	v_max_f32_e32 v51, v54, v51
	v_sub_f32_e32 v54, v172, v51
	v_exp_f32_e32 v54, v54
	v_mov_b32_e32 v172, v51
	v_pk_mul_f32 v[32:33], v[32:33], v[54:55] op_sel_hi:[1,0]
	v_pk_mul_f32 v[30:31], v[30:31], v[54:55] op_sel_hi:[1,0]
	v_pk_mul_f32 v[28:29], v[28:29], v[54:55] op_sel_hi:[1,0]
	v_pk_mul_f32 v[26:27], v[26:27], v[54:55] op_sel_hi:[1,0]
	v_pk_mul_f32 v[24:25], v[24:25], v[54:55] op_sel_hi:[1,0]
	v_pk_mul_f32 v[22:23], v[22:23], v[54:55] op_sel_hi:[1,0]
	v_pk_mul_f32 v[20:21], v[20:21], v[54:55] op_sel_hi:[1,0]
	v_pk_mul_f32 v[18:19], v[18:19], v[54:55] op_sel_hi:[1,0]
	v_pk_mul_f32 v[16:17], v[16:17], v[54:55] op_sel_hi:[1,0]
	v_pk_mul_f32 v[14:15], v[14:15], v[54:55] op_sel_hi:[1,0]
	v_pk_mul_f32 v[12:13], v[12:13], v[54:55] op_sel_hi:[1,0]
	v_pk_mul_f32 v[10:11], v[10:11], v[54:55] op_sel_hi:[1,0]
	v_pk_mul_f32 v[8:9], v[8:9], v[54:55] op_sel_hi:[1,0]
	v_pk_mul_f32 v[6:7], v[6:7], v[54:55] op_sel_hi:[1,0]
	v_pk_mul_f32 v[4:5], v[4:5], v[54:55] op_sel_hi:[1,0]
	v_pk_mul_f32 v[2:3], v[2:3], v[54:55] op_sel_hi:[1,0]
	v_mul_f32_e32 v34, v34, v54
; __device__ __forceinline__ unsigned cvt_pk_bf16(float lo, float hi) { unsigned r; asm volatile("v_cvt_pk_bf16_f32 %0, %1, %2" : "=v"(r) : "v"(lo), "v"(hi)); return r; }
; #define LAS __attribute__((address_space(3)))
; __device__ __forceinline__ unsigned pk2(float lo, float hi) { return f2bf(lo) | (f2bf(hi) << 16); }
; #define MFMA32(a, b, c) __builtin_amdgcn_mfma_f32_32x32x16_bf16((a), (b), (c), 0, 0, 0)
; template <int STAGE, int OFF> __device__ __forceinline__ void attn32_unit(const bf16* base, bf16* yrow0, int blk0, int u, LAS unsigned char* xtab, LAS unsigned char* kbuf, LAS unsigned char* vbuf, int lane, ...
;     ...
;         }
;         float ps = 0.f;
; #pragma unroll
;         for (int rg = 0; rg < 16; ++rg) { sc[rg] = __builtin_amdgcn_exp2f(sc[rg] - m); ps += sc[rg]; }
;         l += ps;
;         bf16x8 pb[2];
; #pragma unroll
;         for (int s2 = 0; s2 < 2; ++s2) { v4u w; w.x = pg8::cvt_pk_bf16(sc[8 * s2], sc[8 * s2 + 1]); w.y = pg8::cvt_pk_bf16(sc[8 * s2 + 2], sc[8 * s2 + 3]); w.z = pg8::cvt_pk_bf16(sc[8 * s2 + 4], sc[8 * s2 + 5]); w.w = pg8::cvt_pk_bf16(sc[8 * s2 + 6], sc[8 * s2 + 7]); pb[s2] = __builtin_bit_cast(bf16x8, w); }
; #pragma unroll
;         for (int mb = 0; mb < 2; ++mb)
; #pragma unroll
;             for (int s2 = 0; s2 < 2; ++s2) {
;                 LAS unsigned char* vp = vbuf + tr_off + (16 * s2) * 160 + 64 * mb;
;                 const v4i16 a0 = __builtin_amdgcn_ds_read_tr16_b64_v4i16((LAS v4i16*)vp), a1 = __builtin_amdgcn_ds_read_tr16_b64_v4i16((LAS v4i16*)(vp + 8 * 160));
;                 const bf16x8 va = __builtin_shufflevector(a0, a1, 0, 1, 2, 3, 4, 5, 6, 7);
;                 o[mb] = MFMA32(va, pb[s2], o[mb]);
;             }
;         asm volatile("" ::: "memory");
;     }
;     l += __shfl_xor(l, 32);
;     if (STAGE < 2) {
; #pragma unroll
;         for (int mb = 0; mb < 2; ++mb)
; #pragma unroll
;             for (int gq = 0; gq < 4; ++gq) { v2u w; w.x = pk2(o[mb][4 * gq], o[mb][4 * gq + 1]); w.y = pk2(o[mb][4 * gq + 2], o[mb][4 * gq + 3]); *(LAS v2u*)(xrow + 2 * (32 * mb + 8 * gq + 4 * h)) = w; }
;         if (h == 0) { *(LAS float*)(xrow + 128) = m; *(LAS float*)(xrow + 132) = l; }
.LBB0_368:
	v_sub_f32_e32 v36, v36, v172
	v_exp_f32_e32 v138, v36
	v_sub_f32_e32 v36, v37, v172
	v_exp_f32_e32 v139, v36
	v_sub_f32_e32 v36, v38, v172
	v_exp_f32_e32 v140, v36
	v_sub_f32_e32 v36, v39, v172
	v_exp_f32_e32 v141, v36
	v_sub_f32_e32 v36, v40, v172
	v_exp_f32_e32 v142, v36
	v_sub_f32_e32 v36, v41, v172
	v_exp_f32_e32 v143, v36
	v_sub_f32_e32 v36, v42, v172
	v_exp_f32_e32 v144, v36
	v_sub_f32_e32 v36, v43, v172
	v_exp_f32_e32 v145, v36
	v_sub_f32_e32 v36, v44, v172
	v_exp_f32_e32 v146, v36
	v_sub_f32_e32 v36, v45, v172
	v_exp_f32_e32 v147, v36
	v_sub_f32_e32 v36, v46, v172
	v_exp_f32_e32 v148, v36
	v_sub_f32_e32 v36, v47, v172
	v_exp_f32_e32 v149, v36
	v_sub_f32_e32 v36, v48, v172
	v_sub_f32_e32 v50, v50, v172
	v_sub_f32_e32 v35, v35, v172
	v_exp_f32_e32 v150, v36
	v_sub_f32_e32 v36, v49, v172
	v_exp_f32_e32 v54, v50
	v_exp_f32_e32 v35, v35
	v_exp_f32_e32 v151, v36
	v_cvt_pk_bf16_f32 v36, v54, v35
	v_cvt_pk_bf16_f32 v37, v138, v139
	v_cvt_pk_bf16_f32 v38, v140, v141
	v_cvt_pk_bf16_f32 v39, v142, v143
	v_cvt_pk_bf16_f32 v40, v144, v145
	v_cvt_pk_bf16_f32 v41, v146, v147
	v_cvt_pk_bf16_f32 v42, v148, v149
	v_cvt_pk_bf16_f32 v43, v150, v151
	ds_read_b64_tr_b16 v[44:45], v181 offset:4608
	ds_read_b64_tr_b16 v[46:47], v181 offset:5888
	ds_read_b64_tr_b16 v[50:51], v181 offset:5952
	ds_read_b64_tr_b16 v[48:49], v181 offset:4672
	s_waitcnt lgkmcnt(2)
	v_mfma_f32_32x32x16_bf16 v[18:33], v[44:47], v[36:39], v[18:33]
	ds_read_b64_tr_b16 v[44:45], v181 offset:7168
	ds_read_b64_tr_b16 v[46:47], v181 offset:8448
	v_add_f32_e32 v54, 0, v54
	v_add_f32_e32 v35, v35, v54
	ds_read_b64_tr_b16 v[56:57], v181 offset:8512
	ds_read_b64_tr_b16 v[54:55], v181 offset:7232
	v_add_f32_e32 v35, v138, v35
	v_add_f32_e32 v35, v139, v35
	s_waitcnt lgkmcnt(2)
	v_mfma_f32_32x32x16_bf16 v[18:33], v[44:47], v[40:43], v[18:33]
	v_add_f32_e32 v35, v140, v35
	v_add_f32_e32 v35, v141, v35
	v_add_f32_e32 v35, v142, v35
	v_add_f32_e32 v35, v143, v35
	v_add_f32_e32 v35, v144, v35
	v_add_f32_e32 v35, v145, v35
	v_add_f32_e32 v35, v146, v35
	v_mfma_f32_32x32x16_bf16 v[2:17], v[48:51], v[36:39], v[2:17]
	s_nop 3
	v_bfe_u32 v36, v18, 16, 1
	v_add3_u32 v18, v18, v36, s35
	v_bfe_u32 v36, v19, 16, 1
	v_lshrrev_b32_e32 v18, 16, v18
	v_add3_u32 v19, v19, v36, s35
	v_and_or_b32 v18, v19, s36, v18
	v_bfe_u32 v19, v20, 16, 1
	v_add3_u32 v19, v20, v19, s35
	v_bfe_u32 v20, v21, 16, 1
	v_lshrrev_b32_e32 v19, 16, v19
	v_add3_u32 v20, v21, v20, s35
	v_and_or_b32 v19, v20, s36, v19
	v_bfe_u32 v20, v22, 16, 1
	v_add3_u32 v20, v22, v20, s35
	v_bfe_u32 v21, v23, 16, 1
	v_lshrrev_b32_e32 v20, 16, v20
	v_add3_u32 v21, v23, v21, s35
	v_and_or_b32 v20, v21, s36, v20
	v_bfe_u32 v21, v24, 16, 1
	v_add3_u32 v21, v24, v21, s35
	v_bfe_u32 v22, v25, 16, 1
	v_lshrrev_b32_e32 v21, 16, v21
	v_add3_u32 v22, v25, v22, s35
	v_and_or_b32 v21, v22, s36, v21
	ds_write2_b64 v230, v[18:19], v[20:21] offset1:2
	v_bfe_u32 v18, v26, 16, 1
	v_add3_u32 v18, v26, v18, s35
	v_bfe_u32 v19, v27, 16, 1
	v_lshrrev_b32_e32 v18, 16, v18
	v_add3_u32 v19, v27, v19, s35
	v_and_or_b32 v18, v19, s36, v18
	v_bfe_u32 v19, v28, 16, 1
	v_add3_u32 v19, v28, v19, s35
	v_bfe_u32 v20, v29, 16, 1
	s_waitcnt lgkmcnt(1)
	v_mfma_f32_32x32x16_bf16 v[2:17], v[54:57], v[40:43], v[2:17]
	v_lshrrev_b32_e32 v19, 16, v19
	v_add3_u32 v20, v29, v20, s35
	v_and_or_b32 v19, v20, s36, v19
	v_bfe_u32 v20, v30, 16, 1
	v_add3_u32 v20, v30, v20, s35
	v_bfe_u32 v21, v31, 16, 1
	v_lshrrev_b32_e32 v20, 16, v20
	v_add3_u32 v21, v31, v21, s35
	v_and_or_b32 v20, v21, s36, v20
	v_bfe_u32 v21, v32, 16, 1
	v_add3_u32 v21, v32, v21, s35
	v_bfe_u32 v22, v33, 16, 1
	v_lshrrev_b32_e32 v21, 16, v21
	v_add3_u32 v22, v33, v22, s35
	v_and_or_b32 v21, v22, s36, v21
	ds_write2_b64 v230, v[18:19], v[20:21] offset0:4 offset1:6
	v_bfe_u32 v18, v2, 16, 1
	v_add3_u32 v2, v2, v18, s35
	v_bfe_u32 v18, v3, 16, 1
	v_lshrrev_b32_e32 v2, 16, v2
	v_add3_u32 v3, v3, v18, s35
	v_and_or_b32 v2, v3, s36, v2
	v_bfe_u32 v3, v4, 16, 1
	v_add3_u32 v3, v4, v3, s35
	v_bfe_u32 v4, v5, 16, 1
	v_lshrrev_b32_e32 v3, 16, v3
	v_add3_u32 v4, v5, v4, s35
	v_and_or_b32 v3, v4, s36, v3
	v_bfe_u32 v4, v6, 16, 1
	v_add3_u32 v4, v6, v4, s35
	v_bfe_u32 v5, v7, 16, 1
	v_lshrrev_b32_e32 v4, 16, v4
	v_add3_u32 v5, v7, v5, s35
	v_and_or_b32 v4, v5, s36, v4
	v_bfe_u32 v5, v8, 16, 1
	v_add3_u32 v5, v8, v5, s35
	v_bfe_u32 v6, v9, 16, 1
	v_lshrrev_b32_e32 v5, 16, v5
	v_add3_u32 v6, v9, v6, s35
	v_and_or_b32 v5, v6, s36, v5
	ds_write2_b64 v230, v[2:3], v[4:5] offset0:8 offset1:10
	v_bfe_u32 v2, v10, 16, 1
	v_add3_u32 v2, v10, v2, s35
	v_bfe_u32 v3, v11, 16, 1
	v_add_f32_e32 v35, v147, v35
	v_lshrrev_b32_e32 v2, 16, v2
	v_add3_u32 v3, v11, v3, s35
	v_add_f32_e32 v35, v148, v35
	v_and_or_b32 v2, v3, s36, v2
	v_bfe_u32 v3, v12, 16, 1
	v_add_f32_e32 v35, v149, v35
	v_add3_u32 v3, v12, v3, s35
	v_bfe_u32 v4, v13, 16, 1
	v_add_f32_e32 v35, v150, v35
	v_lshrrev_b32_e32 v3, 16, v3
	v_add3_u32 v4, v13, v4, s35
	v_add_f32_e32 v35, v151, v35
	v_and_or_b32 v3, v4, s36, v3
	v_bfe_u32 v4, v14, 16, 1
	v_add_f32_e32 v34, v34, v35
	v_add3_u32 v4, v14, v4, s35
	v_bfe_u32 v5, v15, 16, 1
	v_mov_b32_e32 v35, v34
	s_nop 1
	v_permlane32_swap_b32_e32 v35, v34
	v_lshrrev_b32_e32 v4, 16, v4
	v_add3_u32 v5, v15, v5, s35
	v_and_or_b32 v4, v5, s36, v4
	v_bfe_u32 v5, v16, 16, 1
	v_add3_u32 v5, v16, v5, s35
	v_bfe_u32 v6, v17, 16, 1
	v_lshrrev_b32_e32 v5, 16, v5
	v_add3_u32 v6, v17, v6, s35
	v_and_or_b32 v5, v6, s36, v5
	ds_write2_b64 v230, v[2:3], v[4:5] offset0:12 offset1:14
	s_and_saveexec_b64 s[14:15], s[4:5]
	s_cbranch_execz .LBB0_370
	s_waitcnt lgkmcnt(1)
	v_add_f32_e32 v173, v34, v35
	ds_write_b64 v182, v[172:173] offset:128
; template <int STAGE, int OFF> __device__ __forceinline__ void attn32_unit(const bf16* base, bf16* yrow0, int blk0, int u, LAS unsigned char* xtab, LAS unsigned char* kbuf, LAS unsigned char* vbuf, int lane, ...
;     ...
;     if (STAGE == 0) {
; #pragma unroll
;         for (int i = 0; i < 16; ++i) { o[0][i] = 0.f; o[1][i] = 0.f; }
;         m = -1e30f; l = 0.f;
;     } else {
; #pragma unroll
;         for (int mb = 0; mb < 2; ++mb)
; #pragma unroll
;             for (int gq = 0; gq < 4; ++gq) { const v2u w = *(const LAS v2u*)(xrow + 2 * (32 * mb + 8 * gq + 4 * h)); o[mb][4 * gq] = bf_lo(w.x); o[mb][4 * gq + 1] = bf_hi(w.x); o[mb][4 * gq + 2] = bf_lo(w.y); o[mb][4 * gq + 3] = bf_hi(w.y); }
;         m = *(const LAS float*)(xrow + 128); l = h == 0 ? *(const LAS float*)(xrow + 132) : 0.f;
;     }
;     const int hi = qi, lo = max(qi - 128, -(t0 >> SH));
;     const unsigned mspan = (unsigned)(hi - lo);
; #pragma unroll
;     for (int pp = 0; pp < 5; ++pp) {
;         constexpr int dummy = 0; (void)dummy;
;         const int set = (pp + OFF) % 2, n0 = -128 + 32 * pp;
; #pragma unroll
;         for (int c = 0; c < 4; ++c) { *(LAS v4u*)(kbuf + (8 * c + lrow) * 144 + lch * 16) = kr[set][c]; *(LAS v4u*)(vbuf + (8 * c + lrow) * 160 + lch * 16) = vr[set][c]; }
;         if (pp + 2 < 5) { ATT32_LOAD(set, pp + 2, t0, SH); }
;         else { const bf16* base_ = base; { const bf16* base = nbase; ATT32_LOAD(set, pp + 2 - 5, nt0, nsh); } (void)base_; }
;         f32x16 sc;
; #pragma unroll
;         for (int i = 0; i < 16; ++i) sc[i] = 0.f;
; #pragma unroll
;         for (int ks = 0; ks < 4; ++ks) { const bf16x8 ka = *(const LAS bf16x8*)(kbuf + qi * 144 + 32 * ks + 16 * h); sc = MFMA32(ka, qb[ks], sc); }
;         if (pp == 4) {
; #pragma unroll
;             for (int ks = 0; ks < 4; ++ks) qb[ks] = *(const bf16x8*)(nbase + (size_t)min(nt0 + (qi << nsh), SEQ - 1) * 1536 + 16 * ks + 8 * h);
;         }
;         const int mbase = n0 + 4 * h - lo; float mx = -INFINITY;
; #pragma unroll
;         for (int rg = 0; rg < 16; ++rg) { sc[rg] = ((unsigned)(mbase + (rg & 3) + 8 * (rg >> 2)) <= mspan) ? sc[rg] : -INFINITY; mx = fmaxf(mx, sc[rg]); }
;         mx = fmaxf(mx, __shfl_xor(mx, 32));
;         if (__any(mx > m)) {
;             const float mn = fmaxf(m, mx), alpha = __builtin_amdgcn_exp2f(m - mn); m = mn; l *= alpha;
; #pragma unroll
.LBB0_370:
	s_or_b64 exec, exec, s[14:15]
	s_waitcnt vmcnt(19)
	ds_write_b128 v231, v[74:77]
	s_waitcnt vmcnt(18)
	ds_write_b128 v232, v[78:81] offset:4608
	s_waitcnt vmcnt(17)
	ds_write_b128 v231, v[82:85] offset:1152
	s_waitcnt vmcnt(16)
	ds_write_b128 v232, v[86:89] offset:5888
	s_waitcnt vmcnt(15)
	ds_write_b128 v231, v[90:93] offset:2304
	s_waitcnt vmcnt(14)
	ds_write_b128 v232, v[94:97] offset:7168
	s_waitcnt vmcnt(13)
	ds_write_b128 v231, v[98:101] offset:3456
	s_waitcnt vmcnt(12)
	ds_write_b128 v232, v[102:105] offset:8448
	ds_read_b128 v[2:5], v177
	ds_read_b128 v[18:21], v177 offset:32
	s_sub_i32 s0, 0, s10
	v_max_i32_e32 v22, s0, v175
	v_add_u32_e32 v153, s10, v174
	v_sub_u32_e32 v151, v1, v22
	v_sub_u32_e32 v152, v178, v22
	v_med3_i32 v22, v153, 0, v233
	v_mul_u32_u24_e32 v22, 0xc00, v22
	s_waitcnt vmcnt(3) lgkmcnt(1)
	v_mfma_f32_32x32x16_bf16 v[2:17], v[2:5], v[66:69], 0
	v_or_b32_e32 v30, v22, v176
	ds_read_b128 v[22:25], v177 offset:96
	ds_read_b128 v[26:29], v177 offset:64
	global_load_dwordx4 v[78:81], v30, s[8:9] offset:1024
	global_load_dwordx4 v[82:85], v30, s[8:9] offset:2048
	v_cmp_le_u32_e32 vcc, v152, v151
	s_waitcnt vmcnt(4) lgkmcnt(2)
	v_mfma_f32_32x32x16_bf16 v[2:17], v[18:21], v[62:65], v[2:17]
	v_or_b32_e32 v18, 8, v153
	v_med3_i32 v18, v18, 0, v233
	v_mul_u32_u24_e32 v18, 0xc00, v18
	v_or_b32_e32 v18, v18, v176
	global_load_dwordx4 v[86:89], v18, s[8:9] offset:1024
	global_load_dwordx4 v[90:93], v18, s[8:9] offset:2048
	v_or_b32_e32 v18, 16, v153
	v_med3_i32 v18, v18, 0, v233
	s_waitcnt vmcnt(5) lgkmcnt(0)
	v_mfma_f32_32x32x16_bf16 v[2:17], v[26:29], v[58:61], v[2:17]
	v_mul_u32_u24_e32 v18, 0xc00, v18
	v_or_b32_e32 v18, v18, v176
	global_load_dwordx4 v[102:105], v18, s[8:9] offset:1024
	global_load_dwordx4 v[138:141], v18, s[8:9] offset:2048
	v_add_u32_e32 v18, 1, v152
	v_add_u32_e32 v19, 2, v152
	v_or_b32_e32 v20, 24, v153
	v_med3_i32 v20, v20, 0, v233
	s_waitcnt vmcnt(6)
	v_mfma_f32_32x32x16_bf16 v[2:17], v[22:25], v[70:73], v[2:17]
	v_mul_u32_u24_e32 v20, 0xc00, v20
	v_or_b32_e32 v20, v20, v176
	global_load_dwordx4 v[142:145], v20, s[8:9] offset:1024
	global_load_dwordx4 v[146:149], v20, s[8:9] offset:2048
	s_nop 7
	v_cndmask_b32_e32 v2, v234, v2, vcc
	v_cmp_le_u32_e32 vcc, v18, v151
	s_nop 1
	v_cndmask_b32_e32 v3, v234, v3, vcc
	v_cmp_le_u32_e32 vcc, v19, v151
	v_add_u32_e32 v19, 3, v152
	v_max3_f32 v18, v2, s31, v3
	v_cndmask_b32_e32 v4, v234, v4, vcc
	v_cmp_le_u32_e32 vcc, v19, v151
	v_add_u32_e32 v19, 8, v152
	s_nop 0
	v_cndmask_b32_e32 v5, v234, v5, vcc
	v_cmp_le_u32_e32 vcc, v19, v151
	v_add_u32_e32 v19, 9, v152
	v_max3_f32 v18, v18, v4, v5
	v_cndmask_b32_e32 v6, v234, v6, vcc
	v_cmp_le_u32_e32 vcc, v19, v151
	v_add_u32_e32 v19, 10, v152
	s_nop 0
	v_cndmask_b32_e32 v7, v234, v7, vcc
	v_cmp_le_u32_e32 vcc, v19, v151
	v_add_u32_e32 v19, 11, v152
	v_max3_f32 v18, v18, v6, v7
	v_cndmask_b32_e32 v8, v234, v8, vcc
	v_cmp_le_u32_e32 vcc, v19, v151
	v_add_u32_e32 v19, 16, v152
	s_nop 0
	v_cndmask_b32_e32 v9, v234, v9, vcc
	v_cmp_le_u32_e32 vcc, v19, v151
	v_add_u32_e32 v19, 17, v152
	v_max3_f32 v18, v18, v8, v9
	v_cndmask_b32_e32 v10, v234, v10, vcc
	v_cmp_le_u32_e32 vcc, v19, v151
	v_add_u32_e32 v19, 18, v152
	s_nop 0
	v_cndmask_b32_e32 v11, v234, v11, vcc
	v_cmp_le_u32_e32 vcc, v19, v151
	v_add_u32_e32 v19, 19, v152
	v_max3_f32 v18, v18, v10, v11
	v_cndmask_b32_e32 v12, v234, v12, vcc
	v_cmp_le_u32_e32 vcc, v19, v151
	v_add_u32_e32 v19, 24, v152
	s_nop 0
	v_cndmask_b32_e32 v13, v234, v13, vcc
	v_cmp_le_u32_e32 vcc, v19, v151
	v_add_u32_e32 v19, 25, v152
	v_max3_f32 v18, v18, v12, v13
	v_cndmask_b32_e32 v14, v234, v14, vcc
	v_cmp_le_u32_e32 vcc, v19, v151
	v_add_u32_e32 v19, 26, v152
	s_nop 0
	v_cndmask_b32_e32 v15, v234, v15, vcc
	v_cmp_le_u32_e32 vcc, v19, v151
	v_add_u32_e32 v19, 27, v152
	v_max3_f32 v18, v18, v14, v15
	v_cndmask_b32_e32 v16, v234, v16, vcc
	v_cmp_le_u32_e32 vcc, v19, v151
	s_nop 1
	v_cndmask_b32_e32 v17, v234, v17, vcc
	v_max3_f32 v18, v18, v16, v17
	v_mov_b32_e32 v19, v18
	s_nop 1
	v_permlane32_swap_b32_e32 v19, v18
	s_waitcnt lgkmcnt(0)
	v_max_f32_e32 v19, v19, v19
	v_max_f32_e32 v18, v18, v19
	v_cmp_lt_f32_e32 vcc, s34, v18
	s_cmp_eq_u64 vcc, 0
	v_max_f32_e32 v19, 0xf149f2ca, v18
	s_cselect_b64 vcc, -1, 0
	v_cndmask_b32_e32 v150, v19, v235, vcc
	v_sub_f32_e32 v2, v2, v150
	v_exp_f32_e32 v50, v2
	v_sub_f32_e32 v2, v3, v150
	v_exp_f32_e32 v51, v2
	v_sub_f32_e32 v2, v4, v150
	v_exp_f32_e32 v94, v2
	v_sub_f32_e32 v2, v5, v150
	v_exp_f32_e32 v95, v2
	v_sub_f32_e32 v2, v6, v150
	v_exp_f32_e32 v6, v2
	v_sub_f32_e32 v2, v7, v150
	v_exp_f32_e32 v7, v2
	v_sub_f32_e32 v2, v8, v150
	v_exp_f32_e32 v8, v2
	v_sub_f32_e32 v2, v9, v150
	v_exp_f32_e32 v9, v2
	v_sub_f32_e32 v2, v10, v150
	v_exp_f32_e32 v162, v2
	v_sub_f32_e32 v2, v11, v150
	v_exp_f32_e32 v163, v2
	v_sub_f32_e32 v2, v12, v150
	v_exp_f32_e32 v164, v2
	v_sub_f32_e32 v2, v13, v150
	v_exp_f32_e32 v165, v2
	v_sub_f32_e32 v2, v14, v150
	v_sub_f32_e32 v21, 0xf149f2ca, v19
	v_exp_f32_e32 v171, v2
	v_sub_f32_e32 v2, v15, v150
	v_exp_f32_e32 v21, v21
	v_exp_f32_e32 v172, v2
	v_sub_f32_e32 v2, v16, v150
	v_exp_f32_e32 v173, v2
	v_sub_f32_e32 v2, v17, v150
	v_exp_f32_e32 v237, v2
	v_cvt_pk_bf16_f32 v54, v50, v51
	v_cvt_pk_bf16_f32 v55, v94, v95
	v_cvt_pk_bf16_f32 v56, v6, v7
	v_cvt_pk_bf16_f32 v57, v8, v9
	v_cvt_pk_bf16_f32 v154, v162, v163
	v_cvt_pk_bf16_f32 v155, v164, v165
	v_cvt_pk_bf16_f32 v156, v171, v172
	v_cvt_pk_bf16_f32 v157, v173, v237
	ds_read_b64_tr_b16 v[2:3], v181 offset:4608
	ds_read_b64_tr_b16 v[4:5], v181 offset:5888
	v_mul_f32_e32 v18, 0, v21
	v_cndmask_b32_e64 v34, v18, 0, vcc
	v_mov_b32_e32 v35, v34
	v_mov_b32_e32 v36, v34
	v_mov_b32_e32 v37, v34
	v_mov_b32_e32 v38, v34
	v_mov_b32_e32 v39, v34
	v_mov_b32_e32 v40, v34
	v_mov_b32_e32 v41, v34
	v_mov_b32_e32 v42, v34
	v_mov_b32_e32 v43, v34
	v_mov_b32_e32 v44, v34
	v_mov_b32_e32 v45, v34
	v_mov_b32_e32 v46, v34
	v_mov_b32_e32 v47, v34
	v_mov_b32_e32 v48, v34
	v_mov_b32_e32 v49, v34
	ds_read_b64_tr_b16 v[76:77], v181 offset:5952
	ds_read_b64_tr_b16 v[74:75], v181 offset:4672
	s_waitcnt lgkmcnt(2)
; template <int STAGE, int OFF> __device__ __forceinline__ void attn32_unit(const bf16* base, bf16* yrow0, int blk0, int u, LAS unsigned char* xtab, LAS unsigned char* kbuf, LAS unsigned char* vbuf, int lane, ...
;     ...
;         const int set = (pp + OFF) % 2, n0 = -128 + 32 * pp;
; #pragma unroll
;         for (int c = 0; c < 4; ++c) { *(LAS v4u*)(kbuf + (8 * c + lrow) * 144 + lch * 16) = kr[set][c]; *(LAS v4u*)(vbuf + (8 * c + lrow) * 160 + lch * 16) = vr[set][c]; }
;         if (pp + 2 < 5) { ATT32_LOAD(set, pp + 2, t0, SH); }
;         else { const bf16* base_ = base; { const bf16* base = nbase; ATT32_LOAD(set, pp + 2 - 5, nt0, nsh); } (void)base_; }
;         f32x16 sc;
; #pragma unroll
;         for (int i = 0; i < 16; ++i) sc[i] = 0.f;
; #pragma unroll
;         for (int ks = 0; ks < 4; ++ks) { const bf16x8 ka = *(const LAS bf16x8*)(kbuf + qi * 144 + 32 * ks + 16 * h); sc = MFMA32(ka, qb[ks], sc); }
;         if (pp == 4) {
; #pragma unroll
;             for (int ks = 0; ks < 4; ++ks) qb[ks] = *(const bf16x8*)(nbase + (size_t)min(nt0 + (qi << nsh), SEQ - 1) * 1536 + 16 * ks + 8 * h);
;         }
;         const int mbase = n0 + 4 * h - lo; float mx = -INFINITY;
; #pragma unroll
;         for (int rg = 0; rg < 16; ++rg) { sc[rg] = ((unsigned)(mbase + (rg & 3) + 8 * (rg >> 2)) <= mspan) ? sc[rg] : -INFINITY; mx = fmaxf(mx, sc[rg]); }
;         mx = fmaxf(mx, __shfl_xor(mx, 32));
;         if (__any(mx > m)) {
;             const float mn = fmaxf(m, mx), alpha = __builtin_amdgcn_exp2f(m - mn); m = mn; l *= alpha;
; #pragma unroll
;             for (int i = 0; i < 16; ++i) { o[0][i] *= alpha; o[1][i] *= alpha; }
;         }
;         float ps = 0.f;
; #pragma unroll
;         for (int rg = 0; rg < 16; ++rg) { sc[rg] = __builtin_amdgcn_exp2f(sc[rg] - m); ps += sc[rg]; }
;         l += ps;
;         bf16x8 pb[2];
; #pragma unroll
;         for (int s2 = 0; s2 < 2; ++s2) { v4u w; w.x = pg8::cvt_pk_bf16(sc[8 * s2], sc[8 * s2 + 1]); w.y = pg8::cvt_pk_bf16(sc[8 * s2 + 2], sc[8 * s2 + 3]); w.z = pg8::cvt_pk_bf16(sc[8 * s2 + 4], sc[8 * s2 + 5]); w.w = pg8::cvt_pk_bf16(sc[8 * s2 + 6], sc[8 * s2 + 7]); pb[s2] = __builtin_bit_cast(bf16x8, w); }
; #pragma unroll
;         for (int mb = 0; mb < 2; ++mb)
; #pragma unroll
;             for (int s2 = 0; s2 < 2; ++s2) {
;                 LAS unsigned char* vp = vbuf + tr_off + (16 * s2) * 160 + 64 * mb;
	v_mfma_f32_32x32x16_bf16 v[18:33], v[2:5], v[54:57], v[34:49]
	ds_read_b64_tr_b16 v[2:3], v181 offset:7168
	ds_read_b64_tr_b16 v[4:5], v181 offset:8448
	v_add_f32_e32 v10, 0, v50
	v_add_f32_e32 v10, v51, v10
	ds_read_b64_tr_b16 v[160:161], v181 offset:8512
	ds_read_b64_tr_b16 v[158:159], v181 offset:7232
	ds_write_b128 v231, v[106:109]
	ds_write_b128 v232, v[110:113] offset:4608
	ds_write_b128 v231, v[114:117] offset:1152
	ds_write_b128 v232, v[118:121] offset:5888
	ds_write_b128 v231, v[122:125] offset:2304
	ds_write_b128 v232, v[126:129] offset:7168
	ds_write_b128 v231, v[130:133] offset:3456
	ds_write_b128 v232, v[134:137] offset:8448
	s_waitcnt lgkmcnt(10)
	v_mfma_f32_32x32x16_bf16 v[18:33], v[2:5], v[154:157], v[18:33]
	v_add_f32_e32 v2, v94, v10
	v_add_f32_e32 v2, v95, v2
	v_add_f32_e32 v2, v6, v2
	v_add_f32_e32 v2, v7, v2
	v_add_f32_e32 v2, v8, v2
	v_add_f32_e32 v238, v9, v2
	v_mov_b64_e32 v[2:3], v[34:35]
	v_mov_b64_e32 v[4:5], v[36:37]
	v_mov_b64_e32 v[6:7], v[38:39]
	v_mov_b64_e32 v[8:9], v[40:41]
	v_mov_b64_e32 v[10:11], v[42:43]
	v_mov_b64_e32 v[12:13], v[44:45]
	v_mov_b64_e32 v[14:15], v[46:47]
	v_mov_b64_e32 v[16:17], v[48:49]
	v_max_i32_e32 v35, 0xffffffe0, v153
	v_add_u32_e32 v35, 32, v35
	v_min_u32_e32 v35, 0x3fff, v35
	v_mul_u32_u24_e32 v35, 0xc00, v35
	v_or_b32_e32 v35, v35, v176
	v_mfma_f32_32x32x16_bf16 v[2:17], v[74:77], v[54:57], v[2:17]
	global_load_dwordx4 v[54:57], v35, s[8:9] offset:1024
	global_load_dwordx4 v[74:77], v35, s[8:9] offset:2048
	ds_read_b128 v[36:39], v177
	v_max_i32_e32 v35, 0xffffffd8, v153
	v_add_u32_e32 v35, 40, v35
	v_min_u32_e32 v35, 0x3fff, v35
	v_mul_u32_u24_e32 v35, 0xc00, v35
	v_or_b32_e32 v35, v35, v176
	global_load_dwordx4 v[94:97], v35, s[8:9] offset:1024
	global_load_dwordx4 v[98:101], v35, s[8:9] offset:2048
	v_max_i32_e32 v35, 0xffffffd0, v153
	v_add_u32_e32 v35, 48, v35
	ds_read_b128 v[114:117], v177 offset:32
	s_waitcnt lgkmcnt(1)
	v_mfma_f32_32x32x16_bf16 v[36:51], v[36:39], v[66:69], 0
	v_min_u32_e32 v35, 0x3fff, v35
	v_mul_u32_u24_e32 v35, 0xc00, v35
	v_or_b32_e32 v35, v35, v176
	global_load_dwordx4 v[106:109], v35, s[8:9] offset:1024
	global_load_dwordx4 v[110:113], v35, s[8:9] offset:2048
	v_max_i32_e32 v35, 0xffffffc8, v153
	v_add_u32_e32 v35, 56, v35
	v_min_u32_e32 v35, 0x3fff, v35
	v_mul_u32_u24_e32 v35, 0xc00, v35
	v_or_b32_e32 v35, v35, v176
	ds_read_b128 v[122:125], v177 offset:96
	ds_read_b128 v[126:129], v177 offset:64
	s_waitcnt lgkmcnt(2)
	v_mfma_f32_32x32x16_bf16 v[36:51], v[114:117], v[62:65], v[36:51]
	global_load_dwordx4 v[114:117], v35, s[8:9] offset:1024
	global_load_dwordx4 v[118:121], v35, s[8:9] offset:2048
	v_add_f32_e32 v35, v162, v238
	v_add_f32_e32 v35, v163, v35
	v_add_f32_e32 v35, v164, v35
	v_add_f32_e32 v35, v165, v35
	v_add_f32_e32 v35, v171, v35
	v_add_f32_e32 v35, v172, v35
	s_waitcnt lgkmcnt(0)
	v_mfma_f32_32x32x16_bf16 v[36:51], v[126:129], v[58:61], v[36:51]
	v_add_f32_e32 v126, v173, v35
	v_add_u32_e32 v35, 32, v152
	v_cmp_le_u32_e32 vcc, v35, v151
	v_mfma_f32_32x32x16_bf16 v[36:51], v[122:125], v[70:73], v[36:51]
	v_mfma_f32_32x32x16_bf16 v[2:17], v[158:161], v[154:157], v[2:17]
	s_nop 10
	v_cndmask_b32_e32 v35, v234, v36, vcc
	v_add_u32_e32 v36, 33, v152
	v_cmp_le_u32_e32 vcc, v36, v151
	s_nop 1
	v_cndmask_b32_e32 v36, v234, v37, vcc
	v_add_u32_e32 v37, 34, v152
	v_cmp_le_u32_e32 vcc, v37, v151
	v_max3_f32 v122, v35, s31, v36
	s_nop 0
	v_cndmask_b32_e32 v37, v234, v38, vcc
	v_add_u32_e32 v38, 35, v152
	v_cmp_le_u32_e32 vcc, v38, v151
	s_nop 1
	v_cndmask_b32_e32 v38, v234, v39, vcc
	v_add_u32_e32 v39, 40, v152
	v_cmp_le_u32_e32 vcc, v39, v151
	v_max3_f32 v122, v122, v37, v38
	s_nop 0
	v_cndmask_b32_e32 v39, v234, v40, vcc
	v_add_u32_e32 v40, 41, v152
	v_cmp_le_u32_e32 vcc, v40, v151
	s_nop 1
	v_cndmask_b32_e32 v40, v234, v41, vcc
	v_add_u32_e32 v41, 42, v152
	v_cmp_le_u32_e32 vcc, v41, v151
	v_max3_f32 v122, v122, v39, v40
	s_nop 0
	v_cndmask_b32_e32 v41, v234, v42, vcc
	v_add_u32_e32 v42, 43, v152
	v_cmp_le_u32_e32 vcc, v42, v151
	s_nop 1
	v_cndmask_b32_e32 v42, v234, v43, vcc
	v_add_u32_e32 v43, 48, v152
	v_cmp_le_u32_e32 vcc, v43, v151
	v_max3_f32 v122, v122, v41, v42
	s_nop 0
	v_cndmask_b32_e32 v43, v234, v44, vcc
	v_add_u32_e32 v44, 49, v152
	v_cmp_le_u32_e32 vcc, v44, v151
	s_nop 1
	v_cndmask_b32_e32 v44, v234, v45, vcc
	v_add_u32_e32 v45, 50, v152
	v_cmp_le_u32_e32 vcc, v45, v151
	v_max3_f32 v122, v122, v43, v44
	s_nop 0
	v_cndmask_b32_e32 v45, v234, v46, vcc
	v_add_u32_e32 v46, 51, v152
	v_cmp_le_u32_e32 vcc, v46, v151
	s_nop 1
	v_cndmask_b32_e32 v46, v234, v47, vcc
	v_add_u32_e32 v47, 56, v152
	v_cmp_le_u32_e32 vcc, v47, v151
	v_max3_f32 v122, v122, v45, v46
	s_nop 0
	v_cndmask_b32_e32 v47, v234, v48, vcc
	v_add_u32_e32 v48, 57, v152
	v_cmp_le_u32_e32 vcc, v48, v151
	s_nop 1
	v_cndmask_b32_e32 v48, v234, v49, vcc
	v_add_u32_e32 v49, 58, v152
	v_cmp_le_u32_e32 vcc, v49, v151
	v_max3_f32 v122, v122, v47, v48
	s_nop 0
	v_cndmask_b32_e32 v49, v234, v50, vcc
	v_add_u32_e32 v50, 59, v152
	v_cmp_le_u32_e32 vcc, v50, v151
	v_add_f32_e32 v50, v237, v126
	v_add_f32_e32 v50, v34, v50
	v_cndmask_b32_e32 v51, v234, v51, vcc
	v_max3_f32 v122, v122, v49, v51
	v_mov_b32_e32 v123, v122
	s_nop 1
	v_permlane32_swap_b32_e32 v123, v122
	s_waitcnt lgkmcnt(0)
	v_max_f32_e32 v34, v123, v123
	v_max_f32_e32 v34, v122, v34
	v_cmp_gt_f32_e32 vcc, v34, v150
	s_cbranch_vccz .LBB0_372
	v_max_f32_e32 v34, v34, v34
	v_max_f32_e32 v122, v150, v150
	v_max_f32_e32 v122, v122, v34
	v_sub_f32_e32 v34, v150, v122
	v_exp_f32_e32 v34, v34
	v_mov_b32_e32 v150, v122
	v_pk_mul_f32 v[32:33], v[32:33], v[34:35] op_sel_hi:[1,0]
	v_pk_mul_f32 v[30:31], v[30:31], v[34:35] op_sel_hi:[1,0]
	v_pk_mul_f32 v[28:29], v[28:29], v[34:35] op_sel_hi:[1,0]
	v_pk_mul_f32 v[26:27], v[26:27], v[34:35] op_sel_hi:[1,0]
	v_pk_mul_f32 v[24:25], v[24:25], v[34:35] op_sel_hi:[1,0]
	v_pk_mul_f32 v[22:23], v[22:23], v[34:35] op_sel_hi:[1,0]
	v_pk_mul_f32 v[20:21], v[20:21], v[34:35] op_sel_hi:[1,0]
	v_pk_mul_f32 v[18:19], v[18:19], v[34:35] op_sel_hi:[1,0]
	v_pk_mul_f32 v[16:17], v[16:17], v[34:35] op_sel_hi:[1,0]
	v_pk_mul_f32 v[14:15], v[14:15], v[34:35] op_sel_hi:[1,0]
	v_pk_mul_f32 v[12:13], v[12:13], v[34:35] op_sel_hi:[1,0]
	v_pk_mul_f32 v[10:11], v[10:11], v[34:35] op_sel_hi:[1,0]
	v_pk_mul_f32 v[8:9], v[8:9], v[34:35] op_sel_hi:[1,0]
	v_pk_mul_f32 v[6:7], v[6:7], v[34:35] op_sel_hi:[1,0]
	v_pk_mul_f32 v[4:5], v[4:5], v[34:35] op_sel_hi:[1,0]
	v_pk_mul_f32 v[2:3], v[2:3], v[34:35] op_sel_hi:[1,0]
	v_mul_f32_e32 v50, v50, v34
; template <int STAGE, int OFF> __device__ __forceinline__ void attn32_unit(const bf16* base, bf16* yrow0, int blk0, int u, LAS unsigned char* xtab, LAS unsigned char* kbuf, LAS unsigned char* vbuf, int lane, ...
;     ...
;     for (int pp = 0; pp < 5; ++pp) {
;         constexpr int dummy = 0; (void)dummy;
;         const int set = (pp + OFF) % 2, n0 = -128 + 32 * pp;
; #pragma unroll
;         for (int c = 0; c < 4; ++c) { *(LAS v4u*)(kbuf + (8 * c + lrow) * 144 + lch * 16) = kr[set][c]; *(LAS v4u*)(vbuf + (8 * c + lrow) * 160 + lch * 16) = vr[set][c]; }
;         if (pp + 2 < 5) { ATT32_LOAD(set, pp + 2, t0, SH); }
;         else { const bf16* base_ = base; { const bf16* base = nbase; ATT32_LOAD(set, pp + 2 - 5, nt0, nsh); } (void)base_; }
;         f32x16 sc;
; #pragma unroll
;         for (int i = 0; i < 16; ++i) sc[i] = 0.f;
; #pragma unroll
;         for (int ks = 0; ks < 4; ++ks) { const bf16x8 ka = *(const LAS bf16x8*)(kbuf + qi * 144 + 32 * ks + 16 * h); sc = MFMA32(ka, qb[ks], sc); }
;         if (pp == 4) {
; #pragma unroll
;             for (int ks = 0; ks < 4; ++ks) qb[ks] = *(const bf16x8*)(nbase + (size_t)min(nt0 + (qi << nsh), SEQ - 1) * 1536 + 16 * ks + 8 * h);
;         }
;         const int mbase = n0 + 4 * h - lo; float mx = -INFINITY;
; #pragma unroll
;         for (int rg = 0; rg < 16; ++rg) { sc[rg] = ((unsigned)(mbase + (rg & 3) + 8 * (rg >> 2)) <= mspan) ? sc[rg] : -INFINITY; mx = fmaxf(mx, sc[rg]); }
;         mx = fmaxf(mx, __shfl_xor(mx, 32));
;         if (__any(mx > m)) {
;             const float mn = fmaxf(m, mx), alpha = __builtin_amdgcn_exp2f(m - mn); m = mn; l *= alpha;
; #pragma unroll
;             for (int i = 0; i < 16; ++i) { o[0][i] *= alpha; o[1][i] *= alpha; }
;         }
;         float ps = 0.f;
; #pragma unroll
;         for (int rg = 0; rg < 16; ++rg) { sc[rg] = __builtin_amdgcn_exp2f(sc[rg] - m); ps += sc[rg]; }
;         l += ps;
;         bf16x8 pb[2];
; #pragma unroll
;         for (int s2 = 0; s2 < 2; ++s2) { v4u w; w.x = pg8::cvt_pk_bf16(sc[8 * s2], sc[8 * s2 + 1]); w.y = pg8::cvt_pk_bf16(sc[8 * s2 + 2], sc[8 * s2 + 3]); w.z = pg8::cvt_pk_bf16(sc[8 * s2 + 4], sc[8 * s2 + 5]); w.w = pg8::cvt_pk_bf16(sc[8 * s2 + 6], sc[8 * s2 + 7]); pb[s2] = __builtin_bit_cast(bf16x8, w); }
; #pragma unroll
;         for (int mb = 0; mb < 2; ++mb)
; #pragma unroll
;             for (int s2 = 0; s2 < 2; ++s2) {
.LBB0_372:
	v_sub_f32_e32 v34, v35, v150
	v_exp_f32_e32 v126, v34
	v_sub_f32_e32 v34, v36, v150
	v_exp_f32_e32 v130, v34
	v_sub_f32_e32 v34, v37, v150
	v_exp_f32_e32 v131, v34
	v_sub_f32_e32 v34, v38, v150
	v_exp_f32_e32 v132, v34
	v_sub_f32_e32 v34, v39, v150
	v_exp_f32_e32 v133, v34
	v_sub_f32_e32 v34, v40, v150
	v_exp_f32_e32 v134, v34
	v_sub_f32_e32 v34, v41, v150
	v_exp_f32_e32 v135, v34
	v_sub_f32_e32 v34, v42, v150
	v_exp_f32_e32 v136, v34
	v_sub_f32_e32 v34, v43, v150
	v_exp_f32_e32 v154, v34
	v_sub_f32_e32 v34, v44, v150
	v_exp_f32_e32 v155, v34
	v_sub_f32_e32 v34, v45, v150
	v_exp_f32_e32 v156, v34
	v_sub_f32_e32 v34, v46, v150
	v_exp_f32_e32 v157, v34
	v_sub_f32_e32 v34, v47, v150
	v_exp_f32_e32 v158, v34
	v_sub_f32_e32 v34, v48, v150
	v_exp_f32_e32 v159, v34
	v_sub_f32_e32 v34, v49, v150
	v_exp_f32_e32 v160, v34
	v_sub_f32_e32 v34, v51, v150
	v_exp_f32_e32 v51, v34
	v_cvt_pk_bf16_f32 v34, v126, v130
	v_cvt_pk_bf16_f32 v35, v131, v132
	v_cvt_pk_bf16_f32 v36, v133, v134
	v_cvt_pk_bf16_f32 v37, v135, v136
	v_cvt_pk_bf16_f32 v122, v154, v155
	v_cvt_pk_bf16_f32 v123, v156, v157
	v_cvt_pk_bf16_f32 v124, v158, v159
	v_cvt_pk_bf16_f32 v125, v160, v51
	ds_read_b64_tr_b16 v[38:39], v181 offset:4608
	ds_read_b64_tr_b16 v[40:41], v181 offset:5888
	ds_read_b64_tr_b16 v[44:45], v181 offset:5952
	ds_read_b64_tr_b16 v[42:43], v181 offset:4672
	s_waitcnt lgkmcnt(2)
	v_mfma_f32_32x32x16_bf16 v[18:33], v[38:41], v[34:37], v[18:33]
	ds_read_b64_tr_b16 v[38:39], v181 offset:7168
	ds_read_b64_tr_b16 v[40:41], v181 offset:8448
	v_add_f32_e32 v46, 0, v126
	ds_read_b64_tr_b16 v[128:129], v181 offset:8512
	ds_read_b64_tr_b16 v[126:127], v181 offset:7232
	s_waitcnt vmcnt(15)
	ds_write_b128 v231, v[78:81]
	s_waitcnt vmcnt(14)
	ds_write_b128 v232, v[82:85] offset:4608
	s_waitcnt vmcnt(13)
	ds_write_b128 v231, v[86:89] offset:1152
	s_waitcnt vmcnt(12)
	ds_write_b128 v232, v[90:93] offset:5888
	s_waitcnt vmcnt(11)
	ds_write_b128 v231, v[102:105] offset:2304
	s_waitcnt vmcnt(10)
	ds_write_b128 v232, v[138:141] offset:7168
	s_waitcnt vmcnt(9)
	ds_write_b128 v231, v[142:145] offset:3456
	s_waitcnt vmcnt(8)
	ds_write_b128 v232, v[146:149] offset:8448
	v_add_u32_e32 v142, 0x58, v153
	v_med3_i32 v142, v142, 0, v233
	s_waitcnt lgkmcnt(10)
	v_mfma_f32_32x32x16_bf16 v[18:33], v[38:41], v[122:125], v[18:33]
	v_add_f32_e32 v38, v130, v46
	v_add_f32_e32 v38, v131, v38
	v_add_f32_e32 v38, v132, v38
	v_add_f32_e32 v38, v133, v38
	v_add_f32_e32 v38, v134, v38
	v_add_f32_e32 v38, v135, v38
	v_add_f32_e32 v161, v136, v38
	v_mfma_f32_32x32x16_bf16 v[2:17], v[42:45], v[34:37], v[2:17]
	v_or_b32_e32 v34, s10, v53
	v_min_u32_e32 v34, 0x3fff, v34
	v_mul_u32_u24_e32 v38, 0xc00, v34
	ds_read_b128 v[34:37], v177
	v_or_b32_e32 v38, v38, v176
	global_load_dwordx4 v[78:81], v38, s[8:9] offset:1024
	global_load_dwordx4 v[82:85], v38, s[8:9] offset:2048
	v_add_u32_e32 v38, 0x48, v153
	v_med3_i32 v38, v38, 0, v233
	v_mul_u32_u24_e32 v38, 0xc00, v38
	ds_read_b128 v[102:105], v177 offset:32
	v_or_b32_e32 v90, v38, v176
	s_waitcnt lgkmcnt(1)
	v_mfma_f32_32x32x16_bf16 v[34:49], v[34:37], v[66:69], 0
	v_add_u32_e32 v130, 0x50, v153
	v_med3_i32 v130, v130, 0, v233
	v_mul_u32_u24_e32 v130, 0xc00, v130
	v_mul_u32_u24_e32 v142, 0xc00, v142
	v_or_b32_e32 v138, v130, v176
	v_or_b32_e32 v146, v142, v176
	global_load_dwordx4 v[86:89], v90, s[8:9] offset:1024
	s_nop 0
	global_load_dwordx4 v[90:93], v90, s[8:9] offset:2048
	ds_read_b128 v[130:133], v177 offset:96
	ds_read_b128 v[134:137], v177 offset:64
	s_waitcnt lgkmcnt(2)
	v_mfma_f32_32x32x16_bf16 v[34:49], v[102:105], v[62:65], v[34:49]
	global_load_dwordx4 v[102:105], v138, s[8:9] offset:1024
	s_nop 0
	global_load_dwordx4 v[138:141], v138, s[8:9] offset:2048
	s_nop 0
	global_load_dwordx4 v[142:145], v146, s[8:9] offset:1024
	s_nop 0
	global_load_dwordx4 v[146:149], v146, s[8:9] offset:2048
	s_waitcnt lgkmcnt(0)
	v_mfma_f32_32x32x16_bf16 v[34:49], v[134:137], v[58:61], v[34:49]
	v_add_f32_e32 v134, v154, v161
	v_add_f32_e32 v134, v155, v134
	v_add_f32_e32 v134, v156, v134
	v_add_f32_e32 v134, v157, v134
	v_add_f32_e32 v134, v158, v134
	v_add_f32_e32 v134, v159, v134
	v_add_f32_e32 v134, v160, v134
	v_mfma_f32_32x32x16_bf16 v[34:49], v[130:133], v[70:73], v[34:49]
	v_add_u32_e32 v130, 64, v152
	v_cmp_le_u32_e32 vcc, v130, v151
	v_add_u32_e32 v130, 0x41, v152
	v_add_u32_e32 v131, 0x42, v152
	v_add_f32_e32 v51, v51, v134
	v_add_f32_e32 v50, v50, v51
	s_nop 5
	v_cndmask_b32_e32 v34, v234, v34, vcc
	v_cmp_le_u32_e32 vcc, v130, v151
	v_mfma_f32_32x32x16_bf16 v[2:17], v[126:129], v[122:125], v[2:17]
	s_nop 0
	v_cndmask_b32_e32 v35, v234, v35, vcc
	v_cmp_le_u32_e32 vcc, v131, v151
	v_add_u32_e32 v131, 0x43, v152
	v_max3_f32 v130, v34, s31, v35
	v_cndmask_b32_e32 v36, v234, v36, vcc
	v_cmp_le_u32_e32 vcc, v131, v151
	v_add_u32_e32 v131, 0x48, v152
	s_nop 0
	v_cndmask_b32_e32 v37, v234, v37, vcc
	v_cmp_le_u32_e32 vcc, v131, v151
	v_add_u32_e32 v131, 0x49, v152
	v_max3_f32 v130, v130, v36, v37
	v_cndmask_b32_e32 v38, v234, v38, vcc
	v_cmp_le_u32_e32 vcc, v131, v151
	v_add_u32_e32 v131, 0x4a, v152
	s_nop 0
	v_cndmask_b32_e32 v39, v234, v39, vcc
	v_cmp_le_u32_e32 vcc, v131, v151
	v_add_u32_e32 v131, 0x4b, v152
	v_max3_f32 v130, v130, v38, v39
	v_cndmask_b32_e32 v40, v234, v40, vcc
	v_cmp_le_u32_e32 vcc, v131, v151
	v_add_u32_e32 v131, 0x50, v152
	s_nop 0
	v_cndmask_b32_e32 v41, v234, v41, vcc
	v_cmp_le_u32_e32 vcc, v131, v151
	v_add_u32_e32 v131, 0x51, v152
	v_max3_f32 v130, v130, v40, v41
	v_cndmask_b32_e32 v42, v234, v42, vcc
	v_cmp_le_u32_e32 vcc, v131, v151
	v_add_u32_e32 v131, 0x52, v152
	s_nop 0
	v_cndmask_b32_e32 v43, v234, v43, vcc
	v_cmp_le_u32_e32 vcc, v131, v151
	v_add_u32_e32 v131, 0x53, v152
	v_max3_f32 v130, v130, v42, v43
	v_cndmask_b32_e32 v44, v234, v44, vcc
	v_cmp_le_u32_e32 vcc, v131, v151
	v_add_u32_e32 v131, 0x58, v152
	s_nop 0
	v_cndmask_b32_e32 v45, v234, v45, vcc
	v_cmp_le_u32_e32 vcc, v131, v151
	v_add_u32_e32 v131, 0x59, v152
	v_max3_f32 v130, v130, v44, v45
	v_cndmask_b32_e32 v46, v234, v46, vcc
	v_cmp_le_u32_e32 vcc, v131, v151
	v_add_u32_e32 v131, 0x5a, v152
	s_nop 0
	v_cndmask_b32_e32 v47, v234, v47, vcc
	v_cmp_le_u32_e32 vcc, v131, v151
	v_add_u32_e32 v131, 0x5b, v152
	v_max3_f32 v130, v130, v46, v47
	v_cndmask_b32_e32 v48, v234, v48, vcc
	v_cmp_le_u32_e32 vcc, v131, v151
	s_nop 1
	v_cndmask_b32_e32 v49, v234, v49, vcc
	v_max3_f32 v130, v130, v48, v49
	v_mov_b32_e32 v131, v130
	s_nop 1
	v_permlane32_swap_b32_e32 v131, v130
	s_waitcnt lgkmcnt(0)
	v_max_f32_e32 v51, v131, v131
	v_max_f32_e32 v51, v130, v51
	v_cmp_gt_f32_e32 vcc, v51, v150
	s_cbranch_vccz .LBB0_374
; __device__ __forceinline__ unsigned cvt_pk_bf16(float lo, float hi) { unsigned r; asm volatile("v_cvt_pk_bf16_f32 %0, %1, %2" : "=v"(r) : "v"(lo), "v"(hi)); return r; }
; #define LAS __attribute__((address_space(3)))
; template <int STAGE, int OFF> __device__ __forceinline__ void attn32_unit(const bf16* base, bf16* yrow0, int blk0, int u, LAS unsigned char* xtab, LAS unsigned char* kbuf, LAS unsigned char* vbuf, int lane, ...
;     ...
;         for (int c = 0; c < 4; ++c) { *(LAS v4u*)(kbuf + (8 * c + lrow) * 144 + lch * 16) = kr[set][c]; *(LAS v4u*)(vbuf + (8 * c + lrow) * 160 + lch * 16) = vr[set][c]; }
;         if (pp + 2 < 5) { ATT32_LOAD(set, pp + 2, t0, SH); }
;         else { const bf16* base_ = base; { const bf16* base = nbase; ATT32_LOAD(set, pp + 2 - 5, nt0, nsh); } (void)base_; }
;         f32x16 sc;
; #pragma unroll
;         for (int i = 0; i < 16; ++i) sc[i] = 0.f;
; #pragma unroll
;         for (int ks = 0; ks < 4; ++ks) { const bf16x8 ka = *(const LAS bf16x8*)(kbuf + qi * 144 + 32 * ks + 16 * h); sc = MFMA32(ka, qb[ks], sc); }
;     ...
;         if (__any(mx > m)) {
;             const float mn = fmaxf(m, mx), alpha = __builtin_amdgcn_exp2f(m - mn); m = mn; l *= alpha;
; #pragma unroll
;             for (int i = 0; i < 16; ++i) { o[0][i] *= alpha; o[1][i] *= alpha; }
;         }
;         float ps = 0.f;
; #pragma unroll
;         for (int rg = 0; rg < 16; ++rg) { sc[rg] = __builtin_amdgcn_exp2f(sc[rg] - m); ps += sc[rg]; }
;         l += ps;
;         bf16x8 pb[2];
; #pragma unroll
;         for (int s2 = 0; s2 < 2; ++s2) { v4u w; w.x = pg8::cvt_pk_bf16(sc[8 * s2], sc[8 * s2 + 1]); w.y = pg8::cvt_pk_bf16(sc[8 * s2 + 2], sc[8 * s2 + 3]); w.z = pg8::cvt_pk_bf16(sc[8 * s2 + 4], sc[8 * s2 + 5]); w.w = pg8::cvt_pk_bf16(sc[8 * s2 + 6], sc[8 * s2 + 7]); pb[s2] = __builtin_bit_cast(bf16x8, w); }
; #pragma unroll
;         for (int mb = 0; mb < 2; ++mb)
; #pragma unroll
;             for (int s2 = 0; s2 < 2; ++s2) {
;                 LAS unsigned char* vp = vbuf + tr_off + (16 * s2) * 160 + 64 * mb;
;                 const v4i16 a0 = __builtin_amdgcn_ds_read_tr16_b64_v4i16((LAS v4i16*)vp), a1 = __builtin_amdgcn_ds_read_tr16_b64_v4i16((LAS v4i16*)(vp + 8 * 160));
;                 const bf16x8 va = __builtin_shufflevector(a0, a1, 0, 1, 2, 3, 4, 5, 6, 7);
;                 o[mb] = MFMA32(va, pb[s2], o[mb]);
;             }
	v_max_f32_e32 v51, v51, v51
	v_max_f32_e32 v122, v150, v150
	v_max_f32_e32 v51, v122, v51
	v_sub_f32_e32 v122, v150, v51
	v_exp_f32_e32 v122, v122
	v_mov_b32_e32 v150, v51
	v_pk_mul_f32 v[32:33], v[32:33], v[122:123] op_sel_hi:[1,0]
	v_pk_mul_f32 v[30:31], v[30:31], v[122:123] op_sel_hi:[1,0]
	v_pk_mul_f32 v[28:29], v[28:29], v[122:123] op_sel_hi:[1,0]
	v_pk_mul_f32 v[26:27], v[26:27], v[122:123] op_sel_hi:[1,0]
	v_pk_mul_f32 v[24:25], v[24:25], v[122:123] op_sel_hi:[1,0]
	v_pk_mul_f32 v[22:23], v[22:23], v[122:123] op_sel_hi:[1,0]
	v_pk_mul_f32 v[20:21], v[20:21], v[122:123] op_sel_hi:[1,0]
	v_pk_mul_f32 v[18:19], v[18:19], v[122:123] op_sel_hi:[1,0]
	v_pk_mul_f32 v[16:17], v[16:17], v[122:123] op_sel_hi:[1,0]
	v_pk_mul_f32 v[14:15], v[14:15], v[122:123] op_sel_hi:[1,0]
	v_pk_mul_f32 v[12:13], v[12:13], v[122:123] op_sel_hi:[1,0]
	v_pk_mul_f32 v[10:11], v[10:11], v[122:123] op_sel_hi:[1,0]
	v_pk_mul_f32 v[8:9], v[8:9], v[122:123] op_sel_hi:[1,0]
	v_pk_mul_f32 v[6:7], v[6:7], v[122:123] op_sel_hi:[1,0]
	v_pk_mul_f32 v[4:5], v[4:5], v[122:123] op_sel_hi:[1,0]
	v_pk_mul_f32 v[2:3], v[2:3], v[122:123] op_sel_hi:[1,0]
	v_mul_f32_e32 v50, v50, v122
.LBB0_374:
	v_sub_f32_e32 v34, v34, v150
	v_exp_f32_e32 v51, v34
	v_sub_f32_e32 v34, v35, v150
	v_exp_f32_e32 v122, v34
	v_sub_f32_e32 v34, v36, v150
	v_exp_f32_e32 v123, v34
	v_sub_f32_e32 v34, v37, v150
	v_exp_f32_e32 v124, v34
	v_sub_f32_e32 v34, v38, v150
	v_exp_f32_e32 v125, v34
	v_sub_f32_e32 v34, v39, v150
	v_exp_f32_e32 v126, v34
	v_sub_f32_e32 v34, v40, v150
	v_exp_f32_e32 v127, v34
	v_sub_f32_e32 v34, v41, v150
	v_exp_f32_e32 v128, v34
	v_sub_f32_e32 v34, v42, v150
	v_exp_f32_e32 v153, v34
	v_sub_f32_e32 v34, v43, v150
	v_exp_f32_e32 v162, v34
	v_sub_f32_e32 v34, v44, v150
	v_exp_f32_e32 v163, v34
	v_sub_f32_e32 v34, v45, v150
	v_exp_f32_e32 v164, v34
	v_sub_f32_e32 v34, v46, v150
	v_exp_f32_e32 v165, v34
	v_sub_f32_e32 v34, v47, v150
	v_exp_f32_e32 v171, v34
	v_sub_f32_e32 v34, v48, v150
	v_exp_f32_e32 v172, v34
	v_sub_f32_e32 v34, v49, v150
	v_exp_f32_e32 v173, v34
	v_cvt_pk_bf16_f32 v34, v51, v122
	v_cvt_pk_bf16_f32 v35, v123, v124
	v_cvt_pk_bf16_f32 v36, v125, v126
	v_cvt_pk_bf16_f32 v37, v127, v128
	v_cvt_pk_bf16_f32 v154, v153, v162
	v_cvt_pk_bf16_f32 v155, v163, v164
	v_cvt_pk_bf16_f32 v156, v165, v171
	v_cvt_pk_bf16_f32 v157, v172, v173
	ds_read_b64_tr_b16 v[38:39], v181 offset:4608
	ds_read_b64_tr_b16 v[40:41], v181 offset:5888
	ds_read_b64_tr_b16 v[44:45], v181 offset:5952
	ds_read_b64_tr_b16 v[42:43], v181 offset:4672
	s_waitcnt lgkmcnt(2)
	v_mfma_f32_32x32x16_bf16 v[18:33], v[38:41], v[34:37], v[18:33]
	ds_read_b64_tr_b16 v[38:39], v181 offset:7168
	ds_read_b64_tr_b16 v[40:41], v181 offset:8448
	v_add_f32_e32 v46, 0, v51
	s_add_i32 s10, s13, s24
	ds_read_b64_tr_b16 v[160:161], v181 offset:8512
	ds_read_b64_tr_b16 v[158:159], v181 offset:7232
	s_waitcnt vmcnt(15)
	ds_write_b128 v231, v[54:57]
	s_waitcnt vmcnt(14)
	ds_write_b128 v232, v[74:77] offset:4608
	s_waitcnt vmcnt(13)
	ds_write_b128 v231, v[94:97] offset:1152
	s_waitcnt vmcnt(12)
	ds_write_b128 v232, v[98:101] offset:5888
	s_waitcnt vmcnt(11)
	ds_write_b128 v231, v[106:109] offset:2304
	s_waitcnt vmcnt(10)
	ds_write_b128 v232, v[110:113] offset:7168
	s_waitcnt vmcnt(9)
	ds_write_b128 v231, v[114:117] offset:3456
	s_waitcnt vmcnt(8)
	ds_write_b128 v232, v[118:121] offset:8448
	s_waitcnt lgkmcnt(10)
	v_mfma_f32_32x32x16_bf16 v[18:33], v[38:41], v[154:157], v[18:33]
	v_add_f32_e32 v38, v122, v46
	v_add_f32_e32 v38, v123, v38
	v_add_f32_e32 v38, v124, v38
	v_add_f32_e32 v38, v125, v38
	v_add_f32_e32 v38, v126, v38
	v_add_f32_e32 v38, v127, v38
	v_add_f32_e32 v51, v128, v38
	v_mfma_f32_32x32x16_bf16 v[2:17], v[42:45], v[34:37], v[2:17]
	v_add_u32_e32 v34, s10, v185
	v_med3_i32 v34, v34, 0, v233
	v_mul_u32_u24_e32 v38, 0xc00, v34
	ds_read_b128 v[34:37], v177
	v_or_b32_e32 v38, v38, v176
	global_load_dwordx4 v[106:109], v38, s[8:9] offset:1024
	global_load_dwordx4 v[110:113], v38, s[8:9] offset:2048
	v_add_u32_e32 v38, s10, v186
	v_med3_i32 v38, v38, 0, v233
	v_mul_u32_u24_e32 v38, 0xc00, v38
	ds_read_b128 v[54:57], v177 offset:32
	v_or_b32_e32 v74, v38, v176
	s_waitcnt lgkmcnt(1)
	v_mfma_f32_32x32x16_bf16 v[34:49], v[34:37], v[66:69], 0
	global_load_dwordx4 v[114:117], v74, s[8:9] offset:1024
	global_load_dwordx4 v[118:121], v74, s[8:9] offset:2048
	v_add_u32_e32 v74, s10, v187
	v_med3_i32 v74, v74, 0, v233
	v_mul_u32_u24_e32 v74, 0xc00, v74
	v_or_b32_e32 v98, v74, v176
	ds_read_b128 v[74:77], v177 offset:96
	ds_read_b128 v[94:97], v177 offset:64
	global_load_dwordx4 v[122:125], v98, s[8:9] offset:1024
	global_load_dwordx4 v[126:129], v98, s[8:9] offset:2048
	s_waitcnt lgkmcnt(2)
	v_mfma_f32_32x32x16_bf16 v[34:49], v[54:57], v[62:65], v[34:49]
	v_add_u32_e32 v54, s10, v188
	v_med3_i32 v54, v54, 0, v233
	v_mul_u32_u24_e32 v54, 0xc00, v54
	v_or_b32_e32 v54, v54, v176
	global_load_dwordx4 v[130:133], v54, s[8:9] offset:1024
	global_load_dwordx4 v[134:137], v54, s[8:9] offset:2048
	v_add_u32_e32 v54, 0x60, v152
	v_cmp_le_u32_e32 vcc, v54, v151
	s_waitcnt lgkmcnt(0)
; __device__ __forceinline__ unsigned cvt_pk_bf16(float lo, float hi) { unsigned r; asm volatile("v_cvt_pk_bf16_f32 %0, %1, %2" : "=v"(r) : "v"(lo), "v"(hi)); return r; }
; #define LAS __attribute__((address_space(3)))
; template <int STAGE, int OFF> __device__ __forceinline__ void attn32_unit(const bf16* base, bf16* yrow0, int blk0, int u, LAS unsigned char* xtab, LAS unsigned char* kbuf, LAS unsigned char* vbuf, int lane, ...
;     ...
;         for (int ks = 0; ks < 4; ++ks) { const bf16x8 ka = *(const LAS bf16x8*)(kbuf + qi * 144 + 32 * ks + 16 * h); sc = MFMA32(ka, qb[ks], sc); }
;         if (pp == 4) {
; #pragma unroll
;             for (int ks = 0; ks < 4; ++ks) qb[ks] = *(const bf16x8*)(nbase + (size_t)min(nt0 + (qi << nsh), SEQ - 1) * 1536 + 16 * ks + 8 * h);
;         }
;         const int mbase = n0 + 4 * h - lo; float mx = -INFINITY;
; #pragma unroll
;         for (int rg = 0; rg < 16; ++rg) { sc[rg] = ((unsigned)(mbase + (rg & 3) + 8 * (rg >> 2)) <= mspan) ? sc[rg] : -INFINITY; mx = fmaxf(mx, sc[rg]); }
;         mx = fmaxf(mx, __shfl_xor(mx, 32));
;         if (__any(mx > m)) {
;             const float mn = fmaxf(m, mx), alpha = __builtin_amdgcn_exp2f(m - mn); m = mn; l *= alpha;
; #pragma unroll
;             for (int i = 0; i < 16; ++i) { o[0][i] *= alpha; o[1][i] *= alpha; }
;         }
;         float ps = 0.f;
; #pragma unroll
;         for (int rg = 0; rg < 16; ++rg) { sc[rg] = __builtin_amdgcn_exp2f(sc[rg] - m); ps += sc[rg]; }
;         l += ps;
;         bf16x8 pb[2];
; #pragma unroll
;         for (int s2 = 0; s2 < 2; ++s2) { v4u w; w.x = pg8::cvt_pk_bf16(sc[8 * s2], sc[8 * s2 + 1]); w.y = pg8::cvt_pk_bf16(sc[8 * s2 + 2], sc[8 * s2 + 3]); w.z = pg8::cvt_pk_bf16(sc[8 * s2 + 4], sc[8 * s2 + 5]); w.w = pg8::cvt_pk_bf16(sc[8 * s2 + 6], sc[8 * s2 + 7]); pb[s2] = __builtin_bit_cast(bf16x8, w); }
; #pragma unroll
;         for (int mb = 0; mb < 2; ++mb)
; #pragma unroll
;             for (int s2 = 0; s2 < 2; ++s2) {
;                 LAS unsigned char* vp = vbuf + tr_off + (16 * s2) * 160 + 64 * mb;
;                 const v4i16 a0 = __builtin_amdgcn_ds_read_tr16_b64_v4i16((LAS v4i16*)vp), a1 = __builtin_amdgcn_ds_read_tr16_b64_v4i16((LAS v4i16*)(vp + 8 * 160));
;                 const bf16x8 va = __builtin_shufflevector(a0, a1, 0, 1, 2, 3, 4, 5, 6, 7);
;                 o[mb] = MFMA32(va, pb[s2], o[mb]);
;             }
	v_mfma_f32_32x32x16_bf16 v[34:49], v[94:97], v[58:61], v[34:49]
	v_add_u32_e32 v54, 0x61, v152
	v_add_u32_e32 v55, 0x62, v152
	v_add_f32_e32 v51, v153, v51
	v_add_f32_e32 v51, v162, v51
	v_add_f32_e32 v51, v163, v51
	v_add_f32_e32 v51, v164, v51
	v_add_f32_e32 v51, v165, v51
	v_mfma_f32_32x32x16_bf16 v[34:49], v[74:77], v[70:73], v[34:49]
	v_add_f32_e32 v51, v171, v51
	v_add_f32_e32 v51, v172, v51
	v_add_f32_e32 v51, v173, v51
	v_add_f32_e32 v50, v50, v51
	v_mfma_f32_32x32x16_bf16 v[2:17], v[158:161], v[154:157], v[2:17]
	s_nop 6
	v_cndmask_b32_e32 v34, v234, v34, vcc
	v_cmp_le_u32_e32 vcc, v54, v151
	s_nop 1
	v_cndmask_b32_e32 v35, v234, v35, vcc
	v_cmp_le_u32_e32 vcc, v55, v151
	v_add_u32_e32 v55, 0x63, v152
	v_max3_f32 v54, v34, s31, v35
	v_cndmask_b32_e32 v36, v234, v36, vcc
	v_cmp_le_u32_e32 vcc, v55, v151
	v_add_u32_e32 v55, 0x68, v152
	s_nop 0
	v_cndmask_b32_e32 v37, v234, v37, vcc
	v_cmp_le_u32_e32 vcc, v55, v151
	v_add_u32_e32 v55, 0x69, v152
	v_max3_f32 v54, v54, v36, v37
	v_cndmask_b32_e32 v38, v234, v38, vcc
	v_cmp_le_u32_e32 vcc, v55, v151
	v_add_u32_e32 v55, 0x6a, v152
	s_nop 0
	v_cndmask_b32_e32 v39, v234, v39, vcc
	v_cmp_le_u32_e32 vcc, v55, v151
	v_add_u32_e32 v55, 0x6b, v152
	v_max3_f32 v54, v54, v38, v39
	v_cndmask_b32_e32 v40, v234, v40, vcc
	v_cmp_le_u32_e32 vcc, v55, v151
	v_add_u32_e32 v55, 0x70, v152
	s_nop 0
	v_cndmask_b32_e32 v41, v234, v41, vcc
	v_cmp_le_u32_e32 vcc, v55, v151
	v_add_u32_e32 v55, 0x71, v152
	v_max3_f32 v54, v54, v40, v41
	v_cndmask_b32_e32 v42, v234, v42, vcc
	v_cmp_le_u32_e32 vcc, v55, v151
	v_add_u32_e32 v55, 0x72, v152
	s_nop 0
	v_cndmask_b32_e32 v43, v234, v43, vcc
	v_cmp_le_u32_e32 vcc, v55, v151
	v_add_u32_e32 v55, 0x73, v152
	v_max3_f32 v54, v54, v42, v43
	v_cndmask_b32_e32 v44, v234, v44, vcc
	v_cmp_le_u32_e32 vcc, v55, v151
	v_add_u32_e32 v55, 0x78, v152
	s_nop 0
	v_cndmask_b32_e32 v45, v234, v45, vcc
	v_cmp_le_u32_e32 vcc, v55, v151
	v_add_u32_e32 v55, 0x79, v152
	v_max3_f32 v54, v54, v44, v45
	v_cndmask_b32_e32 v46, v234, v46, vcc
	v_cmp_le_u32_e32 vcc, v55, v151
	v_add_u32_e32 v55, 0x7a, v152
	s_nop 0
	v_cndmask_b32_e32 v47, v234, v47, vcc
	v_cmp_le_u32_e32 vcc, v55, v151
	v_add_u32_e32 v55, 0x7b, v152
	v_max3_f32 v54, v54, v46, v47
	v_cndmask_b32_e32 v48, v234, v48, vcc
	v_cmp_le_u32_e32 vcc, v55, v151
	s_nop 1
	v_cndmask_b32_e32 v49, v234, v49, vcc
	v_max3_f32 v54, v54, v48, v49
	v_mov_b32_e32 v55, v54
	s_nop 1
	v_permlane32_swap_b32_e32 v55, v54
	s_waitcnt lgkmcnt(0)
	v_max_f32_e32 v51, v55, v55
	v_max_f32_e32 v51, v54, v51
	v_cmp_gt_f32_e32 vcc, v51, v150
	s_cbranch_vccz .LBB0_376
	v_max_f32_e32 v51, v51, v51
	v_max_f32_e32 v54, v150, v150
	v_max_f32_e32 v51, v54, v51
	v_sub_f32_e32 v54, v150, v51
	v_exp_f32_e32 v54, v54
	v_mov_b32_e32 v150, v51
	v_pk_mul_f32 v[32:33], v[32:33], v[54:55] op_sel_hi:[1,0]
	v_pk_mul_f32 v[30:31], v[30:31], v[54:55] op_sel_hi:[1,0]
	v_pk_mul_f32 v[28:29], v[28:29], v[54:55] op_sel_hi:[1,0]
	v_pk_mul_f32 v[26:27], v[26:27], v[54:55] op_sel_hi:[1,0]
	v_pk_mul_f32 v[24:25], v[24:25], v[54:55] op_sel_hi:[1,0]
	v_pk_mul_f32 v[22:23], v[22:23], v[54:55] op_sel_hi:[1,0]
	v_pk_mul_f32 v[20:21], v[20:21], v[54:55] op_sel_hi:[1,0]
	v_pk_mul_f32 v[18:19], v[18:19], v[54:55] op_sel_hi:[1,0]
	v_pk_mul_f32 v[16:17], v[16:17], v[54:55] op_sel_hi:[1,0]
	v_pk_mul_f32 v[14:15], v[14:15], v[54:55] op_sel_hi:[1,0]
	v_pk_mul_f32 v[12:13], v[12:13], v[54:55] op_sel_hi:[1,0]
	v_pk_mul_f32 v[10:11], v[10:11], v[54:55] op_sel_hi:[1,0]
	v_pk_mul_f32 v[8:9], v[8:9], v[54:55] op_sel_hi:[1,0]
	v_pk_mul_f32 v[6:7], v[6:7], v[54:55] op_sel_hi:[1,0]
	v_pk_mul_f32 v[4:5], v[4:5], v[54:55] op_sel_hi:[1,0]
	v_pk_mul_f32 v[2:3], v[2:3], v[54:55] op_sel_hi:[1,0]
	v_mul_f32_e32 v50, v50, v54
.LBB0_376:
	v_sub_f32_e32 v34, v34, v150
	v_exp_f32_e32 v51, v34
	v_sub_f32_e32 v34, v35, v150
	v_exp_f32_e32 v54, v34
	v_sub_f32_e32 v34, v36, v150
	v_exp_f32_e32 v55, v34
	v_sub_f32_e32 v34, v37, v150
	v_exp_f32_e32 v56, v34
	v_sub_f32_e32 v34, v38, v150
	v_exp_f32_e32 v57, v34
	v_sub_f32_e32 v34, v39, v150
	v_exp_f32_e32 v74, v34
	v_sub_f32_e32 v34, v40, v150
	v_exp_f32_e32 v75, v34
	v_sub_f32_e32 v34, v41, v150
	v_exp_f32_e32 v76, v34
	v_sub_f32_e32 v34, v42, v150
	v_exp_f32_e32 v153, v34
	v_sub_f32_e32 v34, v43, v150
	v_exp_f32_e32 v164, v34
	v_sub_f32_e32 v34, v44, v150
	v_exp_f32_e32 v165, v34
	v_sub_f32_e32 v34, v45, v150
	v_exp_f32_e32 v171, v34
	v_sub_f32_e32 v34, v46, v150
	v_exp_f32_e32 v172, v34
	v_sub_f32_e32 v34, v47, v150
	v_exp_f32_e32 v173, v34
	v_sub_f32_e32 v34, v48, v150
	v_exp_f32_e32 v237, v34
	v_sub_f32_e32 v34, v49, v150
	v_exp_f32_e32 v238, v34
	v_cvt_pk_bf16_f32 v34, v51, v54
	v_cvt_pk_bf16_f32 v35, v55, v56
	v_cvt_pk_bf16_f32 v36, v57, v74
	v_cvt_pk_bf16_f32 v37, v75, v76
	v_cvt_pk_bf16_f32 v154, v153, v164
	v_cvt_pk_bf16_f32 v155, v165, v171
	v_cvt_pk_bf16_f32 v156, v172, v173
	v_cvt_pk_bf16_f32 v157, v237, v238
	ds_read_b64_tr_b16 v[38:39], v181 offset:4608
	ds_read_b64_tr_b16 v[40:41], v181 offset:5888
	v_or_b32_e32 v42, s10, v183
	v_min_i32_e32 v77, 0x3fff, v42
	s_waitcnt lgkmcnt(0)
	v_mfma_f32_32x32x16_bf16 v[18:33], v[38:41], v[34:37], v[18:33]
	v_mov_b64_e32 v[38:39], s[8:9]
	v_mad_i64_i32 v[38:39], s[14:15], v77, s30, v[38:39]
	ds_read_b64_tr_b16 v[42:43], v181 offset:7168
	ds_read_b64_tr_b16 v[44:45], v181 offset:8448
	ds_read_b64_tr_b16 v[48:49], v181 offset:5952
	ds_read_b64_tr_b16 v[46:47], v181 offset:4672
	v_lshl_add_u64 v[162:163], v[38:39], 0, v[168:169]
	v_add_f32_e32 v38, 0, v51
	v_add_f32_e32 v38, v54, v38
	v_add_f32_e32 v38, v55, v38
	v_add_f32_e32 v38, v56, v38
	v_add_f32_e32 v38, v57, v38
	v_add_f32_e32 v38, v74, v38
	s_waitcnt lgkmcnt(0)
; #define LAS __attribute__((address_space(3)))
; template <int STAGE, int OFF> __device__ __forceinline__ void attn32_unit(const bf16* base, bf16* yrow0, int blk0, int u, LAS unsigned char* xtab, LAS unsigned char* kbuf, LAS unsigned char* vbuf, int lane, ...
;     ...
;         for (int c = 0; c < 4; ++c) { *(LAS v4u*)(kbuf + (8 * c + lrow) * 144 + lch * 16) = kr[set][c]; *(LAS v4u*)(vbuf + (8 * c + lrow) * 160 + lch * 16) = vr[set][c]; }
;         if (pp + 2 < 5) { ATT32_LOAD(set, pp + 2, t0, SH); }
;         else { const bf16* base_ = base; { const bf16* base = nbase; ATT32_LOAD(set, pp + 2 - 5, nt0, nsh); } (void)base_; }
;         f32x16 sc;
; #pragma unroll
;         for (int i = 0; i < 16; ++i) sc[i] = 0.f;
; #pragma unroll
;         for (int ks = 0; ks < 4; ++ks) { const bf16x8 ka = *(const LAS bf16x8*)(kbuf + qi * 144 + 32 * ks + 16 * h); sc = MFMA32(ka, qb[ks], sc); }
;         if (pp == 4) {
; #pragma unroll
;             for (int ks = 0; ks < 4; ++ks) qb[ks] = *(const bf16x8*)(nbase + (size_t)min(nt0 + (qi << nsh), SEQ - 1) * 1536 + 16 * ks + 8 * h);
;         }
;         const int mbase = n0 + 4 * h - lo; float mx = -INFINITY;
; #pragma unroll
;         for (int rg = 0; rg < 16; ++rg) { sc[rg] = ((unsigned)(mbase + (rg & 3) + 8 * (rg >> 2)) <= mspan) ? sc[rg] : -INFINITY; mx = fmaxf(mx, sc[rg]); }
;         mx = fmaxf(mx, __shfl_xor(mx, 32));
;         if (__any(mx > m)) {
;             const float mn = fmaxf(m, mx), alpha = __builtin_amdgcn_exp2f(m - mn); m = mn; l *= alpha;
; #pragma unroll
;             for (int i = 0; i < 16; ++i) { o[0][i] *= alpha; o[1][i] *= alpha; }
;         }
;         float ps = 0.f;
; #pragma unroll
;         for (int rg = 0; rg < 16; ++rg) { sc[rg] = __builtin_amdgcn_exp2f(sc[rg] - m); ps += sc[rg]; }
;         l += ps;
;         bf16x8 pb[2];
; #pragma unroll
;         for (int s2 = 0; s2 < 2; ++s2) { v4u w; w.x = pg8::cvt_pk_bf16(sc[8 * s2], sc[8 * s2 + 1]); w.y = pg8::cvt_pk_bf16(sc[8 * s2 + 2], sc[8 * s2 + 3]); w.z = pg8::cvt_pk_bf16(sc[8 * s2 + 4], sc[8 * s2 + 5]); w.w = pg8::cvt_pk_bf16(sc[8 * s2 + 6], sc[8 * s2 + 7]); pb[s2] = __builtin_bit_cast(bf16x8, w); }
; #pragma unroll
;         for (int mb = 0; mb < 2; ++mb)
; #pragma unroll
;             for (int s2 = 0; s2 < 2; ++s2) {
;                 LAS unsigned char* vp = vbuf + tr_off + (16 * s2) * 160 + 64 * mb;
	v_mfma_f32_32x32x16_bf16 v[2:17], v[46:49], v[34:37], v[2:17]
	v_add_u32_e32 v34, s10, v189
	ds_read_b64_tr_b16 v[160:161], v181 offset:8512
	ds_read_b64_tr_b16 v[158:159], v181 offset:7232
	v_add_f32_e32 v38, v75, v38
	s_waitcnt vmcnt(15)
	ds_write_b128 v231, v[78:81]
	s_waitcnt vmcnt(14)
	ds_write_b128 v232, v[82:85] offset:4608
	s_waitcnt vmcnt(13)
	ds_write_b128 v231, v[86:89] offset:1152
	s_waitcnt vmcnt(12)
	ds_write_b128 v232, v[90:93] offset:5888
	s_waitcnt vmcnt(11)
	ds_write_b128 v231, v[102:105] offset:2304
	s_waitcnt vmcnt(10)
	ds_write_b128 v232, v[138:141] offset:7168
	s_waitcnt vmcnt(9)
	ds_write_b128 v231, v[142:145] offset:3456
	s_waitcnt vmcnt(8)
	ds_write_b128 v232, v[146:149] offset:8448
	v_med3_i32 v34, v34, 0, v233
	v_add_f32_e32 v51, v76, v38
	v_mul_u32_u24_e32 v38, 0xc00, v34
	ds_read_b128 v[34:37], v177
	v_or_b32_e32 v38, v38, v176
	global_load_dwordx4 v[74:77], v38, s[8:9] offset:1024
	global_load_dwordx4 v[78:81], v38, s[8:9] offset:2048
	v_add_u32_e32 v38, s10, v190
	v_med3_i32 v38, v38, 0, v233
	v_mul_u32_u24_e32 v38, 0xc00, v38
	ds_read_b128 v[54:57], v177 offset:32
	v_mfma_f32_32x32x16_bf16 v[18:33], v[42:45], v[154:157], v[18:33]
	v_or_b32_e32 v86, v38, v176
	global_load_dwordx4 v[82:85], v86, s[8:9] offset:1024
	s_nop 0
	global_load_dwordx4 v[86:89], v86, s[8:9] offset:2048
	v_add_f32_e32 v51, v153, v51
	v_add_f32_e32 v51, v164, v51
	v_add_f32_e32 v51, v165, v51
	v_add_f32_e32 v51, v171, v51
	v_add_f32_e32 v51, v172, v51
	s_waitcnt lgkmcnt(1)
	v_mfma_f32_32x32x16_bf16 v[34:49], v[34:37], v[66:69], 0
	v_add_u32_e32 v66, s10, v191
	v_med3_i32 v66, v66, 0, v233
	v_mul_u32_u24_e32 v66, 0xc00, v66
	v_or_b32_e32 v94, v66, v176
	ds_read_b128 v[138:141], v177 offset:96
	ds_read_b128 v[66:69], v177 offset:64
	global_load_dwordx4 v[90:93], v94, s[8:9] offset:1024
	s_nop 0
	global_load_dwordx4 v[94:97], v94, s[8:9] offset:2048
	v_add_f32_e32 v51, v173, v51
	s_waitcnt lgkmcnt(2)
	v_mfma_f32_32x32x16_bf16 v[34:49], v[54:57], v[62:65], v[34:49]
	v_add_u32_e32 v54, s10, v192
	v_med3_i32 v54, v54, 0, v233
	v_mul_u32_u24_e32 v54, 0xc00, v54
	v_or_b32_e32 v54, v54, v176
	global_load_dwordx4 v[98:101], v54, s[8:9] offset:1024
	global_load_dwordx4 v[102:105], v54, s[8:9] offset:2048
	v_add_f32_e32 v142, v237, v51
	v_add_u32_e32 v51, 0x80, v152
	s_waitcnt lgkmcnt(0)
	v_mfma_f32_32x32x16_bf16 v[34:49], v[66:69], v[58:61], v[34:49]
	global_load_dwordx4 v[66:69], v[162:163], off
	global_load_dwordx4 v[62:65], v[162:163], off offset:32
	global_load_dwordx4 v[58:61], v[162:163], off offset:64
	global_load_dwordx4 v[54:57], v[162:163], off offset:96
	v_cmp_le_u32_e32 vcc, v51, v151
	v_mfma_f32_32x32x16_bf16 v[34:49], v[138:141], v[70:73], v[34:49]
	v_add_u32_e32 v70, 0x82, v152
	v_mfma_f32_32x32x16_bf16 v[2:17], v[158:161], v[154:157], v[2:17]
	s_nop 9
	v_cndmask_b32_e32 v51, v234, v34, vcc
	v_add_u32_e32 v34, 0x81, v152
	v_cmp_le_u32_e32 vcc, v34, v151
	s_nop 1
	v_cndmask_b32_e32 v35, v234, v35, vcc
	v_cmp_le_u32_e32 vcc, v70, v151
	v_add_u32_e32 v70, 0x83, v152
	v_max3_f32 v34, v51, s31, v35
	v_cndmask_b32_e32 v36, v234, v36, vcc
	v_cmp_le_u32_e32 vcc, v70, v151
	v_add_u32_e32 v70, 0x88, v152
	s_nop 0
	v_cndmask_b32_e32 v37, v234, v37, vcc
	v_cmp_le_u32_e32 vcc, v70, v151
	v_add_u32_e32 v70, 0x89, v152
	v_max3_f32 v34, v34, v36, v37
	v_cndmask_b32_e32 v38, v234, v38, vcc
	v_cmp_le_u32_e32 vcc, v70, v151
	v_add_u32_e32 v70, 0x8a, v152
	s_nop 0
	v_cndmask_b32_e32 v39, v234, v39, vcc
	v_cmp_le_u32_e32 vcc, v70, v151
	v_add_u32_e32 v70, 0x8b, v152
	v_max3_f32 v34, v34, v38, v39
	v_cndmask_b32_e32 v40, v234, v40, vcc
	v_cmp_le_u32_e32 vcc, v70, v151
	v_add_u32_e32 v70, 0x90, v152
	s_nop 0
	v_cndmask_b32_e32 v41, v234, v41, vcc
	v_cmp_le_u32_e32 vcc, v70, v151
	v_add_u32_e32 v70, 0x91, v152
	v_max3_f32 v34, v34, v40, v41
	v_cndmask_b32_e32 v42, v234, v42, vcc
	v_cmp_le_u32_e32 vcc, v70, v151
	v_add_u32_e32 v70, 0x92, v152
	s_nop 0
	v_cndmask_b32_e32 v43, v234, v43, vcc
	v_cmp_le_u32_e32 vcc, v70, v151
	v_add_u32_e32 v70, 0x93, v152
	v_max3_f32 v34, v34, v42, v43
	v_cndmask_b32_e32 v44, v234, v44, vcc
	v_cmp_le_u32_e32 vcc, v70, v151
	v_add_u32_e32 v70, 0x98, v152
	s_nop 0
	v_cndmask_b32_e32 v45, v234, v45, vcc
	v_cmp_le_u32_e32 vcc, v70, v151
	v_add_u32_e32 v70, 0x99, v152
	v_max3_f32 v34, v34, v44, v45
	v_cndmask_b32_e32 v46, v234, v46, vcc
	v_cmp_le_u32_e32 vcc, v70, v151
	v_add_u32_e32 v70, 0x9a, v152
	s_nop 0
	v_cndmask_b32_e32 v47, v234, v47, vcc
	v_cmp_le_u32_e32 vcc, v70, v151
	v_add_u32_e32 v70, 0x9b, v152
	v_max3_f32 v34, v34, v46, v47
	v_cndmask_b32_e32 v48, v234, v48, vcc
	v_cmp_le_u32_e32 vcc, v70, v151
	s_nop 1
	v_cndmask_b32_e32 v49, v234, v49, vcc
	v_max3_f32 v70, v34, v48, v49
	v_mov_b32_e32 v71, v70
	s_nop 1
	v_permlane32_swap_b32_e32 v71, v70
	v_add_f32_e32 v34, v238, v142
	v_add_f32_e32 v34, v50, v34
	s_waitcnt lgkmcnt(0)
	v_max_f32_e32 v50, v71, v71
	v_max_f32_e32 v50, v70, v50
	v_cmp_gt_f32_e32 vcc, v50, v150
	s_cbranch_vccz .LBB0_378
	v_max_f32_e32 v50, v50, v50
	v_max_f32_e32 v70, v150, v150
	v_max_f32_e32 v70, v70, v50
	v_sub_f32_e32 v50, v150, v70
	v_exp_f32_e32 v50, v50
	v_mov_b32_e32 v150, v70
	v_pk_mul_f32 v[32:33], v[32:33], v[50:51] op_sel_hi:[1,0]
	v_pk_mul_f32 v[30:31], v[30:31], v[50:51] op_sel_hi:[1,0]
	v_pk_mul_f32 v[28:29], v[28:29], v[50:51] op_sel_hi:[1,0]
	v_pk_mul_f32 v[26:27], v[26:27], v[50:51] op_sel_hi:[1,0]
	v_pk_mul_f32 v[24:25], v[24:25], v[50:51] op_sel_hi:[1,0]
	v_pk_mul_f32 v[22:23], v[22:23], v[50:51] op_sel_hi:[1,0]
	v_pk_mul_f32 v[20:21], v[20:21], v[50:51] op_sel_hi:[1,0]
	v_pk_mul_f32 v[18:19], v[18:19], v[50:51] op_sel_hi:[1,0]
	v_pk_mul_f32 v[16:17], v[16:17], v[50:51] op_sel_hi:[1,0]
	v_pk_mul_f32 v[14:15], v[14:15], v[50:51] op_sel_hi:[1,0]
	v_pk_mul_f32 v[12:13], v[12:13], v[50:51] op_sel_hi:[1,0]
	v_pk_mul_f32 v[10:11], v[10:11], v[50:51] op_sel_hi:[1,0]
	v_pk_mul_f32 v[8:9], v[8:9], v[50:51] op_sel_hi:[1,0]
	v_pk_mul_f32 v[6:7], v[6:7], v[50:51] op_sel_hi:[1,0]
	v_pk_mul_f32 v[4:5], v[4:5], v[50:51] op_sel_hi:[1,0]
	v_pk_mul_f32 v[2:3], v[2:3], v[50:51] op_sel_hi:[1,0]
	v_mul_f32_e32 v34, v34, v50
; __device__ __forceinline__ unsigned cvt_pk_bf16(float lo, float hi) { unsigned r; asm volatile("v_cvt_pk_bf16_f32 %0, %1, %2" : "=v"(r) : "v"(lo), "v"(hi)); return r; }
; #define LAS __attribute__((address_space(3)))
; __device__ __forceinline__ unsigned pk2(float lo, float hi) { return f2bf(lo) | (f2bf(hi) << 16); }
; #define MFMA32(a, b, c) __builtin_amdgcn_mfma_f32_32x32x16_bf16((a), (b), (c), 0, 0, 0)
; template <int STAGE, int OFF> __device__ __forceinline__ void attn32_unit(const bf16* base, bf16* yrow0, int blk0, int u, LAS unsigned char* xtab, LAS unsigned char* kbuf, LAS unsigned char* vbuf, int lane, ...
;     ...
;         for (int rg = 0; rg < 16; ++rg) { sc[rg] = __builtin_amdgcn_exp2f(sc[rg] - m); ps += sc[rg]; }
;         l += ps;
;         bf16x8 pb[2];
; #pragma unroll
;         for (int s2 = 0; s2 < 2; ++s2) { v4u w; w.x = pg8::cvt_pk_bf16(sc[8 * s2], sc[8 * s2 + 1]); w.y = pg8::cvt_pk_bf16(sc[8 * s2 + 2], sc[8 * s2 + 3]); w.z = pg8::cvt_pk_bf16(sc[8 * s2 + 4], sc[8 * s2 + 5]); w.w = pg8::cvt_pk_bf16(sc[8 * s2 + 6], sc[8 * s2 + 7]); pb[s2] = __builtin_bit_cast(bf16x8, w); }
; #pragma unroll
;         for (int mb = 0; mb < 2; ++mb)
; #pragma unroll
;             for (int s2 = 0; s2 < 2; ++s2) {
;                 LAS unsigned char* vp = vbuf + tr_off + (16 * s2) * 160 + 64 * mb;
;                 const v4i16 a0 = __builtin_amdgcn_ds_read_tr16_b64_v4i16((LAS v4i16*)vp), a1 = __builtin_amdgcn_ds_read_tr16_b64_v4i16((LAS v4i16*)(vp + 8 * 160));
;                 const bf16x8 va = __builtin_shufflevector(a0, a1, 0, 1, 2, 3, 4, 5, 6, 7);
;                 o[mb] = MFMA32(va, pb[s2], o[mb]);
;             }
;         asm volatile("" ::: "memory");
;     }
;     l += __shfl_xor(l, 32);
;     if (STAGE < 2) {
; #pragma unroll
;         for (int mb = 0; mb < 2; ++mb)
; #pragma unroll
;             for (int gq = 0; gq < 4; ++gq) { v2u w; w.x = pk2(o[mb][4 * gq], o[mb][4 * gq + 1]); w.y = pk2(o[mb][4 * gq + 2], o[mb][4 * gq + 3]); *(LAS v2u*)(xrow + 2 * (32 * mb + 8 * gq + 4 * h)) = w; }
;         if (h == 0) { *(LAS float*)(xrow + 128) = m; *(LAS float*)(xrow + 132) = l; }
.LBB0_378:
	v_sub_f32_e32 v36, v36, v150
	v_exp_f32_e32 v138, v36
	v_sub_f32_e32 v36, v37, v150
	v_exp_f32_e32 v139, v36
	v_sub_f32_e32 v36, v38, v150
	v_exp_f32_e32 v140, v36
	v_sub_f32_e32 v36, v39, v150
	v_exp_f32_e32 v141, v36
	v_sub_f32_e32 v36, v40, v150
	v_exp_f32_e32 v142, v36
	v_sub_f32_e32 v36, v41, v150
	v_exp_f32_e32 v143, v36
	v_sub_f32_e32 v36, v42, v150
	v_exp_f32_e32 v144, v36
	v_sub_f32_e32 v36, v43, v150
	v_exp_f32_e32 v145, v36
	v_sub_f32_e32 v36, v44, v150
	v_exp_f32_e32 v146, v36
	v_sub_f32_e32 v36, v45, v150
	v_exp_f32_e32 v147, v36
	v_sub_f32_e32 v36, v46, v150
	v_exp_f32_e32 v148, v36
	v_sub_f32_e32 v36, v47, v150
	v_exp_f32_e32 v149, v36
	v_sub_f32_e32 v36, v48, v150
	v_sub_f32_e32 v50, v51, v150
	v_sub_f32_e32 v35, v35, v150
	v_exp_f32_e32 v151, v36
	v_sub_f32_e32 v36, v49, v150
	v_exp_f32_e32 v70, v50
	v_exp_f32_e32 v35, v35
	v_exp_f32_e32 v152, v36
	v_cvt_pk_bf16_f32 v36, v70, v35
	v_cvt_pk_bf16_f32 v37, v138, v139
	v_cvt_pk_bf16_f32 v38, v140, v141
	v_cvt_pk_bf16_f32 v39, v142, v143
	v_cvt_pk_bf16_f32 v40, v144, v145
	v_cvt_pk_bf16_f32 v41, v146, v147
	v_cvt_pk_bf16_f32 v42, v148, v149
	v_cvt_pk_bf16_f32 v43, v151, v152
	ds_read_b64_tr_b16 v[44:45], v181 offset:4608
	ds_read_b64_tr_b16 v[46:47], v181 offset:5888
	ds_read_b64_tr_b16 v[50:51], v181 offset:5952
	ds_read_b64_tr_b16 v[48:49], v181 offset:4672
	s_waitcnt lgkmcnt(2)
	v_mfma_f32_32x32x16_bf16 v[18:33], v[44:47], v[36:39], v[18:33]
	ds_read_b64_tr_b16 v[44:45], v181 offset:7168
	ds_read_b64_tr_b16 v[46:47], v181 offset:8448
	v_add_f32_e32 v70, 0, v70
	v_add_f32_e32 v35, v35, v70
	ds_read_b64_tr_b16 v[72:73], v181 offset:8512
	ds_read_b64_tr_b16 v[70:71], v181 offset:7232
	v_add_f32_e32 v35, v138, v35
	v_add_f32_e32 v35, v139, v35
	s_waitcnt lgkmcnt(2)
	v_mfma_f32_32x32x16_bf16 v[18:33], v[44:47], v[40:43], v[18:33]
	v_add_f32_e32 v35, v140, v35
	v_add_f32_e32 v35, v141, v35
	v_add_f32_e32 v35, v142, v35
	v_add_f32_e32 v35, v143, v35
	v_add_f32_e32 v35, v144, v35
	v_add_f32_e32 v35, v145, v35
	v_add_f32_e32 v35, v146, v35
	v_mfma_f32_32x32x16_bf16 v[2:17], v[48:51], v[36:39], v[2:17]
	s_nop 3
	v_bfe_u32 v36, v18, 16, 1
	v_add3_u32 v18, v18, v36, s35
	v_bfe_u32 v36, v19, 16, 1
	v_lshrrev_b32_e32 v18, 16, v18
	v_add3_u32 v19, v19, v36, s35
	v_and_or_b32 v18, v19, s36, v18
	v_bfe_u32 v19, v20, 16, 1
	v_add3_u32 v19, v20, v19, s35
	v_bfe_u32 v20, v21, 16, 1
	v_lshrrev_b32_e32 v19, 16, v19
	v_add3_u32 v20, v21, v20, s35
	v_and_or_b32 v19, v20, s36, v19
	v_bfe_u32 v20, v22, 16, 1
	v_add3_u32 v20, v22, v20, s35
	v_bfe_u32 v21, v23, 16, 1
	v_lshrrev_b32_e32 v20, 16, v20
	v_add3_u32 v21, v23, v21, s35
	v_and_or_b32 v20, v21, s36, v20
	v_bfe_u32 v21, v24, 16, 1
	v_add3_u32 v21, v24, v21, s35
	v_bfe_u32 v22, v25, 16, 1
	v_lshrrev_b32_e32 v21, 16, v21
	v_add3_u32 v22, v25, v22, s35
	v_add_u32_e32 v36, v193, v166
	v_and_or_b32 v21, v22, s36, v21
	ds_write2_b64 v36, v[18:19], v[20:21] offset1:2
	v_bfe_u32 v18, v26, 16, 1
	v_add3_u32 v18, v26, v18, s35
	v_bfe_u32 v19, v27, 16, 1
	v_lshrrev_b32_e32 v18, 16, v18
	v_add3_u32 v19, v27, v19, s35
	v_and_or_b32 v18, v19, s36, v18
	v_bfe_u32 v19, v28, 16, 1
	v_add3_u32 v19, v28, v19, s35
	v_bfe_u32 v20, v29, 16, 1
	s_waitcnt lgkmcnt(1)
	v_mfma_f32_32x32x16_bf16 v[2:17], v[70:73], v[40:43], v[2:17]
	v_lshrrev_b32_e32 v19, 16, v19
	v_add3_u32 v20, v29, v20, s35
	v_and_or_b32 v19, v20, s36, v19
	v_bfe_u32 v20, v30, 16, 1
	v_add3_u32 v20, v30, v20, s35
	v_bfe_u32 v21, v31, 16, 1
	v_lshrrev_b32_e32 v20, 16, v20
	v_add3_u32 v21, v31, v21, s35
	v_and_or_b32 v20, v21, s36, v20
	v_bfe_u32 v21, v32, 16, 1
	v_add3_u32 v21, v32, v21, s35
	v_bfe_u32 v22, v33, 16, 1
	v_lshrrev_b32_e32 v21, 16, v21
	v_add3_u32 v22, v33, v22, s35
	v_and_or_b32 v21, v22, s36, v21
	ds_write2_b64 v36, v[18:19], v[20:21] offset0:4 offset1:6
	v_bfe_u32 v18, v2, 16, 1
	v_add3_u32 v2, v2, v18, s35
	v_bfe_u32 v18, v3, 16, 1
	v_lshrrev_b32_e32 v2, 16, v2
	v_add3_u32 v3, v3, v18, s35
	v_and_or_b32 v2, v3, s36, v2
	v_bfe_u32 v3, v4, 16, 1
	v_add3_u32 v3, v4, v3, s35
	v_bfe_u32 v4, v5, 16, 1
	v_lshrrev_b32_e32 v3, 16, v3
	v_add3_u32 v4, v5, v4, s35
	v_and_or_b32 v3, v4, s36, v3
	v_bfe_u32 v4, v6, 16, 1
	v_add3_u32 v4, v6, v4, s35
	v_bfe_u32 v5, v7, 16, 1
	v_lshrrev_b32_e32 v4, 16, v4
	v_add3_u32 v5, v7, v5, s35
	v_and_or_b32 v4, v5, s36, v4
	v_bfe_u32 v5, v8, 16, 1
	v_add3_u32 v5, v8, v5, s35
	v_bfe_u32 v6, v9, 16, 1
	v_lshrrev_b32_e32 v5, 16, v5
	v_add3_u32 v6, v9, v6, s35
	v_and_or_b32 v5, v6, s36, v5
	ds_write2_b64 v36, v[2:3], v[4:5] offset0:8 offset1:10
	v_bfe_u32 v2, v10, 16, 1
	v_add3_u32 v2, v10, v2, s35
	v_bfe_u32 v3, v11, 16, 1
	v_add_f32_e32 v35, v147, v35
	v_lshrrev_b32_e32 v2, 16, v2
	v_add3_u32 v3, v11, v3, s35
	v_add_f32_e32 v35, v148, v35
	v_and_or_b32 v2, v3, s36, v2
	v_bfe_u32 v3, v12, 16, 1
	v_add_f32_e32 v35, v149, v35
	v_add3_u32 v3, v12, v3, s35
	v_bfe_u32 v4, v13, 16, 1
	v_add_f32_e32 v35, v151, v35
	v_lshrrev_b32_e32 v3, 16, v3
	v_add3_u32 v4, v13, v4, s35
	v_add_f32_e32 v35, v152, v35
	v_and_or_b32 v3, v4, s36, v3
	v_bfe_u32 v4, v14, 16, 1
	v_add_f32_e32 v34, v34, v35
	v_add3_u32 v4, v14, v4, s35
	v_bfe_u32 v5, v15, 16, 1
	v_mov_b32_e32 v35, v34
	s_nop 1
	v_permlane32_swap_b32_e32 v35, v34
	v_lshrrev_b32_e32 v4, 16, v4
	v_add3_u32 v5, v15, v5, s35
	v_and_or_b32 v4, v5, s36, v4
	v_bfe_u32 v5, v16, 16, 1
	v_add3_u32 v5, v16, v5, s35
	v_bfe_u32 v6, v17, 16, 1
	v_lshrrev_b32_e32 v5, 16, v5
	v_add3_u32 v6, v17, v6, s35
	v_and_or_b32 v5, v6, s36, v5
	ds_write2_b64 v36, v[2:3], v[4:5] offset0:12 offset1:14
	s_and_saveexec_b64 s[14:15], s[4:5]
	s_cbranch_execz .LBB0_380
	s_waitcnt lgkmcnt(1)
	v_add_f32_e32 v151, v34, v35
	ds_write_b64 v193, v[150:151] offset:128
; __device__ __forceinline__ float bf_lo(unsigned w) { return __uint_as_float(w << 16); }
; template <int STAGE, int OFF> __device__ __forceinline__ void attn32_unit(const bf16* base, bf16* yrow0, int blk0, int u, LAS unsigned char* xtab, LAS unsigned char* kbuf, LAS unsigned char* vbuf, int lane, ...
;     ...
;     } else {
; #pragma unroll
;         for (int mb = 0; mb < 2; ++mb)
; #pragma unroll
;             for (int gq = 0; gq < 4; ++gq) { const v2u w = *(const LAS v2u*)(xrow + 2 * (32 * mb + 8 * gq + 4 * h)); o[mb][4 * gq] = bf_lo(w.x); o[mb][4 * gq + 1] = bf_hi(w.x); o[mb][4 * gq + 2] = bf_lo(w.y); o[mb][4 * gq + 3] = bf_hi(w.y); }
;         m = *(const LAS float*)(xrow + 128); l = h == 0 ? *(const LAS float*)(xrow + 132) : 0.f;
;     }
;     const int hi = qi, lo = max(qi - 128, -(t0 >> SH));
;     const unsigned mspan = (unsigned)(hi - lo);
; #pragma unroll
;     for (int pp = 0; pp < 5; ++pp) {
;         constexpr int dummy = 0; (void)dummy;
;         const int set = (pp + OFF) % 2, n0 = -128 + 32 * pp;
; #pragma unroll
;         for (int c = 0; c < 4; ++c) { *(LAS v4u*)(kbuf + (8 * c + lrow) * 144 + lch * 16) = kr[set][c]; *(LAS v4u*)(vbuf + (8 * c + lrow) * 160 + lch * 16) = vr[set][c]; }
;         if (pp + 2 < 5) { ATT32_LOAD(set, pp + 2, t0, SH); }
;         else { const bf16* base_ = base; { const bf16* base = nbase; ATT32_LOAD(set, pp + 2 - 5, nt0, nsh); } (void)base_; }
;         f32x16 sc;
; #pragma unroll
;         for (int i = 0; i < 16; ++i) sc[i] = 0.f;
; #pragma unroll
;         for (int ks = 0; ks < 4; ++ks) { const bf16x8 ka = *(const LAS bf16x8*)(kbuf + qi * 144 + 32 * ks + 16 * h); sc = MFMA32(ka, qb[ks], sc); }
;         if (pp == 4) {
; #pragma unroll
;             for (int ks = 0; ks < 4; ++ks) qb[ks] = *(const bf16x8*)(nbase + (size_t)min(nt0 + (qi << nsh), SEQ - 1) * 1536 + 16 * ks + 8 * h);
;         }
;         const int mbase = n0 + 4 * h - lo; float mx = -INFINITY;
; #pragma unroll
;         for (int rg = 0; rg < 16; ++rg) { sc[rg] = ((unsigned)(mbase + (rg & 3) + 8 * (rg >> 2)) <= mspan) ? sc[rg] : -INFINITY; mx = fmaxf(mx, sc[rg]); }
;         mx = fmaxf(mx, __shfl_xor(mx, 32));
;         if (__any(mx > m)) {
;             const float mn = fmaxf(m, mx), alpha = __builtin_amdgcn_exp2f(m - mn); m = mn; l *= alpha;
; #pragma unroll
;             for (int i = 0; i < 16; ++i) { o[0][i] *= alpha; o[1][i] *= alpha; }
;         }
.LBB0_380:
	s_or_b64 exec, exec, s[14:15]
	v_add_u32_e32 v51, v194, v166
	s_waitcnt lgkmcnt(0)
	s_barrier
	ds_read2_b64 v[10:13], v51 offset1:2
	ds_read2_b64 v[2:5], v51 offset0:4 offset1:6
	ds_read2_b64 v[6:9], v51 offset0:8 offset1:10
	ds_read2_b64 v[14:17], v51 offset0:12 offset1:14
	ds_read_b32 v50, v194 offset:128
	v_mov_b32_e32 v138, 0
	s_and_saveexec_b64 s[14:15], s[4:5]
	ds_read_b32 v138, v194 offset:132
	s_or_b64 exec, exec, s[14:15]
	s_waitcnt vmcnt(19)
	ds_write_b128 v231, v[106:109]
	s_waitcnt vmcnt(18)
	ds_write_b128 v232, v[110:113] offset:4608
	s_waitcnt vmcnt(17)
	ds_write_b128 v231, v[114:117] offset:1152
	s_waitcnt vmcnt(16)
	ds_write_b128 v232, v[118:121] offset:5888
	s_waitcnt vmcnt(15)
	ds_write_b128 v231, v[122:125] offset:2304
	s_waitcnt vmcnt(14)
	ds_write_b128 v232, v[126:129] offset:7168
	s_waitcnt vmcnt(13)
	ds_write_b128 v231, v[130:133] offset:3456
	s_waitcnt vmcnt(12)
	ds_write_b128 v232, v[134:137] offset:8448
	ds_read_b128 v[34:37], v177
	s_waitcnt lgkmcnt(13)
	v_lshlrev_b32_e32 v22, 16, v12
	v_and_b32_e32 v23, 0xffff0000, v12
	v_add_u32_e32 v12, s10, v195
	v_med3_i32 v12, v12, 0, v233
	v_mul_u32_u24_e32 v12, 0xc00, v12
	v_or_b32_e32 v12, v12, v176
	global_load_dwordx4 v[70:73], v12, s[8:9] offset:1024
	global_load_dwordx4 v[106:109], v12, s[8:9] offset:2048
	ds_read_b128 v[118:121], v177 offset:32
	v_add_u32_e32 v12, s10, v196
	s_waitcnt vmcnt(5) lgkmcnt(1)
	v_mfma_f32_32x32x16_bf16 v[34:49], v[34:37], v[66:69], 0
	v_med3_i32 v12, v12, 0, v233
	v_mul_u32_u24_e32 v12, 0xc00, v12
	v_or_b32_e32 v12, v12, v176
	global_load_dwordx4 v[110:113], v12, s[8:9] offset:1024
	global_load_dwordx4 v[114:117], v12, s[8:9] offset:2048
	v_add_u32_e32 v12, s10, v197
	v_med3_i32 v12, v12, 0, v233
	v_mul_u32_u24_e32 v12, 0xc00, v12
	v_or_b32_e32 v12, v12, v176
	ds_read_b128 v[134:137], v177 offset:96
	ds_read_b128 v[140:143], v177 offset:64
	s_waitcnt vmcnt(6) lgkmcnt(2)
	v_mfma_f32_32x32x16_bf16 v[34:49], v[118:121], v[62:65], v[34:49]
	global_load_dwordx4 v[118:121], v12, s[8:9] offset:1024
	global_load_dwordx4 v[122:125], v12, s[8:9] offset:2048
	v_add_u32_e32 v12, s10, v198
	v_med3_i32 v12, v12, 0, v233
	v_mul_u32_u24_e32 v12, 0xc00, v12
	v_or_b32_e32 v12, v12, v176
	global_load_dwordx4 v[126:129], v12, s[8:9] offset:1024
	global_load_dwordx4 v[130:133], v12, s[8:9] offset:2048
	s_ashr_i32 s0, s10, 2
	s_waitcnt vmcnt(9) lgkmcnt(0)
	v_mfma_f32_32x32x16_bf16 v[34:49], v[140:143], v[58:61], v[34:49]
	s_sub_i32 s0, 0, s0
	v_lshlrev_b32_e32 v18, 16, v10
	v_and_b32_e32 v19, 0xffff0000, v10
	v_lshlrev_b32_e32 v20, 16, v11
	v_and_b32_e32 v21, 0xffff0000, v11
	v_lshlrev_b32_e32 v10, 16, v14
	v_and_b32_e32 v11, 0xffff0000, v14
	s_waitcnt vmcnt(8)
	v_mfma_f32_32x32x16_bf16 v[34:49], v[134:137], v[54:57], v[34:49]
	v_max_i32_e32 v14, s0, v175
	v_sub_u32_e32 v162, v1, v14
	v_sub_u32_e32 v163, v178, v14
	v_cmp_le_u32_e32 vcc, v163, v162
	v_add_u32_e32 v14, 1, v163
	v_lshlrev_b32_e32 v24, 16, v13
	v_and_b32_e32 v25, 0xffff0000, v13
	v_lshlrev_b32_e32 v12, 16, v15
	v_and_b32_e32 v13, 0xffff0000, v15
	s_nop 2
	v_cndmask_b32_e32 v34, v234, v34, vcc
	v_cmp_le_u32_e32 vcc, v14, v162
	v_add_u32_e32 v15, 2, v163
	v_lshlrev_b32_e32 v26, 16, v2
	v_cndmask_b32_e32 v35, v234, v35, vcc
	v_cmp_le_u32_e32 vcc, v15, v162
	v_add_u32_e32 v15, 3, v163
	v_max3_f32 v14, v34, s31, v35
	v_cndmask_b32_e32 v36, v234, v36, vcc
	v_cmp_le_u32_e32 vcc, v15, v162
	v_add_u32_e32 v15, 8, v163
	v_and_b32_e32 v27, 0xffff0000, v2
	v_cndmask_b32_e32 v37, v234, v37, vcc
	v_cmp_le_u32_e32 vcc, v15, v162
	v_add_u32_e32 v15, 9, v163
	v_max3_f32 v14, v14, v36, v37
	v_cndmask_b32_e32 v38, v234, v38, vcc
	v_cmp_le_u32_e32 vcc, v15, v162
	v_add_u32_e32 v15, 10, v163
	v_lshlrev_b32_e32 v28, 16, v3
	v_cndmask_b32_e32 v39, v234, v39, vcc
	v_cmp_le_u32_e32 vcc, v15, v162
	v_add_u32_e32 v15, 11, v163
	v_max3_f32 v14, v14, v38, v39
	v_cndmask_b32_e32 v40, v234, v40, vcc
	v_cmp_le_u32_e32 vcc, v15, v162
	v_add_u32_e32 v15, 16, v163
	v_and_b32_e32 v29, 0xffff0000, v3
	v_cndmask_b32_e32 v41, v234, v41, vcc
	v_cmp_le_u32_e32 vcc, v15, v162
	v_add_u32_e32 v15, 17, v163
	v_max3_f32 v14, v14, v40, v41
	v_cndmask_b32_e32 v42, v234, v42, vcc
	v_cmp_le_u32_e32 vcc, v15, v162
	v_add_u32_e32 v15, 18, v163
	v_lshlrev_b32_e32 v30, 16, v4
	v_cndmask_b32_e32 v43, v234, v43, vcc
	v_cmp_le_u32_e32 vcc, v15, v162
	v_add_u32_e32 v15, 19, v163
	v_max3_f32 v14, v14, v42, v43
	v_cndmask_b32_e32 v44, v234, v44, vcc
	v_cmp_le_u32_e32 vcc, v15, v162
	v_add_u32_e32 v15, 24, v163
	v_and_b32_e32 v31, 0xffff0000, v4
	v_cndmask_b32_e32 v45, v234, v45, vcc
	v_cmp_le_u32_e32 vcc, v15, v162
	v_add_u32_e32 v15, 25, v163
	v_max3_f32 v14, v14, v44, v45
	v_cndmask_b32_e32 v46, v234, v46, vcc
	v_cmp_le_u32_e32 vcc, v15, v162
	v_add_u32_e32 v15, 26, v163
	v_lshlrev_b32_e32 v32, 16, v5
	v_cndmask_b32_e32 v47, v234, v47, vcc
	v_cmp_le_u32_e32 vcc, v15, v162
	v_add_u32_e32 v15, 27, v163
	v_max3_f32 v14, v14, v46, v47
	v_cndmask_b32_e32 v48, v234, v48, vcc
	v_cmp_le_u32_e32 vcc, v15, v162
	v_and_b32_e32 v33, 0xffff0000, v5
	v_lshlrev_b32_e32 v2, 16, v6
	v_cndmask_b32_e32 v49, v234, v49, vcc
	v_max3_f32 v134, v14, v48, v49
	v_mov_b32_e32 v135, v134
	s_nop 1
	v_permlane32_swap_b32_e32 v135, v134
	v_and_b32_e32 v3, 0xffff0000, v6
	v_lshlrev_b32_e32 v4, 16, v7
	v_and_b32_e32 v5, 0xffff0000, v7
	v_lshlrev_b32_e32 v6, 16, v8
	s_waitcnt lgkmcnt(0)
	v_max_f32_e32 v135, v135, v135
	v_max_f32_e32 v134, v134, v135
	v_and_b32_e32 v7, 0xffff0000, v8
	v_lshlrev_b32_e32 v8, 16, v9
	v_and_b32_e32 v9, 0xffff0000, v9
	v_lshlrev_b32_e32 v14, 16, v16
	v_and_b32_e32 v15, 0xffff0000, v16
	v_lshlrev_b32_e32 v16, 16, v17
	v_and_b32_e32 v17, 0xffff0000, v17
	v_cmp_gt_f32_e32 vcc, v134, v50
	s_cbranch_vccz .LBB0_384
	v_max_f32_e32 v134, v134, v134
	v_max_f32_e32 v135, v50, v50
	v_max_f32_e32 v134, v135, v134
	v_sub_f32_e32 v50, v50, v134
	v_exp_f32_e32 v50, v50
	s_nop 0
	v_pk_mul_f32 v[16:17], v[50:51], v[16:17] op_sel_hi:[0,1]
	v_pk_mul_f32 v[14:15], v[50:51], v[14:15] op_sel_hi:[0,1]
	v_pk_mul_f32 v[12:13], v[50:51], v[12:13] op_sel_hi:[0,1]
	v_pk_mul_f32 v[10:11], v[50:51], v[10:11] op_sel_hi:[0,1]
	v_pk_mul_f32 v[8:9], v[50:51], v[8:9] op_sel_hi:[0,1]
	v_pk_mul_f32 v[6:7], v[50:51], v[6:7] op_sel_hi:[0,1]
	v_pk_mul_f32 v[4:5], v[50:51], v[4:5] op_sel_hi:[0,1]
	v_pk_mul_f32 v[2:3], v[50:51], v[2:3] op_sel_hi:[0,1]
	v_pk_mul_f32 v[32:33], v[50:51], v[32:33] op_sel_hi:[0,1]
	v_pk_mul_f32 v[30:31], v[50:51], v[30:31] op_sel_hi:[0,1]
	v_pk_mul_f32 v[28:29], v[50:51], v[28:29] op_sel_hi:[0,1]
	v_pk_mul_f32 v[26:27], v[50:51], v[26:27] op_sel_hi:[0,1]
	v_pk_mul_f32 v[24:25], v[50:51], v[24:25] op_sel_hi:[0,1]
	v_pk_mul_f32 v[22:23], v[50:51], v[22:23] op_sel_hi:[0,1]
	v_pk_mul_f32 v[20:21], v[50:51], v[20:21] op_sel_hi:[0,1]
	v_pk_mul_f32 v[18:19], v[50:51], v[18:19] op_sel_hi:[0,1]
	v_mul_f32_e32 v138, v138, v50
	v_mov_b32_e32 v50, v134
; #define LAS __attribute__((address_space(3)))
; template <int STAGE, int OFF> __device__ __forceinline__ void attn32_unit(const bf16* base, bf16* yrow0, int blk0, int u, LAS unsigned char* xtab, LAS unsigned char* kbuf, LAS unsigned char* vbuf, int lane, ...
;     ...
;         for (int c = 0; c < 4; ++c) { *(LAS v4u*)(kbuf + (8 * c + lrow) * 144 + lch * 16) = kr[set][c]; *(LAS v4u*)(vbuf + (8 * c + lrow) * 160 + lch * 16) = vr[set][c]; }
;         if (pp + 2 < 5) { ATT32_LOAD(set, pp + 2, t0, SH); }
;         else { const bf16* base_ = base; { const bf16* base = nbase; ATT32_LOAD(set, pp + 2 - 5, nt0, nsh); } (void)base_; }
;         f32x16 sc;
; #pragma unroll
;         for (int i = 0; i < 16; ++i) sc[i] = 0.f;
; #pragma unroll
;         for (int ks = 0; ks < 4; ++ks) { const bf16x8 ka = *(const LAS bf16x8*)(kbuf + qi * 144 + 32 * ks + 16 * h); sc = MFMA32(ka, qb[ks], sc); }
;         if (pp == 4) {
; #pragma unroll
;             for (int ks = 0; ks < 4; ++ks) qb[ks] = *(const bf16x8*)(nbase + (size_t)min(nt0 + (qi << nsh), SEQ - 1) * 1536 + 16 * ks + 8 * h);
;         }
;         const int mbase = n0 + 4 * h - lo; float mx = -INFINITY;
; #pragma unroll
;         for (int rg = 0; rg < 16; ++rg) { sc[rg] = ((unsigned)(mbase + (rg & 3) + 8 * (rg >> 2)) <= mspan) ? sc[rg] : -INFINITY; mx = fmaxf(mx, sc[rg]); }
;         mx = fmaxf(mx, __shfl_xor(mx, 32));
;         if (__any(mx > m)) {
;             const float mn = fmaxf(m, mx), alpha = __builtin_amdgcn_exp2f(m - mn); m = mn; l *= alpha;
; #pragma unroll
;             for (int i = 0; i < 16; ++i) { o[0][i] *= alpha; o[1][i] *= alpha; }
;         }
;         float ps = 0.f;
; #pragma unroll
;         for (int rg = 0; rg < 16; ++rg) { sc[rg] = __builtin_amdgcn_exp2f(sc[rg] - m); ps += sc[rg]; }
;         l += ps;
;         bf16x8 pb[2];
; #pragma unroll
;         for (int s2 = 0; s2 < 2; ++s2) { v4u w; w.x = pg8::cvt_pk_bf16(sc[8 * s2], sc[8 * s2 + 1]); w.y = pg8::cvt_pk_bf16(sc[8 * s2 + 2], sc[8 * s2 + 3]); w.z = pg8::cvt_pk_bf16(sc[8 * s2 + 4], sc[8 * s2 + 5]); w.w = pg8::cvt_pk_bf16(sc[8 * s2 + 6], sc[8 * s2 + 7]); pb[s2] = __builtin_bit_cast(bf16x8, w); }
; #pragma unroll
;         for (int mb = 0; mb < 2; ++mb)
; #pragma unroll
;             for (int s2 = 0; s2 < 2; ++s2) {
;                 LAS unsigned char* vp = vbuf + tr_off + (16 * s2) * 160 + 64 * mb;
.LBB0_384:
	v_sub_f32_e32 v34, v34, v50
	v_exp_f32_e32 v134, v34
	v_sub_f32_e32 v34, v35, v50
	v_exp_f32_e32 v135, v34
	v_sub_f32_e32 v34, v36, v50
	v_exp_f32_e32 v136, v34
	v_sub_f32_e32 v34, v37, v50
	v_exp_f32_e32 v137, v34
	v_sub_f32_e32 v34, v38, v50
	v_exp_f32_e32 v139, v34
	v_sub_f32_e32 v34, v39, v50
	v_exp_f32_e32 v140, v34
	v_sub_f32_e32 v34, v40, v50
	v_exp_f32_e32 v141, v34
	v_sub_f32_e32 v34, v41, v50
	v_exp_f32_e32 v142, v34
	v_sub_f32_e32 v34, v42, v50
	v_exp_f32_e32 v164, v34
	v_sub_f32_e32 v34, v43, v50
	v_exp_f32_e32 v165, v34
	v_sub_f32_e32 v34, v44, v50
	v_exp_f32_e32 v171, v34
	v_sub_f32_e32 v34, v45, v50
	v_exp_f32_e32 v172, v34
	v_sub_f32_e32 v34, v46, v50
	v_exp_f32_e32 v173, v34
	v_sub_f32_e32 v34, v47, v50
	v_exp_f32_e32 v237, v34
	v_sub_f32_e32 v34, v48, v50
	v_exp_f32_e32 v246, v34
	v_sub_f32_e32 v34, v49, v50
	v_exp_f32_e32 v247, v34
	v_cvt_pk_bf16_f32 v34, v134, v135
	v_cvt_pk_bf16_f32 v35, v136, v137
	v_cvt_pk_bf16_f32 v36, v139, v140
	v_cvt_pk_bf16_f32 v37, v141, v142
	v_cvt_pk_bf16_f32 v238, v164, v165
	v_cvt_pk_bf16_f32 v239, v171, v172
	v_cvt_pk_bf16_f32 v240, v173, v237
	v_cvt_pk_bf16_f32 v241, v246, v247
	ds_read_b64_tr_b16 v[38:39], v181 offset:4608
	ds_read_b64_tr_b16 v[40:41], v181 offset:5888
	ds_read_b64_tr_b16 v[44:45], v181 offset:5952
	ds_read_b64_tr_b16 v[42:43], v181 offset:4672
	s_waitcnt lgkmcnt(2)
	v_mfma_f32_32x32x16_bf16 v[18:33], v[38:41], v[34:37], v[18:33]
	ds_read_b64_tr_b16 v[38:39], v181 offset:7168
	ds_read_b64_tr_b16 v[40:41], v181 offset:8448
	v_add_f32_e32 v46, 0, v134
	ds_read_b64_tr_b16 v[244:245], v181 offset:8512
	ds_read_b64_tr_b16 v[242:243], v181 offset:7232
	ds_write_b128 v231, v[74:77]
	ds_write_b128 v232, v[78:81] offset:4608
	ds_write_b128 v231, v[82:85] offset:1152
	ds_write_b128 v232, v[86:89] offset:5888
	ds_write_b128 v231, v[90:93] offset:2304
	ds_write_b128 v232, v[94:97] offset:7168
	ds_write_b128 v231, v[98:101] offset:3456
	ds_write_b128 v232, v[102:105] offset:8448
	s_waitcnt lgkmcnt(10)
	v_mfma_f32_32x32x16_bf16 v[18:33], v[38:41], v[238:241], v[18:33]
	v_add_f32_e32 v38, v135, v46
	v_add_f32_e32 v38, v136, v38
	v_add_f32_e32 v38, v137, v38
	v_add_f32_e32 v38, v139, v38
	v_add_f32_e32 v38, v140, v38
	v_add_f32_e32 v38, v141, v38
	v_add_f32_e32 v139, v142, v38
	v_mfma_f32_32x32x16_bf16 v[2:17], v[42:45], v[34:37], v[2:17]
	v_add_u32_e32 v34, s10, v199
	v_med3_i32 v34, v34, 0, v233
	v_mul_u32_u24_e32 v38, 0xc00, v34
	ds_read_b128 v[34:37], v177
	v_or_b32_e32 v38, v38, v176
	global_load_dwordx4 v[86:89], v38, s[8:9] offset:1024
	global_load_dwordx4 v[90:93], v38, s[8:9] offset:2048
	v_add_u32_e32 v38, s10, v200
	v_med3_i32 v38, v38, 0, v233
	v_mul_u32_u24_e32 v38, 0xc00, v38
	ds_read_b128 v[74:77], v177 offset:32
	v_or_b32_e32 v78, v38, v176
	s_waitcnt lgkmcnt(1)
	v_mfma_f32_32x32x16_bf16 v[34:49], v[34:37], v[66:69], 0
	global_load_dwordx4 v[134:137], v78, s[8:9] offset:1024
	global_load_dwordx4 v[142:145], v78, s[8:9] offset:2048
	v_add_u32_e32 v78, s10, v201
	v_med3_i32 v78, v78, 0, v233
	v_mul_u32_u24_e32 v78, 0xc00, v78
	v_or_b32_e32 v94, v78, v176
	ds_read_b128 v[78:81], v177 offset:96
	ds_read_b128 v[82:85], v177 offset:64
	global_load_dwordx4 v[146:149], v94, s[8:9] offset:1024
	global_load_dwordx4 v[150:153], v94, s[8:9] offset:2048
	s_waitcnt lgkmcnt(2)
	v_mfma_f32_32x32x16_bf16 v[34:49], v[74:77], v[62:65], v[34:49]
	v_add_u32_e32 v74, s10, v202
	v_med3_i32 v74, v74, 0, v233
	v_mul_u32_u24_e32 v74, 0xc00, v74
	v_or_b32_e32 v74, v74, v176
	global_load_dwordx4 v[154:157], v74, s[8:9] offset:1024
	global_load_dwordx4 v[158:161], v74, s[8:9] offset:2048
	v_add_u32_e32 v75, 32, v163
	v_cmp_le_u32_e32 vcc, v75, v162
	s_waitcnt lgkmcnt(0)
	v_mfma_f32_32x32x16_bf16 v[34:49], v[82:85], v[58:61], v[34:49]
	v_add_u32_e32 v75, 33, v163
	v_add_u32_e32 v76, 34, v163
	v_add_f32_e32 v74, v164, v139
	v_add_f32_e32 v74, v165, v74
	v_add_f32_e32 v74, v171, v74
	v_add_f32_e32 v74, v172, v74
	v_add_f32_e32 v74, v173, v74
	v_mfma_f32_32x32x16_bf16 v[34:49], v[78:81], v[54:57], v[34:49]
	v_add_f32_e32 v74, v237, v74
	v_add_f32_e32 v74, v246, v74
	v_add_f32_e32 v74, v247, v74
	v_add_f32_e32 v164, v138, v74
	v_mfma_f32_32x32x16_bf16 v[2:17], v[242:245], v[238:241], v[2:17]
	s_nop 6
	v_cndmask_b32_e32 v34, v234, v34, vcc
	v_cmp_le_u32_e32 vcc, v75, v162
	s_nop 1
	v_cndmask_b32_e32 v35, v234, v35, vcc
	v_cmp_le_u32_e32 vcc, v76, v162
	v_add_u32_e32 v76, 35, v163
	v_max3_f32 v75, v34, s31, v35
	v_cndmask_b32_e32 v36, v234, v36, vcc
	v_cmp_le_u32_e32 vcc, v76, v162
	v_add_u32_e32 v76, 40, v163
	s_nop 0
	v_cndmask_b32_e32 v37, v234, v37, vcc
	v_cmp_le_u32_e32 vcc, v76, v162
	v_add_u32_e32 v76, 41, v163
	v_max3_f32 v75, v75, v36, v37
	v_cndmask_b32_e32 v38, v234, v38, vcc
	v_cmp_le_u32_e32 vcc, v76, v162
	v_add_u32_e32 v76, 42, v163
	s_nop 0
	v_cndmask_b32_e32 v39, v234, v39, vcc
	v_cmp_le_u32_e32 vcc, v76, v162
	v_add_u32_e32 v76, 43, v163
	v_max3_f32 v75, v75, v38, v39
	v_cndmask_b32_e32 v40, v234, v40, vcc
	v_cmp_le_u32_e32 vcc, v76, v162
	v_add_u32_e32 v76, 48, v163
	s_nop 0
	v_cndmask_b32_e32 v41, v234, v41, vcc
	v_cmp_le_u32_e32 vcc, v76, v162
	v_add_u32_e32 v76, 49, v163
	v_max3_f32 v75, v75, v40, v41
	v_cndmask_b32_e32 v42, v234, v42, vcc
	v_cmp_le_u32_e32 vcc, v76, v162
	v_add_u32_e32 v76, 50, v163
	s_nop 0
	v_cndmask_b32_e32 v43, v234, v43, vcc
	v_cmp_le_u32_e32 vcc, v76, v162
	v_add_u32_e32 v76, 51, v163
	v_max3_f32 v75, v75, v42, v43
	v_cndmask_b32_e32 v44, v234, v44, vcc
	v_cmp_le_u32_e32 vcc, v76, v162
	v_add_u32_e32 v76, 56, v163
	s_nop 0
	v_cndmask_b32_e32 v45, v234, v45, vcc
	v_cmp_le_u32_e32 vcc, v76, v162
	v_add_u32_e32 v76, 57, v163
	v_max3_f32 v75, v75, v44, v45
	v_cndmask_b32_e32 v46, v234, v46, vcc
	v_cmp_le_u32_e32 vcc, v76, v162
	v_add_u32_e32 v76, 58, v163
	s_nop 0
	v_cndmask_b32_e32 v47, v234, v47, vcc
	v_cmp_le_u32_e32 vcc, v76, v162
	v_add_u32_e32 v76, 59, v163
	v_max3_f32 v75, v75, v46, v47
	v_cndmask_b32_e32 v48, v234, v48, vcc
	v_cmp_le_u32_e32 vcc, v76, v162
	s_nop 1
	v_cndmask_b32_e32 v49, v234, v49, vcc
	v_max3_f32 v75, v75, v48, v49
	v_mov_b32_e32 v76, v75
	s_nop 1
	v_permlane32_swap_b32_e32 v76, v75
	s_waitcnt lgkmcnt(0)
	v_max_f32_e32 v74, v76, v76
	v_max_f32_e32 v74, v75, v74
	v_cmp_gt_f32_e32 vcc, v74, v50
	s_cbranch_vccz .LBB0_386
; __device__ __forceinline__ unsigned cvt_pk_bf16(float lo, float hi) { unsigned r; asm volatile("v_cvt_pk_bf16_f32 %0, %1, %2" : "=v"(r) : "v"(lo), "v"(hi)); return r; }
; #define LAS __attribute__((address_space(3)))
; template <int STAGE, int OFF> __device__ __forceinline__ void attn32_unit(const bf16* base, bf16* yrow0, int blk0, int u, LAS unsigned char* xtab, LAS unsigned char* kbuf, LAS unsigned char* vbuf, int lane, ...
;     ...
;         for (int c = 0; c < 4; ++c) { *(LAS v4u*)(kbuf + (8 * c + lrow) * 144 + lch * 16) = kr[set][c]; *(LAS v4u*)(vbuf + (8 * c + lrow) * 160 + lch * 16) = vr[set][c]; }
;         if (pp + 2 < 5) { ATT32_LOAD(set, pp + 2, t0, SH); }
;         else { const bf16* base_ = base; { const bf16* base = nbase; ATT32_LOAD(set, pp + 2 - 5, nt0, nsh); } (void)base_; }
;         f32x16 sc;
; #pragma unroll
;         for (int i = 0; i < 16; ++i) sc[i] = 0.f;
; #pragma unroll
;         for (int ks = 0; ks < 4; ++ks) { const bf16x8 ka = *(const LAS bf16x8*)(kbuf + qi * 144 + 32 * ks + 16 * h); sc = MFMA32(ka, qb[ks], sc); }
;     ...
;         if (__any(mx > m)) {
;             const float mn = fmaxf(m, mx), alpha = __builtin_amdgcn_exp2f(m - mn); m = mn; l *= alpha;
; #pragma unroll
;             for (int i = 0; i < 16; ++i) { o[0][i] *= alpha; o[1][i] *= alpha; }
;         }
;         float ps = 0.f;
; #pragma unroll
;         for (int rg = 0; rg < 16; ++rg) { sc[rg] = __builtin_amdgcn_exp2f(sc[rg] - m); ps += sc[rg]; }
;         l += ps;
;         bf16x8 pb[2];
; #pragma unroll
;         for (int s2 = 0; s2 < 2; ++s2) { v4u w; w.x = pg8::cvt_pk_bf16(sc[8 * s2], sc[8 * s2 + 1]); w.y = pg8::cvt_pk_bf16(sc[8 * s2 + 2], sc[8 * s2 + 3]); w.z = pg8::cvt_pk_bf16(sc[8 * s2 + 4], sc[8 * s2 + 5]); w.w = pg8::cvt_pk_bf16(sc[8 * s2 + 6], sc[8 * s2 + 7]); pb[s2] = __builtin_bit_cast(bf16x8, w); }
; #pragma unroll
;         for (int mb = 0; mb < 2; ++mb)
; #pragma unroll
;             for (int s2 = 0; s2 < 2; ++s2) {
;                 LAS unsigned char* vp = vbuf + tr_off + (16 * s2) * 160 + 64 * mb;
;                 const v4i16 a0 = __builtin_amdgcn_ds_read_tr16_b64_v4i16((LAS v4i16*)vp), a1 = __builtin_amdgcn_ds_read_tr16_b64_v4i16((LAS v4i16*)(vp + 8 * 160));
;                 const bf16x8 va = __builtin_shufflevector(a0, a1, 0, 1, 2, 3, 4, 5, 6, 7);
;                 o[mb] = MFMA32(va, pb[s2], o[mb]);
;             }
	v_max_f32_e32 v74, v74, v74
	v_max_f32_e32 v75, v50, v50
	v_max_f32_e32 v74, v75, v74
	v_sub_f32_e32 v50, v50, v74
	v_exp_f32_e32 v50, v50
	s_nop 0
	v_pk_mul_f32 v[32:33], v[32:33], v[50:51] op_sel_hi:[1,0]
	v_pk_mul_f32 v[30:31], v[30:31], v[50:51] op_sel_hi:[1,0]
	v_pk_mul_f32 v[28:29], v[28:29], v[50:51] op_sel_hi:[1,0]
	v_pk_mul_f32 v[26:27], v[26:27], v[50:51] op_sel_hi:[1,0]
	v_pk_mul_f32 v[24:25], v[24:25], v[50:51] op_sel_hi:[1,0]
	v_pk_mul_f32 v[22:23], v[22:23], v[50:51] op_sel_hi:[1,0]
	v_pk_mul_f32 v[20:21], v[20:21], v[50:51] op_sel_hi:[1,0]
	v_pk_mul_f32 v[18:19], v[18:19], v[50:51] op_sel_hi:[1,0]
	v_pk_mul_f32 v[16:17], v[16:17], v[50:51] op_sel_hi:[1,0]
	v_pk_mul_f32 v[14:15], v[14:15], v[50:51] op_sel_hi:[1,0]
	v_pk_mul_f32 v[12:13], v[12:13], v[50:51] op_sel_hi:[1,0]
	v_pk_mul_f32 v[10:11], v[10:11], v[50:51] op_sel_hi:[1,0]
	v_pk_mul_f32 v[8:9], v[8:9], v[50:51] op_sel_hi:[1,0]
	v_pk_mul_f32 v[6:7], v[6:7], v[50:51] op_sel_hi:[1,0]
	v_pk_mul_f32 v[4:5], v[4:5], v[50:51] op_sel_hi:[1,0]
	v_pk_mul_f32 v[2:3], v[2:3], v[50:51] op_sel_hi:[1,0]
	v_mul_f32_e32 v164, v164, v50
	v_mov_b32_e32 v50, v74
.LBB0_386:
	v_sub_f32_e32 v34, v34, v50
	v_exp_f32_e32 v74, v34
	v_sub_f32_e32 v34, v35, v50
	v_exp_f32_e32 v75, v34
	v_sub_f32_e32 v34, v36, v50
	v_exp_f32_e32 v76, v34
	v_sub_f32_e32 v34, v37, v50
	v_exp_f32_e32 v77, v34
	v_sub_f32_e32 v34, v38, v50
	v_exp_f32_e32 v78, v34
	v_sub_f32_e32 v34, v39, v50
	v_exp_f32_e32 v79, v34
	v_sub_f32_e32 v34, v40, v50
	v_exp_f32_e32 v80, v34
	v_sub_f32_e32 v34, v41, v50
	v_exp_f32_e32 v81, v34
	v_sub_f32_e32 v34, v42, v50
	v_exp_f32_e32 v165, v34
	v_sub_f32_e32 v34, v43, v50
	v_exp_f32_e32 v171, v34
	v_sub_f32_e32 v34, v44, v50
	v_exp_f32_e32 v172, v34
	v_sub_f32_e32 v34, v45, v50
	v_exp_f32_e32 v173, v34
	v_sub_f32_e32 v34, v46, v50
	v_exp_f32_e32 v237, v34
	v_sub_f32_e32 v34, v47, v50
	v_exp_f32_e32 v246, v34
	v_sub_f32_e32 v34, v48, v50
	v_exp_f32_e32 v247, v34
	v_sub_f32_e32 v34, v49, v50
	v_exp_f32_e32 v248, v34
	v_cvt_pk_bf16_f32 v34, v74, v75
	v_cvt_pk_bf16_f32 v35, v76, v77
	v_cvt_pk_bf16_f32 v36, v78, v79
	v_cvt_pk_bf16_f32 v37, v80, v81
	v_cvt_pk_bf16_f32 v238, v165, v171
	v_cvt_pk_bf16_f32 v239, v172, v173
	v_cvt_pk_bf16_f32 v240, v237, v246
	v_cvt_pk_bf16_f32 v241, v247, v248
	ds_read_b64_tr_b16 v[38:39], v181 offset:4608
	ds_read_b64_tr_b16 v[40:41], v181 offset:5888
	ds_read_b64_tr_b16 v[44:45], v181 offset:5952
	ds_read_b64_tr_b16 v[42:43], v181 offset:4672
	s_waitcnt lgkmcnt(2)
	v_mfma_f32_32x32x16_bf16 v[18:33], v[38:41], v[34:37], v[18:33]
	ds_read_b64_tr_b16 v[38:39], v181 offset:7168
	ds_read_b64_tr_b16 v[40:41], v181 offset:8448
	v_add_f32_e32 v46, 0, v74
	ds_read_b64_tr_b16 v[244:245], v181 offset:8512
	ds_read_b64_tr_b16 v[242:243], v181 offset:7232
	s_waitcnt vmcnt(15)
	ds_write_b128 v231, v[70:73]
	s_waitcnt vmcnt(14)
	ds_write_b128 v232, v[106:109] offset:4608
	s_waitcnt vmcnt(13)
	ds_write_b128 v231, v[110:113] offset:1152
	s_waitcnt vmcnt(12)
	ds_write_b128 v232, v[114:117] offset:5888
	s_waitcnt vmcnt(11)
	ds_write_b128 v231, v[118:121] offset:2304
	s_waitcnt vmcnt(10)
	ds_write_b128 v232, v[122:125] offset:7168
	s_waitcnt vmcnt(9)
	ds_write_b128 v231, v[126:129] offset:3456
	s_waitcnt vmcnt(8)
	ds_write_b128 v232, v[130:133] offset:8448
	v_or_b32_e32 v98, s10, v204
	v_or_b32_e32 v102, s10, v205
	s_waitcnt lgkmcnt(10)
	v_mfma_f32_32x32x16_bf16 v[18:33], v[38:41], v[238:241], v[18:33]
	v_add_f32_e32 v38, v75, v46
	v_add_f32_e32 v38, v76, v38
	v_add_f32_e32 v38, v77, v38
	v_add_f32_e32 v38, v78, v38
	v_add_f32_e32 v38, v79, v38
	v_add_f32_e32 v38, v80, v38
	v_add_f32_e32 v249, v81, v38
	v_mfma_f32_32x32x16_bf16 v[2:17], v[42:45], v[34:37], v[2:17]
	v_or_b32_e32 v34, s10, v184
	v_min_u32_e32 v34, 0x3fff, v34
	v_mul_u32_u24_e32 v38, 0xc00, v34
	ds_read_b128 v[34:37], v177
	v_or_b32_e32 v38, v38, v176
	global_load_dwordx4 v[70:73], v38, s[8:9] offset:1024
	global_load_dwordx4 v[74:77], v38, s[8:9] offset:2048
	v_or_b32_e32 v38, s10, v203
	v_min_u32_e32 v38, 0x3fff, v38
	v_mul_u32_u24_e32 v38, 0xc00, v38
	ds_read_b128 v[94:97], v177 offset:32
	v_or_b32_e32 v82, v38, v176
	s_waitcnt lgkmcnt(1)
	v_mfma_f32_32x32x16_bf16 v[34:49], v[34:37], v[66:69], 0
	v_min_u32_e32 v98, 0x3fff, v98
	v_min_u32_e32 v102, 0x3fff, v102
	v_mul_u32_u24_e32 v98, 0xc00, v98
	v_mul_u32_u24_e32 v102, 0xc00, v102
	v_or_b32_e32 v98, v98, v176
	v_or_b32_e32 v114, v102, v176
	global_load_dwordx4 v[78:81], v82, s[8:9] offset:1024
	s_nop 0
	global_load_dwordx4 v[82:85], v82, s[8:9] offset:2048
	ds_read_b128 v[106:109], v177 offset:96
	ds_read_b128 v[110:113], v177 offset:64
	s_waitcnt lgkmcnt(2)
	v_mfma_f32_32x32x16_bf16 v[34:49], v[94:97], v[62:65], v[34:49]
	global_load_dwordx4 v[94:97], v98, s[8:9] offset:1024
	s_nop 0
	global_load_dwordx4 v[98:101], v98, s[8:9] offset:2048
	s_nop 0
	global_load_dwordx4 v[102:105], v114, s[8:9] offset:1024
	global_load_dwordx4 v[138:141], v114, s[8:9] offset:2048
	s_waitcnt lgkmcnt(0)
; __device__ __forceinline__ unsigned cvt_pk_bf16(float lo, float hi) { unsigned r; asm volatile("v_cvt_pk_bf16_f32 %0, %1, %2" : "=v"(r) : "v"(lo), "v"(hi)); return r; }
; #define LAS __attribute__((address_space(3)))
; template <int STAGE, int OFF> __device__ __forceinline__ void attn32_unit(const bf16* base, bf16* yrow0, int blk0, int u, LAS unsigned char* xtab, LAS unsigned char* kbuf, LAS unsigned char* vbuf, int lane, ...
;     ...
;         for (int ks = 0; ks < 4; ++ks) { const bf16x8 ka = *(const LAS bf16x8*)(kbuf + qi * 144 + 32 * ks + 16 * h); sc = MFMA32(ka, qb[ks], sc); }
;         if (pp == 4) {
; #pragma unroll
;             for (int ks = 0; ks < 4; ++ks) qb[ks] = *(const bf16x8*)(nbase + (size_t)min(nt0 + (qi << nsh), SEQ - 1) * 1536 + 16 * ks + 8 * h);
;         }
;         const int mbase = n0 + 4 * h - lo; float mx = -INFINITY;
; #pragma unroll
;         for (int rg = 0; rg < 16; ++rg) { sc[rg] = ((unsigned)(mbase + (rg & 3) + 8 * (rg >> 2)) <= mspan) ? sc[rg] : -INFINITY; mx = fmaxf(mx, sc[rg]); }
;         mx = fmaxf(mx, __shfl_xor(mx, 32));
;         if (__any(mx > m)) {
;             const float mn = fmaxf(m, mx), alpha = __builtin_amdgcn_exp2f(m - mn); m = mn; l *= alpha;
; #pragma unroll
;             for (int i = 0; i < 16; ++i) { o[0][i] *= alpha; o[1][i] *= alpha; }
;         }
;         float ps = 0.f;
; #pragma unroll
;         for (int rg = 0; rg < 16; ++rg) { sc[rg] = __builtin_amdgcn_exp2f(sc[rg] - m); ps += sc[rg]; }
;         l += ps;
;         bf16x8 pb[2];
; #pragma unroll
;         for (int s2 = 0; s2 < 2; ++s2) { v4u w; w.x = pg8::cvt_pk_bf16(sc[8 * s2], sc[8 * s2 + 1]); w.y = pg8::cvt_pk_bf16(sc[8 * s2 + 2], sc[8 * s2 + 3]); w.z = pg8::cvt_pk_bf16(sc[8 * s2 + 4], sc[8 * s2 + 5]); w.w = pg8::cvt_pk_bf16(sc[8 * s2 + 6], sc[8 * s2 + 7]); pb[s2] = __builtin_bit_cast(bf16x8, w); }
; #pragma unroll
;         for (int mb = 0; mb < 2; ++mb)
; #pragma unroll
;             for (int s2 = 0; s2 < 2; ++s2) {
;                 LAS unsigned char* vp = vbuf + tr_off + (16 * s2) * 160 + 64 * mb;
;                 const v4i16 a0 = __builtin_amdgcn_ds_read_tr16_b64_v4i16((LAS v4i16*)vp), a1 = __builtin_amdgcn_ds_read_tr16_b64_v4i16((LAS v4i16*)(vp + 8 * 160));
;                 const bf16x8 va = __builtin_shufflevector(a0, a1, 0, 1, 2, 3, 4, 5, 6, 7);
;                 o[mb] = MFMA32(va, pb[s2], o[mb]);
;             }
	v_mfma_f32_32x32x16_bf16 v[34:49], v[110:113], v[58:61], v[34:49]
	v_add_f32_e32 v110, v165, v249
	v_add_f32_e32 v110, v171, v110
	v_add_f32_e32 v110, v172, v110
	v_add_f32_e32 v110, v173, v110
	v_add_f32_e32 v110, v237, v110
	v_add_f32_e32 v110, v246, v110
	v_add_f32_e32 v110, v247, v110
	v_mfma_f32_32x32x16_bf16 v[34:49], v[106:109], v[54:57], v[34:49]
	v_add_u32_e32 v106, 64, v163
	v_cmp_le_u32_e32 vcc, v106, v162
	v_add_u32_e32 v106, 0x41, v163
	v_add_u32_e32 v107, 0x42, v163
	v_add_f32_e32 v108, v248, v110
	v_add_f32_e32 v164, v164, v108
	s_nop 5
	v_cndmask_b32_e32 v34, v234, v34, vcc
	v_cmp_le_u32_e32 vcc, v106, v162
	v_mfma_f32_32x32x16_bf16 v[2:17], v[242:245], v[238:241], v[2:17]
	s_nop 0
	v_cndmask_b32_e32 v35, v234, v35, vcc
	v_cmp_le_u32_e32 vcc, v107, v162
	v_add_u32_e32 v107, 0x43, v163
	v_max3_f32 v106, v34, s31, v35
	v_cndmask_b32_e32 v36, v234, v36, vcc
	v_cmp_le_u32_e32 vcc, v107, v162
	v_add_u32_e32 v107, 0x48, v163
	s_nop 0
	v_cndmask_b32_e32 v37, v234, v37, vcc
	v_cmp_le_u32_e32 vcc, v107, v162
	v_add_u32_e32 v107, 0x49, v163
	v_max3_f32 v106, v106, v36, v37
	v_cndmask_b32_e32 v38, v234, v38, vcc
	v_cmp_le_u32_e32 vcc, v107, v162
	v_add_u32_e32 v107, 0x4a, v163
	s_nop 0
	v_cndmask_b32_e32 v39, v234, v39, vcc
	v_cmp_le_u32_e32 vcc, v107, v162
	v_add_u32_e32 v107, 0x4b, v163
	v_max3_f32 v106, v106, v38, v39
	v_cndmask_b32_e32 v40, v234, v40, vcc
	v_cmp_le_u32_e32 vcc, v107, v162
	v_add_u32_e32 v107, 0x50, v163
	s_nop 0
	v_cndmask_b32_e32 v41, v234, v41, vcc
	v_cmp_le_u32_e32 vcc, v107, v162
	v_add_u32_e32 v107, 0x51, v163
	v_max3_f32 v106, v106, v40, v41
	v_cndmask_b32_e32 v42, v234, v42, vcc
	v_cmp_le_u32_e32 vcc, v107, v162
	v_add_u32_e32 v107, 0x52, v163
	s_nop 0
	v_cndmask_b32_e32 v43, v234, v43, vcc
	v_cmp_le_u32_e32 vcc, v107, v162
	v_add_u32_e32 v107, 0x53, v163
	v_max3_f32 v106, v106, v42, v43
	v_cndmask_b32_e32 v44, v234, v44, vcc
	v_cmp_le_u32_e32 vcc, v107, v162
	v_add_u32_e32 v107, 0x58, v163
	s_nop 0
	v_cndmask_b32_e32 v45, v234, v45, vcc
	v_cmp_le_u32_e32 vcc, v107, v162
	v_add_u32_e32 v107, 0x59, v163
	v_max3_f32 v106, v106, v44, v45
	v_cndmask_b32_e32 v46, v234, v46, vcc
	v_cmp_le_u32_e32 vcc, v107, v162
	v_add_u32_e32 v107, 0x5a, v163
	s_nop 0
	v_cndmask_b32_e32 v47, v234, v47, vcc
	v_cmp_le_u32_e32 vcc, v107, v162
	v_add_u32_e32 v107, 0x5b, v163
	v_max3_f32 v106, v106, v46, v47
	v_cndmask_b32_e32 v48, v234, v48, vcc
	v_cmp_le_u32_e32 vcc, v107, v162
	s_nop 1
	v_cndmask_b32_e32 v49, v234, v49, vcc
	v_max3_f32 v106, v106, v48, v49
	v_mov_b32_e32 v107, v106
	s_nop 1
	v_permlane32_swap_b32_e32 v107, v106
	s_waitcnt lgkmcnt(0)
	v_max_f32_e32 v107, v107, v107
	v_max_f32_e32 v106, v106, v107
	v_cmp_gt_f32_e32 vcc, v106, v50
	s_cbranch_vccz .LBB0_388
	v_max_f32_e32 v106, v106, v106
	v_max_f32_e32 v107, v50, v50
	v_max_f32_e32 v106, v107, v106
	v_sub_f32_e32 v50, v50, v106
	v_exp_f32_e32 v50, v50
	s_nop 0
	v_pk_mul_f32 v[32:33], v[32:33], v[50:51] op_sel_hi:[1,0]
	v_pk_mul_f32 v[30:31], v[30:31], v[50:51] op_sel_hi:[1,0]
	v_pk_mul_f32 v[28:29], v[28:29], v[50:51] op_sel_hi:[1,0]
	v_pk_mul_f32 v[26:27], v[26:27], v[50:51] op_sel_hi:[1,0]
	v_pk_mul_f32 v[24:25], v[24:25], v[50:51] op_sel_hi:[1,0]
	v_pk_mul_f32 v[22:23], v[22:23], v[50:51] op_sel_hi:[1,0]
	v_pk_mul_f32 v[20:21], v[20:21], v[50:51] op_sel_hi:[1,0]
	v_pk_mul_f32 v[18:19], v[18:19], v[50:51] op_sel_hi:[1,0]
	v_pk_mul_f32 v[16:17], v[16:17], v[50:51] op_sel_hi:[1,0]
	v_pk_mul_f32 v[14:15], v[14:15], v[50:51] op_sel_hi:[1,0]
	v_pk_mul_f32 v[12:13], v[12:13], v[50:51] op_sel_hi:[1,0]
	v_pk_mul_f32 v[10:11], v[10:11], v[50:51] op_sel_hi:[1,0]
	v_pk_mul_f32 v[8:9], v[8:9], v[50:51] op_sel_hi:[1,0]
	v_pk_mul_f32 v[6:7], v[6:7], v[50:51] op_sel_hi:[1,0]
	v_pk_mul_f32 v[4:5], v[4:5], v[50:51] op_sel_hi:[1,0]
	v_pk_mul_f32 v[2:3], v[2:3], v[50:51] op_sel_hi:[1,0]
	v_mul_f32_e32 v164, v164, v50
	v_mov_b32_e32 v50, v106
.LBB0_388:
	v_sub_f32_e32 v34, v34, v50
	v_exp_f32_e32 v106, v34
	v_sub_f32_e32 v34, v35, v50
	v_exp_f32_e32 v107, v34
	v_sub_f32_e32 v34, v36, v50
	v_exp_f32_e32 v108, v34
	v_sub_f32_e32 v34, v37, v50
	v_exp_f32_e32 v109, v34
	v_sub_f32_e32 v34, v38, v50
	v_exp_f32_e32 v110, v34
	v_sub_f32_e32 v34, v39, v50
	v_exp_f32_e32 v111, v34
	v_sub_f32_e32 v34, v40, v50
	v_exp_f32_e32 v112, v34
	v_sub_f32_e32 v34, v41, v50
	v_exp_f32_e32 v113, v34
	v_sub_f32_e32 v34, v42, v50
	v_exp_f32_e32 v165, v34
	v_sub_f32_e32 v34, v43, v50
	v_exp_f32_e32 v171, v34
	v_sub_f32_e32 v34, v44, v50
	v_exp_f32_e32 v172, v34
	v_sub_f32_e32 v34, v45, v50
	v_exp_f32_e32 v173, v34
	v_sub_f32_e32 v34, v46, v50
	v_exp_f32_e32 v237, v34
	v_sub_f32_e32 v34, v47, v50
	v_exp_f32_e32 v246, v34
	v_sub_f32_e32 v34, v48, v50
	v_exp_f32_e32 v247, v34
	v_sub_f32_e32 v34, v49, v50
	v_exp_f32_e32 v248, v34
	v_cvt_pk_bf16_f32 v34, v106, v107
	v_cvt_pk_bf16_f32 v35, v108, v109
	v_cvt_pk_bf16_f32 v36, v110, v111
	v_cvt_pk_bf16_f32 v37, v112, v113
	v_cvt_pk_bf16_f32 v238, v165, v171
	v_cvt_pk_bf16_f32 v239, v172, v173
	v_cvt_pk_bf16_f32 v240, v237, v246
	v_cvt_pk_bf16_f32 v241, v247, v248
	ds_read_b64_tr_b16 v[38:39], v181 offset:4608
	ds_read_b64_tr_b16 v[40:41], v181 offset:5888
	ds_read_b64_tr_b16 v[44:45], v181 offset:5952
	ds_read_b64_tr_b16 v[42:43], v181 offset:4672
	s_waitcnt lgkmcnt(2)
	v_mfma_f32_32x32x16_bf16 v[18:33], v[38:41], v[34:37], v[18:33]
	ds_read_b64_tr_b16 v[38:39], v181 offset:7168
	ds_read_b64_tr_b16 v[40:41], v181 offset:8448
	v_add_f32_e32 v46, 0, v106
	s_add_i32 s10, s13, s25
	ds_read_b64_tr_b16 v[244:245], v181 offset:8512
	ds_read_b64_tr_b16 v[242:243], v181 offset:7232
	s_waitcnt vmcnt(15)
	ds_write_b128 v231, v[86:89]
	s_waitcnt vmcnt(14)
; #define LAS __attribute__((address_space(3)))
; template <int STAGE, int OFF> __device__ __forceinline__ void attn32_unit(const bf16* base, bf16* yrow0, int blk0, int u, LAS unsigned char* xtab, LAS unsigned char* kbuf, LAS unsigned char* vbuf, int lane, ...
;     ...
;         for (int c = 0; c < 4; ++c) { *(LAS v4u*)(kbuf + (8 * c + lrow) * 144 + lch * 16) = kr[set][c]; *(LAS v4u*)(vbuf + (8 * c + lrow) * 160 + lch * 16) = vr[set][c]; }
;         if (pp + 2 < 5) { ATT32_LOAD(set, pp + 2, t0, SH); }
;         else { const bf16* base_ = base; { const bf16* base = nbase; ATT32_LOAD(set, pp + 2 - 5, nt0, nsh); } (void)base_; }
;         f32x16 sc;
; #pragma unroll
;         for (int i = 0; i < 16; ++i) sc[i] = 0.f;
; #pragma unroll
;         for (int ks = 0; ks < 4; ++ks) { const bf16x8 ka = *(const LAS bf16x8*)(kbuf + qi * 144 + 32 * ks + 16 * h); sc = MFMA32(ka, qb[ks], sc); }
;         if (pp == 4) {
; #pragma unroll
;             for (int ks = 0; ks < 4; ++ks) qb[ks] = *(const bf16x8*)(nbase + (size_t)min(nt0 + (qi << nsh), SEQ - 1) * 1536 + 16 * ks + 8 * h);
;         }
;         const int mbase = n0 + 4 * h - lo; float mx = -INFINITY;
; #pragma unroll
;         for (int rg = 0; rg < 16; ++rg) { sc[rg] = ((unsigned)(mbase + (rg & 3) + 8 * (rg >> 2)) <= mspan) ? sc[rg] : -INFINITY; mx = fmaxf(mx, sc[rg]); }
;         mx = fmaxf(mx, __shfl_xor(mx, 32));
;         if (__any(mx > m)) {
;             const float mn = fmaxf(m, mx), alpha = __builtin_amdgcn_exp2f(m - mn); m = mn; l *= alpha;
; #pragma unroll
;             for (int i = 0; i < 16; ++i) { o[0][i] *= alpha; o[1][i] *= alpha; }
;         }
;         float ps = 0.f;
; #pragma unroll
;         for (int rg = 0; rg < 16; ++rg) { sc[rg] = __builtin_amdgcn_exp2f(sc[rg] - m); ps += sc[rg]; }
;         l += ps;
;         bf16x8 pb[2];
; #pragma unroll
;         for (int s2 = 0; s2 < 2; ++s2) { v4u w; w.x = pg8::cvt_pk_bf16(sc[8 * s2], sc[8 * s2 + 1]); w.y = pg8::cvt_pk_bf16(sc[8 * s2 + 2], sc[8 * s2 + 3]); w.z = pg8::cvt_pk_bf16(sc[8 * s2 + 4], sc[8 * s2 + 5]); w.w = pg8::cvt_pk_bf16(sc[8 * s2 + 6], sc[8 * s2 + 7]); pb[s2] = __builtin_bit_cast(bf16x8, w); }
; #pragma unroll
;         for (int mb = 0; mb < 2; ++mb)
; #pragma unroll
;             for (int s2 = 0; s2 < 2; ++s2) {
;                 LAS unsigned char* vp = vbuf + tr_off + (16 * s2) * 160 + 64 * mb;
	ds_write_b128 v232, v[90:93] offset:4608
	s_waitcnt vmcnt(13)
	ds_write_b128 v231, v[134:137] offset:1152
	s_waitcnt vmcnt(12)
	ds_write_b128 v232, v[142:145] offset:5888
	s_waitcnt vmcnt(11)
	ds_write_b128 v231, v[146:149] offset:2304
	s_waitcnt vmcnt(10)
	ds_write_b128 v232, v[150:153] offset:7168
	s_waitcnt vmcnt(9)
	ds_write_b128 v231, v[154:157] offset:3456
	s_waitcnt vmcnt(8)
	ds_write_b128 v232, v[158:161] offset:8448
	s_waitcnt lgkmcnt(10)
	v_mfma_f32_32x32x16_bf16 v[18:33], v[38:41], v[238:241], v[18:33]
	v_add_f32_e32 v38, v107, v46
	v_add_f32_e32 v38, v108, v38
	v_add_f32_e32 v38, v109, v38
	v_add_f32_e32 v38, v110, v38
	v_add_f32_e32 v38, v111, v38
	v_add_f32_e32 v38, v112, v38
	v_add_f32_e32 v249, v113, v38
	v_mfma_f32_32x32x16_bf16 v[2:17], v[42:45], v[34:37], v[2:17]
	v_add_u32_e32 v34, s10, v185
	v_med3_i32 v34, v34, 0, v233
	v_mul_u32_u24_e32 v38, 0xc00, v34
	ds_read_b128 v[34:37], v177
	v_or_b32_e32 v38, v38, v176
	global_load_dwordx4 v[106:109], v38, s[8:9] offset:1024
	global_load_dwordx4 v[110:113], v38, s[8:9] offset:2048
	v_add_u32_e32 v38, s10, v186
	v_med3_i32 v38, v38, 0, v233
	v_mul_u32_u24_e32 v38, 0xc00, v38
	ds_read_b128 v[86:89], v177 offset:32
	v_or_b32_e32 v90, v38, v176
	s_waitcnt lgkmcnt(1)
	v_mfma_f32_32x32x16_bf16 v[34:49], v[34:37], v[66:69], 0
	global_load_dwordx4 v[114:117], v90, s[8:9] offset:1024
	global_load_dwordx4 v[118:121], v90, s[8:9] offset:2048
	v_add_u32_e32 v90, s10, v187
	v_med3_i32 v90, v90, 0, v233
	v_mul_u32_u24_e32 v90, 0xc00, v90
	v_or_b32_e32 v126, v90, v176
	ds_read_b128 v[90:93], v177 offset:96
	ds_read_b128 v[142:145], v177 offset:64
	global_load_dwordx4 v[122:125], v126, s[8:9] offset:1024
	s_nop 0
	global_load_dwordx4 v[126:129], v126, s[8:9] offset:2048
	s_waitcnt lgkmcnt(2)
	v_mfma_f32_32x32x16_bf16 v[34:49], v[86:89], v[62:65], v[34:49]
	v_add_u32_e32 v86, s10, v188
	v_med3_i32 v86, v86, 0, v233
	v_mul_u32_u24_e32 v86, 0xc00, v86
	v_or_b32_e32 v86, v86, v176
	global_load_dwordx4 v[130:133], v86, s[8:9] offset:1024
	global_load_dwordx4 v[134:137], v86, s[8:9] offset:2048
	v_add_u32_e32 v87, 0x60, v163
	v_cmp_le_u32_e32 vcc, v87, v162
	s_waitcnt lgkmcnt(0)
	v_mfma_f32_32x32x16_bf16 v[34:49], v[142:145], v[58:61], v[34:49]
	v_add_u32_e32 v87, 0x61, v163
	v_add_u32_e32 v88, 0x62, v163
	v_add_f32_e32 v86, v165, v249
	v_add_f32_e32 v86, v171, v86
	v_add_f32_e32 v86, v172, v86
	v_add_f32_e32 v86, v173, v86
	v_add_f32_e32 v86, v237, v86
	v_mfma_f32_32x32x16_bf16 v[34:49], v[90:93], v[54:57], v[34:49]
	v_add_f32_e32 v86, v246, v86
	v_add_f32_e32 v86, v247, v86
	v_add_f32_e32 v86, v248, v86
	v_add_f32_e32 v142, v164, v86
	v_mfma_f32_32x32x16_bf16 v[2:17], v[242:245], v[238:241], v[2:17]
	s_nop 6
	v_cndmask_b32_e32 v34, v234, v34, vcc
	v_cmp_le_u32_e32 vcc, v87, v162
	s_nop 1
	v_cndmask_b32_e32 v35, v234, v35, vcc
	v_cmp_le_u32_e32 vcc, v88, v162
	v_add_u32_e32 v88, 0x63, v163
	v_max3_f32 v87, v34, s31, v35
	v_cndmask_b32_e32 v36, v234, v36, vcc
	v_cmp_le_u32_e32 vcc, v88, v162
	v_add_u32_e32 v88, 0x68, v163
	s_nop 0
	v_cndmask_b32_e32 v37, v234, v37, vcc
	v_cmp_le_u32_e32 vcc, v88, v162
	v_add_u32_e32 v88, 0x69, v163
	v_max3_f32 v87, v87, v36, v37
	v_cndmask_b32_e32 v38, v234, v38, vcc
	v_cmp_le_u32_e32 vcc, v88, v162
	v_add_u32_e32 v88, 0x6a, v163
	s_nop 0
	v_cndmask_b32_e32 v39, v234, v39, vcc
	v_cmp_le_u32_e32 vcc, v88, v162
	v_add_u32_e32 v88, 0x6b, v163
	v_max3_f32 v87, v87, v38, v39
	v_cndmask_b32_e32 v40, v234, v40, vcc
	v_cmp_le_u32_e32 vcc, v88, v162
	v_add_u32_e32 v88, 0x70, v163
	s_nop 0
	v_cndmask_b32_e32 v41, v234, v41, vcc
	v_cmp_le_u32_e32 vcc, v88, v162
	v_add_u32_e32 v88, 0x71, v163
	v_max3_f32 v87, v87, v40, v41
	v_cndmask_b32_e32 v42, v234, v42, vcc
	v_cmp_le_u32_e32 vcc, v88, v162
	v_add_u32_e32 v88, 0x72, v163
	s_nop 0
	v_cndmask_b32_e32 v43, v234, v43, vcc
	v_cmp_le_u32_e32 vcc, v88, v162
	v_add_u32_e32 v88, 0x73, v163
	v_max3_f32 v87, v87, v42, v43
	v_cndmask_b32_e32 v44, v234, v44, vcc
	v_cmp_le_u32_e32 vcc, v88, v162
	v_add_u32_e32 v88, 0x78, v163
	s_nop 0
	v_cndmask_b32_e32 v45, v234, v45, vcc
	v_cmp_le_u32_e32 vcc, v88, v162
	v_add_u32_e32 v88, 0x79, v163
	v_max3_f32 v87, v87, v44, v45
	v_cndmask_b32_e32 v46, v234, v46, vcc
	v_cmp_le_u32_e32 vcc, v88, v162
	v_add_u32_e32 v88, 0x7a, v163
	s_nop 0
	v_cndmask_b32_e32 v47, v234, v47, vcc
	v_cmp_le_u32_e32 vcc, v88, v162
	v_add_u32_e32 v88, 0x7b, v163
	v_max3_f32 v87, v87, v46, v47
	v_cndmask_b32_e32 v48, v234, v48, vcc
	v_cmp_le_u32_e32 vcc, v88, v162
	s_nop 1
	v_cndmask_b32_e32 v49, v234, v49, vcc
	v_max3_f32 v87, v87, v48, v49
	v_mov_b32_e32 v88, v87
	s_nop 1
	v_permlane32_swap_b32_e32 v88, v87
	s_waitcnt lgkmcnt(0)
	v_max_f32_e32 v86, v88, v88
	v_max_f32_e32 v86, v87, v86
	v_cmp_gt_f32_e32 vcc, v86, v50
	s_cbranch_vccz .LBB0_390
	v_max_f32_e32 v86, v86, v86
	v_max_f32_e32 v87, v50, v50
	v_max_f32_e32 v86, v87, v86
	v_sub_f32_e32 v50, v50, v86
	v_exp_f32_e32 v50, v50
	s_nop 0
	v_pk_mul_f32 v[32:33], v[32:33], v[50:51] op_sel_hi:[1,0]
	v_pk_mul_f32 v[30:31], v[30:31], v[50:51] op_sel_hi:[1,0]
	v_pk_mul_f32 v[28:29], v[28:29], v[50:51] op_sel_hi:[1,0]
	v_pk_mul_f32 v[26:27], v[26:27], v[50:51] op_sel_hi:[1,0]
	v_pk_mul_f32 v[24:25], v[24:25], v[50:51] op_sel_hi:[1,0]
	v_pk_mul_f32 v[22:23], v[22:23], v[50:51] op_sel_hi:[1,0]
	v_pk_mul_f32 v[20:21], v[20:21], v[50:51] op_sel_hi:[1,0]
	v_pk_mul_f32 v[18:19], v[18:19], v[50:51] op_sel_hi:[1,0]
	v_pk_mul_f32 v[16:17], v[16:17], v[50:51] op_sel_hi:[1,0]
	v_pk_mul_f32 v[14:15], v[14:15], v[50:51] op_sel_hi:[1,0]
	v_pk_mul_f32 v[12:13], v[12:13], v[50:51] op_sel_hi:[1,0]
	v_pk_mul_f32 v[10:11], v[10:11], v[50:51] op_sel_hi:[1,0]
	v_pk_mul_f32 v[8:9], v[8:9], v[50:51] op_sel_hi:[1,0]
	v_pk_mul_f32 v[6:7], v[6:7], v[50:51] op_sel_hi:[1,0]
	v_pk_mul_f32 v[4:5], v[4:5], v[50:51] op_sel_hi:[1,0]
	v_pk_mul_f32 v[2:3], v[2:3], v[50:51] op_sel_hi:[1,0]
	v_mul_f32_e32 v142, v142, v50
	v_mov_b32_e32 v50, v86
; #define LAS __attribute__((address_space(3)))
; template <int STAGE, int OFF> __device__ __forceinline__ void attn32_unit(const bf16* base, bf16* yrow0, int blk0, int u, LAS unsigned char* xtab, LAS unsigned char* kbuf, LAS unsigned char* vbuf, int lane, ...
;     ...
;         for (int c = 0; c < 4; ++c) { *(LAS v4u*)(kbuf + (8 * c + lrow) * 144 + lch * 16) = kr[set][c]; *(LAS v4u*)(vbuf + (8 * c + lrow) * 160 + lch * 16) = vr[set][c]; }
;         if (pp + 2 < 5) { ATT32_LOAD(set, pp + 2, t0, SH); }
;         else { const bf16* base_ = base; { const bf16* base = nbase; ATT32_LOAD(set, pp + 2 - 5, nt0, nsh); } (void)base_; }
;         f32x16 sc;
; #pragma unroll
;         for (int i = 0; i < 16; ++i) sc[i] = 0.f;
; #pragma unroll
;         for (int ks = 0; ks < 4; ++ks) { const bf16x8 ka = *(const LAS bf16x8*)(kbuf + qi * 144 + 32 * ks + 16 * h); sc = MFMA32(ka, qb[ks], sc); }
;         if (pp == 4) {
; #pragma unroll
;             for (int ks = 0; ks < 4; ++ks) qb[ks] = *(const bf16x8*)(nbase + (size_t)min(nt0 + (qi << nsh), SEQ - 1) * 1536 + 16 * ks + 8 * h);
;         }
;         const int mbase = n0 + 4 * h - lo; float mx = -INFINITY;
; #pragma unroll
;         for (int rg = 0; rg < 16; ++rg) { sc[rg] = ((unsigned)(mbase + (rg & 3) + 8 * (rg >> 2)) <= mspan) ? sc[rg] : -INFINITY; mx = fmaxf(mx, sc[rg]); }
;         mx = fmaxf(mx, __shfl_xor(mx, 32));
;         if (__any(mx > m)) {
;             const float mn = fmaxf(m, mx), alpha = __builtin_amdgcn_exp2f(m - mn); m = mn; l *= alpha;
; #pragma unroll
;             for (int i = 0; i < 16; ++i) { o[0][i] *= alpha; o[1][i] *= alpha; }
;         }
;         float ps = 0.f;
; #pragma unroll
;         for (int rg = 0; rg < 16; ++rg) { sc[rg] = __builtin_amdgcn_exp2f(sc[rg] - m); ps += sc[rg]; }
;         l += ps;
;         bf16x8 pb[2];
; #pragma unroll
;         for (int s2 = 0; s2 < 2; ++s2) { v4u w; w.x = pg8::cvt_pk_bf16(sc[8 * s2], sc[8 * s2 + 1]); w.y = pg8::cvt_pk_bf16(sc[8 * s2 + 2], sc[8 * s2 + 3]); w.z = pg8::cvt_pk_bf16(sc[8 * s2 + 4], sc[8 * s2 + 5]); w.w = pg8::cvt_pk_bf16(sc[8 * s2 + 6], sc[8 * s2 + 7]); pb[s2] = __builtin_bit_cast(bf16x8, w); }
; #pragma unroll
;         for (int mb = 0; mb < 2; ++mb)
; #pragma unroll
;             for (int s2 = 0; s2 < 2; ++s2) {
;                 LAS unsigned char* vp = vbuf + tr_off + (16 * s2) * 160 + 64 * mb;
.LBB0_390:
	v_sub_f32_e32 v34, v34, v50
	v_exp_f32_e32 v86, v34
	v_sub_f32_e32 v34, v35, v50
	v_exp_f32_e32 v87, v34
	v_sub_f32_e32 v34, v36, v50
	v_exp_f32_e32 v88, v34
	v_sub_f32_e32 v34, v37, v50
	v_exp_f32_e32 v89, v34
	v_sub_f32_e32 v34, v38, v50
	v_exp_f32_e32 v90, v34
	v_sub_f32_e32 v34, v39, v50
	v_exp_f32_e32 v91, v34
	v_sub_f32_e32 v34, v40, v50
	v_exp_f32_e32 v92, v34
	v_sub_f32_e32 v34, v41, v50
	v_exp_f32_e32 v93, v34
	v_sub_f32_e32 v34, v42, v50
	v_exp_f32_e32 v143, v34
	v_sub_f32_e32 v34, v43, v50
	v_exp_f32_e32 v154, v34
	v_sub_f32_e32 v34, v44, v50
	v_exp_f32_e32 v155, v34
	v_sub_f32_e32 v34, v45, v50
	v_exp_f32_e32 v156, v34
	v_sub_f32_e32 v34, v46, v50
	v_exp_f32_e32 v157, v34
	v_sub_f32_e32 v34, v47, v50
	v_exp_f32_e32 v158, v34
	v_sub_f32_e32 v34, v48, v50
	v_exp_f32_e32 v159, v34
	v_sub_f32_e32 v34, v49, v50
	v_exp_f32_e32 v160, v34
	v_cvt_pk_bf16_f32 v34, v86, v87
	v_cvt_pk_bf16_f32 v35, v88, v89
	v_cvt_pk_bf16_f32 v36, v90, v91
	v_cvt_pk_bf16_f32 v37, v92, v93
	v_cvt_pk_bf16_f32 v144, v143, v154
	v_cvt_pk_bf16_f32 v145, v155, v156
	v_cvt_pk_bf16_f32 v146, v157, v158
	v_cvt_pk_bf16_f32 v147, v159, v160
	ds_read_b64_tr_b16 v[38:39], v181 offset:4608
	ds_read_b64_tr_b16 v[40:41], v181 offset:5888
	v_or_b32_e32 v42, s10, v183
	v_min_i32_e32 v148, 0x3fff, v42
	s_waitcnt lgkmcnt(0)
	v_mfma_f32_32x32x16_bf16 v[18:33], v[38:41], v[34:37], v[18:33]
	v_mul_u32_u24_e32 v38, 0xc00, v148
	v_mov_b32_e32 v39, v169
	v_lshl_add_u64 v[38:39], s[8:9], 0, v[38:39]
	ds_read_b64_tr_b16 v[42:43], v181 offset:7168
	ds_read_b64_tr_b16 v[44:45], v181 offset:8448
	ds_read_b64_tr_b16 v[48:49], v181 offset:5952
	ds_read_b64_tr_b16 v[46:47], v181 offset:4672
	v_lshl_add_u64 v[152:153], v[38:39], 0, v[168:169]
	v_add_f32_e32 v38, 0, v86
	v_add_f32_e32 v38, v87, v38
	v_add_f32_e32 v38, v88, v38
	v_add_f32_e32 v38, v89, v38
	v_add_f32_e32 v38, v90, v38
	v_add_f32_e32 v38, v91, v38
	s_waitcnt lgkmcnt(0)
	v_mfma_f32_32x32x16_bf16 v[2:17], v[46:49], v[34:37], v[2:17]
	v_add_u32_e32 v34, s10, v189
	ds_read_b64_tr_b16 v[150:151], v181 offset:8512
	ds_read_b64_tr_b16 v[148:149], v181 offset:7232
	v_add_f32_e32 v38, v92, v38
	s_waitcnt vmcnt(15)
	ds_write_b128 v231, v[70:73]
	s_waitcnt vmcnt(14)
	ds_write_b128 v232, v[74:77] offset:4608
	s_waitcnt vmcnt(13)
	ds_write_b128 v231, v[78:81] offset:1152
	s_waitcnt vmcnt(12)
	ds_write_b128 v232, v[82:85] offset:5888
	s_waitcnt vmcnt(11)
	ds_write_b128 v231, v[94:97] offset:2304
	s_waitcnt vmcnt(10)
	ds_write_b128 v232, v[98:101] offset:7168
	s_waitcnt vmcnt(9)
	ds_write_b128 v231, v[102:105] offset:3456
	s_waitcnt vmcnt(8)
	ds_write_b128 v232, v[138:141] offset:8448
	v_med3_i32 v34, v34, 0, v233
	v_add_f32_e32 v161, v93, v38
	v_mul_u32_u24_e32 v38, 0xc00, v34
	ds_read_b128 v[34:37], v177
	v_or_b32_e32 v38, v38, v176
	global_load_dwordx4 v[74:77], v38, s[8:9] offset:1024
	global_load_dwordx4 v[78:81], v38, s[8:9] offset:2048
	v_add_u32_e32 v38, s10, v190
	v_med3_i32 v38, v38, 0, v233
	v_mul_u32_u24_e32 v38, 0xc00, v38
	ds_read_b128 v[70:73], v177 offset:32
	v_mfma_f32_32x32x16_bf16 v[18:33], v[42:45], v[144:147], v[18:33]
	v_or_b32_e32 v86, v38, v176
	global_load_dwordx4 v[82:85], v86, s[8:9] offset:1024
	s_nop 0
	global_load_dwordx4 v[86:89], v86, s[8:9] offset:2048
	v_add_f32_e32 v143, v143, v161
	v_add_f32_e32 v143, v154, v143
	v_add_f32_e32 v143, v155, v143
	v_add_f32_e32 v143, v156, v143
	v_add_f32_e32 v143, v157, v143
	s_waitcnt lgkmcnt(1)
	v_mfma_f32_32x32x16_bf16 v[34:49], v[34:37], v[66:69], 0
	v_add_u32_e32 v66, s10, v191
	v_med3_i32 v66, v66, 0, v233
	v_mul_u32_u24_e32 v66, 0xc00, v66
	v_or_b32_e32 v94, v66, v176
	ds_read_b128 v[138:141], v177 offset:96
	ds_read_b128 v[66:69], v177 offset:64
	global_load_dwordx4 v[90:93], v94, s[8:9] offset:1024
	s_nop 0
	global_load_dwordx4 v[94:97], v94, s[8:9] offset:2048
	v_add_f32_e32 v143, v158, v143
	s_waitcnt lgkmcnt(2)
	v_mfma_f32_32x32x16_bf16 v[34:49], v[70:73], v[62:65], v[34:49]
	v_add_u32_e32 v62, s10, v192
	v_med3_i32 v62, v62, 0, v233
	v_mul_u32_u24_e32 v62, 0xc00, v62
	v_or_b32_e32 v62, v62, v176
	global_load_dwordx4 v[98:101], v62, s[8:9] offset:1024
	global_load_dwordx4 v[102:105], v62, s[8:9] offset:2048
	v_add_f32_e32 v143, v159, v143
	s_waitcnt lgkmcnt(0)
	v_mfma_f32_32x32x16_bf16 v[34:49], v[66:69], v[58:61], v[34:49]
	global_load_dwordx4 v[70:73], v[152:153], off
	global_load_dwordx4 v[66:69], v[152:153], off offset:32
	global_load_dwordx4 v[62:65], v[152:153], off offset:64
	global_load_dwordx4 v[58:61], v[152:153], off offset:96
	v_mfma_f32_32x32x16_bf16 v[34:49], v[138:141], v[54:57], v[34:49]
	v_add_u32_e32 v54, 0x80, v163
	v_cmp_le_u32_e32 vcc, v54, v162
	v_add_u32_e32 v55, 0x82, v163
	v_mfma_f32_32x32x16_bf16 v[2:17], v[148:151], v[144:147], v[2:17]
	s_nop 7
	v_cndmask_b32_e32 v54, v234, v34, vcc
	v_add_u32_e32 v34, 0x81, v163
	v_cmp_le_u32_e32 vcc, v34, v162
	s_nop 1
	v_cndmask_b32_e32 v35, v234, v35, vcc
	v_cmp_le_u32_e32 vcc, v55, v162
	v_add_u32_e32 v55, 0x83, v163
	v_max3_f32 v34, v54, s31, v35
	v_cndmask_b32_e32 v36, v234, v36, vcc
	v_cmp_le_u32_e32 vcc, v55, v162
	v_add_u32_e32 v55, 0x88, v163
	s_nop 0
	v_cndmask_b32_e32 v37, v234, v37, vcc
	v_cmp_le_u32_e32 vcc, v55, v162
	v_add_u32_e32 v55, 0x89, v163
	v_max3_f32 v34, v34, v36, v37
	v_cndmask_b32_e32 v38, v234, v38, vcc
	v_cmp_le_u32_e32 vcc, v55, v162
	v_add_u32_e32 v55, 0x8a, v163
	s_nop 0
	v_cndmask_b32_e32 v39, v234, v39, vcc
	v_cmp_le_u32_e32 vcc, v55, v162
	v_add_u32_e32 v55, 0x8b, v163
	v_max3_f32 v34, v34, v38, v39
	v_cndmask_b32_e32 v40, v234, v40, vcc
	v_cmp_le_u32_e32 vcc, v55, v162
	v_add_u32_e32 v55, 0x90, v163
	s_nop 0
	v_cndmask_b32_e32 v41, v234, v41, vcc
	v_cmp_le_u32_e32 vcc, v55, v162
	v_add_u32_e32 v55, 0x91, v163
	v_max3_f32 v34, v34, v40, v41
	v_cndmask_b32_e32 v42, v234, v42, vcc
	v_cmp_le_u32_e32 vcc, v55, v162
	v_add_u32_e32 v55, 0x92, v163
	s_nop 0
	v_cndmask_b32_e32 v43, v234, v43, vcc
	v_cmp_le_u32_e32 vcc, v55, v162
	v_add_u32_e32 v55, 0x93, v163
	v_max3_f32 v34, v34, v42, v43
	v_cndmask_b32_e32 v44, v234, v44, vcc
	v_cmp_le_u32_e32 vcc, v55, v162
	v_add_u32_e32 v55, 0x98, v163
	s_nop 0
	v_cndmask_b32_e32 v45, v234, v45, vcc
	v_cmp_le_u32_e32 vcc, v55, v162
	v_add_u32_e32 v55, 0x99, v163
	v_max3_f32 v34, v34, v44, v45
	v_cndmask_b32_e32 v46, v234, v46, vcc
	v_cmp_le_u32_e32 vcc, v55, v162
	v_add_u32_e32 v55, 0x9a, v163
	s_nop 0
	v_cndmask_b32_e32 v47, v234, v47, vcc
	v_cmp_le_u32_e32 vcc, v55, v162
	v_add_u32_e32 v55, 0x9b, v163
	v_max3_f32 v34, v34, v46, v47
	v_cndmask_b32_e32 v48, v234, v48, vcc
	v_cmp_le_u32_e32 vcc, v55, v162
	s_nop 1
	v_cndmask_b32_e32 v49, v234, v49, vcc
	v_max3_f32 v55, v34, v48, v49
	v_mov_b32_e32 v56, v55
	s_nop 1
	v_permlane32_swap_b32_e32 v56, v55
	v_add_f32_e32 v34, v160, v143
	v_add_f32_e32 v34, v142, v34
	s_waitcnt lgkmcnt(0)
	v_max_f32_e32 v56, v56, v56
	v_max_f32_e32 v55, v55, v56
	v_cmp_gt_f32_e32 vcc, v55, v50
	s_cbranch_vccz .LBB0_392
; __device__ __forceinline__ unsigned cvt_pk_bf16(float lo, float hi) { unsigned r; asm volatile("v_cvt_pk_bf16_f32 %0, %1, %2" : "=v"(r) : "v"(lo), "v"(hi)); return r; }
; #define LAS __attribute__((address_space(3)))
; __device__ __forceinline__ unsigned pk2(float lo, float hi) { return f2bf(lo) | (f2bf(hi) << 16); }
; #define MFMA32(a, b, c) __builtin_amdgcn_mfma_f32_32x32x16_bf16((a), (b), (c), 0, 0, 0)
; template <int STAGE, int OFF> __device__ __forceinline__ void attn32_unit(const bf16* base, bf16* yrow0, int blk0, int u, LAS unsigned char* xtab, LAS unsigned char* kbuf, LAS unsigned char* vbuf, int lane, ...
;     ...
;         if (__any(mx > m)) {
;             const float mn = fmaxf(m, mx), alpha = __builtin_amdgcn_exp2f(m - mn); m = mn; l *= alpha;
; #pragma unroll
;             for (int i = 0; i < 16; ++i) { o[0][i] *= alpha; o[1][i] *= alpha; }
;         }
;         float ps = 0.f;
; #pragma unroll
;         for (int rg = 0; rg < 16; ++rg) { sc[rg] = __builtin_amdgcn_exp2f(sc[rg] - m); ps += sc[rg]; }
;         l += ps;
;         bf16x8 pb[2];
; #pragma unroll
;         for (int s2 = 0; s2 < 2; ++s2) { v4u w; w.x = pg8::cvt_pk_bf16(sc[8 * s2], sc[8 * s2 + 1]); w.y = pg8::cvt_pk_bf16(sc[8 * s2 + 2], sc[8 * s2 + 3]); w.z = pg8::cvt_pk_bf16(sc[8 * s2 + 4], sc[8 * s2 + 5]); w.w = pg8::cvt_pk_bf16(sc[8 * s2 + 6], sc[8 * s2 + 7]); pb[s2] = __builtin_bit_cast(bf16x8, w); }
; #pragma unroll
;         for (int mb = 0; mb < 2; ++mb)
; #pragma unroll
;             for (int s2 = 0; s2 < 2; ++s2) {
;                 LAS unsigned char* vp = vbuf + tr_off + (16 * s2) * 160 + 64 * mb;
;                 const v4i16 a0 = __builtin_amdgcn_ds_read_tr16_b64_v4i16((LAS v4i16*)vp), a1 = __builtin_amdgcn_ds_read_tr16_b64_v4i16((LAS v4i16*)(vp + 8 * 160));
;                 const bf16x8 va = __builtin_shufflevector(a0, a1, 0, 1, 2, 3, 4, 5, 6, 7);
;                 o[mb] = MFMA32(va, pb[s2], o[mb]);
;             }
;         asm volatile("" ::: "memory");
;     }
;     l += __shfl_xor(l, 32);
;     if (STAGE < 2) {
; #pragma unroll
;         for (int mb = 0; mb < 2; ++mb)
; #pragma unroll
;             for (int gq = 0; gq < 4; ++gq) { v2u w; w.x = pk2(o[mb][4 * gq], o[mb][4 * gq + 1]); w.y = pk2(o[mb][4 * gq + 2], o[mb][4 * gq + 3]); *(LAS v2u*)(xrow + 2 * (32 * mb + 8 * gq + 4 * h)) = w; }
;         if (h == 0) { *(LAS float*)(xrow + 128) = m; *(LAS float*)(xrow + 132) = l; }
	v_max_f32_e32 v55, v55, v55
	v_max_f32_e32 v56, v50, v50
	v_max_f32_e32 v55, v56, v55
	v_sub_f32_e32 v50, v50, v55
	v_exp_f32_e32 v50, v50
	s_nop 0
	v_pk_mul_f32 v[32:33], v[32:33], v[50:51] op_sel_hi:[1,0]
	v_pk_mul_f32 v[30:31], v[30:31], v[50:51] op_sel_hi:[1,0]
	v_pk_mul_f32 v[28:29], v[28:29], v[50:51] op_sel_hi:[1,0]
	v_pk_mul_f32 v[26:27], v[26:27], v[50:51] op_sel_hi:[1,0]
	v_pk_mul_f32 v[24:25], v[24:25], v[50:51] op_sel_hi:[1,0]
	v_pk_mul_f32 v[22:23], v[22:23], v[50:51] op_sel_hi:[1,0]
	v_pk_mul_f32 v[20:21], v[20:21], v[50:51] op_sel_hi:[1,0]
	v_pk_mul_f32 v[18:19], v[18:19], v[50:51] op_sel_hi:[1,0]
	v_pk_mul_f32 v[16:17], v[16:17], v[50:51] op_sel_hi:[1,0]
	v_pk_mul_f32 v[14:15], v[14:15], v[50:51] op_sel_hi:[1,0]
	v_pk_mul_f32 v[12:13], v[12:13], v[50:51] op_sel_hi:[1,0]
	v_pk_mul_f32 v[10:11], v[10:11], v[50:51] op_sel_hi:[1,0]
	v_pk_mul_f32 v[8:9], v[8:9], v[50:51] op_sel_hi:[1,0]
	v_pk_mul_f32 v[6:7], v[6:7], v[50:51] op_sel_hi:[1,0]
	v_pk_mul_f32 v[4:5], v[4:5], v[50:51] op_sel_hi:[1,0]
	v_pk_mul_f32 v[2:3], v[2:3], v[50:51] op_sel_hi:[1,0]
	v_mul_f32_e32 v34, v34, v50
	v_mov_b32_e32 v50, v55
.LBB0_392:
	v_sub_f32_e32 v36, v36, v50
	v_exp_f32_e32 v142, v36
	v_sub_f32_e32 v36, v37, v50
	v_exp_f32_e32 v143, v36
	v_sub_f32_e32 v36, v38, v50
	v_exp_f32_e32 v144, v36
	v_sub_f32_e32 v36, v39, v50
	v_exp_f32_e32 v145, v36
	v_sub_f32_e32 v36, v40, v50
	v_exp_f32_e32 v146, v36
	v_sub_f32_e32 v36, v41, v50
	v_exp_f32_e32 v147, v36
	v_sub_f32_e32 v36, v42, v50
	v_exp_f32_e32 v148, v36
	v_sub_f32_e32 v36, v43, v50
	v_exp_f32_e32 v149, v36
	v_sub_f32_e32 v36, v44, v50
	v_exp_f32_e32 v150, v36
	v_sub_f32_e32 v36, v45, v50
	v_exp_f32_e32 v151, v36
	v_sub_f32_e32 v36, v46, v50
	v_exp_f32_e32 v152, v36
	v_sub_f32_e32 v36, v47, v50
	v_exp_f32_e32 v153, v36
	v_sub_f32_e32 v36, v48, v50
	v_sub_f32_e32 v54, v54, v50
	v_sub_f32_e32 v35, v35, v50
	v_exp_f32_e32 v48, v36
	v_sub_f32_e32 v36, v49, v50
	v_exp_f32_e32 v138, v54
	v_exp_f32_e32 v35, v35
	v_exp_f32_e32 v49, v36
	v_cvt_pk_bf16_f32 v36, v138, v35
	v_cvt_pk_bf16_f32 v37, v142, v143
	v_cvt_pk_bf16_f32 v38, v144, v145
	v_cvt_pk_bf16_f32 v39, v146, v147
	v_cvt_pk_bf16_f32 v40, v148, v149
	v_cvt_pk_bf16_f32 v41, v150, v151
	v_cvt_pk_bf16_f32 v42, v152, v153
	v_cvt_pk_bf16_f32 v43, v48, v49
	ds_read_b64_tr_b16 v[44:45], v181 offset:4608
	ds_read_b64_tr_b16 v[46:47], v181 offset:5888
	ds_read_b64_tr_b16 v[56:57], v181 offset:5952
	ds_read_b64_tr_b16 v[54:55], v181 offset:4672
	s_waitcnt lgkmcnt(2)
	v_mfma_f32_32x32x16_bf16 v[18:33], v[44:47], v[36:39], v[18:33]
	ds_read_b64_tr_b16 v[44:45], v181 offset:7168
	ds_read_b64_tr_b16 v[46:47], v181 offset:8448
	v_add_f32_e32 v138, 0, v138
	v_add_f32_e32 v35, v35, v138
	ds_read_b64_tr_b16 v[140:141], v181 offset:8512
	ds_read_b64_tr_b16 v[138:139], v181 offset:7232
	v_add_f32_e32 v35, v142, v35
	v_add_f32_e32 v35, v143, v35
	s_waitcnt lgkmcnt(2)
	v_mfma_f32_32x32x16_bf16 v[18:33], v[44:47], v[40:43], v[18:33]
	v_add_f32_e32 v35, v144, v35
	v_add_f32_e32 v35, v145, v35
	v_add_f32_e32 v35, v146, v35
	v_add_f32_e32 v35, v147, v35
	v_add_f32_e32 v35, v148, v35
	v_add_f32_e32 v35, v149, v35
	v_add_f32_e32 v35, v150, v35
	v_mfma_f32_32x32x16_bf16 v[2:17], v[54:57], v[36:39], v[2:17]
	s_nop 3
	v_bfe_u32 v36, v18, 16, 1
	v_add3_u32 v18, v18, v36, s35
	v_bfe_u32 v36, v19, 16, 1
	v_lshrrev_b32_e32 v18, 16, v18
	v_add3_u32 v19, v19, v36, s35
	v_and_or_b32 v18, v19, s36, v18
	v_bfe_u32 v19, v20, 16, 1
	v_add3_u32 v19, v20, v19, s35
	v_bfe_u32 v20, v21, 16, 1
	v_lshrrev_b32_e32 v19, 16, v19
	v_add3_u32 v20, v21, v20, s35
	v_and_or_b32 v19, v20, s36, v19
	v_bfe_u32 v20, v22, 16, 1
	v_add3_u32 v20, v22, v20, s35
	v_bfe_u32 v21, v23, 16, 1
	v_lshrrev_b32_e32 v20, 16, v20
	v_add3_u32 v21, v23, v21, s35
	v_and_or_b32 v20, v21, s36, v20
	v_bfe_u32 v21, v24, 16, 1
	v_add3_u32 v21, v24, v21, s35
	v_bfe_u32 v22, v25, 16, 1
	v_lshrrev_b32_e32 v21, 16, v21
	v_add3_u32 v22, v25, v22, s35
	v_and_or_b32 v21, v22, s36, v21
	ds_write2_b64 v51, v[18:19], v[20:21] offset1:2
	v_bfe_u32 v18, v26, 16, 1
	v_add3_u32 v18, v26, v18, s35
	v_bfe_u32 v19, v27, 16, 1
	v_lshrrev_b32_e32 v18, 16, v18
	v_add3_u32 v19, v27, v19, s35
	v_and_or_b32 v18, v19, s36, v18
	v_bfe_u32 v19, v28, 16, 1
	v_add3_u32 v19, v28, v19, s35
	v_bfe_u32 v20, v29, 16, 1
	s_waitcnt lgkmcnt(1)
	v_mfma_f32_32x32x16_bf16 v[2:17], v[138:141], v[40:43], v[2:17]
	v_lshrrev_b32_e32 v19, 16, v19
	v_add3_u32 v20, v29, v20, s35
	v_and_or_b32 v19, v20, s36, v19
	v_bfe_u32 v20, v30, 16, 1
	v_add3_u32 v20, v30, v20, s35
	v_bfe_u32 v21, v31, 16, 1
	v_lshrrev_b32_e32 v20, 16, v20
	v_add3_u32 v21, v31, v21, s35
	v_and_or_b32 v20, v21, s36, v20
	v_bfe_u32 v21, v32, 16, 1
	v_add3_u32 v21, v32, v21, s35
	v_bfe_u32 v22, v33, 16, 1
	v_lshrrev_b32_e32 v21, 16, v21
	v_add3_u32 v22, v33, v22, s35
	v_and_or_b32 v21, v22, s36, v21
	ds_write2_b64 v51, v[18:19], v[20:21] offset0:4 offset1:6
	v_bfe_u32 v18, v2, 16, 1
	v_add3_u32 v2, v2, v18, s35
	v_bfe_u32 v18, v3, 16, 1
	v_lshrrev_b32_e32 v2, 16, v2
	v_add3_u32 v3, v3, v18, s35
	v_and_or_b32 v2, v3, s36, v2
	v_bfe_u32 v3, v4, 16, 1
	v_add3_u32 v3, v4, v3, s35
	v_bfe_u32 v4, v5, 16, 1
	v_lshrrev_b32_e32 v3, 16, v3
	v_add3_u32 v4, v5, v4, s35
	v_and_or_b32 v3, v4, s36, v3
	v_bfe_u32 v4, v6, 16, 1
	v_add3_u32 v4, v6, v4, s35
	v_bfe_u32 v5, v7, 16, 1
	v_lshrrev_b32_e32 v4, 16, v4
	v_add3_u32 v5, v7, v5, s35
	v_and_or_b32 v4, v5, s36, v4
	v_bfe_u32 v5, v8, 16, 1
	v_add3_u32 v5, v8, v5, s35
	v_bfe_u32 v6, v9, 16, 1
	v_lshrrev_b32_e32 v5, 16, v5
	v_add3_u32 v6, v9, v6, s35
	v_and_or_b32 v5, v6, s36, v5
	ds_write2_b64 v51, v[2:3], v[4:5] offset0:8 offset1:10
	v_bfe_u32 v2, v10, 16, 1
	v_add3_u32 v2, v10, v2, s35
	v_bfe_u32 v3, v11, 16, 1
	v_add_f32_e32 v35, v151, v35
	v_lshrrev_b32_e32 v2, 16, v2
	v_add3_u32 v3, v11, v3, s35
	v_add_f32_e32 v35, v152, v35
	v_and_or_b32 v2, v3, s36, v2
	v_bfe_u32 v3, v12, 16, 1
	v_add_f32_e32 v35, v153, v35
	v_add3_u32 v3, v12, v3, s35
	v_bfe_u32 v4, v13, 16, 1
	v_add_f32_e32 v35, v48, v35
	v_lshrrev_b32_e32 v3, 16, v3
	v_add3_u32 v4, v13, v4, s35
	v_add_f32_e32 v35, v49, v35
	v_and_or_b32 v3, v4, s36, v3
	v_bfe_u32 v4, v14, 16, 1
	v_add_f32_e32 v34, v34, v35
	v_add3_u32 v4, v14, v4, s35
	v_bfe_u32 v5, v15, 16, 1
	v_mov_b32_e32 v35, v34
	s_nop 1
	v_permlane32_swap_b32_e32 v35, v34
	v_lshrrev_b32_e32 v4, 16, v4
	v_add3_u32 v5, v15, v5, s35
	v_and_or_b32 v4, v5, s36, v4
	v_bfe_u32 v5, v16, 16, 1
	v_add3_u32 v5, v16, v5, s35
	v_bfe_u32 v6, v17, 16, 1
	v_lshrrev_b32_e32 v5, 16, v5
	v_add3_u32 v6, v17, v6, s35
	v_and_or_b32 v5, v6, s36, v5
	ds_write2_b64 v51, v[2:3], v[4:5] offset0:12 offset1:14
	s_and_saveexec_b64 s[14:15], s[4:5]
	s_cbranch_execz .LBB0_394
	s_waitcnt lgkmcnt(1)
	v_add_f32_e32 v51, v34, v35
	ds_write_b64 v194, v[50:51] offset:128
; __device__ __forceinline__ float bf_lo(unsigned w) { return __uint_as_float(w << 16); }
; template <int STAGE, int OFF> __device__ __forceinline__ void attn32_unit(const bf16* base, bf16* yrow0, int blk0, int u, LAS unsigned char* xtab, LAS unsigned char* kbuf, LAS unsigned char* vbuf, int lane, ...
;     ...
;     } else {
; #pragma unroll
;         for (int mb = 0; mb < 2; ++mb)
; #pragma unroll
;             for (int gq = 0; gq < 4; ++gq) { const v2u w = *(const LAS v2u*)(xrow + 2 * (32 * mb + 8 * gq + 4 * h)); o[mb][4 * gq] = bf_lo(w.x); o[mb][4 * gq + 1] = bf_hi(w.x); o[mb][4 * gq + 2] = bf_lo(w.y); o[mb][4 * gq + 3] = bf_hi(w.y); }
;         m = *(const LAS float*)(xrow + 128); l = h == 0 ? *(const LAS float*)(xrow + 132) : 0.f;
;     }
;     const int hi = qi, lo = max(qi - 128, -(t0 >> SH));
;     const unsigned mspan = (unsigned)(hi - lo);
; #pragma unroll
;     for (int pp = 0; pp < 5; ++pp) {
;         constexpr int dummy = 0; (void)dummy;
;         const int set = (pp + OFF) % 2, n0 = -128 + 32 * pp;
; #pragma unroll
;         for (int c = 0; c < 4; ++c) { *(LAS v4u*)(kbuf + (8 * c + lrow) * 144 + lch * 16) = kr[set][c]; *(LAS v4u*)(vbuf + (8 * c + lrow) * 160 + lch * 16) = vr[set][c]; }
;         if (pp + 2 < 5) { ATT32_LOAD(set, pp + 2, t0, SH); }
;         else { const bf16* base_ = base; { const bf16* base = nbase; ATT32_LOAD(set, pp + 2 - 5, nt0, nsh); } (void)base_; }
;         f32x16 sc;
; #pragma unroll
;         for (int i = 0; i < 16; ++i) sc[i] = 0.f;
; #pragma unroll
;         for (int ks = 0; ks < 4; ++ks) { const bf16x8 ka = *(const LAS bf16x8*)(kbuf + qi * 144 + 32 * ks + 16 * h); sc = MFMA32(ka, qb[ks], sc); }
;         if (pp == 4) {
; #pragma unroll
;             for (int ks = 0; ks < 4; ++ks) qb[ks] = *(const bf16x8*)(nbase + (size_t)min(nt0 + (qi << nsh), SEQ - 1) * 1536 + 16 * ks + 8 * h);
;         }
;         const int mbase = n0 + 4 * h - lo; float mx = -INFINITY;
; #pragma unroll
;         for (int rg = 0; rg < 16; ++rg) { sc[rg] = ((unsigned)(mbase + (rg & 3) + 8 * (rg >> 2)) <= mspan) ? sc[rg] : -INFINITY; mx = fmaxf(mx, sc[rg]); }
;         mx = fmaxf(mx, __shfl_xor(mx, 32));
;         if (__any(mx > m)) {
;             const float mn = fmaxf(m, mx), alpha = __builtin_amdgcn_exp2f(m - mn); m = mn; l *= alpha;
; #pragma unroll
;             for (int i = 0; i < 16; ++i) { o[0][i] *= alpha; o[1][i] *= alpha; }
;         }
.LBB0_394:
	s_or_b64 exec, exec, s[14:15]
	v_add_u32_e32 v51, v206, v166
	ds_read2_b64 v[10:13], v51 offset1:2
	ds_read2_b64 v[2:5], v51 offset0:4 offset1:6
	ds_read2_b64 v[6:9], v51 offset0:8 offset1:10
	ds_read2_b64 v[14:17], v51 offset0:12 offset1:14
	ds_read_b32 v50, v206 offset:128
	v_mov_b32_e32 v138, 0
	s_and_saveexec_b64 s[14:15], s[4:5]
	ds_read_b32 v138, v206 offset:132
	s_or_b64 exec, exec, s[14:15]
	s_waitcnt vmcnt(19)
	ds_write_b128 v231, v[106:109]
	s_waitcnt vmcnt(18)
	ds_write_b128 v232, v[110:113] offset:4608
	s_waitcnt vmcnt(17)
	ds_write_b128 v231, v[114:117] offset:1152
	s_waitcnt vmcnt(16)
	ds_write_b128 v232, v[118:121] offset:5888
	s_waitcnt vmcnt(15)
	ds_write_b128 v231, v[122:125] offset:2304
	s_waitcnt vmcnt(14)
	ds_write_b128 v232, v[126:129] offset:7168
	s_waitcnt vmcnt(13)
	ds_write_b128 v231, v[130:133] offset:3456
	s_waitcnt vmcnt(12)
	ds_write_b128 v232, v[134:137] offset:8448
	s_waitcnt lgkmcnt(14)
	ds_read_b128 v[34:37], v177
	s_waitcnt lgkmcnt(13)
	v_lshlrev_b32_e32 v22, 16, v12
	v_and_b32_e32 v23, 0xffff0000, v12
	v_add_u32_e32 v12, s10, v195
	v_med3_i32 v12, v12, 0, v233
	v_mul_u32_u24_e32 v12, 0xc00, v12
	v_or_b32_e32 v12, v12, v176
	global_load_dwordx4 v[54:57], v12, s[8:9] offset:1024
	global_load_dwordx4 v[106:109], v12, s[8:9] offset:2048
	ds_read_b128 v[118:121], v177 offset:32
	v_add_u32_e32 v12, s10, v196
	s_waitcnt vmcnt(5) lgkmcnt(1)
	v_mfma_f32_32x32x16_bf16 v[34:49], v[34:37], v[70:73], 0
	v_med3_i32 v12, v12, 0, v233
	v_mul_u32_u24_e32 v12, 0xc00, v12
	v_or_b32_e32 v12, v12, v176
	global_load_dwordx4 v[110:113], v12, s[8:9] offset:1024
	global_load_dwordx4 v[114:117], v12, s[8:9] offset:2048
	v_add_u32_e32 v12, s10, v197
	v_med3_i32 v12, v12, 0, v233
	v_mul_u32_u24_e32 v12, 0xc00, v12
	v_or_b32_e32 v12, v12, v176
	ds_read_b128 v[134:137], v177 offset:96
	ds_read_b128 v[140:143], v177 offset:64
	s_waitcnt vmcnt(6) lgkmcnt(2)
	v_mfma_f32_32x32x16_bf16 v[34:49], v[118:121], v[66:69], v[34:49]
	global_load_dwordx4 v[118:121], v12, s[8:9] offset:1024
	global_load_dwordx4 v[122:125], v12, s[8:9] offset:2048
	v_add_u32_e32 v12, s10, v198
	v_med3_i32 v12, v12, 0, v233
	v_mul_u32_u24_e32 v12, 0xc00, v12
	v_or_b32_e32 v12, v12, v176
	global_load_dwordx4 v[126:129], v12, s[8:9] offset:1024
	global_load_dwordx4 v[130:133], v12, s[8:9] offset:2048
	s_lshr_b32 s0, s10, 2
	s_waitcnt vmcnt(9) lgkmcnt(0)
	v_mfma_f32_32x32x16_bf16 v[34:49], v[140:143], v[62:65], v[34:49]
	s_sub_i32 s0, 0, s0
	v_lshlrev_b32_e32 v18, 16, v10
	v_and_b32_e32 v19, 0xffff0000, v10
	v_lshlrev_b32_e32 v20, 16, v11
	v_and_b32_e32 v21, 0xffff0000, v11
	v_lshlrev_b32_e32 v10, 16, v14
	v_and_b32_e32 v11, 0xffff0000, v14
	s_waitcnt vmcnt(8)
	v_mfma_f32_32x32x16_bf16 v[34:49], v[134:137], v[58:61], v[34:49]
	v_max_i32_e32 v14, s0, v175
	v_sub_u32_e32 v163, v1, v14
	v_sub_u32_e32 v164, v178, v14
	v_cmp_le_u32_e32 vcc, v164, v163
	v_add_u32_e32 v14, 1, v164
	v_lshlrev_b32_e32 v24, 16, v13
	v_and_b32_e32 v25, 0xffff0000, v13
	v_lshlrev_b32_e32 v12, 16, v15
	v_and_b32_e32 v13, 0xffff0000, v15
	s_nop 2
	v_cndmask_b32_e32 v34, v234, v34, vcc
	v_cmp_le_u32_e32 vcc, v14, v163
	v_add_u32_e32 v15, 2, v164
	v_lshlrev_b32_e32 v26, 16, v2
	v_cndmask_b32_e32 v35, v234, v35, vcc
	v_cmp_le_u32_e32 vcc, v15, v163
	v_add_u32_e32 v15, 3, v164
	v_max3_f32 v14, v34, s31, v35
	v_cndmask_b32_e32 v36, v234, v36, vcc
	v_cmp_le_u32_e32 vcc, v15, v163
	v_add_u32_e32 v15, 8, v164
	v_and_b32_e32 v27, 0xffff0000, v2
	v_cndmask_b32_e32 v37, v234, v37, vcc
	v_cmp_le_u32_e32 vcc, v15, v163
	v_add_u32_e32 v15, 9, v164
	v_max3_f32 v14, v14, v36, v37
	v_cndmask_b32_e32 v38, v234, v38, vcc
	v_cmp_le_u32_e32 vcc, v15, v163
	v_add_u32_e32 v15, 10, v164
	v_lshlrev_b32_e32 v28, 16, v3
	v_cndmask_b32_e32 v39, v234, v39, vcc
	v_cmp_le_u32_e32 vcc, v15, v163
	v_add_u32_e32 v15, 11, v164
	v_max3_f32 v14, v14, v38, v39
	v_cndmask_b32_e32 v40, v234, v40, vcc
	v_cmp_le_u32_e32 vcc, v15, v163
	v_add_u32_e32 v15, 16, v164
	v_and_b32_e32 v29, 0xffff0000, v3
	v_cndmask_b32_e32 v41, v234, v41, vcc
	v_cmp_le_u32_e32 vcc, v15, v163
	v_add_u32_e32 v15, 17, v164
	v_max3_f32 v14, v14, v40, v41
	v_cndmask_b32_e32 v42, v234, v42, vcc
	v_cmp_le_u32_e32 vcc, v15, v163
	v_add_u32_e32 v15, 18, v164
	v_lshlrev_b32_e32 v30, 16, v4
	v_cndmask_b32_e32 v43, v234, v43, vcc
	v_cmp_le_u32_e32 vcc, v15, v163
	v_add_u32_e32 v15, 19, v164
	v_max3_f32 v14, v14, v42, v43
	v_cndmask_b32_e32 v44, v234, v44, vcc
	v_cmp_le_u32_e32 vcc, v15, v163
	v_add_u32_e32 v15, 24, v164
	v_and_b32_e32 v31, 0xffff0000, v4
	v_cndmask_b32_e32 v45, v234, v45, vcc
	v_cmp_le_u32_e32 vcc, v15, v163
	v_add_u32_e32 v15, 25, v164
	v_max3_f32 v14, v14, v44, v45
	v_cndmask_b32_e32 v46, v234, v46, vcc
	v_cmp_le_u32_e32 vcc, v15, v163
	v_add_u32_e32 v15, 26, v164
	v_lshlrev_b32_e32 v32, 16, v5
	v_cndmask_b32_e32 v47, v234, v47, vcc
	v_cmp_le_u32_e32 vcc, v15, v163
	v_add_u32_e32 v15, 27, v164
	v_max3_f32 v14, v14, v46, v47
	v_cndmask_b32_e32 v48, v234, v48, vcc
	v_cmp_le_u32_e32 vcc, v15, v163
	v_and_b32_e32 v33, 0xffff0000, v5
	v_lshlrev_b32_e32 v2, 16, v6
	v_cndmask_b32_e32 v49, v234, v49, vcc
	v_max3_f32 v134, v14, v48, v49
	v_mov_b32_e32 v135, v134
	s_nop 1
	v_permlane32_swap_b32_e32 v135, v134
	v_and_b32_e32 v3, 0xffff0000, v6
	v_lshlrev_b32_e32 v4, 16, v7
	v_and_b32_e32 v5, 0xffff0000, v7
	v_lshlrev_b32_e32 v6, 16, v8
	s_waitcnt lgkmcnt(0)
	v_max_f32_e32 v135, v135, v135
	v_max_f32_e32 v134, v134, v135
	v_and_b32_e32 v7, 0xffff0000, v8
	v_lshlrev_b32_e32 v8, 16, v9
	v_and_b32_e32 v9, 0xffff0000, v9
	v_lshlrev_b32_e32 v14, 16, v16
	v_and_b32_e32 v15, 0xffff0000, v16
	v_lshlrev_b32_e32 v16, 16, v17
	v_and_b32_e32 v17, 0xffff0000, v17
	v_cmp_gt_f32_e32 vcc, v134, v50
	s_cbranch_vccz .LBB0_398
	v_max_f32_e32 v134, v134, v134
	v_max_f32_e32 v135, v50, v50
	v_max_f32_e32 v134, v135, v134
	v_sub_f32_e32 v50, v50, v134
	v_exp_f32_e32 v50, v50
	s_nop 0
	v_pk_mul_f32 v[16:17], v[50:51], v[16:17] op_sel_hi:[0,1]
	v_pk_mul_f32 v[14:15], v[50:51], v[14:15] op_sel_hi:[0,1]
	v_pk_mul_f32 v[12:13], v[50:51], v[12:13] op_sel_hi:[0,1]
	v_pk_mul_f32 v[10:11], v[50:51], v[10:11] op_sel_hi:[0,1]
	v_pk_mul_f32 v[8:9], v[50:51], v[8:9] op_sel_hi:[0,1]
	v_pk_mul_f32 v[6:7], v[50:51], v[6:7] op_sel_hi:[0,1]
	v_pk_mul_f32 v[4:5], v[50:51], v[4:5] op_sel_hi:[0,1]
	v_pk_mul_f32 v[2:3], v[50:51], v[2:3] op_sel_hi:[0,1]
	v_pk_mul_f32 v[32:33], v[50:51], v[32:33] op_sel_hi:[0,1]
	v_pk_mul_f32 v[30:31], v[50:51], v[30:31] op_sel_hi:[0,1]
	v_pk_mul_f32 v[28:29], v[50:51], v[28:29] op_sel_hi:[0,1]
	v_pk_mul_f32 v[26:27], v[50:51], v[26:27] op_sel_hi:[0,1]
	v_pk_mul_f32 v[24:25], v[50:51], v[24:25] op_sel_hi:[0,1]
	v_pk_mul_f32 v[22:23], v[50:51], v[22:23] op_sel_hi:[0,1]
	v_pk_mul_f32 v[20:21], v[50:51], v[20:21] op_sel_hi:[0,1]
	v_pk_mul_f32 v[18:19], v[50:51], v[18:19] op_sel_hi:[0,1]
	v_mul_f32_e32 v138, v138, v50
	v_mov_b32_e32 v50, v134
; #define LAS __attribute__((address_space(3)))
; template <int STAGE, int OFF> __device__ __forceinline__ void attn32_unit(const bf16* base, bf16* yrow0, int blk0, int u, LAS unsigned char* xtab, LAS unsigned char* kbuf, LAS unsigned char* vbuf, int lane, ...
;     ...
;         for (int c = 0; c < 4; ++c) { *(LAS v4u*)(kbuf + (8 * c + lrow) * 144 + lch * 16) = kr[set][c]; *(LAS v4u*)(vbuf + (8 * c + lrow) * 160 + lch * 16) = vr[set][c]; }
;         if (pp + 2 < 5) { ATT32_LOAD(set, pp + 2, t0, SH); }
;         else { const bf16* base_ = base; { const bf16* base = nbase; ATT32_LOAD(set, pp + 2 - 5, nt0, nsh); } (void)base_; }
;         f32x16 sc;
; #pragma unroll
;         for (int i = 0; i < 16; ++i) sc[i] = 0.f;
; #pragma unroll
;         for (int ks = 0; ks < 4; ++ks) { const bf16x8 ka = *(const LAS bf16x8*)(kbuf + qi * 144 + 32 * ks + 16 * h); sc = MFMA32(ka, qb[ks], sc); }
;         if (pp == 4) {
; #pragma unroll
;             for (int ks = 0; ks < 4; ++ks) qb[ks] = *(const bf16x8*)(nbase + (size_t)min(nt0 + (qi << nsh), SEQ - 1) * 1536 + 16 * ks + 8 * h);
;         }
;         const int mbase = n0 + 4 * h - lo; float mx = -INFINITY;
; #pragma unroll
;         for (int rg = 0; rg < 16; ++rg) { sc[rg] = ((unsigned)(mbase + (rg & 3) + 8 * (rg >> 2)) <= mspan) ? sc[rg] : -INFINITY; mx = fmaxf(mx, sc[rg]); }
;         mx = fmaxf(mx, __shfl_xor(mx, 32));
;         if (__any(mx > m)) {
;             const float mn = fmaxf(m, mx), alpha = __builtin_amdgcn_exp2f(m - mn); m = mn; l *= alpha;
; #pragma unroll
;             for (int i = 0; i < 16; ++i) { o[0][i] *= alpha; o[1][i] *= alpha; }
;         }
;         float ps = 0.f;
; #pragma unroll
;         for (int rg = 0; rg < 16; ++rg) { sc[rg] = __builtin_amdgcn_exp2f(sc[rg] - m); ps += sc[rg]; }
;         l += ps;
;         bf16x8 pb[2];
; #pragma unroll
;         for (int s2 = 0; s2 < 2; ++s2) { v4u w; w.x = pg8::cvt_pk_bf16(sc[8 * s2], sc[8 * s2 + 1]); w.y = pg8::cvt_pk_bf16(sc[8 * s2 + 2], sc[8 * s2 + 3]); w.z = pg8::cvt_pk_bf16(sc[8 * s2 + 4], sc[8 * s2 + 5]); w.w = pg8::cvt_pk_bf16(sc[8 * s2 + 6], sc[8 * s2 + 7]); pb[s2] = __builtin_bit_cast(bf16x8, w); }
; #pragma unroll
;         for (int mb = 0; mb < 2; ++mb)
; #pragma unroll
;             for (int s2 = 0; s2 < 2; ++s2) {
;                 LAS unsigned char* vp = vbuf + tr_off + (16 * s2) * 160 + 64 * mb;
.LBB0_398:
	v_sub_f32_e32 v34, v34, v50
	v_exp_f32_e32 v134, v34
	v_sub_f32_e32 v34, v35, v50
	v_exp_f32_e32 v135, v34
	v_sub_f32_e32 v34, v36, v50
	v_exp_f32_e32 v136, v34
	v_sub_f32_e32 v34, v37, v50
	v_exp_f32_e32 v137, v34
	v_sub_f32_e32 v34, v38, v50
	v_exp_f32_e32 v139, v34
	v_sub_f32_e32 v34, v39, v50
	v_exp_f32_e32 v140, v34
	v_sub_f32_e32 v34, v40, v50
	v_exp_f32_e32 v141, v34
	v_sub_f32_e32 v34, v41, v50
	v_exp_f32_e32 v142, v34
	v_sub_f32_e32 v34, v42, v50
	v_exp_f32_e32 v162, v34
	v_sub_f32_e32 v34, v43, v50
	v_exp_f32_e32 v165, v34
	v_sub_f32_e32 v34, v44, v50
	v_exp_f32_e32 v171, v34
	v_sub_f32_e32 v34, v45, v50
	v_exp_f32_e32 v172, v34
	v_sub_f32_e32 v34, v46, v50
	v_exp_f32_e32 v173, v34
	v_sub_f32_e32 v34, v47, v50
	v_exp_f32_e32 v237, v34
	v_sub_f32_e32 v34, v48, v50
	v_exp_f32_e32 v246, v34
	v_sub_f32_e32 v34, v49, v50
	v_exp_f32_e32 v247, v34
	v_cvt_pk_bf16_f32 v34, v134, v135
	v_cvt_pk_bf16_f32 v35, v136, v137
	v_cvt_pk_bf16_f32 v36, v139, v140
	v_cvt_pk_bf16_f32 v37, v141, v142
	v_cvt_pk_bf16_f32 v238, v162, v165
	v_cvt_pk_bf16_f32 v239, v171, v172
	v_cvt_pk_bf16_f32 v240, v173, v237
	v_cvt_pk_bf16_f32 v241, v246, v247
	ds_read_b64_tr_b16 v[38:39], v181 offset:4608
	ds_read_b64_tr_b16 v[40:41], v181 offset:5888
	ds_read_b64_tr_b16 v[44:45], v181 offset:5952
	ds_read_b64_tr_b16 v[42:43], v181 offset:4672
	s_waitcnt lgkmcnt(2)
	v_mfma_f32_32x32x16_bf16 v[18:33], v[38:41], v[34:37], v[18:33]
	ds_read_b64_tr_b16 v[38:39], v181 offset:7168
	ds_read_b64_tr_b16 v[40:41], v181 offset:8448
	v_add_f32_e32 v46, 0, v134
	ds_read_b64_tr_b16 v[244:245], v181 offset:8512
	ds_read_b64_tr_b16 v[242:243], v181 offset:7232
	ds_write_b128 v231, v[74:77]
	ds_write_b128 v232, v[78:81] offset:4608
	ds_write_b128 v231, v[82:85] offset:1152
	ds_write_b128 v232, v[86:89] offset:5888
	ds_write_b128 v231, v[90:93] offset:2304
	ds_write_b128 v232, v[94:97] offset:7168
	ds_write_b128 v231, v[98:101] offset:3456
	ds_write_b128 v232, v[102:105] offset:8448
	s_waitcnt lgkmcnt(10)
	v_mfma_f32_32x32x16_bf16 v[18:33], v[38:41], v[238:241], v[18:33]
	v_add_f32_e32 v38, v135, v46
	v_add_f32_e32 v38, v136, v38
	v_add_f32_e32 v38, v137, v38
	v_add_f32_e32 v38, v139, v38
	v_add_f32_e32 v38, v140, v38
	v_add_f32_e32 v38, v141, v38
	v_add_f32_e32 v139, v142, v38
	v_mfma_f32_32x32x16_bf16 v[2:17], v[42:45], v[34:37], v[2:17]
	v_add_u32_e32 v34, s10, v199
	v_med3_i32 v34, v34, 0, v233
	v_mul_u32_u24_e32 v38, 0xc00, v34
	ds_read_b128 v[34:37], v177
	v_or_b32_e32 v38, v38, v176
	global_load_dwordx4 v[86:89], v38, s[8:9] offset:1024
	global_load_dwordx4 v[90:93], v38, s[8:9] offset:2048
	v_add_u32_e32 v38, s10, v200
	v_med3_i32 v38, v38, 0, v233
	v_mul_u32_u24_e32 v38, 0xc00, v38
	ds_read_b128 v[74:77], v177 offset:32
	v_or_b32_e32 v78, v38, v176
	s_waitcnt lgkmcnt(1)
	v_mfma_f32_32x32x16_bf16 v[34:49], v[34:37], v[70:73], 0
	global_load_dwordx4 v[134:137], v78, s[8:9] offset:1024
	global_load_dwordx4 v[142:145], v78, s[8:9] offset:2048
	v_add_u32_e32 v78, s10, v201
	v_med3_i32 v78, v78, 0, v233
	v_mul_u32_u24_e32 v78, 0xc00, v78
	v_or_b32_e32 v94, v78, v176
	ds_read_b128 v[78:81], v177 offset:96
	ds_read_b128 v[82:85], v177 offset:64
	global_load_dwordx4 v[146:149], v94, s[8:9] offset:1024
	global_load_dwordx4 v[150:153], v94, s[8:9] offset:2048
	s_waitcnt lgkmcnt(2)
	v_mfma_f32_32x32x16_bf16 v[34:49], v[74:77], v[66:69], v[34:49]
	v_add_u32_e32 v74, s10, v202
	v_med3_i32 v74, v74, 0, v233
	v_mul_u32_u24_e32 v74, 0xc00, v74
	v_or_b32_e32 v74, v74, v176
	global_load_dwordx4 v[154:157], v74, s[8:9] offset:1024
	global_load_dwordx4 v[158:161], v74, s[8:9] offset:2048
	v_add_u32_e32 v75, 32, v164
	v_cmp_le_u32_e32 vcc, v75, v163
	s_waitcnt lgkmcnt(0)
	v_mfma_f32_32x32x16_bf16 v[34:49], v[82:85], v[62:65], v[34:49]
	v_add_u32_e32 v75, 33, v164
	v_add_u32_e32 v76, 34, v164
	v_add_f32_e32 v74, v162, v139
	v_add_f32_e32 v74, v165, v74
	v_add_f32_e32 v74, v171, v74
	v_add_f32_e32 v74, v172, v74
	v_add_f32_e32 v74, v173, v74
	v_mfma_f32_32x32x16_bf16 v[34:49], v[78:81], v[58:61], v[34:49]
	v_add_f32_e32 v74, v237, v74
	v_add_f32_e32 v74, v246, v74
	v_add_f32_e32 v74, v247, v74
	v_add_f32_e32 v162, v138, v74
	v_mfma_f32_32x32x16_bf16 v[2:17], v[242:245], v[238:241], v[2:17]
	s_nop 6
	v_cndmask_b32_e32 v34, v234, v34, vcc
	v_cmp_le_u32_e32 vcc, v75, v163
	s_nop 1
	v_cndmask_b32_e32 v35, v234, v35, vcc
	v_cmp_le_u32_e32 vcc, v76, v163
	v_add_u32_e32 v76, 35, v164
	v_max3_f32 v75, v34, s31, v35
	v_cndmask_b32_e32 v36, v234, v36, vcc
	v_cmp_le_u32_e32 vcc, v76, v163
	v_add_u32_e32 v76, 40, v164
	s_nop 0
	v_cndmask_b32_e32 v37, v234, v37, vcc
	v_cmp_le_u32_e32 vcc, v76, v163
	v_add_u32_e32 v76, 41, v164
	v_max3_f32 v75, v75, v36, v37
	v_cndmask_b32_e32 v38, v234, v38, vcc
	v_cmp_le_u32_e32 vcc, v76, v163
	v_add_u32_e32 v76, 42, v164
	s_nop 0
	v_cndmask_b32_e32 v39, v234, v39, vcc
	v_cmp_le_u32_e32 vcc, v76, v163
	v_add_u32_e32 v76, 43, v164
	v_max3_f32 v75, v75, v38, v39
	v_cndmask_b32_e32 v40, v234, v40, vcc
	v_cmp_le_u32_e32 vcc, v76, v163
	v_add_u32_e32 v76, 48, v164
	s_nop 0
	v_cndmask_b32_e32 v41, v234, v41, vcc
	v_cmp_le_u32_e32 vcc, v76, v163
	v_add_u32_e32 v76, 49, v164
	v_max3_f32 v75, v75, v40, v41
	v_cndmask_b32_e32 v42, v234, v42, vcc
	v_cmp_le_u32_e32 vcc, v76, v163
	v_add_u32_e32 v76, 50, v164
	s_nop 0
	v_cndmask_b32_e32 v43, v234, v43, vcc
	v_cmp_le_u32_e32 vcc, v76, v163
	v_add_u32_e32 v76, 51, v164
	v_max3_f32 v75, v75, v42, v43
	v_cndmask_b32_e32 v44, v234, v44, vcc
	v_cmp_le_u32_e32 vcc, v76, v163
	v_add_u32_e32 v76, 56, v164
	s_nop 0
	v_cndmask_b32_e32 v45, v234, v45, vcc
	v_cmp_le_u32_e32 vcc, v76, v163
	v_add_u32_e32 v76, 57, v164
	v_max3_f32 v75, v75, v44, v45
	v_cndmask_b32_e32 v46, v234, v46, vcc
	v_cmp_le_u32_e32 vcc, v76, v163
	v_add_u32_e32 v76, 58, v164
	s_nop 0
	v_cndmask_b32_e32 v47, v234, v47, vcc
	v_cmp_le_u32_e32 vcc, v76, v163
	v_add_u32_e32 v76, 59, v164
	v_max3_f32 v75, v75, v46, v47
	v_cndmask_b32_e32 v48, v234, v48, vcc
	v_cmp_le_u32_e32 vcc, v76, v163
	s_nop 1
	v_cndmask_b32_e32 v49, v234, v49, vcc
	v_max3_f32 v75, v75, v48, v49
	v_mov_b32_e32 v76, v75
	s_nop 1
	v_permlane32_swap_b32_e32 v76, v75
	s_waitcnt lgkmcnt(0)
	v_max_f32_e32 v74, v76, v76
	v_max_f32_e32 v74, v75, v74
	v_cmp_gt_f32_e32 vcc, v74, v50
	s_cbranch_vccz .LBB0_400
; __device__ __forceinline__ unsigned cvt_pk_bf16(float lo, float hi) { unsigned r; asm volatile("v_cvt_pk_bf16_f32 %0, %1, %2" : "=v"(r) : "v"(lo), "v"(hi)); return r; }
; #define LAS __attribute__((address_space(3)))
; template <int STAGE, int OFF> __device__ __forceinline__ void attn32_unit(const bf16* base, bf16* yrow0, int blk0, int u, LAS unsigned char* xtab, LAS unsigned char* kbuf, LAS unsigned char* vbuf, int lane, ...
;     ...
;         for (int c = 0; c < 4; ++c) { *(LAS v4u*)(kbuf + (8 * c + lrow) * 144 + lch * 16) = kr[set][c]; *(LAS v4u*)(vbuf + (8 * c + lrow) * 160 + lch * 16) = vr[set][c]; }
;         if (pp + 2 < 5) { ATT32_LOAD(set, pp + 2, t0, SH); }
;         else { const bf16* base_ = base; { const bf16* base = nbase; ATT32_LOAD(set, pp + 2 - 5, nt0, nsh); } (void)base_; }
;         f32x16 sc;
; #pragma unroll
;         for (int i = 0; i < 16; ++i) sc[i] = 0.f;
; #pragma unroll
;         for (int ks = 0; ks < 4; ++ks) { const bf16x8 ka = *(const LAS bf16x8*)(kbuf + qi * 144 + 32 * ks + 16 * h); sc = MFMA32(ka, qb[ks], sc); }
;     ...
;         if (__any(mx > m)) {
;             const float mn = fmaxf(m, mx), alpha = __builtin_amdgcn_exp2f(m - mn); m = mn; l *= alpha;
; #pragma unroll
;             for (int i = 0; i < 16; ++i) { o[0][i] *= alpha; o[1][i] *= alpha; }
;         }
;         float ps = 0.f;
; #pragma unroll
;         for (int rg = 0; rg < 16; ++rg) { sc[rg] = __builtin_amdgcn_exp2f(sc[rg] - m); ps += sc[rg]; }
;         l += ps;
;         bf16x8 pb[2];
; #pragma unroll
;         for (int s2 = 0; s2 < 2; ++s2) { v4u w; w.x = pg8::cvt_pk_bf16(sc[8 * s2], sc[8 * s2 + 1]); w.y = pg8::cvt_pk_bf16(sc[8 * s2 + 2], sc[8 * s2 + 3]); w.z = pg8::cvt_pk_bf16(sc[8 * s2 + 4], sc[8 * s2 + 5]); w.w = pg8::cvt_pk_bf16(sc[8 * s2 + 6], sc[8 * s2 + 7]); pb[s2] = __builtin_bit_cast(bf16x8, w); }
; #pragma unroll
;         for (int mb = 0; mb < 2; ++mb)
; #pragma unroll
;             for (int s2 = 0; s2 < 2; ++s2) {
;                 LAS unsigned char* vp = vbuf + tr_off + (16 * s2) * 160 + 64 * mb;
;                 const v4i16 a0 = __builtin_amdgcn_ds_read_tr16_b64_v4i16((LAS v4i16*)vp), a1 = __builtin_amdgcn_ds_read_tr16_b64_v4i16((LAS v4i16*)(vp + 8 * 160));
;                 const bf16x8 va = __builtin_shufflevector(a0, a1, 0, 1, 2, 3, 4, 5, 6, 7);
;                 o[mb] = MFMA32(va, pb[s2], o[mb]);
;             }
	v_max_f32_e32 v74, v74, v74
	v_max_f32_e32 v75, v50, v50
	v_max_f32_e32 v74, v75, v74
	v_sub_f32_e32 v50, v50, v74
	v_exp_f32_e32 v50, v50
	s_nop 0
	v_pk_mul_f32 v[32:33], v[32:33], v[50:51] op_sel_hi:[1,0]
	v_pk_mul_f32 v[30:31], v[30:31], v[50:51] op_sel_hi:[1,0]
	v_pk_mul_f32 v[28:29], v[28:29], v[50:51] op_sel_hi:[1,0]
	v_pk_mul_f32 v[26:27], v[26:27], v[50:51] op_sel_hi:[1,0]
	v_pk_mul_f32 v[24:25], v[24:25], v[50:51] op_sel_hi:[1,0]
	v_pk_mul_f32 v[22:23], v[22:23], v[50:51] op_sel_hi:[1,0]
	v_pk_mul_f32 v[20:21], v[20:21], v[50:51] op_sel_hi:[1,0]
	v_pk_mul_f32 v[18:19], v[18:19], v[50:51] op_sel_hi:[1,0]
	v_pk_mul_f32 v[16:17], v[16:17], v[50:51] op_sel_hi:[1,0]
	v_pk_mul_f32 v[14:15], v[14:15], v[50:51] op_sel_hi:[1,0]
	v_pk_mul_f32 v[12:13], v[12:13], v[50:51] op_sel_hi:[1,0]
	v_pk_mul_f32 v[10:11], v[10:11], v[50:51] op_sel_hi:[1,0]
	v_pk_mul_f32 v[8:9], v[8:9], v[50:51] op_sel_hi:[1,0]
	v_pk_mul_f32 v[6:7], v[6:7], v[50:51] op_sel_hi:[1,0]
	v_pk_mul_f32 v[4:5], v[4:5], v[50:51] op_sel_hi:[1,0]
	v_pk_mul_f32 v[2:3], v[2:3], v[50:51] op_sel_hi:[1,0]
	v_mul_f32_e32 v162, v162, v50
	v_mov_b32_e32 v50, v74
.LBB0_400:
	v_sub_f32_e32 v34, v34, v50
	v_exp_f32_e32 v74, v34
	v_sub_f32_e32 v34, v35, v50
	v_exp_f32_e32 v75, v34
	v_sub_f32_e32 v34, v36, v50
	v_exp_f32_e32 v76, v34
	v_sub_f32_e32 v34, v37, v50
	v_exp_f32_e32 v77, v34
	v_sub_f32_e32 v34, v38, v50
	v_exp_f32_e32 v78, v34
	v_sub_f32_e32 v34, v39, v50
	v_exp_f32_e32 v79, v34
	v_sub_f32_e32 v34, v40, v50
	v_exp_f32_e32 v80, v34
	v_sub_f32_e32 v34, v41, v50
	v_exp_f32_e32 v81, v34
	v_sub_f32_e32 v34, v42, v50
	v_exp_f32_e32 v165, v34
	v_sub_f32_e32 v34, v43, v50
	v_exp_f32_e32 v171, v34
	v_sub_f32_e32 v34, v44, v50
	v_exp_f32_e32 v172, v34
	v_sub_f32_e32 v34, v45, v50
	v_exp_f32_e32 v173, v34
	v_sub_f32_e32 v34, v46, v50
	v_exp_f32_e32 v237, v34
	v_sub_f32_e32 v34, v47, v50
	v_exp_f32_e32 v246, v34
	v_sub_f32_e32 v34, v48, v50
	v_exp_f32_e32 v247, v34
	v_sub_f32_e32 v34, v49, v50
	v_exp_f32_e32 v248, v34
	v_cvt_pk_bf16_f32 v34, v74, v75
	v_cvt_pk_bf16_f32 v35, v76, v77
	v_cvt_pk_bf16_f32 v36, v78, v79
	v_cvt_pk_bf16_f32 v37, v80, v81
	v_cvt_pk_bf16_f32 v238, v165, v171
	v_cvt_pk_bf16_f32 v239, v172, v173
	v_cvt_pk_bf16_f32 v240, v237, v246
	v_cvt_pk_bf16_f32 v241, v247, v248
	ds_read_b64_tr_b16 v[38:39], v181 offset:4608
	ds_read_b64_tr_b16 v[40:41], v181 offset:5888
	ds_read_b64_tr_b16 v[44:45], v181 offset:5952
	ds_read_b64_tr_b16 v[42:43], v181 offset:4672
	s_waitcnt lgkmcnt(2)
	v_mfma_f32_32x32x16_bf16 v[18:33], v[38:41], v[34:37], v[18:33]
	ds_read_b64_tr_b16 v[38:39], v181 offset:7168
	ds_read_b64_tr_b16 v[40:41], v181 offset:8448
	v_add_f32_e32 v46, 0, v74
	ds_read_b64_tr_b16 v[244:245], v181 offset:8512
	ds_read_b64_tr_b16 v[242:243], v181 offset:7232
	s_waitcnt vmcnt(15)
	ds_write_b128 v231, v[54:57]
	s_waitcnt vmcnt(14)
	ds_write_b128 v232, v[106:109] offset:4608
	s_waitcnt vmcnt(13)
	ds_write_b128 v231, v[110:113] offset:1152
	s_waitcnt vmcnt(12)
	ds_write_b128 v232, v[114:117] offset:5888
	s_waitcnt vmcnt(11)
	ds_write_b128 v231, v[118:121] offset:2304
	s_waitcnt vmcnt(10)
	ds_write_b128 v232, v[122:125] offset:7168
	s_waitcnt vmcnt(9)
	ds_write_b128 v231, v[126:129] offset:3456
	s_waitcnt vmcnt(8)
	ds_write_b128 v232, v[130:133] offset:8448
	v_or_b32_e32 v98, s10, v204
	v_or_b32_e32 v102, s10, v205
	s_waitcnt lgkmcnt(10)
	v_mfma_f32_32x32x16_bf16 v[18:33], v[38:41], v[238:241], v[18:33]
	v_add_f32_e32 v38, v75, v46
	v_add_f32_e32 v38, v76, v38
	v_add_f32_e32 v38, v77, v38
	v_add_f32_e32 v38, v78, v38
	v_add_f32_e32 v38, v79, v38
	v_add_f32_e32 v38, v80, v38
	v_add_f32_e32 v249, v81, v38
	v_mfma_f32_32x32x16_bf16 v[2:17], v[42:45], v[34:37], v[2:17]
	v_or_b32_e32 v34, s10, v184
	v_min_u32_e32 v34, 0x3fff, v34
	v_mul_u32_u24_e32 v38, 0xc00, v34
	ds_read_b128 v[34:37], v177
	v_or_b32_e32 v38, v38, v176
	global_load_dwordx4 v[54:57], v38, s[8:9] offset:1024
	global_load_dwordx4 v[74:77], v38, s[8:9] offset:2048
	v_or_b32_e32 v38, s10, v203
	v_min_u32_e32 v38, 0x3fff, v38
	v_mul_u32_u24_e32 v38, 0xc00, v38
	ds_read_b128 v[94:97], v177 offset:32
	v_or_b32_e32 v82, v38, v176
	s_waitcnt lgkmcnt(1)
	v_mfma_f32_32x32x16_bf16 v[34:49], v[34:37], v[70:73], 0
	v_min_u32_e32 v98, 0x3fff, v98
	v_min_u32_e32 v102, 0x3fff, v102
	v_mul_u32_u24_e32 v98, 0xc00, v98
	v_mul_u32_u24_e32 v102, 0xc00, v102
	v_or_b32_e32 v98, v98, v176
	v_or_b32_e32 v114, v102, v176
	global_load_dwordx4 v[78:81], v82, s[8:9] offset:1024
	s_nop 0
	global_load_dwordx4 v[82:85], v82, s[8:9] offset:2048
	ds_read_b128 v[106:109], v177 offset:96
	ds_read_b128 v[110:113], v177 offset:64
	s_waitcnt lgkmcnt(2)
	v_mfma_f32_32x32x16_bf16 v[34:49], v[94:97], v[66:69], v[34:49]
	global_load_dwordx4 v[94:97], v98, s[8:9] offset:1024
	s_nop 0
	global_load_dwordx4 v[98:101], v98, s[8:9] offset:2048
	s_nop 0
	global_load_dwordx4 v[102:105], v114, s[8:9] offset:1024
	global_load_dwordx4 v[138:141], v114, s[8:9] offset:2048
	s_waitcnt lgkmcnt(0)
; __device__ __forceinline__ unsigned cvt_pk_bf16(float lo, float hi) { unsigned r; asm volatile("v_cvt_pk_bf16_f32 %0, %1, %2" : "=v"(r) : "v"(lo), "v"(hi)); return r; }
; #define LAS __attribute__((address_space(3)))
; template <int STAGE, int OFF> __device__ __forceinline__ void attn32_unit(const bf16* base, bf16* yrow0, int blk0, int u, LAS unsigned char* xtab, LAS unsigned char* kbuf, LAS unsigned char* vbuf, int lane, ...
;     ...
;         for (int ks = 0; ks < 4; ++ks) { const bf16x8 ka = *(const LAS bf16x8*)(kbuf + qi * 144 + 32 * ks + 16 * h); sc = MFMA32(ka, qb[ks], sc); }
;         if (pp == 4) {
; #pragma unroll
;             for (int ks = 0; ks < 4; ++ks) qb[ks] = *(const bf16x8*)(nbase + (size_t)min(nt0 + (qi << nsh), SEQ - 1) * 1536 + 16 * ks + 8 * h);
;         }
;         const int mbase = n0 + 4 * h - lo; float mx = -INFINITY;
; #pragma unroll
;         for (int rg = 0; rg < 16; ++rg) { sc[rg] = ((unsigned)(mbase + (rg & 3) + 8 * (rg >> 2)) <= mspan) ? sc[rg] : -INFINITY; mx = fmaxf(mx, sc[rg]); }
;         mx = fmaxf(mx, __shfl_xor(mx, 32));
;         if (__any(mx > m)) {
;             const float mn = fmaxf(m, mx), alpha = __builtin_amdgcn_exp2f(m - mn); m = mn; l *= alpha;
; #pragma unroll
;             for (int i = 0; i < 16; ++i) { o[0][i] *= alpha; o[1][i] *= alpha; }
;         }
;         float ps = 0.f;
; #pragma unroll
;         for (int rg = 0; rg < 16; ++rg) { sc[rg] = __builtin_amdgcn_exp2f(sc[rg] - m); ps += sc[rg]; }
;         l += ps;
;         bf16x8 pb[2];
; #pragma unroll
;         for (int s2 = 0; s2 < 2; ++s2) { v4u w; w.x = pg8::cvt_pk_bf16(sc[8 * s2], sc[8 * s2 + 1]); w.y = pg8::cvt_pk_bf16(sc[8 * s2 + 2], sc[8 * s2 + 3]); w.z = pg8::cvt_pk_bf16(sc[8 * s2 + 4], sc[8 * s2 + 5]); w.w = pg8::cvt_pk_bf16(sc[8 * s2 + 6], sc[8 * s2 + 7]); pb[s2] = __builtin_bit_cast(bf16x8, w); }
; #pragma unroll
;         for (int mb = 0; mb < 2; ++mb)
; #pragma unroll
;             for (int s2 = 0; s2 < 2; ++s2) {
;                 LAS unsigned char* vp = vbuf + tr_off + (16 * s2) * 160 + 64 * mb;
;                 const v4i16 a0 = __builtin_amdgcn_ds_read_tr16_b64_v4i16((LAS v4i16*)vp), a1 = __builtin_amdgcn_ds_read_tr16_b64_v4i16((LAS v4i16*)(vp + 8 * 160));
;                 const bf16x8 va = __builtin_shufflevector(a0, a1, 0, 1, 2, 3, 4, 5, 6, 7);
;                 o[mb] = MFMA32(va, pb[s2], o[mb]);
;             }
	v_mfma_f32_32x32x16_bf16 v[34:49], v[110:113], v[62:65], v[34:49]
	v_add_f32_e32 v110, v165, v249
	v_add_f32_e32 v110, v171, v110
	v_add_f32_e32 v110, v172, v110
	v_add_f32_e32 v110, v173, v110
	v_add_f32_e32 v110, v237, v110
	v_add_f32_e32 v110, v246, v110
	v_add_f32_e32 v110, v247, v110
	v_mfma_f32_32x32x16_bf16 v[34:49], v[106:109], v[58:61], v[34:49]
	v_add_u32_e32 v106, 64, v164
	v_cmp_le_u32_e32 vcc, v106, v163
	v_add_u32_e32 v106, 0x41, v164
	v_add_u32_e32 v107, 0x42, v164
	v_add_f32_e32 v108, v248, v110
	v_add_f32_e32 v162, v162, v108
	s_nop 5
	v_cndmask_b32_e32 v34, v234, v34, vcc
	v_cmp_le_u32_e32 vcc, v106, v163
	v_mfma_f32_32x32x16_bf16 v[2:17], v[242:245], v[238:241], v[2:17]
	s_nop 0
	v_cndmask_b32_e32 v35, v234, v35, vcc
	v_cmp_le_u32_e32 vcc, v107, v163
	v_add_u32_e32 v107, 0x43, v164
	v_max3_f32 v106, v34, s31, v35
	v_cndmask_b32_e32 v36, v234, v36, vcc
	v_cmp_le_u32_e32 vcc, v107, v163
	v_add_u32_e32 v107, 0x48, v164
	s_nop 0
	v_cndmask_b32_e32 v37, v234, v37, vcc
	v_cmp_le_u32_e32 vcc, v107, v163
	v_add_u32_e32 v107, 0x49, v164
	v_max3_f32 v106, v106, v36, v37
	v_cndmask_b32_e32 v38, v234, v38, vcc
	v_cmp_le_u32_e32 vcc, v107, v163
	v_add_u32_e32 v107, 0x4a, v164
	s_nop 0
	v_cndmask_b32_e32 v39, v234, v39, vcc
	v_cmp_le_u32_e32 vcc, v107, v163
	v_add_u32_e32 v107, 0x4b, v164
	v_max3_f32 v106, v106, v38, v39
	v_cndmask_b32_e32 v40, v234, v40, vcc
	v_cmp_le_u32_e32 vcc, v107, v163
	v_add_u32_e32 v107, 0x50, v164
	s_nop 0
	v_cndmask_b32_e32 v41, v234, v41, vcc
	v_cmp_le_u32_e32 vcc, v107, v163
	v_add_u32_e32 v107, 0x51, v164
	v_max3_f32 v106, v106, v40, v41
	v_cndmask_b32_e32 v42, v234, v42, vcc
	v_cmp_le_u32_e32 vcc, v107, v163
	v_add_u32_e32 v107, 0x52, v164
	s_nop 0
	v_cndmask_b32_e32 v43, v234, v43, vcc
	v_cmp_le_u32_e32 vcc, v107, v163
	v_add_u32_e32 v107, 0x53, v164
	v_max3_f32 v106, v106, v42, v43
	v_cndmask_b32_e32 v44, v234, v44, vcc
	v_cmp_le_u32_e32 vcc, v107, v163
	v_add_u32_e32 v107, 0x58, v164
	s_nop 0
	v_cndmask_b32_e32 v45, v234, v45, vcc
	v_cmp_le_u32_e32 vcc, v107, v163
	v_add_u32_e32 v107, 0x59, v164
	v_max3_f32 v106, v106, v44, v45
	v_cndmask_b32_e32 v46, v234, v46, vcc
	v_cmp_le_u32_e32 vcc, v107, v163
	v_add_u32_e32 v107, 0x5a, v164
	s_nop 0
	v_cndmask_b32_e32 v47, v234, v47, vcc
	v_cmp_le_u32_e32 vcc, v107, v163
	v_add_u32_e32 v107, 0x5b, v164
	v_max3_f32 v106, v106, v46, v47
	v_cndmask_b32_e32 v48, v234, v48, vcc
	v_cmp_le_u32_e32 vcc, v107, v163
	s_nop 1
	v_cndmask_b32_e32 v49, v234, v49, vcc
	v_max3_f32 v106, v106, v48, v49
	v_mov_b32_e32 v107, v106
	s_nop 1
	v_permlane32_swap_b32_e32 v107, v106
	s_waitcnt lgkmcnt(0)
	v_max_f32_e32 v107, v107, v107
	v_max_f32_e32 v106, v106, v107
	v_cmp_gt_f32_e32 vcc, v106, v50
	s_cbranch_vccz .LBB0_402
	v_max_f32_e32 v106, v106, v106
	v_max_f32_e32 v107, v50, v50
	v_max_f32_e32 v106, v107, v106
	v_sub_f32_e32 v50, v50, v106
	v_exp_f32_e32 v50, v50
	s_nop 0
	v_pk_mul_f32 v[32:33], v[32:33], v[50:51] op_sel_hi:[1,0]
	v_pk_mul_f32 v[30:31], v[30:31], v[50:51] op_sel_hi:[1,0]
	v_pk_mul_f32 v[28:29], v[28:29], v[50:51] op_sel_hi:[1,0]
	v_pk_mul_f32 v[26:27], v[26:27], v[50:51] op_sel_hi:[1,0]
	v_pk_mul_f32 v[24:25], v[24:25], v[50:51] op_sel_hi:[1,0]
	v_pk_mul_f32 v[22:23], v[22:23], v[50:51] op_sel_hi:[1,0]
	v_pk_mul_f32 v[20:21], v[20:21], v[50:51] op_sel_hi:[1,0]
	v_pk_mul_f32 v[18:19], v[18:19], v[50:51] op_sel_hi:[1,0]
	v_pk_mul_f32 v[16:17], v[16:17], v[50:51] op_sel_hi:[1,0]
	v_pk_mul_f32 v[14:15], v[14:15], v[50:51] op_sel_hi:[1,0]
	v_pk_mul_f32 v[12:13], v[12:13], v[50:51] op_sel_hi:[1,0]
	v_pk_mul_f32 v[10:11], v[10:11], v[50:51] op_sel_hi:[1,0]
	v_pk_mul_f32 v[8:9], v[8:9], v[50:51] op_sel_hi:[1,0]
	v_pk_mul_f32 v[6:7], v[6:7], v[50:51] op_sel_hi:[1,0]
	v_pk_mul_f32 v[4:5], v[4:5], v[50:51] op_sel_hi:[1,0]
	v_pk_mul_f32 v[2:3], v[2:3], v[50:51] op_sel_hi:[1,0]
	v_mul_f32_e32 v162, v162, v50
	v_mov_b32_e32 v50, v106
.LBB0_402:
	v_sub_f32_e32 v34, v34, v50
	v_exp_f32_e32 v106, v34
	v_sub_f32_e32 v34, v35, v50
	v_exp_f32_e32 v107, v34
	v_sub_f32_e32 v34, v36, v50
	v_exp_f32_e32 v108, v34
	v_sub_f32_e32 v34, v37, v50
	v_exp_f32_e32 v109, v34
	v_sub_f32_e32 v34, v38, v50
	v_exp_f32_e32 v110, v34
	v_sub_f32_e32 v34, v39, v50
	v_exp_f32_e32 v111, v34
	v_sub_f32_e32 v34, v40, v50
	v_exp_f32_e32 v112, v34
	v_sub_f32_e32 v34, v41, v50
	v_exp_f32_e32 v113, v34
	v_sub_f32_e32 v34, v42, v50
	v_exp_f32_e32 v165, v34
	v_sub_f32_e32 v34, v43, v50
	v_exp_f32_e32 v171, v34
	v_sub_f32_e32 v34, v44, v50
	v_exp_f32_e32 v172, v34
	v_sub_f32_e32 v34, v45, v50
	v_exp_f32_e32 v173, v34
	v_sub_f32_e32 v34, v46, v50
	v_exp_f32_e32 v237, v34
	v_sub_f32_e32 v34, v47, v50
	v_exp_f32_e32 v246, v34
	v_sub_f32_e32 v34, v48, v50
	v_exp_f32_e32 v247, v34
	v_sub_f32_e32 v34, v49, v50
	v_exp_f32_e32 v248, v34
	v_cvt_pk_bf16_f32 v34, v106, v107
	v_cvt_pk_bf16_f32 v35, v108, v109
	v_cvt_pk_bf16_f32 v36, v110, v111
	v_cvt_pk_bf16_f32 v37, v112, v113
	v_cvt_pk_bf16_f32 v238, v165, v171
	v_cvt_pk_bf16_f32 v239, v172, v173
	v_cvt_pk_bf16_f32 v240, v237, v246
	v_cvt_pk_bf16_f32 v241, v247, v248
	ds_read_b64_tr_b16 v[38:39], v181 offset:4608
	ds_read_b64_tr_b16 v[40:41], v181 offset:5888
	ds_read_b64_tr_b16 v[44:45], v181 offset:5952
	ds_read_b64_tr_b16 v[42:43], v181 offset:4672
	s_waitcnt lgkmcnt(2)
	v_mfma_f32_32x32x16_bf16 v[18:33], v[38:41], v[34:37], v[18:33]
	ds_read_b64_tr_b16 v[38:39], v181 offset:7168
	ds_read_b64_tr_b16 v[40:41], v181 offset:8448
	v_add_f32_e32 v46, 0, v106
	s_add_i32 s10, s13, s20
	ds_read_b64_tr_b16 v[244:245], v181 offset:8512
	ds_read_b64_tr_b16 v[242:243], v181 offset:7232
	s_waitcnt vmcnt(15)
	ds_write_b128 v231, v[86:89]
	s_waitcnt vmcnt(14)
; #define LAS __attribute__((address_space(3)))
; template <int STAGE, int OFF> __device__ __forceinline__ void attn32_unit(const bf16* base, bf16* yrow0, int blk0, int u, LAS unsigned char* xtab, LAS unsigned char* kbuf, LAS unsigned char* vbuf, int lane, ...
;     ...
;         for (int c = 0; c < 4; ++c) { *(LAS v4u*)(kbuf + (8 * c + lrow) * 144 + lch * 16) = kr[set][c]; *(LAS v4u*)(vbuf + (8 * c + lrow) * 160 + lch * 16) = vr[set][c]; }
;         if (pp + 2 < 5) { ATT32_LOAD(set, pp + 2, t0, SH); }
;         else { const bf16* base_ = base; { const bf16* base = nbase; ATT32_LOAD(set, pp + 2 - 5, nt0, nsh); } (void)base_; }
;         f32x16 sc;
; #pragma unroll
;         for (int i = 0; i < 16; ++i) sc[i] = 0.f;
; #pragma unroll
;         for (int ks = 0; ks < 4; ++ks) { const bf16x8 ka = *(const LAS bf16x8*)(kbuf + qi * 144 + 32 * ks + 16 * h); sc = MFMA32(ka, qb[ks], sc); }
;         if (pp == 4) {
; #pragma unroll
;             for (int ks = 0; ks < 4; ++ks) qb[ks] = *(const bf16x8*)(nbase + (size_t)min(nt0 + (qi << nsh), SEQ - 1) * 1536 + 16 * ks + 8 * h);
;         }
;         const int mbase = n0 + 4 * h - lo; float mx = -INFINITY;
; #pragma unroll
;         for (int rg = 0; rg < 16; ++rg) { sc[rg] = ((unsigned)(mbase + (rg & 3) + 8 * (rg >> 2)) <= mspan) ? sc[rg] : -INFINITY; mx = fmaxf(mx, sc[rg]); }
;         mx = fmaxf(mx, __shfl_xor(mx, 32));
;         if (__any(mx > m)) {
;             const float mn = fmaxf(m, mx), alpha = __builtin_amdgcn_exp2f(m - mn); m = mn; l *= alpha;
; #pragma unroll
;             for (int i = 0; i < 16; ++i) { o[0][i] *= alpha; o[1][i] *= alpha; }
;         }
;         float ps = 0.f;
; #pragma unroll
;         for (int rg = 0; rg < 16; ++rg) { sc[rg] = __builtin_amdgcn_exp2f(sc[rg] - m); ps += sc[rg]; }
;         l += ps;
;         bf16x8 pb[2];
; #pragma unroll
;         for (int s2 = 0; s2 < 2; ++s2) { v4u w; w.x = pg8::cvt_pk_bf16(sc[8 * s2], sc[8 * s2 + 1]); w.y = pg8::cvt_pk_bf16(sc[8 * s2 + 2], sc[8 * s2 + 3]); w.z = pg8::cvt_pk_bf16(sc[8 * s2 + 4], sc[8 * s2 + 5]); w.w = pg8::cvt_pk_bf16(sc[8 * s2 + 6], sc[8 * s2 + 7]); pb[s2] = __builtin_bit_cast(bf16x8, w); }
; #pragma unroll
;         for (int mb = 0; mb < 2; ++mb)
; #pragma unroll
;             for (int s2 = 0; s2 < 2; ++s2) {
;                 LAS unsigned char* vp = vbuf + tr_off + (16 * s2) * 160 + 64 * mb;
	ds_write_b128 v232, v[90:93] offset:4608
	s_waitcnt vmcnt(13)
	ds_write_b128 v231, v[134:137] offset:1152
	s_waitcnt vmcnt(12)
	ds_write_b128 v232, v[142:145] offset:5888
	s_waitcnt vmcnt(11)
	ds_write_b128 v231, v[146:149] offset:2304
	s_waitcnt vmcnt(10)
	ds_write_b128 v232, v[150:153] offset:7168
	s_waitcnt vmcnt(9)
	ds_write_b128 v231, v[154:157] offset:3456
	s_waitcnt vmcnt(8)
	ds_write_b128 v232, v[158:161] offset:8448
	s_waitcnt lgkmcnt(10)
	v_mfma_f32_32x32x16_bf16 v[18:33], v[38:41], v[238:241], v[18:33]
	v_add_f32_e32 v38, v107, v46
	v_add_f32_e32 v38, v108, v38
	v_add_f32_e32 v38, v109, v38
	v_add_f32_e32 v38, v110, v38
	v_add_f32_e32 v38, v111, v38
	v_add_f32_e32 v38, v112, v38
	v_add_f32_e32 v249, v113, v38
	v_mfma_f32_32x32x16_bf16 v[2:17], v[42:45], v[34:37], v[2:17]
	v_add_u32_e32 v34, s10, v208
	v_med3_i32 v34, v34, 0, v233
	v_mul_u32_u24_e32 v38, 0xc00, v34
	ds_read_b128 v[34:37], v177
	v_or_b32_e32 v38, v38, v176
	global_load_dwordx4 v[106:109], v38, s[8:9] offset:1024
	global_load_dwordx4 v[110:113], v38, s[8:9] offset:2048
	v_add_u32_e32 v38, s10, v209
	v_med3_i32 v38, v38, 0, v233
	v_mul_u32_u24_e32 v38, 0xc00, v38
	ds_read_b128 v[86:89], v177 offset:32
	v_or_b32_e32 v90, v38, v176
	s_waitcnt lgkmcnt(1)
	v_mfma_f32_32x32x16_bf16 v[34:49], v[34:37], v[70:73], 0
	global_load_dwordx4 v[114:117], v90, s[8:9] offset:1024
	global_load_dwordx4 v[118:121], v90, s[8:9] offset:2048
	v_add_u32_e32 v90, s10, v211
	v_med3_i32 v90, v90, 0, v233
	v_mul_u32_u24_e32 v90, 0xc00, v90
	v_or_b32_e32 v126, v90, v176
	ds_read_b128 v[90:93], v177 offset:96
	ds_read_b128 v[142:145], v177 offset:64
	global_load_dwordx4 v[122:125], v126, s[8:9] offset:1024
	s_nop 0
	global_load_dwordx4 v[126:129], v126, s[8:9] offset:2048
	s_waitcnt lgkmcnt(2)
	v_mfma_f32_32x32x16_bf16 v[34:49], v[86:89], v[66:69], v[34:49]
	v_add_u32_e32 v86, s10, v212
	v_med3_i32 v86, v86, 0, v233
	v_mul_u32_u24_e32 v86, 0xc00, v86
	v_or_b32_e32 v86, v86, v176
	global_load_dwordx4 v[130:133], v86, s[8:9] offset:1024
	global_load_dwordx4 v[134:137], v86, s[8:9] offset:2048
	v_add_u32_e32 v87, 0x60, v164
	v_cmp_le_u32_e32 vcc, v87, v163
	s_waitcnt lgkmcnt(0)
	v_mfma_f32_32x32x16_bf16 v[34:49], v[142:145], v[62:65], v[34:49]
	v_add_u32_e32 v87, 0x61, v164
	v_add_u32_e32 v88, 0x62, v164
	v_add_f32_e32 v86, v165, v249
	v_add_f32_e32 v86, v171, v86
	v_add_f32_e32 v86, v172, v86
	v_add_f32_e32 v86, v173, v86
	v_add_f32_e32 v86, v237, v86
	v_mfma_f32_32x32x16_bf16 v[34:49], v[90:93], v[58:61], v[34:49]
	v_add_f32_e32 v86, v246, v86
	v_add_f32_e32 v86, v247, v86
	v_add_f32_e32 v86, v248, v86
	v_add_f32_e32 v142, v162, v86
	v_mfma_f32_32x32x16_bf16 v[2:17], v[242:245], v[238:241], v[2:17]
	s_nop 6
	v_cndmask_b32_e32 v34, v234, v34, vcc
	v_cmp_le_u32_e32 vcc, v87, v163
	s_nop 1
	v_cndmask_b32_e32 v35, v234, v35, vcc
	v_cmp_le_u32_e32 vcc, v88, v163
	v_add_u32_e32 v88, 0x63, v164
	v_max3_f32 v87, v34, s31, v35
	v_cndmask_b32_e32 v36, v234, v36, vcc
	v_cmp_le_u32_e32 vcc, v88, v163
	v_add_u32_e32 v88, 0x68, v164
	s_nop 0
	v_cndmask_b32_e32 v37, v234, v37, vcc
	v_cmp_le_u32_e32 vcc, v88, v163
	v_add_u32_e32 v88, 0x69, v164
	v_max3_f32 v87, v87, v36, v37
	v_cndmask_b32_e32 v38, v234, v38, vcc
	v_cmp_le_u32_e32 vcc, v88, v163
	v_add_u32_e32 v88, 0x6a, v164
	s_nop 0
	v_cndmask_b32_e32 v39, v234, v39, vcc
	v_cmp_le_u32_e32 vcc, v88, v163
	v_add_u32_e32 v88, 0x6b, v164
	v_max3_f32 v87, v87, v38, v39
	v_cndmask_b32_e32 v40, v234, v40, vcc
	v_cmp_le_u32_e32 vcc, v88, v163
	v_add_u32_e32 v88, 0x70, v164
	s_nop 0
	v_cndmask_b32_e32 v41, v234, v41, vcc
	v_cmp_le_u32_e32 vcc, v88, v163
	v_add_u32_e32 v88, 0x71, v164
	v_max3_f32 v87, v87, v40, v41
	v_cndmask_b32_e32 v42, v234, v42, vcc
	v_cmp_le_u32_e32 vcc, v88, v163
	v_add_u32_e32 v88, 0x72, v164
	s_nop 0
	v_cndmask_b32_e32 v43, v234, v43, vcc
	v_cmp_le_u32_e32 vcc, v88, v163
	v_add_u32_e32 v88, 0x73, v164
	v_max3_f32 v87, v87, v42, v43
	v_cndmask_b32_e32 v44, v234, v44, vcc
	v_cmp_le_u32_e32 vcc, v88, v163
	v_add_u32_e32 v88, 0x78, v164
	s_nop 0
	v_cndmask_b32_e32 v45, v234, v45, vcc
	v_cmp_le_u32_e32 vcc, v88, v163
	v_add_u32_e32 v88, 0x79, v164
	v_max3_f32 v87, v87, v44, v45
	v_cndmask_b32_e32 v46, v234, v46, vcc
	v_cmp_le_u32_e32 vcc, v88, v163
	v_add_u32_e32 v88, 0x7a, v164
	s_nop 0
	v_cndmask_b32_e32 v47, v234, v47, vcc
	v_cmp_le_u32_e32 vcc, v88, v163
	v_add_u32_e32 v88, 0x7b, v164
	v_max3_f32 v87, v87, v46, v47
	v_cndmask_b32_e32 v48, v234, v48, vcc
	v_cmp_le_u32_e32 vcc, v88, v163
	s_nop 1
	v_cndmask_b32_e32 v49, v234, v49, vcc
	v_max3_f32 v87, v87, v48, v49
	v_mov_b32_e32 v88, v87
	s_nop 1
	v_permlane32_swap_b32_e32 v88, v87
	s_waitcnt lgkmcnt(0)
	v_max_f32_e32 v86, v88, v88
	v_max_f32_e32 v86, v87, v86
	v_cmp_gt_f32_e32 vcc, v86, v50
	s_cbranch_vccz .LBB0_404
	v_max_f32_e32 v86, v86, v86
	v_max_f32_e32 v87, v50, v50
	v_max_f32_e32 v86, v87, v86
	v_sub_f32_e32 v50, v50, v86
	v_exp_f32_e32 v50, v50
	s_nop 0
	v_pk_mul_f32 v[32:33], v[32:33], v[50:51] op_sel_hi:[1,0]
	v_pk_mul_f32 v[30:31], v[30:31], v[50:51] op_sel_hi:[1,0]
	v_pk_mul_f32 v[28:29], v[28:29], v[50:51] op_sel_hi:[1,0]
	v_pk_mul_f32 v[26:27], v[26:27], v[50:51] op_sel_hi:[1,0]
	v_pk_mul_f32 v[24:25], v[24:25], v[50:51] op_sel_hi:[1,0]
	v_pk_mul_f32 v[22:23], v[22:23], v[50:51] op_sel_hi:[1,0]
	v_pk_mul_f32 v[20:21], v[20:21], v[50:51] op_sel_hi:[1,0]
	v_pk_mul_f32 v[18:19], v[18:19], v[50:51] op_sel_hi:[1,0]
	v_pk_mul_f32 v[16:17], v[16:17], v[50:51] op_sel_hi:[1,0]
	v_pk_mul_f32 v[14:15], v[14:15], v[50:51] op_sel_hi:[1,0]
	v_pk_mul_f32 v[12:13], v[12:13], v[50:51] op_sel_hi:[1,0]
	v_pk_mul_f32 v[10:11], v[10:11], v[50:51] op_sel_hi:[1,0]
	v_pk_mul_f32 v[8:9], v[8:9], v[50:51] op_sel_hi:[1,0]
	v_pk_mul_f32 v[6:7], v[6:7], v[50:51] op_sel_hi:[1,0]
	v_pk_mul_f32 v[4:5], v[4:5], v[50:51] op_sel_hi:[1,0]
	v_pk_mul_f32 v[2:3], v[2:3], v[50:51] op_sel_hi:[1,0]
	v_mul_f32_e32 v142, v142, v50
	v_mov_b32_e32 v50, v86
; #define LAS __attribute__((address_space(3)))
; template <int STAGE, int OFF> __device__ __forceinline__ void attn32_unit(const bf16* base, bf16* yrow0, int blk0, int u, LAS unsigned char* xtab, LAS unsigned char* kbuf, LAS unsigned char* vbuf, int lane, ...
;     ...
;         for (int c = 0; c < 4; ++c) { *(LAS v4u*)(kbuf + (8 * c + lrow) * 144 + lch * 16) = kr[set][c]; *(LAS v4u*)(vbuf + (8 * c + lrow) * 160 + lch * 16) = vr[set][c]; }
;         if (pp + 2 < 5) { ATT32_LOAD(set, pp + 2, t0, SH); }
;         else { const bf16* base_ = base; { const bf16* base = nbase; ATT32_LOAD(set, pp + 2 - 5, nt0, nsh); } (void)base_; }
;         f32x16 sc;
; #pragma unroll
;         for (int i = 0; i < 16; ++i) sc[i] = 0.f;
; #pragma unroll
;         for (int ks = 0; ks < 4; ++ks) { const bf16x8 ka = *(const LAS bf16x8*)(kbuf + qi * 144 + 32 * ks + 16 * h); sc = MFMA32(ka, qb[ks], sc); }
;         if (pp == 4) {
; #pragma unroll
;             for (int ks = 0; ks < 4; ++ks) qb[ks] = *(const bf16x8*)(nbase + (size_t)min(nt0 + (qi << nsh), SEQ - 1) * 1536 + 16 * ks + 8 * h);
;         }
;         const int mbase = n0 + 4 * h - lo; float mx = -INFINITY;
; #pragma unroll
;         for (int rg = 0; rg < 16; ++rg) { sc[rg] = ((unsigned)(mbase + (rg & 3) + 8 * (rg >> 2)) <= mspan) ? sc[rg] : -INFINITY; mx = fmaxf(mx, sc[rg]); }
;         mx = fmaxf(mx, __shfl_xor(mx, 32));
;         if (__any(mx > m)) {
;             const float mn = fmaxf(m, mx), alpha = __builtin_amdgcn_exp2f(m - mn); m = mn; l *= alpha;
; #pragma unroll
;             for (int i = 0; i < 16; ++i) { o[0][i] *= alpha; o[1][i] *= alpha; }
;         }
;         float ps = 0.f;
; #pragma unroll
;         for (int rg = 0; rg < 16; ++rg) { sc[rg] = __builtin_amdgcn_exp2f(sc[rg] - m); ps += sc[rg]; }
;         l += ps;
;         bf16x8 pb[2];
; #pragma unroll
;         for (int s2 = 0; s2 < 2; ++s2) { v4u w; w.x = pg8::cvt_pk_bf16(sc[8 * s2], sc[8 * s2 + 1]); w.y = pg8::cvt_pk_bf16(sc[8 * s2 + 2], sc[8 * s2 + 3]); w.z = pg8::cvt_pk_bf16(sc[8 * s2 + 4], sc[8 * s2 + 5]); w.w = pg8::cvt_pk_bf16(sc[8 * s2 + 6], sc[8 * s2 + 7]); pb[s2] = __builtin_bit_cast(bf16x8, w); }
; #pragma unroll
;         for (int mb = 0; mb < 2; ++mb)
; #pragma unroll
;             for (int s2 = 0; s2 < 2; ++s2) {
;                 LAS unsigned char* vp = vbuf + tr_off + (16 * s2) * 160 + 64 * mb;
.LBB0_404:
	v_sub_f32_e32 v34, v34, v50
	v_exp_f32_e32 v86, v34
	v_sub_f32_e32 v34, v35, v50
	v_exp_f32_e32 v87, v34
	v_sub_f32_e32 v34, v36, v50
	v_exp_f32_e32 v88, v34
	v_sub_f32_e32 v34, v37, v50
	v_exp_f32_e32 v89, v34
	v_sub_f32_e32 v34, v38, v50
	v_exp_f32_e32 v90, v34
	v_sub_f32_e32 v34, v39, v50
	v_exp_f32_e32 v91, v34
	v_sub_f32_e32 v34, v40, v50
	v_exp_f32_e32 v92, v34
	v_sub_f32_e32 v34, v41, v50
	v_exp_f32_e32 v93, v34
	v_sub_f32_e32 v34, v42, v50
	v_exp_f32_e32 v143, v34
	v_sub_f32_e32 v34, v43, v50
	v_exp_f32_e32 v154, v34
	v_sub_f32_e32 v34, v44, v50
	v_exp_f32_e32 v155, v34
	v_sub_f32_e32 v34, v45, v50
	v_exp_f32_e32 v156, v34
	v_sub_f32_e32 v34, v46, v50
	v_exp_f32_e32 v157, v34
	v_sub_f32_e32 v34, v47, v50
	v_exp_f32_e32 v158, v34
	v_sub_f32_e32 v34, v48, v50
	v_exp_f32_e32 v159, v34
	v_sub_f32_e32 v34, v49, v50
	v_exp_f32_e32 v160, v34
	v_cvt_pk_bf16_f32 v34, v86, v87
	v_cvt_pk_bf16_f32 v35, v88, v89
	v_cvt_pk_bf16_f32 v36, v90, v91
	v_cvt_pk_bf16_f32 v37, v92, v93
	v_cvt_pk_bf16_f32 v144, v143, v154
	v_cvt_pk_bf16_f32 v145, v155, v156
	v_cvt_pk_bf16_f32 v146, v157, v158
	v_cvt_pk_bf16_f32 v147, v159, v160
	ds_read_b64_tr_b16 v[38:39], v181 offset:4608
	ds_read_b64_tr_b16 v[40:41], v181 offset:5888
	v_add_u32_e32 v162, s10, v52
	v_min_i32_e32 v148, 0x3fff, v162
	s_waitcnt lgkmcnt(0)
	v_mfma_f32_32x32x16_bf16 v[18:33], v[38:41], v[34:37], v[18:33]
	v_mul_u32_u24_e32 v38, 0xc00, v148
	v_mov_b32_e32 v39, v169
	v_lshl_add_u64 v[38:39], s[8:9], 0, v[38:39]
	ds_read_b64_tr_b16 v[42:43], v181 offset:7168
	ds_read_b64_tr_b16 v[44:45], v181 offset:8448
	ds_read_b64_tr_b16 v[48:49], v181 offset:5952
	ds_read_b64_tr_b16 v[46:47], v181 offset:4672
	v_lshl_add_u64 v[152:153], v[38:39], 0, v[168:169]
	v_add_f32_e32 v38, 0, v86
	v_add_f32_e32 v38, v87, v38
	v_add_f32_e32 v38, v88, v38
	v_add_f32_e32 v38, v89, v38
	v_add_f32_e32 v38, v90, v38
	v_add_f32_e32 v38, v91, v38
	s_waitcnt lgkmcnt(0)
	v_mfma_f32_32x32x16_bf16 v[2:17], v[46:49], v[34:37], v[2:17]
	v_add_u32_e32 v34, s10, v213
	ds_read_b64_tr_b16 v[150:151], v181 offset:8512
	ds_read_b64_tr_b16 v[148:149], v181 offset:7232
	v_add_f32_e32 v38, v92, v38
	s_waitcnt vmcnt(15)
	ds_write_b128 v231, v[54:57]
	s_waitcnt vmcnt(14)
	ds_write_b128 v232, v[74:77] offset:4608
	s_waitcnt vmcnt(13)
	ds_write_b128 v231, v[78:81] offset:1152
	s_waitcnt vmcnt(12)
	ds_write_b128 v232, v[82:85] offset:5888
	s_waitcnt vmcnt(11)
	ds_write_b128 v231, v[94:97] offset:2304
	s_waitcnt vmcnt(10)
	ds_write_b128 v232, v[98:101] offset:7168
	s_waitcnt vmcnt(9)
	ds_write_b128 v231, v[102:105] offset:3456
	s_waitcnt vmcnt(8)
	ds_write_b128 v232, v[138:141] offset:8448
	v_med3_i32 v34, v34, 0, v233
	v_add_f32_e32 v161, v93, v38
	v_mul_u32_u24_e32 v38, 0xc00, v34
	ds_read_b128 v[34:37], v177
	v_or_b32_e32 v38, v38, v176
	global_load_dwordx4 v[74:77], v38, s[8:9] offset:1024
	global_load_dwordx4 v[78:81], v38, s[8:9] offset:2048
	v_add_u32_e32 v38, s10, v214
	v_med3_i32 v38, v38, 0, v233
	v_mul_u32_u24_e32 v38, 0xc00, v38
	ds_read_b128 v[54:57], v177 offset:32
	v_mfma_f32_32x32x16_bf16 v[18:33], v[42:45], v[144:147], v[18:33]
	v_or_b32_e32 v86, v38, v176
	global_load_dwordx4 v[82:85], v86, s[8:9] offset:1024
	s_nop 0
	global_load_dwordx4 v[86:89], v86, s[8:9] offset:2048
	v_add_f32_e32 v143, v143, v161
	v_add_f32_e32 v143, v154, v143
	v_add_f32_e32 v143, v155, v143
	v_add_f32_e32 v143, v156, v143
	v_add_f32_e32 v143, v157, v143
	s_waitcnt lgkmcnt(1)
	v_mfma_f32_32x32x16_bf16 v[34:49], v[34:37], v[70:73], 0
	v_add_u32_e32 v70, s10, v215
	v_med3_i32 v70, v70, 0, v233
	v_mul_u32_u24_e32 v70, 0xc00, v70
	v_or_b32_e32 v94, v70, v176
	ds_read_b128 v[138:141], v177 offset:96
	ds_read_b128 v[70:73], v177 offset:64
	global_load_dwordx4 v[90:93], v94, s[8:9] offset:1024
	s_nop 0
	global_load_dwordx4 v[94:97], v94, s[8:9] offset:2048
	v_add_f32_e32 v143, v158, v143
	s_waitcnt lgkmcnt(2)
	v_mfma_f32_32x32x16_bf16 v[34:49], v[54:57], v[66:69], v[34:49]
	v_add_u32_e32 v54, s10, v216
	v_med3_i32 v54, v54, 0, v233
	v_mul_u32_u24_e32 v54, 0xc00, v54
	v_or_b32_e32 v54, v54, v176
	global_load_dwordx4 v[98:101], v54, s[8:9] offset:1024
	global_load_dwordx4 v[102:105], v54, s[8:9] offset:2048
	v_add_f32_e32 v143, v159, v143
	s_waitcnt lgkmcnt(0)
	v_mfma_f32_32x32x16_bf16 v[34:49], v[70:73], v[62:65], v[34:49]
	global_load_dwordx4 v[70:73], v[152:153], off
	global_load_dwordx4 v[62:65], v[152:153], off offset:32
	global_load_dwordx4 v[54:57], v[152:153], off offset:64
	global_load_dwordx4 v[66:69], v[152:153], off offset:96
	v_mfma_f32_32x32x16_bf16 v[34:49], v[138:141], v[58:61], v[34:49]
	v_add_u32_e32 v58, 0x80, v164
	v_cmp_le_u32_e32 vcc, v58, v163
	v_add_u32_e32 v59, 0x82, v164
	v_mfma_f32_32x32x16_bf16 v[2:17], v[148:151], v[144:147], v[2:17]
	s_nop 7
	v_cndmask_b32_e32 v58, v234, v34, vcc
	v_add_u32_e32 v34, 0x81, v164
	v_cmp_le_u32_e32 vcc, v34, v163
	s_nop 1
	v_cndmask_b32_e32 v35, v234, v35, vcc
	v_cmp_le_u32_e32 vcc, v59, v163
	v_add_u32_e32 v59, 0x83, v164
	v_max3_f32 v34, v58, s31, v35
	v_cndmask_b32_e32 v36, v234, v36, vcc
	v_cmp_le_u32_e32 vcc, v59, v163
	v_add_u32_e32 v59, 0x88, v164
	s_nop 0
	v_cndmask_b32_e32 v37, v234, v37, vcc
	v_cmp_le_u32_e32 vcc, v59, v163
	v_add_u32_e32 v59, 0x89, v164
	v_max3_f32 v34, v34, v36, v37
	v_cndmask_b32_e32 v38, v234, v38, vcc
	v_cmp_le_u32_e32 vcc, v59, v163
	v_add_u32_e32 v59, 0x8a, v164
	s_nop 0
	v_cndmask_b32_e32 v39, v234, v39, vcc
	v_cmp_le_u32_e32 vcc, v59, v163
	v_add_u32_e32 v59, 0x8b, v164
	v_max3_f32 v34, v34, v38, v39
	v_cndmask_b32_e32 v40, v234, v40, vcc
	v_cmp_le_u32_e32 vcc, v59, v163
	v_add_u32_e32 v59, 0x90, v164
	s_nop 0
	v_cndmask_b32_e32 v41, v234, v41, vcc
	v_cmp_le_u32_e32 vcc, v59, v163
	v_add_u32_e32 v59, 0x91, v164
	v_max3_f32 v34, v34, v40, v41
	v_cndmask_b32_e32 v42, v234, v42, vcc
	v_cmp_le_u32_e32 vcc, v59, v163
	v_add_u32_e32 v59, 0x92, v164
	s_nop 0
	v_cndmask_b32_e32 v43, v234, v43, vcc
	v_cmp_le_u32_e32 vcc, v59, v163
	v_add_u32_e32 v59, 0x93, v164
	v_max3_f32 v34, v34, v42, v43
	v_cndmask_b32_e32 v44, v234, v44, vcc
	v_cmp_le_u32_e32 vcc, v59, v163
	v_add_u32_e32 v59, 0x98, v164
	s_nop 0
	v_cndmask_b32_e32 v45, v234, v45, vcc
	v_cmp_le_u32_e32 vcc, v59, v163
	v_add_u32_e32 v59, 0x99, v164
	v_max3_f32 v34, v34, v44, v45
	v_cndmask_b32_e32 v46, v234, v46, vcc
	v_cmp_le_u32_e32 vcc, v59, v163
	v_add_u32_e32 v59, 0x9a, v164
	s_nop 0
	v_cndmask_b32_e32 v47, v234, v47, vcc
	v_cmp_le_u32_e32 vcc, v59, v163
	v_add_u32_e32 v59, 0x9b, v164
	v_max3_f32 v34, v34, v46, v47
	v_cndmask_b32_e32 v48, v234, v48, vcc
	v_cmp_le_u32_e32 vcc, v59, v163
	s_nop 1
	v_cndmask_b32_e32 v49, v234, v49, vcc
	v_max3_f32 v59, v34, v48, v49
	v_mov_b32_e32 v60, v59
	s_nop 1
	v_permlane32_swap_b32_e32 v60, v59
	v_add_f32_e32 v34, v160, v143
	v_add_f32_e32 v34, v142, v34
	s_waitcnt lgkmcnt(0)
	v_max_f32_e32 v60, v60, v60
	v_max_f32_e32 v59, v59, v60
	v_cmp_gt_f32_e32 vcc, v59, v50
	s_cbranch_vccz .LBB0_406
; __device__ __forceinline__ unsigned cvt_pk_bf16(float lo, float hi) { unsigned r; asm volatile("v_cvt_pk_bf16_f32 %0, %1, %2" : "=v"(r) : "v"(lo), "v"(hi)); return r; }
; #define LAS __attribute__((address_space(3)))
; __device__ __forceinline__ unsigned pk2(float lo, float hi) { return f2bf(lo) | (f2bf(hi) << 16); }
; #define MFMA32(a, b, c) __builtin_amdgcn_mfma_f32_32x32x16_bf16((a), (b), (c), 0, 0, 0)
; template <int STAGE, int OFF> __device__ __forceinline__ void attn32_unit(const bf16* base, bf16* yrow0, int blk0, int u, LAS unsigned char* xtab, LAS unsigned char* kbuf, LAS unsigned char* vbuf, int lane, ...
;     ...
;         if (__any(mx > m)) {
;             const float mn = fmaxf(m, mx), alpha = __builtin_amdgcn_exp2f(m - mn); m = mn; l *= alpha;
; #pragma unroll
;             for (int i = 0; i < 16; ++i) { o[0][i] *= alpha; o[1][i] *= alpha; }
;         }
;         float ps = 0.f;
; #pragma unroll
;         for (int rg = 0; rg < 16; ++rg) { sc[rg] = __builtin_amdgcn_exp2f(sc[rg] - m); ps += sc[rg]; }
;         l += ps;
;         bf16x8 pb[2];
; #pragma unroll
;         for (int s2 = 0; s2 < 2; ++s2) { v4u w; w.x = pg8::cvt_pk_bf16(sc[8 * s2], sc[8 * s2 + 1]); w.y = pg8::cvt_pk_bf16(sc[8 * s2 + 2], sc[8 * s2 + 3]); w.z = pg8::cvt_pk_bf16(sc[8 * s2 + 4], sc[8 * s2 + 5]); w.w = pg8::cvt_pk_bf16(sc[8 * s2 + 6], sc[8 * s2 + 7]); pb[s2] = __builtin_bit_cast(bf16x8, w); }
; #pragma unroll
;         for (int mb = 0; mb < 2; ++mb)
; #pragma unroll
;             for (int s2 = 0; s2 < 2; ++s2) {
;                 LAS unsigned char* vp = vbuf + tr_off + (16 * s2) * 160 + 64 * mb;
;                 const v4i16 a0 = __builtin_amdgcn_ds_read_tr16_b64_v4i16((LAS v4i16*)vp), a1 = __builtin_amdgcn_ds_read_tr16_b64_v4i16((LAS v4i16*)(vp + 8 * 160));
;                 const bf16x8 va = __builtin_shufflevector(a0, a1, 0, 1, 2, 3, 4, 5, 6, 7);
;                 o[mb] = MFMA32(va, pb[s2], o[mb]);
;             }
;         asm volatile("" ::: "memory");
;     }
;     l += __shfl_xor(l, 32);
;     if (STAGE < 2) {
; #pragma unroll
;         for (int mb = 0; mb < 2; ++mb)
; #pragma unroll
;             for (int gq = 0; gq < 4; ++gq) { v2u w; w.x = pk2(o[mb][4 * gq], o[mb][4 * gq + 1]); w.y = pk2(o[mb][4 * gq + 2], o[mb][4 * gq + 3]); *(LAS v2u*)(xrow + 2 * (32 * mb + 8 * gq + 4 * h)) = w; }
;         if (h == 0) { *(LAS float*)(xrow + 128) = m; *(LAS float*)(xrow + 132) = l; }
	v_max_f32_e32 v59, v59, v59
	v_max_f32_e32 v60, v50, v50
	v_max_f32_e32 v59, v60, v59
	v_sub_f32_e32 v50, v50, v59
	v_exp_f32_e32 v50, v50
	s_nop 0
	v_pk_mul_f32 v[32:33], v[32:33], v[50:51] op_sel_hi:[1,0]
	v_pk_mul_f32 v[30:31], v[30:31], v[50:51] op_sel_hi:[1,0]
	v_pk_mul_f32 v[28:29], v[28:29], v[50:51] op_sel_hi:[1,0]
	v_pk_mul_f32 v[26:27], v[26:27], v[50:51] op_sel_hi:[1,0]
	v_pk_mul_f32 v[24:25], v[24:25], v[50:51] op_sel_hi:[1,0]
	v_pk_mul_f32 v[22:23], v[22:23], v[50:51] op_sel_hi:[1,0]
	v_pk_mul_f32 v[20:21], v[20:21], v[50:51] op_sel_hi:[1,0]
	v_pk_mul_f32 v[18:19], v[18:19], v[50:51] op_sel_hi:[1,0]
	v_pk_mul_f32 v[16:17], v[16:17], v[50:51] op_sel_hi:[1,0]
	v_pk_mul_f32 v[14:15], v[14:15], v[50:51] op_sel_hi:[1,0]
	v_pk_mul_f32 v[12:13], v[12:13], v[50:51] op_sel_hi:[1,0]
	v_pk_mul_f32 v[10:11], v[10:11], v[50:51] op_sel_hi:[1,0]
	v_pk_mul_f32 v[8:9], v[8:9], v[50:51] op_sel_hi:[1,0]
	v_pk_mul_f32 v[6:7], v[6:7], v[50:51] op_sel_hi:[1,0]
	v_pk_mul_f32 v[4:5], v[4:5], v[50:51] op_sel_hi:[1,0]
	v_pk_mul_f32 v[2:3], v[2:3], v[50:51] op_sel_hi:[1,0]
	v_mul_f32_e32 v34, v34, v50
	v_mov_b32_e32 v50, v59
.LBB0_406:
	v_sub_f32_e32 v36, v36, v50
	v_exp_f32_e32 v142, v36
	v_sub_f32_e32 v36, v37, v50
	v_exp_f32_e32 v143, v36
	v_sub_f32_e32 v36, v38, v50
	v_exp_f32_e32 v144, v36
	v_sub_f32_e32 v36, v39, v50
	v_exp_f32_e32 v145, v36
	v_sub_f32_e32 v36, v40, v50
	v_exp_f32_e32 v146, v36
	v_sub_f32_e32 v36, v41, v50
	v_exp_f32_e32 v147, v36
	v_sub_f32_e32 v36, v42, v50
	v_exp_f32_e32 v148, v36
	v_sub_f32_e32 v36, v43, v50
	v_exp_f32_e32 v149, v36
	v_sub_f32_e32 v36, v44, v50
	v_exp_f32_e32 v150, v36
	v_sub_f32_e32 v36, v45, v50
	v_exp_f32_e32 v151, v36
	v_sub_f32_e32 v36, v46, v50
	v_exp_f32_e32 v152, v36
	v_sub_f32_e32 v36, v47, v50
	v_exp_f32_e32 v153, v36
	v_sub_f32_e32 v36, v48, v50
	v_sub_f32_e32 v58, v58, v50
	v_sub_f32_e32 v35, v35, v50
	v_exp_f32_e32 v48, v36
	v_sub_f32_e32 v36, v49, v50
	v_exp_f32_e32 v138, v58
	v_exp_f32_e32 v35, v35
	v_exp_f32_e32 v49, v36
	v_cvt_pk_bf16_f32 v36, v138, v35
	v_cvt_pk_bf16_f32 v37, v142, v143
	v_cvt_pk_bf16_f32 v38, v144, v145
	v_cvt_pk_bf16_f32 v39, v146, v147
	v_cvt_pk_bf16_f32 v40, v148, v149
	v_cvt_pk_bf16_f32 v41, v150, v151
	v_cvt_pk_bf16_f32 v42, v152, v153
	v_cvt_pk_bf16_f32 v43, v48, v49
	ds_read_b64_tr_b16 v[44:45], v181 offset:4608
	ds_read_b64_tr_b16 v[46:47], v181 offset:5888
	ds_read_b64_tr_b16 v[60:61], v181 offset:5952
	ds_read_b64_tr_b16 v[58:59], v181 offset:4672
	s_waitcnt lgkmcnt(2)
	v_mfma_f32_32x32x16_bf16 v[18:33], v[44:47], v[36:39], v[18:33]
	ds_read_b64_tr_b16 v[44:45], v181 offset:7168
	ds_read_b64_tr_b16 v[46:47], v181 offset:8448
	v_add_f32_e32 v138, 0, v138
	v_add_f32_e32 v35, v35, v138
	ds_read_b64_tr_b16 v[140:141], v181 offset:8512
	ds_read_b64_tr_b16 v[138:139], v181 offset:7232
	v_add_f32_e32 v35, v142, v35
	v_add_f32_e32 v35, v143, v35
	s_waitcnt lgkmcnt(2)
	v_mfma_f32_32x32x16_bf16 v[18:33], v[44:47], v[40:43], v[18:33]
	v_add_f32_e32 v35, v144, v35
	v_add_f32_e32 v35, v145, v35
	v_add_f32_e32 v35, v146, v35
	v_add_f32_e32 v35, v147, v35
	v_add_f32_e32 v35, v148, v35
	v_add_f32_e32 v35, v149, v35
	v_add_f32_e32 v35, v150, v35
	v_mfma_f32_32x32x16_bf16 v[2:17], v[58:61], v[36:39], v[2:17]
	s_nop 3
	v_bfe_u32 v36, v18, 16, 1
	v_add3_u32 v18, v18, v36, s35
	v_bfe_u32 v36, v19, 16, 1
	v_lshrrev_b32_e32 v18, 16, v18
	v_add3_u32 v19, v19, v36, s35
	v_and_or_b32 v18, v19, s36, v18
	v_bfe_u32 v19, v20, 16, 1
	v_add3_u32 v19, v20, v19, s35
	v_bfe_u32 v20, v21, 16, 1
	v_lshrrev_b32_e32 v19, 16, v19
	v_add3_u32 v20, v21, v20, s35
	v_and_or_b32 v19, v20, s36, v19
	v_bfe_u32 v20, v22, 16, 1
	v_add3_u32 v20, v22, v20, s35
	v_bfe_u32 v21, v23, 16, 1
	v_lshrrev_b32_e32 v20, 16, v20
	v_add3_u32 v21, v23, v21, s35
	v_and_or_b32 v20, v21, s36, v20
	v_bfe_u32 v21, v24, 16, 1
	v_add3_u32 v21, v24, v21, s35
	v_bfe_u32 v22, v25, 16, 1
	v_lshrrev_b32_e32 v21, 16, v21
	v_add3_u32 v22, v25, v22, s35
	v_and_or_b32 v21, v22, s36, v21
	ds_write2_b64 v51, v[18:19], v[20:21] offset1:2
	v_bfe_u32 v18, v26, 16, 1
	v_add3_u32 v18, v26, v18, s35
	v_bfe_u32 v19, v27, 16, 1
	v_lshrrev_b32_e32 v18, 16, v18
	v_add3_u32 v19, v27, v19, s35
	v_and_or_b32 v18, v19, s36, v18
	v_bfe_u32 v19, v28, 16, 1
	v_add3_u32 v19, v28, v19, s35
	v_bfe_u32 v20, v29, 16, 1
	s_waitcnt lgkmcnt(1)
	v_mfma_f32_32x32x16_bf16 v[2:17], v[138:141], v[40:43], v[2:17]
	v_lshrrev_b32_e32 v19, 16, v19
	v_add3_u32 v20, v29, v20, s35
	v_and_or_b32 v19, v20, s36, v19
	v_bfe_u32 v20, v30, 16, 1
	v_add3_u32 v20, v30, v20, s35
	v_bfe_u32 v21, v31, 16, 1
	v_lshrrev_b32_e32 v20, 16, v20
	v_add3_u32 v21, v31, v21, s35
	v_and_or_b32 v20, v21, s36, v20
	v_bfe_u32 v21, v32, 16, 1
	v_add3_u32 v21, v32, v21, s35
	v_bfe_u32 v22, v33, 16, 1
	v_lshrrev_b32_e32 v21, 16, v21
	v_add3_u32 v22, v33, v22, s35
	v_and_or_b32 v21, v22, s36, v21
	ds_write2_b64 v51, v[18:19], v[20:21] offset0:4 offset1:6
	v_bfe_u32 v18, v2, 16, 1
	v_add3_u32 v2, v2, v18, s35
	v_bfe_u32 v18, v3, 16, 1
	v_lshrrev_b32_e32 v2, 16, v2
	v_add3_u32 v3, v3, v18, s35
	v_and_or_b32 v2, v3, s36, v2
	v_bfe_u32 v3, v4, 16, 1
	v_add3_u32 v3, v4, v3, s35
	v_bfe_u32 v4, v5, 16, 1
	v_lshrrev_b32_e32 v3, 16, v3
	v_add3_u32 v4, v5, v4, s35
	v_and_or_b32 v3, v4, s36, v3
	v_bfe_u32 v4, v6, 16, 1
	v_add3_u32 v4, v6, v4, s35
	v_bfe_u32 v5, v7, 16, 1
	v_lshrrev_b32_e32 v4, 16, v4
	v_add3_u32 v5, v7, v5, s35
	v_and_or_b32 v4, v5, s36, v4
	v_bfe_u32 v5, v8, 16, 1
	v_add3_u32 v5, v8, v5, s35
	v_bfe_u32 v6, v9, 16, 1
	v_lshrrev_b32_e32 v5, 16, v5
	v_add3_u32 v6, v9, v6, s35
	v_and_or_b32 v5, v6, s36, v5
	ds_write2_b64 v51, v[2:3], v[4:5] offset0:8 offset1:10
	v_bfe_u32 v2, v10, 16, 1
	v_add3_u32 v2, v10, v2, s35
	v_bfe_u32 v3, v11, 16, 1
	v_add_f32_e32 v35, v151, v35
	v_lshrrev_b32_e32 v2, 16, v2
	v_add3_u32 v3, v11, v3, s35
	v_add_f32_e32 v35, v152, v35
	v_and_or_b32 v2, v3, s36, v2
	v_bfe_u32 v3, v12, 16, 1
	v_add_f32_e32 v35, v153, v35
	v_add3_u32 v3, v12, v3, s35
	v_bfe_u32 v4, v13, 16, 1
	v_add_f32_e32 v35, v48, v35
	v_lshrrev_b32_e32 v3, 16, v3
	v_add3_u32 v4, v13, v4, s35
	v_add_f32_e32 v35, v49, v35
	v_and_or_b32 v3, v4, s36, v3
	v_bfe_u32 v4, v14, 16, 1
	v_add_f32_e32 v34, v34, v35
	v_add3_u32 v4, v14, v4, s35
	v_bfe_u32 v5, v15, 16, 1
	v_mov_b32_e32 v35, v34
	s_nop 1
	v_permlane32_swap_b32_e32 v35, v34
	v_lshrrev_b32_e32 v4, 16, v4
	v_add3_u32 v5, v15, v5, s35
	v_and_or_b32 v4, v5, s36, v4
	v_bfe_u32 v5, v16, 16, 1
	v_add3_u32 v5, v16, v5, s35
	v_bfe_u32 v6, v17, 16, 1
	v_lshrrev_b32_e32 v5, 16, v5
	v_add3_u32 v6, v17, v6, s35
	v_and_or_b32 v5, v6, s36, v5
	ds_write2_b64 v51, v[2:3], v[4:5] offset0:12 offset1:14
	s_and_saveexec_b64 s[14:15], s[4:5]
	s_cbranch_execz .LBB0_408
	s_waitcnt lgkmcnt(1)
	v_add_f32_e32 v51, v34, v35
	ds_write_b64 v206, v[50:51] offset:128
; __device__ __forceinline__ float bf_lo(unsigned w) { return __uint_as_float(w << 16); }
; template <int STAGE, int OFF> __device__ __forceinline__ void attn32_unit(const bf16* base, bf16* yrow0, int blk0, int u, LAS unsigned char* xtab, LAS unsigned char* kbuf, LAS unsigned char* vbuf, int lane, ...
;     ...
;     } else {
; #pragma unroll
;         for (int mb = 0; mb < 2; ++mb)
; #pragma unroll
;             for (int gq = 0; gq < 4; ++gq) { const v2u w = *(const LAS v2u*)(xrow + 2 * (32 * mb + 8 * gq + 4 * h)); o[mb][4 * gq] = bf_lo(w.x); o[mb][4 * gq + 1] = bf_hi(w.x); o[mb][4 * gq + 2] = bf_lo(w.y); o[mb][4 * gq + 3] = bf_hi(w.y); }
;         m = *(const LAS float*)(xrow + 128); l = h == 0 ? *(const LAS float*)(xrow + 132) : 0.f;
;     }
;     const int hi = qi, lo = max(qi - 128, -(t0 >> SH));
;     const unsigned mspan = (unsigned)(hi - lo);
; #pragma unroll
;     for (int pp = 0; pp < 5; ++pp) {
;         constexpr int dummy = 0; (void)dummy;
;         const int set = (pp + OFF) % 2, n0 = -128 + 32 * pp;
; #pragma unroll
;         for (int c = 0; c < 4; ++c) { *(LAS v4u*)(kbuf + (8 * c + lrow) * 144 + lch * 16) = kr[set][c]; *(LAS v4u*)(vbuf + (8 * c + lrow) * 160 + lch * 16) = vr[set][c]; }
;         if (pp + 2 < 5) { ATT32_LOAD(set, pp + 2, t0, SH); }
;         else { const bf16* base_ = base; { const bf16* base = nbase; ATT32_LOAD(set, pp + 2 - 5, nt0, nsh); } (void)base_; }
;         f32x16 sc;
; #pragma unroll
;         for (int i = 0; i < 16; ++i) sc[i] = 0.f;
; #pragma unroll
;         for (int ks = 0; ks < 4; ++ks) { const bf16x8 ka = *(const LAS bf16x8*)(kbuf + qi * 144 + 32 * ks + 16 * h); sc = MFMA32(ka, qb[ks], sc); }
;         if (pp == 4) {
; #pragma unroll
;             for (int ks = 0; ks < 4; ++ks) qb[ks] = *(const bf16x8*)(nbase + (size_t)min(nt0 + (qi << nsh), SEQ - 1) * 1536 + 16 * ks + 8 * h);
;         }
;         const int mbase = n0 + 4 * h - lo; float mx = -INFINITY;
; #pragma unroll
;         for (int rg = 0; rg < 16; ++rg) { sc[rg] = ((unsigned)(mbase + (rg & 3) + 8 * (rg >> 2)) <= mspan) ? sc[rg] : -INFINITY; mx = fmaxf(mx, sc[rg]); }
;         mx = fmaxf(mx, __shfl_xor(mx, 32));
;         if (__any(mx > m)) {
;             const float mn = fmaxf(m, mx), alpha = __builtin_amdgcn_exp2f(m - mn); m = mn; l *= alpha;
; #pragma unroll
;             for (int i = 0; i < 16; ++i) { o[0][i] *= alpha; o[1][i] *= alpha; }
;         }
.LBB0_408:
	s_or_b64 exec, exec, s[14:15]
	v_add_u32_e32 v14, v217, v166
	s_waitcnt lgkmcnt(0)
	s_barrier
	ds_read2_b64 v[10:13], v14 offset1:2
	ds_read2_b64 v[2:5], v14 offset0:4 offset1:6
	ds_read2_b64 v[6:9], v14 offset0:8 offset1:10
	ds_read2_b64 v[14:17], v14 offset0:12 offset1:14
	ds_read_b32 v164, v217 offset:128
	v_mov_b32_e32 v50, 0
	s_and_saveexec_b64 s[14:15], s[4:5]
	ds_read_b32 v50, v217 offset:132
	s_or_b64 exec, exec, s[14:15]
	s_waitcnt vmcnt(19)
	ds_write_b128 v231, v[106:109]
	s_waitcnt vmcnt(18)
	ds_write_b128 v232, v[110:113] offset:4608
	s_waitcnt vmcnt(17)
	ds_write_b128 v231, v[114:117] offset:1152
	s_waitcnt vmcnt(16)
	ds_write_b128 v232, v[118:121] offset:5888
	s_waitcnt vmcnt(15)
	ds_write_b128 v231, v[122:125] offset:2304
	s_waitcnt vmcnt(14)
	ds_write_b128 v232, v[126:129] offset:7168
	s_waitcnt vmcnt(13)
	ds_write_b128 v231, v[130:133] offset:3456
	s_waitcnt vmcnt(12)
	ds_write_b128 v232, v[134:137] offset:8448
	ds_read_b128 v[34:37], v177
	s_waitcnt lgkmcnt(13)
	v_lshlrev_b32_e32 v22, 16, v12
	v_and_b32_e32 v23, 0xffff0000, v12
	v_add_u32_e32 v12, s10, v218
	v_med3_i32 v12, v12, 0, v233
	v_mul_u32_u24_e32 v12, 0xc00, v12
	v_or_b32_e32 v12, v12, v176
	global_load_dwordx4 v[58:61], v12, s[8:9] offset:1024
	global_load_dwordx4 v[106:109], v12, s[8:9] offset:2048
	ds_read_b128 v[118:121], v177 offset:32
	v_add_u32_e32 v12, s10, v219
	s_waitcnt vmcnt(5) lgkmcnt(1)
	v_mfma_f32_32x32x16_bf16 v[34:49], v[34:37], v[70:73], 0
	v_med3_i32 v12, v12, 0, v233
	v_mul_u32_u24_e32 v12, 0xc00, v12
	v_or_b32_e32 v12, v12, v176
	global_load_dwordx4 v[110:113], v12, s[8:9] offset:1024
	global_load_dwordx4 v[114:117], v12, s[8:9] offset:2048
	v_add_u32_e32 v12, s10, v220
	v_med3_i32 v12, v12, 0, v233
	v_mul_u32_u24_e32 v12, 0xc00, v12
	v_or_b32_e32 v12, v12, v176
	ds_read_b128 v[134:137], v177 offset:96
	ds_read_b128 v[138:141], v177 offset:64
	s_waitcnt vmcnt(6) lgkmcnt(2)
	v_mfma_f32_32x32x16_bf16 v[34:49], v[118:121], v[62:65], v[34:49]
	global_load_dwordx4 v[118:121], v12, s[8:9] offset:1024
	global_load_dwordx4 v[122:125], v12, s[8:9] offset:2048
	v_add_u32_e32 v12, s10, v221
	v_med3_i32 v12, v12, 0, v233
	v_mul_u32_u24_e32 v12, 0xc00, v12
	v_or_b32_e32 v12, v12, v176
	global_load_dwordx4 v[126:129], v12, s[8:9] offset:1024
	global_load_dwordx4 v[130:133], v12, s[8:9] offset:2048
	s_lshr_b32 s0, s10, 4
	s_waitcnt vmcnt(9) lgkmcnt(0)
	v_mfma_f32_32x32x16_bf16 v[34:49], v[138:141], v[54:57], v[34:49]
	s_sub_i32 s0, 0, s0
	v_lshlrev_b32_e32 v18, 16, v10
	v_and_b32_e32 v19, 0xffff0000, v10
	v_lshlrev_b32_e32 v20, 16, v11
	v_and_b32_e32 v21, 0xffff0000, v11
	v_lshlrev_b32_e32 v10, 16, v14
	v_and_b32_e32 v11, 0xffff0000, v14
	s_waitcnt vmcnt(8)
	v_mfma_f32_32x32x16_bf16 v[34:49], v[134:137], v[66:69], v[34:49]
	v_max_i32_e32 v14, s0, v175
	v_sub_u32_e32 v51, v1, v14
	v_sub_u32_e32 v163, v178, v14
	v_cmp_le_u32_e32 vcc, v163, v51
	v_add_u32_e32 v14, 1, v163
	v_lshlrev_b32_e32 v24, 16, v13
	v_and_b32_e32 v25, 0xffff0000, v13
	v_lshlrev_b32_e32 v12, 16, v15
	v_and_b32_e32 v13, 0xffff0000, v15
	s_nop 2
	v_cndmask_b32_e32 v34, v234, v34, vcc
	v_cmp_le_u32_e32 vcc, v14, v51
	v_add_u32_e32 v15, 2, v163
	v_lshlrev_b32_e32 v26, 16, v2
	v_cndmask_b32_e32 v35, v234, v35, vcc
	v_cmp_le_u32_e32 vcc, v15, v51
	v_add_u32_e32 v15, 3, v163
	v_max3_f32 v14, v34, s31, v35
	v_cndmask_b32_e32 v36, v234, v36, vcc
	v_cmp_le_u32_e32 vcc, v15, v51
	v_add_u32_e32 v15, 8, v163
	v_and_b32_e32 v27, 0xffff0000, v2
	v_cndmask_b32_e32 v37, v234, v37, vcc
	v_cmp_le_u32_e32 vcc, v15, v51
	v_add_u32_e32 v15, 9, v163
	v_max3_f32 v14, v14, v36, v37
	v_cndmask_b32_e32 v38, v234, v38, vcc
	v_cmp_le_u32_e32 vcc, v15, v51
	v_add_u32_e32 v15, 10, v163
	v_lshlrev_b32_e32 v28, 16, v3
	v_cndmask_b32_e32 v39, v234, v39, vcc
	v_cmp_le_u32_e32 vcc, v15, v51
	v_add_u32_e32 v15, 11, v163
	v_max3_f32 v14, v14, v38, v39
	v_cndmask_b32_e32 v40, v234, v40, vcc
	v_cmp_le_u32_e32 vcc, v15, v51
	v_add_u32_e32 v15, 16, v163
	v_and_b32_e32 v29, 0xffff0000, v3
	v_cndmask_b32_e32 v41, v234, v41, vcc
	v_cmp_le_u32_e32 vcc, v15, v51
	v_add_u32_e32 v15, 17, v163
	v_max3_f32 v14, v14, v40, v41
	v_cndmask_b32_e32 v42, v234, v42, vcc
	v_cmp_le_u32_e32 vcc, v15, v51
	v_add_u32_e32 v15, 18, v163
	v_lshlrev_b32_e32 v30, 16, v4
	v_cndmask_b32_e32 v43, v234, v43, vcc
	v_cmp_le_u32_e32 vcc, v15, v51
	v_add_u32_e32 v15, 19, v163
	v_max3_f32 v14, v14, v42, v43
	v_cndmask_b32_e32 v44, v234, v44, vcc
	v_cmp_le_u32_e32 vcc, v15, v51
	v_add_u32_e32 v15, 24, v163
	v_and_b32_e32 v31, 0xffff0000, v4
	v_cndmask_b32_e32 v45, v234, v45, vcc
	v_cmp_le_u32_e32 vcc, v15, v51
	v_add_u32_e32 v15, 25, v163
	v_max3_f32 v14, v14, v44, v45
	v_cndmask_b32_e32 v46, v234, v46, vcc
	v_cmp_le_u32_e32 vcc, v15, v51
	v_add_u32_e32 v15, 26, v163
	v_lshlrev_b32_e32 v32, 16, v5
	v_cndmask_b32_e32 v47, v234, v47, vcc
	v_cmp_le_u32_e32 vcc, v15, v51
	v_add_u32_e32 v15, 27, v163
	v_max3_f32 v14, v14, v46, v47
	v_cndmask_b32_e32 v48, v234, v48, vcc
	v_cmp_le_u32_e32 vcc, v15, v51
	v_and_b32_e32 v33, 0xffff0000, v5
	v_lshlrev_b32_e32 v2, 16, v6
	v_cndmask_b32_e32 v49, v234, v49, vcc
	v_max3_f32 v134, v14, v48, v49
	v_mov_b32_e32 v135, v134
	s_nop 1
	v_permlane32_swap_b32_e32 v135, v134
	v_and_b32_e32 v3, 0xffff0000, v6
	v_lshlrev_b32_e32 v4, 16, v7
	v_and_b32_e32 v5, 0xffff0000, v7
	v_lshlrev_b32_e32 v6, 16, v8
	s_waitcnt lgkmcnt(0)
	v_max_f32_e32 v135, v135, v135
	v_max_f32_e32 v134, v134, v135
	v_and_b32_e32 v7, 0xffff0000, v8
	v_lshlrev_b32_e32 v8, 16, v9
	v_and_b32_e32 v9, 0xffff0000, v9
	v_lshlrev_b32_e32 v14, 16, v16
	v_and_b32_e32 v15, 0xffff0000, v16
	v_lshlrev_b32_e32 v16, 16, v17
	v_and_b32_e32 v17, 0xffff0000, v17
	v_cmp_gt_f32_e32 vcc, v134, v164
	s_cbranch_vccz .LBB0_412
	v_max_f32_e32 v134, v134, v134
	v_max_f32_e32 v135, v164, v164
	v_max_f32_e32 v135, v135, v134
	v_sub_f32_e32 v134, v164, v135
	v_exp_f32_e32 v134, v134
	v_mov_b32_e32 v164, v135
	v_pk_mul_f32 v[16:17], v[134:135], v[16:17] op_sel_hi:[0,1]
	v_pk_mul_f32 v[14:15], v[134:135], v[14:15] op_sel_hi:[0,1]
	v_pk_mul_f32 v[12:13], v[134:135], v[12:13] op_sel_hi:[0,1]
	v_pk_mul_f32 v[10:11], v[134:135], v[10:11] op_sel_hi:[0,1]
	v_pk_mul_f32 v[8:9], v[134:135], v[8:9] op_sel_hi:[0,1]
	v_pk_mul_f32 v[6:7], v[134:135], v[6:7] op_sel_hi:[0,1]
	v_pk_mul_f32 v[4:5], v[134:135], v[4:5] op_sel_hi:[0,1]
	v_pk_mul_f32 v[2:3], v[134:135], v[2:3] op_sel_hi:[0,1]
	v_pk_mul_f32 v[32:33], v[134:135], v[32:33] op_sel_hi:[0,1]
	v_pk_mul_f32 v[30:31], v[134:135], v[30:31] op_sel_hi:[0,1]
	v_pk_mul_f32 v[28:29], v[134:135], v[28:29] op_sel_hi:[0,1]
	v_pk_mul_f32 v[26:27], v[134:135], v[26:27] op_sel_hi:[0,1]
	v_pk_mul_f32 v[24:25], v[134:135], v[24:25] op_sel_hi:[0,1]
	v_pk_mul_f32 v[22:23], v[134:135], v[22:23] op_sel_hi:[0,1]
	v_pk_mul_f32 v[20:21], v[134:135], v[20:21] op_sel_hi:[0,1]
	v_pk_mul_f32 v[18:19], v[134:135], v[18:19] op_sel_hi:[0,1]
	v_mul_f32_e32 v50, v50, v134
; #define LAS __attribute__((address_space(3)))
; template <int STAGE, int OFF> __device__ __forceinline__ void attn32_unit(const bf16* base, bf16* yrow0, int blk0, int u, LAS unsigned char* xtab, LAS unsigned char* kbuf, LAS unsigned char* vbuf, int lane, ...
;     ...
;         for (int c = 0; c < 4; ++c) { *(LAS v4u*)(kbuf + (8 * c + lrow) * 144 + lch * 16) = kr[set][c]; *(LAS v4u*)(vbuf + (8 * c + lrow) * 160 + lch * 16) = vr[set][c]; }
;         if (pp + 2 < 5) { ATT32_LOAD(set, pp + 2, t0, SH); }
;         else { const bf16* base_ = base; { const bf16* base = nbase; ATT32_LOAD(set, pp + 2 - 5, nt0, nsh); } (void)base_; }
;         f32x16 sc;
; #pragma unroll
;         for (int i = 0; i < 16; ++i) sc[i] = 0.f;
; #pragma unroll
;         for (int ks = 0; ks < 4; ++ks) { const bf16x8 ka = *(const LAS bf16x8*)(kbuf + qi * 144 + 32 * ks + 16 * h); sc = MFMA32(ka, qb[ks], sc); }
;         if (pp == 4) {
; #pragma unroll
;             for (int ks = 0; ks < 4; ++ks) qb[ks] = *(const bf16x8*)(nbase + (size_t)min(nt0 + (qi << nsh), SEQ - 1) * 1536 + 16 * ks + 8 * h);
;         }
;         const int mbase = n0 + 4 * h - lo; float mx = -INFINITY;
; #pragma unroll
;         for (int rg = 0; rg < 16; ++rg) { sc[rg] = ((unsigned)(mbase + (rg & 3) + 8 * (rg >> 2)) <= mspan) ? sc[rg] : -INFINITY; mx = fmaxf(mx, sc[rg]); }
;         mx = fmaxf(mx, __shfl_xor(mx, 32));
;         if (__any(mx > m)) {
;             const float mn = fmaxf(m, mx), alpha = __builtin_amdgcn_exp2f(m - mn); m = mn; l *= alpha;
; #pragma unroll
;             for (int i = 0; i < 16; ++i) { o[0][i] *= alpha; o[1][i] *= alpha; }
;         }
;         float ps = 0.f;
; #pragma unroll
;         for (int rg = 0; rg < 16; ++rg) { sc[rg] = __builtin_amdgcn_exp2f(sc[rg] - m); ps += sc[rg]; }
;         l += ps;
;         bf16x8 pb[2];
; #pragma unroll
;         for (int s2 = 0; s2 < 2; ++s2) { v4u w; w.x = pg8::cvt_pk_bf16(sc[8 * s2], sc[8 * s2 + 1]); w.y = pg8::cvt_pk_bf16(sc[8 * s2 + 2], sc[8 * s2 + 3]); w.z = pg8::cvt_pk_bf16(sc[8 * s2 + 4], sc[8 * s2 + 5]); w.w = pg8::cvt_pk_bf16(sc[8 * s2 + 6], sc[8 * s2 + 7]); pb[s2] = __builtin_bit_cast(bf16x8, w); }
; #pragma unroll
;         for (int mb = 0; mb < 2; ++mb)
; #pragma unroll
;             for (int s2 = 0; s2 < 2; ++s2) {
;                 LAS unsigned char* vp = vbuf + tr_off + (16 * s2) * 160 + 64 * mb;
.LBB0_412:
	v_sub_f32_e32 v34, v34, v164
	v_exp_f32_e32 v134, v34
	v_sub_f32_e32 v34, v35, v164
	v_exp_f32_e32 v135, v34
	v_sub_f32_e32 v34, v36, v164
	v_exp_f32_e32 v136, v34
	v_sub_f32_e32 v34, v37, v164
	v_exp_f32_e32 v137, v34
	v_sub_f32_e32 v34, v38, v164
	v_exp_f32_e32 v142, v34
	v_sub_f32_e32 v34, v39, v164
	v_exp_f32_e32 v143, v34
	v_sub_f32_e32 v34, v40, v164
	v_exp_f32_e32 v144, v34
	v_sub_f32_e32 v34, v41, v164
	v_exp_f32_e32 v145, v34
	v_sub_f32_e32 v34, v42, v164
	v_exp_f32_e32 v165, v34
	v_sub_f32_e32 v34, v43, v164
	v_exp_f32_e32 v171, v34
	v_sub_f32_e32 v34, v44, v164
	v_exp_f32_e32 v172, v34
	v_sub_f32_e32 v34, v45, v164
	v_exp_f32_e32 v173, v34
	v_sub_f32_e32 v34, v46, v164
	v_exp_f32_e32 v237, v34
	v_sub_f32_e32 v34, v47, v164
	v_exp_f32_e32 v242, v34
	v_sub_f32_e32 v34, v48, v164
	v_exp_f32_e32 v243, v34
	v_sub_f32_e32 v34, v49, v164
	v_exp_f32_e32 v244, v34
	v_cvt_pk_bf16_f32 v34, v134, v135
	v_cvt_pk_bf16_f32 v35, v136, v137
	v_cvt_pk_bf16_f32 v36, v142, v143
	v_cvt_pk_bf16_f32 v37, v144, v145
	v_cvt_pk_bf16_f32 v138, v165, v171
	v_cvt_pk_bf16_f32 v139, v172, v173
	v_cvt_pk_bf16_f32 v140, v237, v242
	v_cvt_pk_bf16_f32 v141, v243, v244
	ds_read_b64_tr_b16 v[38:39], v181 offset:4608
	ds_read_b64_tr_b16 v[40:41], v181 offset:5888
	ds_read_b64_tr_b16 v[44:45], v181 offset:5952
	ds_read_b64_tr_b16 v[42:43], v181 offset:4672
	s_waitcnt lgkmcnt(2)
	v_mfma_f32_32x32x16_bf16 v[18:33], v[38:41], v[34:37], v[18:33]
	ds_read_b64_tr_b16 v[38:39], v181 offset:7168
	ds_read_b64_tr_b16 v[40:41], v181 offset:8448
	v_add_f32_e32 v46, 0, v134
	ds_read_b64_tr_b16 v[240:241], v181 offset:8512
	ds_read_b64_tr_b16 v[238:239], v181 offset:7232
	ds_write_b128 v231, v[74:77]
	ds_write_b128 v232, v[78:81] offset:4608
	ds_write_b128 v231, v[82:85] offset:1152
	ds_write_b128 v232, v[86:89] offset:5888
	ds_write_b128 v231, v[90:93] offset:2304
	ds_write_b128 v232, v[94:97] offset:7168
	ds_write_b128 v231, v[98:101] offset:3456
	ds_write_b128 v232, v[102:105] offset:8448
	s_waitcnt lgkmcnt(10)
	v_mfma_f32_32x32x16_bf16 v[18:33], v[38:41], v[138:141], v[18:33]
	v_add_f32_e32 v38, v135, v46
	v_add_f32_e32 v38, v136, v38
	v_add_f32_e32 v38, v137, v38
	v_add_f32_e32 v38, v142, v38
	v_add_f32_e32 v38, v143, v38
	v_add_f32_e32 v38, v144, v38
	v_add_f32_e32 v245, v145, v38
	v_mfma_f32_32x32x16_bf16 v[2:17], v[42:45], v[34:37], v[2:17]
	v_add_u32_e32 v34, s10, v222
	v_med3_i32 v34, v34, 0, v233
	v_mul_u32_u24_e32 v38, 0xc00, v34
	ds_read_b128 v[34:37], v177
	v_or_b32_e32 v38, v38, v176
	global_load_dwordx4 v[86:89], v38, s[8:9] offset:1024
	global_load_dwordx4 v[90:93], v38, s[8:9] offset:2048
	v_add_u32_e32 v38, s10, v223
	v_med3_i32 v38, v38, 0, v233
	v_mul_u32_u24_e32 v38, 0xc00, v38
	ds_read_b128 v[74:77], v177 offset:32
	v_or_b32_e32 v78, v38, v176
	s_waitcnt lgkmcnt(1)
	v_mfma_f32_32x32x16_bf16 v[34:49], v[34:37], v[70:73], 0
	global_load_dwordx4 v[134:137], v78, s[8:9] offset:1024
	global_load_dwordx4 v[142:145], v78, s[8:9] offset:2048
	v_add_u32_e32 v78, s10, v224
	v_med3_i32 v78, v78, 0, v233
	v_mul_u32_u24_e32 v78, 0xc00, v78
	v_or_b32_e32 v94, v78, v176
	ds_read_b128 v[78:81], v177 offset:96
	ds_read_b128 v[82:85], v177 offset:64
	global_load_dwordx4 v[146:149], v94, s[8:9] offset:1024
	global_load_dwordx4 v[150:153], v94, s[8:9] offset:2048
	s_waitcnt lgkmcnt(2)
	v_mfma_f32_32x32x16_bf16 v[34:49], v[74:77], v[62:65], v[34:49]
	v_add_u32_e32 v74, s10, v225
	v_med3_i32 v74, v74, 0, v233
	v_mul_u32_u24_e32 v74, 0xc00, v74
	v_or_b32_e32 v74, v74, v176
	global_load_dwordx4 v[154:157], v74, s[8:9] offset:1024
	global_load_dwordx4 v[158:161], v74, s[8:9] offset:2048
	v_add_u32_e32 v75, 32, v163
	v_cmp_le_u32_e32 vcc, v75, v51
	s_waitcnt lgkmcnt(0)
	v_mfma_f32_32x32x16_bf16 v[34:49], v[82:85], v[54:57], v[34:49]
	v_add_u32_e32 v75, 33, v163
	v_add_u32_e32 v76, 34, v163
	v_add_f32_e32 v74, v165, v245
	v_add_f32_e32 v74, v171, v74
	v_add_f32_e32 v74, v172, v74
	v_add_f32_e32 v74, v173, v74
	v_add_f32_e32 v74, v237, v74
	v_mfma_f32_32x32x16_bf16 v[34:49], v[78:81], v[66:69], v[34:49]
	v_add_f32_e32 v74, v242, v74
	v_add_f32_e32 v74, v243, v74
	v_add_f32_e32 v74, v244, v74
	v_add_f32_e32 v50, v50, v74
	v_mfma_f32_32x32x16_bf16 v[2:17], v[238:241], v[138:141], v[2:17]
	s_nop 6
	v_cndmask_b32_e32 v34, v234, v34, vcc
	v_cmp_le_u32_e32 vcc, v75, v51
	s_nop 1
	v_cndmask_b32_e32 v35, v234, v35, vcc
	v_cmp_le_u32_e32 vcc, v76, v51
	v_add_u32_e32 v76, 35, v163
	v_max3_f32 v75, v34, s31, v35
	v_cndmask_b32_e32 v36, v234, v36, vcc
	v_cmp_le_u32_e32 vcc, v76, v51
	v_add_u32_e32 v76, 40, v163
	s_nop 0
	v_cndmask_b32_e32 v37, v234, v37, vcc
	v_cmp_le_u32_e32 vcc, v76, v51
	v_add_u32_e32 v76, 41, v163
	v_max3_f32 v75, v75, v36, v37
	v_cndmask_b32_e32 v38, v234, v38, vcc
	v_cmp_le_u32_e32 vcc, v76, v51
	v_add_u32_e32 v76, 42, v163
	s_nop 0
	v_cndmask_b32_e32 v39, v234, v39, vcc
	v_cmp_le_u32_e32 vcc, v76, v51
	v_add_u32_e32 v76, 43, v163
	v_max3_f32 v75, v75, v38, v39
	v_cndmask_b32_e32 v40, v234, v40, vcc
	v_cmp_le_u32_e32 vcc, v76, v51
	v_add_u32_e32 v76, 48, v163
	s_nop 0
	v_cndmask_b32_e32 v41, v234, v41, vcc
	v_cmp_le_u32_e32 vcc, v76, v51
	v_add_u32_e32 v76, 49, v163
	v_max3_f32 v75, v75, v40, v41
	v_cndmask_b32_e32 v42, v234, v42, vcc
	v_cmp_le_u32_e32 vcc, v76, v51
	v_add_u32_e32 v76, 50, v163
	s_nop 0
	v_cndmask_b32_e32 v43, v234, v43, vcc
	v_cmp_le_u32_e32 vcc, v76, v51
	v_add_u32_e32 v76, 51, v163
	v_max3_f32 v75, v75, v42, v43
	v_cndmask_b32_e32 v44, v234, v44, vcc
	v_cmp_le_u32_e32 vcc, v76, v51
	v_add_u32_e32 v76, 56, v163
	s_nop 0
	v_cndmask_b32_e32 v45, v234, v45, vcc
	v_cmp_le_u32_e32 vcc, v76, v51
	v_add_u32_e32 v76, 57, v163
	v_max3_f32 v75, v75, v44, v45
	v_cndmask_b32_e32 v46, v234, v46, vcc
	v_cmp_le_u32_e32 vcc, v76, v51
	v_add_u32_e32 v76, 58, v163
	s_nop 0
	v_cndmask_b32_e32 v47, v234, v47, vcc
	v_cmp_le_u32_e32 vcc, v76, v51
	v_add_u32_e32 v76, 59, v163
	v_max3_f32 v75, v75, v46, v47
	v_cndmask_b32_e32 v48, v234, v48, vcc
	v_cmp_le_u32_e32 vcc, v76, v51
	s_nop 1
	v_cndmask_b32_e32 v49, v234, v49, vcc
	v_max3_f32 v75, v75, v48, v49
	v_mov_b32_e32 v76, v75
	s_nop 1
	v_permlane32_swap_b32_e32 v76, v75
	s_waitcnt lgkmcnt(0)
	v_max_f32_e32 v74, v76, v76
	v_max_f32_e32 v74, v75, v74
	v_cmp_gt_f32_e32 vcc, v74, v164
	s_cbranch_vccz .LBB0_414
; #define LAS __attribute__((address_space(3)))
; template <int STAGE, int OFF> __device__ __forceinline__ void attn32_unit(const bf16* base, bf16* yrow0, int blk0, int u, LAS unsigned char* xtab, LAS unsigned char* kbuf, LAS unsigned char* vbuf, int lane, ...
;     ...
;         for (int c = 0; c < 4; ++c) { *(LAS v4u*)(kbuf + (8 * c + lrow) * 144 + lch * 16) = kr[set][c]; *(LAS v4u*)(vbuf + (8 * c + lrow) * 160 + lch * 16) = vr[set][c]; }
;         if (pp + 2 < 5) { ATT32_LOAD(set, pp + 2, t0, SH); }
;         else { const bf16* base_ = base; { const bf16* base = nbase; ATT32_LOAD(set, pp + 2 - 5, nt0, nsh); } (void)base_; }
;         f32x16 sc;
; #pragma unroll
;         for (int i = 0; i < 16; ++i) sc[i] = 0.f;
; #pragma unroll
;         for (int ks = 0; ks < 4; ++ks) { const bf16x8 ka = *(const LAS bf16x8*)(kbuf + qi * 144 + 32 * ks + 16 * h); sc = MFMA32(ka, qb[ks], sc); }
;         if (pp == 4) {
; #pragma unroll
;             for (int ks = 0; ks < 4; ++ks) qb[ks] = *(const bf16x8*)(nbase + (size_t)min(nt0 + (qi << nsh), SEQ - 1) * 1536 + 16 * ks + 8 * h);
;         }
;         const int mbase = n0 + 4 * h - lo; float mx = -INFINITY;
; #pragma unroll
;         for (int rg = 0; rg < 16; ++rg) { sc[rg] = ((unsigned)(mbase + (rg & 3) + 8 * (rg >> 2)) <= mspan) ? sc[rg] : -INFINITY; mx = fmaxf(mx, sc[rg]); }
;         mx = fmaxf(mx, __shfl_xor(mx, 32));
;         if (__any(mx > m)) {
;             const float mn = fmaxf(m, mx), alpha = __builtin_amdgcn_exp2f(m - mn); m = mn; l *= alpha;
; #pragma unroll
;             for (int i = 0; i < 16; ++i) { o[0][i] *= alpha; o[1][i] *= alpha; }
;         }
;         float ps = 0.f;
; #pragma unroll
;         for (int rg = 0; rg < 16; ++rg) { sc[rg] = __builtin_amdgcn_exp2f(sc[rg] - m); ps += sc[rg]; }
;         l += ps;
;         bf16x8 pb[2];
; #pragma unroll
;         for (int s2 = 0; s2 < 2; ++s2) { v4u w; w.x = pg8::cvt_pk_bf16(sc[8 * s2], sc[8 * s2 + 1]); w.y = pg8::cvt_pk_bf16(sc[8 * s2 + 2], sc[8 * s2 + 3]); w.z = pg8::cvt_pk_bf16(sc[8 * s2 + 4], sc[8 * s2 + 5]); w.w = pg8::cvt_pk_bf16(sc[8 * s2 + 6], sc[8 * s2 + 7]); pb[s2] = __builtin_bit_cast(bf16x8, w); }
; #pragma unroll
;         for (int mb = 0; mb < 2; ++mb)
; #pragma unroll
;             for (int s2 = 0; s2 < 2; ++s2) {
;                 LAS unsigned char* vp = vbuf + tr_off + (16 * s2) * 160 + 64 * mb;
	v_max_f32_e32 v74, v74, v74
	v_max_f32_e32 v75, v164, v164
	v_max_f32_e32 v75, v75, v74
	v_sub_f32_e32 v74, v164, v75
	v_exp_f32_e32 v74, v74
	v_mov_b32_e32 v164, v75
	v_pk_mul_f32 v[32:33], v[32:33], v[74:75] op_sel_hi:[1,0]
	v_pk_mul_f32 v[30:31], v[30:31], v[74:75] op_sel_hi:[1,0]
	v_pk_mul_f32 v[28:29], v[28:29], v[74:75] op_sel_hi:[1,0]
	v_pk_mul_f32 v[26:27], v[26:27], v[74:75] op_sel_hi:[1,0]
	v_pk_mul_f32 v[24:25], v[24:25], v[74:75] op_sel_hi:[1,0]
	v_pk_mul_f32 v[22:23], v[22:23], v[74:75] op_sel_hi:[1,0]
	v_pk_mul_f32 v[20:21], v[20:21], v[74:75] op_sel_hi:[1,0]
	v_pk_mul_f32 v[18:19], v[18:19], v[74:75] op_sel_hi:[1,0]
	v_pk_mul_f32 v[16:17], v[16:17], v[74:75] op_sel_hi:[1,0]
	v_pk_mul_f32 v[14:15], v[14:15], v[74:75] op_sel_hi:[1,0]
	v_pk_mul_f32 v[12:13], v[12:13], v[74:75] op_sel_hi:[1,0]
	v_pk_mul_f32 v[10:11], v[10:11], v[74:75] op_sel_hi:[1,0]
	v_pk_mul_f32 v[8:9], v[8:9], v[74:75] op_sel_hi:[1,0]
	v_pk_mul_f32 v[6:7], v[6:7], v[74:75] op_sel_hi:[1,0]
	v_pk_mul_f32 v[4:5], v[4:5], v[74:75] op_sel_hi:[1,0]
	v_pk_mul_f32 v[2:3], v[2:3], v[74:75] op_sel_hi:[1,0]
	v_mul_f32_e32 v50, v50, v74
.LBB0_414:
	v_sub_f32_e32 v34, v34, v164
	v_exp_f32_e32 v74, v34
	v_sub_f32_e32 v34, v35, v164
	v_exp_f32_e32 v75, v34
	v_sub_f32_e32 v34, v36, v164
	v_exp_f32_e32 v76, v34
	v_sub_f32_e32 v34, v37, v164
	v_exp_f32_e32 v77, v34
	v_sub_f32_e32 v34, v38, v164
	v_exp_f32_e32 v78, v34
	v_sub_f32_e32 v34, v39, v164
	v_exp_f32_e32 v79, v34
	v_sub_f32_e32 v34, v40, v164
	v_exp_f32_e32 v80, v34
	v_sub_f32_e32 v34, v41, v164
	v_exp_f32_e32 v81, v34
	v_sub_f32_e32 v34, v42, v164
	v_exp_f32_e32 v165, v34
	v_sub_f32_e32 v34, v43, v164
	v_exp_f32_e32 v171, v34
	v_sub_f32_e32 v34, v44, v164
	v_exp_f32_e32 v172, v34
	v_sub_f32_e32 v34, v45, v164
	v_exp_f32_e32 v173, v34
	v_sub_f32_e32 v34, v46, v164
	v_exp_f32_e32 v237, v34
	v_sub_f32_e32 v34, v47, v164
	v_exp_f32_e32 v246, v34
	v_sub_f32_e32 v34, v48, v164
	v_exp_f32_e32 v247, v34
	v_sub_f32_e32 v34, v49, v164
	v_exp_f32_e32 v248, v34
	v_cvt_pk_bf16_f32 v34, v74, v75
	v_cvt_pk_bf16_f32 v35, v76, v77
	v_cvt_pk_bf16_f32 v36, v78, v79
	v_cvt_pk_bf16_f32 v37, v80, v81
	v_cvt_pk_bf16_f32 v238, v165, v171
	v_cvt_pk_bf16_f32 v239, v172, v173
	v_cvt_pk_bf16_f32 v240, v237, v246
	v_cvt_pk_bf16_f32 v241, v247, v248
	ds_read_b64_tr_b16 v[38:39], v181 offset:4608
	ds_read_b64_tr_b16 v[40:41], v181 offset:5888
	ds_read_b64_tr_b16 v[44:45], v181 offset:5952
	ds_read_b64_tr_b16 v[42:43], v181 offset:4672
	s_waitcnt lgkmcnt(2)
	v_mfma_f32_32x32x16_bf16 v[18:33], v[38:41], v[34:37], v[18:33]
	ds_read_b64_tr_b16 v[38:39], v181 offset:7168
	ds_read_b64_tr_b16 v[40:41], v181 offset:8448
	v_add_f32_e32 v46, 0, v74
	ds_read_b64_tr_b16 v[244:245], v181 offset:8512
	ds_read_b64_tr_b16 v[242:243], v181 offset:7232
	s_waitcnt vmcnt(15)
	ds_write_b128 v231, v[58:61]
	s_waitcnt vmcnt(14)
	ds_write_b128 v232, v[106:109] offset:4608
	s_waitcnt vmcnt(13)
	ds_write_b128 v231, v[110:113] offset:1152
	s_waitcnt vmcnt(12)
	ds_write_b128 v232, v[114:117] offset:5888
	s_waitcnt vmcnt(11)
	ds_write_b128 v231, v[118:121] offset:2304
	s_waitcnt vmcnt(10)
	ds_write_b128 v232, v[122:125] offset:7168
	s_waitcnt vmcnt(9)
	ds_write_b128 v231, v[126:129] offset:3456
	s_waitcnt vmcnt(8)
	ds_write_b128 v232, v[130:133] offset:8448
	v_add_u32_e32 v98, s10, v227
	v_add_u32_e32 v102, s10, v228
	s_waitcnt lgkmcnt(10)
	v_mfma_f32_32x32x16_bf16 v[18:33], v[38:41], v[238:241], v[18:33]
	v_add_f32_e32 v38, v75, v46
	v_add_f32_e32 v38, v76, v38
	v_add_f32_e32 v38, v77, v38
	v_add_f32_e32 v38, v78, v38
	v_add_f32_e32 v38, v79, v38
	v_add_f32_e32 v38, v80, v38
	v_add_f32_e32 v249, v81, v38
	v_mfma_f32_32x32x16_bf16 v[2:17], v[42:45], v[34:37], v[2:17]
	v_add_u32_e32 v34, s10, v207
	v_min_u32_e32 v34, 0x3fff, v34
	v_mul_u32_u24_e32 v38, 0xc00, v34
	ds_read_b128 v[34:37], v177
	v_or_b32_e32 v38, v38, v176
	global_load_dwordx4 v[58:61], v38, s[8:9] offset:1024
	global_load_dwordx4 v[74:77], v38, s[8:9] offset:2048
	v_add_u32_e32 v38, s10, v226
	v_min_u32_e32 v38, 0x3fff, v38
	v_mul_u32_u24_e32 v38, 0xc00, v38
	ds_read_b128 v[94:97], v177 offset:32
	v_or_b32_e32 v82, v38, v176
	s_waitcnt lgkmcnt(1)
	v_mfma_f32_32x32x16_bf16 v[34:49], v[34:37], v[70:73], 0
	v_min_u32_e32 v98, 0x3fff, v98
	v_min_u32_e32 v102, 0x3fff, v102
	v_mul_u32_u24_e32 v98, 0xc00, v98
	v_mul_u32_u24_e32 v102, 0xc00, v102
	v_or_b32_e32 v98, v98, v176
	v_or_b32_e32 v114, v102, v176
	global_load_dwordx4 v[78:81], v82, s[8:9] offset:1024
	s_nop 0
	global_load_dwordx4 v[82:85], v82, s[8:9] offset:2048
	ds_read_b128 v[106:109], v177 offset:96
	ds_read_b128 v[110:113], v177 offset:64
	s_waitcnt lgkmcnt(2)
	v_mfma_f32_32x32x16_bf16 v[34:49], v[94:97], v[62:65], v[34:49]
	global_load_dwordx4 v[94:97], v98, s[8:9] offset:1024
	s_nop 0
	global_load_dwordx4 v[98:101], v98, s[8:9] offset:2048
	s_nop 0
	global_load_dwordx4 v[102:105], v114, s[8:9] offset:1024
	global_load_dwordx4 v[138:141], v114, s[8:9] offset:2048
	s_waitcnt lgkmcnt(0)
; #define LAS __attribute__((address_space(3)))
; template <int STAGE, int OFF> __device__ __forceinline__ void attn32_unit(const bf16* base, bf16* yrow0, int blk0, int u, LAS unsigned char* xtab, LAS unsigned char* kbuf, LAS unsigned char* vbuf, int lane, ...
;     ...
;         for (int c = 0; c < 4; ++c) { *(LAS v4u*)(kbuf + (8 * c + lrow) * 144 + lch * 16) = kr[set][c]; *(LAS v4u*)(vbuf + (8 * c + lrow) * 160 + lch * 16) = vr[set][c]; }
;         if (pp + 2 < 5) { ATT32_LOAD(set, pp + 2, t0, SH); }
;         else { const bf16* base_ = base; { const bf16* base = nbase; ATT32_LOAD(set, pp + 2 - 5, nt0, nsh); } (void)base_; }
;         f32x16 sc;
; #pragma unroll
;         for (int i = 0; i < 16; ++i) sc[i] = 0.f;
; #pragma unroll
;         for (int ks = 0; ks < 4; ++ks) { const bf16x8 ka = *(const LAS bf16x8*)(kbuf + qi * 144 + 32 * ks + 16 * h); sc = MFMA32(ka, qb[ks], sc); }
;         if (pp == 4) {
; #pragma unroll
;             for (int ks = 0; ks < 4; ++ks) qb[ks] = *(const bf16x8*)(nbase + (size_t)min(nt0 + (qi << nsh), SEQ - 1) * 1536 + 16 * ks + 8 * h);
;         }
;         const int mbase = n0 + 4 * h - lo; float mx = -INFINITY;
; #pragma unroll
;         for (int rg = 0; rg < 16; ++rg) { sc[rg] = ((unsigned)(mbase + (rg & 3) + 8 * (rg >> 2)) <= mspan) ? sc[rg] : -INFINITY; mx = fmaxf(mx, sc[rg]); }
;         mx = fmaxf(mx, __shfl_xor(mx, 32));
;         if (__any(mx > m)) {
;             const float mn = fmaxf(m, mx), alpha = __builtin_amdgcn_exp2f(m - mn); m = mn; l *= alpha;
; #pragma unroll
;             for (int i = 0; i < 16; ++i) { o[0][i] *= alpha; o[1][i] *= alpha; }
;         }
;         float ps = 0.f;
; #pragma unroll
;         for (int rg = 0; rg < 16; ++rg) { sc[rg] = __builtin_amdgcn_exp2f(sc[rg] - m); ps += sc[rg]; }
;         l += ps;
;         bf16x8 pb[2];
; #pragma unroll
;         for (int s2 = 0; s2 < 2; ++s2) { v4u w; w.x = pg8::cvt_pk_bf16(sc[8 * s2], sc[8 * s2 + 1]); w.y = pg8::cvt_pk_bf16(sc[8 * s2 + 2], sc[8 * s2 + 3]); w.z = pg8::cvt_pk_bf16(sc[8 * s2 + 4], sc[8 * s2 + 5]); w.w = pg8::cvt_pk_bf16(sc[8 * s2 + 6], sc[8 * s2 + 7]); pb[s2] = __builtin_bit_cast(bf16x8, w); }
; #pragma unroll
;         for (int mb = 0; mb < 2; ++mb)
; #pragma unroll
;             for (int s2 = 0; s2 < 2; ++s2) {
;                 LAS unsigned char* vp = vbuf + tr_off + (16 * s2) * 160 + 64 * mb;
	v_mfma_f32_32x32x16_bf16 v[34:49], v[110:113], v[54:57], v[34:49]
	v_add_f32_e32 v110, v165, v249
	v_add_f32_e32 v110, v171, v110
	v_add_f32_e32 v110, v172, v110
	v_add_f32_e32 v110, v173, v110
	v_add_f32_e32 v110, v237, v110
	v_add_f32_e32 v110, v246, v110
	v_add_f32_e32 v110, v247, v110
	v_mfma_f32_32x32x16_bf16 v[34:49], v[106:109], v[66:69], v[34:49]
	v_add_u32_e32 v106, 64, v163
	v_cmp_le_u32_e32 vcc, v106, v51
	v_add_u32_e32 v106, 0x41, v163
	v_add_u32_e32 v107, 0x42, v163
	v_add_f32_e32 v108, v248, v110
	v_add_f32_e32 v50, v50, v108
	s_nop 5
	v_cndmask_b32_e32 v34, v234, v34, vcc
	v_cmp_le_u32_e32 vcc, v106, v51
	v_mfma_f32_32x32x16_bf16 v[2:17], v[242:245], v[238:241], v[2:17]
	s_nop 0
	v_cndmask_b32_e32 v35, v234, v35, vcc
	v_cmp_le_u32_e32 vcc, v107, v51
	v_add_u32_e32 v107, 0x43, v163
	v_max3_f32 v106, v34, s31, v35
	v_cndmask_b32_e32 v36, v234, v36, vcc
	v_cmp_le_u32_e32 vcc, v107, v51
	v_add_u32_e32 v107, 0x48, v163
	s_nop 0
	v_cndmask_b32_e32 v37, v234, v37, vcc
	v_cmp_le_u32_e32 vcc, v107, v51
	v_add_u32_e32 v107, 0x49, v163
	v_max3_f32 v106, v106, v36, v37
	v_cndmask_b32_e32 v38, v234, v38, vcc
	v_cmp_le_u32_e32 vcc, v107, v51
	v_add_u32_e32 v107, 0x4a, v163
	s_nop 0
	v_cndmask_b32_e32 v39, v234, v39, vcc
	v_cmp_le_u32_e32 vcc, v107, v51
	v_add_u32_e32 v107, 0x4b, v163
	v_max3_f32 v106, v106, v38, v39
	v_cndmask_b32_e32 v40, v234, v40, vcc
	v_cmp_le_u32_e32 vcc, v107, v51
	v_add_u32_e32 v107, 0x50, v163
	s_nop 0
	v_cndmask_b32_e32 v41, v234, v41, vcc
	v_cmp_le_u32_e32 vcc, v107, v51
	v_add_u32_e32 v107, 0x51, v163
	v_max3_f32 v106, v106, v40, v41
	v_cndmask_b32_e32 v42, v234, v42, vcc
	v_cmp_le_u32_e32 vcc, v107, v51
	v_add_u32_e32 v107, 0x52, v163
	s_nop 0
	v_cndmask_b32_e32 v43, v234, v43, vcc
	v_cmp_le_u32_e32 vcc, v107, v51
	v_add_u32_e32 v107, 0x53, v163
	v_max3_f32 v106, v106, v42, v43
	v_cndmask_b32_e32 v44, v234, v44, vcc
	v_cmp_le_u32_e32 vcc, v107, v51
	v_add_u32_e32 v107, 0x58, v163
	s_nop 0
	v_cndmask_b32_e32 v45, v234, v45, vcc
	v_cmp_le_u32_e32 vcc, v107, v51
	v_add_u32_e32 v107, 0x59, v163
	v_max3_f32 v106, v106, v44, v45
	v_cndmask_b32_e32 v46, v234, v46, vcc
	v_cmp_le_u32_e32 vcc, v107, v51
	v_add_u32_e32 v107, 0x5a, v163
	s_nop 0
	v_cndmask_b32_e32 v47, v234, v47, vcc
	v_cmp_le_u32_e32 vcc, v107, v51
	v_add_u32_e32 v107, 0x5b, v163
	v_max3_f32 v106, v106, v46, v47
	v_cndmask_b32_e32 v48, v234, v48, vcc
	v_cmp_le_u32_e32 vcc, v107, v51
	s_nop 1
	v_cndmask_b32_e32 v49, v234, v49, vcc
	v_max3_f32 v106, v106, v48, v49
	v_mov_b32_e32 v107, v106
	s_nop 1
	v_permlane32_swap_b32_e32 v107, v106
	s_waitcnt lgkmcnt(0)
	v_max_f32_e32 v107, v107, v107
	v_max_f32_e32 v106, v106, v107
	v_cmp_gt_f32_e32 vcc, v106, v164
	s_cbranch_vccz .LBB0_416
	v_max_f32_e32 v106, v106, v106
	v_max_f32_e32 v107, v164, v164
	v_max_f32_e32 v107, v107, v106
	v_sub_f32_e32 v106, v164, v107
	v_exp_f32_e32 v106, v106
	v_mov_b32_e32 v164, v107
	v_pk_mul_f32 v[32:33], v[32:33], v[106:107] op_sel_hi:[1,0]
	v_pk_mul_f32 v[30:31], v[30:31], v[106:107] op_sel_hi:[1,0]
	v_pk_mul_f32 v[28:29], v[28:29], v[106:107] op_sel_hi:[1,0]
	v_pk_mul_f32 v[26:27], v[26:27], v[106:107] op_sel_hi:[1,0]
	v_pk_mul_f32 v[24:25], v[24:25], v[106:107] op_sel_hi:[1,0]
	v_pk_mul_f32 v[22:23], v[22:23], v[106:107] op_sel_hi:[1,0]
	v_pk_mul_f32 v[20:21], v[20:21], v[106:107] op_sel_hi:[1,0]
	v_pk_mul_f32 v[18:19], v[18:19], v[106:107] op_sel_hi:[1,0]
	v_pk_mul_f32 v[16:17], v[16:17], v[106:107] op_sel_hi:[1,0]
	v_pk_mul_f32 v[14:15], v[14:15], v[106:107] op_sel_hi:[1,0]
	v_pk_mul_f32 v[12:13], v[12:13], v[106:107] op_sel_hi:[1,0]
	v_pk_mul_f32 v[10:11], v[10:11], v[106:107] op_sel_hi:[1,0]
	v_pk_mul_f32 v[8:9], v[8:9], v[106:107] op_sel_hi:[1,0]
	v_pk_mul_f32 v[6:7], v[6:7], v[106:107] op_sel_hi:[1,0]
	v_pk_mul_f32 v[4:5], v[4:5], v[106:107] op_sel_hi:[1,0]
	v_pk_mul_f32 v[2:3], v[2:3], v[106:107] op_sel_hi:[1,0]
	v_mul_f32_e32 v50, v50, v106
.LBB0_416:
	v_sub_f32_e32 v34, v34, v164
	v_exp_f32_e32 v106, v34
	v_sub_f32_e32 v34, v35, v164
	v_exp_f32_e32 v107, v34
	v_sub_f32_e32 v34, v36, v164
	v_exp_f32_e32 v108, v34
	v_sub_f32_e32 v34, v37, v164
	v_exp_f32_e32 v109, v34
	v_sub_f32_e32 v34, v38, v164
	v_exp_f32_e32 v110, v34
	v_sub_f32_e32 v34, v39, v164
	v_exp_f32_e32 v111, v34
	v_sub_f32_e32 v34, v40, v164
	v_exp_f32_e32 v112, v34
	v_sub_f32_e32 v34, v41, v164
	v_exp_f32_e32 v113, v34
	v_sub_f32_e32 v34, v42, v164
	v_exp_f32_e32 v165, v34
	v_sub_f32_e32 v34, v43, v164
	v_exp_f32_e32 v171, v34
	v_sub_f32_e32 v34, v44, v164
	v_exp_f32_e32 v172, v34
	v_sub_f32_e32 v34, v45, v164
	v_exp_f32_e32 v173, v34
	v_sub_f32_e32 v34, v46, v164
	v_exp_f32_e32 v237, v34
	v_sub_f32_e32 v34, v47, v164
	v_exp_f32_e32 v246, v34
	v_sub_f32_e32 v34, v48, v164
	v_exp_f32_e32 v247, v34
	v_sub_f32_e32 v34, v49, v164
	v_exp_f32_e32 v248, v34
	v_cvt_pk_bf16_f32 v34, v106, v107
	v_cvt_pk_bf16_f32 v35, v108, v109
	v_cvt_pk_bf16_f32 v36, v110, v111
	v_cvt_pk_bf16_f32 v37, v112, v113
	v_cvt_pk_bf16_f32 v238, v165, v171
	v_cvt_pk_bf16_f32 v239, v172, v173
	v_cvt_pk_bf16_f32 v240, v237, v246
	v_cvt_pk_bf16_f32 v241, v247, v248
	ds_read_b64_tr_b16 v[38:39], v181 offset:4608
	ds_read_b64_tr_b16 v[40:41], v181 offset:5888
	ds_read_b64_tr_b16 v[44:45], v181 offset:5952
	ds_read_b64_tr_b16 v[42:43], v181 offset:4672
	s_waitcnt lgkmcnt(2)
	v_mfma_f32_32x32x16_bf16 v[18:33], v[38:41], v[34:37], v[18:33]
	ds_read_b64_tr_b16 v[38:39], v181 offset:7168
	ds_read_b64_tr_b16 v[40:41], v181 offset:8448
	v_add_f32_e32 v46, 0, v106
	s_add_i32 s10, s13, s21
	ds_read_b64_tr_b16 v[244:245], v181 offset:8512
	ds_read_b64_tr_b16 v[242:243], v181 offset:7232
	s_waitcnt vmcnt(15)
	ds_write_b128 v231, v[86:89]
	s_waitcnt vmcnt(14)
; #define LAS __attribute__((address_space(3)))
; template <int STAGE, int OFF> __device__ __forceinline__ void attn32_unit(const bf16* base, bf16* yrow0, int blk0, int u, LAS unsigned char* xtab, LAS unsigned char* kbuf, LAS unsigned char* vbuf, int lane, ...
;     ...
;         for (int c = 0; c < 4; ++c) { *(LAS v4u*)(kbuf + (8 * c + lrow) * 144 + lch * 16) = kr[set][c]; *(LAS v4u*)(vbuf + (8 * c + lrow) * 160 + lch * 16) = vr[set][c]; }
;         if (pp + 2 < 5) { ATT32_LOAD(set, pp + 2, t0, SH); }
;         else { const bf16* base_ = base; { const bf16* base = nbase; ATT32_LOAD(set, pp + 2 - 5, nt0, nsh); } (void)base_; }
;         f32x16 sc;
; #pragma unroll
;         for (int i = 0; i < 16; ++i) sc[i] = 0.f;
; #pragma unroll
;         for (int ks = 0; ks < 4; ++ks) { const bf16x8 ka = *(const LAS bf16x8*)(kbuf + qi * 144 + 32 * ks + 16 * h); sc = MFMA32(ka, qb[ks], sc); }
;         if (pp == 4) {
; #pragma unroll
;             for (int ks = 0; ks < 4; ++ks) qb[ks] = *(const bf16x8*)(nbase + (size_t)min(nt0 + (qi << nsh), SEQ - 1) * 1536 + 16 * ks + 8 * h);
;         }
;         const int mbase = n0 + 4 * h - lo; float mx = -INFINITY;
; #pragma unroll
;         for (int rg = 0; rg < 16; ++rg) { sc[rg] = ((unsigned)(mbase + (rg & 3) + 8 * (rg >> 2)) <= mspan) ? sc[rg] : -INFINITY; mx = fmaxf(mx, sc[rg]); }
;         mx = fmaxf(mx, __shfl_xor(mx, 32));
;         if (__any(mx > m)) {
;             const float mn = fmaxf(m, mx), alpha = __builtin_amdgcn_exp2f(m - mn); m = mn; l *= alpha;
; #pragma unroll
;             for (int i = 0; i < 16; ++i) { o[0][i] *= alpha; o[1][i] *= alpha; }
;         }
;         float ps = 0.f;
; #pragma unroll
;         for (int rg = 0; rg < 16; ++rg) { sc[rg] = __builtin_amdgcn_exp2f(sc[rg] - m); ps += sc[rg]; }
;         l += ps;
;         bf16x8 pb[2];
; #pragma unroll
;         for (int s2 = 0; s2 < 2; ++s2) { v4u w; w.x = pg8::cvt_pk_bf16(sc[8 * s2], sc[8 * s2 + 1]); w.y = pg8::cvt_pk_bf16(sc[8 * s2 + 2], sc[8 * s2 + 3]); w.z = pg8::cvt_pk_bf16(sc[8 * s2 + 4], sc[8 * s2 + 5]); w.w = pg8::cvt_pk_bf16(sc[8 * s2 + 6], sc[8 * s2 + 7]); pb[s2] = __builtin_bit_cast(bf16x8, w); }
; #pragma unroll
;         for (int mb = 0; mb < 2; ++mb)
; #pragma unroll
;             for (int s2 = 0; s2 < 2; ++s2) {
;                 LAS unsigned char* vp = vbuf + tr_off + (16 * s2) * 160 + 64 * mb;
	ds_write_b128 v232, v[90:93] offset:4608
	s_waitcnt vmcnt(13)
	ds_write_b128 v231, v[134:137] offset:1152
	s_waitcnt vmcnt(12)
	ds_write_b128 v232, v[142:145] offset:5888
	s_waitcnt vmcnt(11)
	ds_write_b128 v231, v[146:149] offset:2304
	s_waitcnt vmcnt(10)
	ds_write_b128 v232, v[150:153] offset:7168
	s_waitcnt vmcnt(9)
	ds_write_b128 v231, v[154:157] offset:3456
	s_waitcnt vmcnt(8)
	ds_write_b128 v232, v[158:161] offset:8448
	s_waitcnt lgkmcnt(10)
	v_mfma_f32_32x32x16_bf16 v[18:33], v[38:41], v[238:241], v[18:33]
	v_add_f32_e32 v38, v107, v46
	v_add_f32_e32 v38, v108, v38
	v_add_f32_e32 v38, v109, v38
	v_add_f32_e32 v38, v110, v38
	v_add_f32_e32 v38, v111, v38
	v_add_f32_e32 v38, v112, v38
	v_add_f32_e32 v249, v113, v38
	v_mfma_f32_32x32x16_bf16 v[2:17], v[42:45], v[34:37], v[2:17]
	v_add_u32_e32 v34, s10, v208
	v_med3_i32 v34, v34, 0, v233
	v_mul_u32_u24_e32 v38, 0xc00, v34
	ds_read_b128 v[34:37], v177
	v_or_b32_e32 v38, v38, v176
	global_load_dwordx4 v[106:109], v38, s[8:9] offset:1024
	global_load_dwordx4 v[110:113], v38, s[8:9] offset:2048
	v_add_u32_e32 v38, s10, v209
	v_med3_i32 v38, v38, 0, v233
	v_mul_u32_u24_e32 v38, 0xc00, v38
	ds_read_b128 v[86:89], v177 offset:32
	v_or_b32_e32 v90, v38, v176
	s_waitcnt lgkmcnt(1)
	v_mfma_f32_32x32x16_bf16 v[34:49], v[34:37], v[70:73], 0
	global_load_dwordx4 v[114:117], v90, s[8:9] offset:1024
	global_load_dwordx4 v[118:121], v90, s[8:9] offset:2048
	v_add_u32_e32 v90, s10, v211
	v_med3_i32 v90, v90, 0, v233
	v_mul_u32_u24_e32 v90, 0xc00, v90
	v_or_b32_e32 v126, v90, v176
	ds_read_b128 v[90:93], v177 offset:96
	ds_read_b128 v[142:145], v177 offset:64
	global_load_dwordx4 v[122:125], v126, s[8:9] offset:1024
	s_nop 0
	global_load_dwordx4 v[126:129], v126, s[8:9] offset:2048
	s_waitcnt lgkmcnt(2)
	v_mfma_f32_32x32x16_bf16 v[34:49], v[86:89], v[62:65], v[34:49]
	v_add_u32_e32 v86, s10, v212
	v_med3_i32 v86, v86, 0, v233
	v_mul_u32_u24_e32 v86, 0xc00, v86
	v_or_b32_e32 v86, v86, v176
	global_load_dwordx4 v[130:133], v86, s[8:9] offset:1024
	global_load_dwordx4 v[134:137], v86, s[8:9] offset:2048
	v_add_u32_e32 v87, 0x60, v163
	v_cmp_le_u32_e32 vcc, v87, v51
	s_waitcnt lgkmcnt(0)
	v_mfma_f32_32x32x16_bf16 v[34:49], v[142:145], v[54:57], v[34:49]
	v_add_u32_e32 v87, 0x61, v163
	v_add_u32_e32 v88, 0x62, v163
	v_add_f32_e32 v86, v165, v249
	v_add_f32_e32 v86, v171, v86
	v_add_f32_e32 v86, v172, v86
	v_add_f32_e32 v86, v173, v86
	v_add_f32_e32 v86, v237, v86
	v_mfma_f32_32x32x16_bf16 v[34:49], v[90:93], v[66:69], v[34:49]
	v_add_f32_e32 v86, v246, v86
	v_add_f32_e32 v86, v247, v86
	v_add_f32_e32 v86, v248, v86
	v_add_f32_e32 v142, v50, v86
	v_mfma_f32_32x32x16_bf16 v[2:17], v[242:245], v[238:241], v[2:17]
	s_nop 6
	v_cndmask_b32_e32 v34, v234, v34, vcc
	v_cmp_le_u32_e32 vcc, v87, v51
	s_nop 1
	v_cndmask_b32_e32 v35, v234, v35, vcc
	v_cmp_le_u32_e32 vcc, v88, v51
	v_add_u32_e32 v88, 0x63, v163
	v_max3_f32 v87, v34, s31, v35
	v_cndmask_b32_e32 v36, v234, v36, vcc
	v_cmp_le_u32_e32 vcc, v88, v51
	v_add_u32_e32 v88, 0x68, v163
	s_nop 0
	v_cndmask_b32_e32 v37, v234, v37, vcc
	v_cmp_le_u32_e32 vcc, v88, v51
	v_add_u32_e32 v88, 0x69, v163
	v_max3_f32 v87, v87, v36, v37
	v_cndmask_b32_e32 v38, v234, v38, vcc
	v_cmp_le_u32_e32 vcc, v88, v51
	v_add_u32_e32 v88, 0x6a, v163
	s_nop 0
	v_cndmask_b32_e32 v39, v234, v39, vcc
	v_cmp_le_u32_e32 vcc, v88, v51
	v_add_u32_e32 v88, 0x6b, v163
	v_max3_f32 v87, v87, v38, v39
	v_cndmask_b32_e32 v40, v234, v40, vcc
	v_cmp_le_u32_e32 vcc, v88, v51
	v_add_u32_e32 v88, 0x70, v163
	s_nop 0
	v_cndmask_b32_e32 v41, v234, v41, vcc
	v_cmp_le_u32_e32 vcc, v88, v51
	v_add_u32_e32 v88, 0x71, v163
	v_max3_f32 v87, v87, v40, v41
	v_cndmask_b32_e32 v42, v234, v42, vcc
	v_cmp_le_u32_e32 vcc, v88, v51
	v_add_u32_e32 v88, 0x72, v163
	s_nop 0
	v_cndmask_b32_e32 v43, v234, v43, vcc
	v_cmp_le_u32_e32 vcc, v88, v51
	v_add_u32_e32 v88, 0x73, v163
	v_max3_f32 v87, v87, v42, v43
	v_cndmask_b32_e32 v44, v234, v44, vcc
	v_cmp_le_u32_e32 vcc, v88, v51
	v_add_u32_e32 v88, 0x78, v163
	s_nop 0
	v_cndmask_b32_e32 v45, v234, v45, vcc
	v_cmp_le_u32_e32 vcc, v88, v51
	v_add_u32_e32 v88, 0x79, v163
	v_max3_f32 v87, v87, v44, v45
	v_cndmask_b32_e32 v46, v234, v46, vcc
	v_cmp_le_u32_e32 vcc, v88, v51
	v_add_u32_e32 v88, 0x7a, v163
	s_nop 0
	v_cndmask_b32_e32 v47, v234, v47, vcc
	v_cmp_le_u32_e32 vcc, v88, v51
	v_add_u32_e32 v88, 0x7b, v163
	v_max3_f32 v87, v87, v46, v47
	v_cndmask_b32_e32 v48, v234, v48, vcc
	v_cmp_le_u32_e32 vcc, v88, v51
	s_nop 1
	v_cndmask_b32_e32 v49, v234, v49, vcc
	v_max3_f32 v87, v87, v48, v49
	v_mov_b32_e32 v88, v87
	s_nop 1
	v_permlane32_swap_b32_e32 v88, v87
	s_waitcnt lgkmcnt(0)
	v_max_f32_e32 v50, v88, v88
	v_max_f32_e32 v50, v87, v50
	v_cmp_gt_f32_e32 vcc, v50, v164
	s_cbranch_vccz .LBB0_418
	v_max_f32_e32 v50, v50, v50
	v_max_f32_e32 v86, v164, v164
	v_max_f32_e32 v86, v86, v50
	v_sub_f32_e32 v50, v164, v86
	v_exp_f32_e32 v50, v50
	v_mov_b32_e32 v164, v86
	v_pk_mul_f32 v[32:33], v[32:33], v[50:51] op_sel_hi:[1,0]
	v_pk_mul_f32 v[30:31], v[30:31], v[50:51] op_sel_hi:[1,0]
	v_pk_mul_f32 v[28:29], v[28:29], v[50:51] op_sel_hi:[1,0]
	v_pk_mul_f32 v[26:27], v[26:27], v[50:51] op_sel_hi:[1,0]
	v_pk_mul_f32 v[24:25], v[24:25], v[50:51] op_sel_hi:[1,0]
	v_pk_mul_f32 v[22:23], v[22:23], v[50:51] op_sel_hi:[1,0]
	v_pk_mul_f32 v[20:21], v[20:21], v[50:51] op_sel_hi:[1,0]
	v_pk_mul_f32 v[18:19], v[18:19], v[50:51] op_sel_hi:[1,0]
	v_pk_mul_f32 v[16:17], v[16:17], v[50:51] op_sel_hi:[1,0]
	v_pk_mul_f32 v[14:15], v[14:15], v[50:51] op_sel_hi:[1,0]
	v_pk_mul_f32 v[12:13], v[12:13], v[50:51] op_sel_hi:[1,0]
	v_pk_mul_f32 v[10:11], v[10:11], v[50:51] op_sel_hi:[1,0]
	v_pk_mul_f32 v[8:9], v[8:9], v[50:51] op_sel_hi:[1,0]
	v_pk_mul_f32 v[6:7], v[6:7], v[50:51] op_sel_hi:[1,0]
	v_pk_mul_f32 v[4:5], v[4:5], v[50:51] op_sel_hi:[1,0]
	v_pk_mul_f32 v[2:3], v[2:3], v[50:51] op_sel_hi:[1,0]
	v_mul_f32_e32 v142, v142, v50
; #define LAS __attribute__((address_space(3)))
; template <int STAGE, int OFF> __device__ __forceinline__ void attn32_unit(const bf16* base, bf16* yrow0, int blk0, int u, LAS unsigned char* xtab, LAS unsigned char* kbuf, LAS unsigned char* vbuf, int lane, ...
;     ...
;         for (int c = 0; c < 4; ++c) { *(LAS v4u*)(kbuf + (8 * c + lrow) * 144 + lch * 16) = kr[set][c]; *(LAS v4u*)(vbuf + (8 * c + lrow) * 160 + lch * 16) = vr[set][c]; }
;         if (pp + 2 < 5) { ATT32_LOAD(set, pp + 2, t0, SH); }
;         else { const bf16* base_ = base; { const bf16* base = nbase; ATT32_LOAD(set, pp + 2 - 5, nt0, nsh); } (void)base_; }
;         f32x16 sc;
; #pragma unroll
;         for (int i = 0; i < 16; ++i) sc[i] = 0.f;
; #pragma unroll
;         for (int ks = 0; ks < 4; ++ks) { const bf16x8 ka = *(const LAS bf16x8*)(kbuf + qi * 144 + 32 * ks + 16 * h); sc = MFMA32(ka, qb[ks], sc); }
;         if (pp == 4) {
; #pragma unroll
;             for (int ks = 0; ks < 4; ++ks) qb[ks] = *(const bf16x8*)(nbase + (size_t)min(nt0 + (qi << nsh), SEQ - 1) * 1536 + 16 * ks + 8 * h);
;         }
;         const int mbase = n0 + 4 * h - lo; float mx = -INFINITY;
; #pragma unroll
;         for (int rg = 0; rg < 16; ++rg) { sc[rg] = ((unsigned)(mbase + (rg & 3) + 8 * (rg >> 2)) <= mspan) ? sc[rg] : -INFINITY; mx = fmaxf(mx, sc[rg]); }
;         mx = fmaxf(mx, __shfl_xor(mx, 32));
;         if (__any(mx > m)) {
;             const float mn = fmaxf(m, mx), alpha = __builtin_amdgcn_exp2f(m - mn); m = mn; l *= alpha;
; #pragma unroll
;             for (int i = 0; i < 16; ++i) { o[0][i] *= alpha; o[1][i] *= alpha; }
;         }
;         float ps = 0.f;
; #pragma unroll
;         for (int rg = 0; rg < 16; ++rg) { sc[rg] = __builtin_amdgcn_exp2f(sc[rg] - m); ps += sc[rg]; }
;         l += ps;
;         bf16x8 pb[2];
; #pragma unroll
;         for (int s2 = 0; s2 < 2; ++s2) { v4u w; w.x = pg8::cvt_pk_bf16(sc[8 * s2], sc[8 * s2 + 1]); w.y = pg8::cvt_pk_bf16(sc[8 * s2 + 2], sc[8 * s2 + 3]); w.z = pg8::cvt_pk_bf16(sc[8 * s2 + 4], sc[8 * s2 + 5]); w.w = pg8::cvt_pk_bf16(sc[8 * s2 + 6], sc[8 * s2 + 7]); pb[s2] = __builtin_bit_cast(bf16x8, w); }
; #pragma unroll
;         for (int mb = 0; mb < 2; ++mb)
; #pragma unroll
;             for (int s2 = 0; s2 < 2; ++s2) {
;                 LAS unsigned char* vp = vbuf + tr_off + (16 * s2) * 160 + 64 * mb;
.LBB0_418:
	v_sub_f32_e32 v34, v34, v164
	v_exp_f32_e32 v86, v34
	v_sub_f32_e32 v34, v35, v164
	v_exp_f32_e32 v87, v34
	v_sub_f32_e32 v34, v36, v164
	v_exp_f32_e32 v88, v34
	v_sub_f32_e32 v34, v37, v164
	v_exp_f32_e32 v89, v34
	v_sub_f32_e32 v34, v38, v164
	v_exp_f32_e32 v90, v34
	v_sub_f32_e32 v34, v39, v164
	v_exp_f32_e32 v91, v34
	v_sub_f32_e32 v34, v40, v164
	v_exp_f32_e32 v92, v34
	v_sub_f32_e32 v34, v41, v164
	v_exp_f32_e32 v93, v34
	v_sub_f32_e32 v34, v42, v164
	v_exp_f32_e32 v143, v34
	v_sub_f32_e32 v34, v43, v164
	v_exp_f32_e32 v154, v34
	v_sub_f32_e32 v34, v44, v164
	v_exp_f32_e32 v155, v34
	v_sub_f32_e32 v34, v45, v164
	v_exp_f32_e32 v156, v34
	v_sub_f32_e32 v34, v46, v164
	v_exp_f32_e32 v157, v34
	v_sub_f32_e32 v34, v47, v164
	v_exp_f32_e32 v158, v34
	v_sub_f32_e32 v34, v48, v164
	v_exp_f32_e32 v159, v34
	v_sub_f32_e32 v34, v49, v164
	v_exp_f32_e32 v160, v34
	v_cvt_pk_bf16_f32 v34, v86, v87
	v_cvt_pk_bf16_f32 v35, v88, v89
	v_cvt_pk_bf16_f32 v36, v90, v91
	v_cvt_pk_bf16_f32 v37, v92, v93
	v_cvt_pk_bf16_f32 v144, v143, v154
	v_cvt_pk_bf16_f32 v145, v155, v156
	v_cvt_pk_bf16_f32 v146, v157, v158
	v_cvt_pk_bf16_f32 v147, v159, v160
	ds_read_b64_tr_b16 v[38:39], v181 offset:4608
	ds_read_b64_tr_b16 v[40:41], v181 offset:5888
	v_add_u32_e32 v50, s10, v52
	v_min_i32_e32 v148, 0x3fff, v50
	s_waitcnt lgkmcnt(0)
	v_mfma_f32_32x32x16_bf16 v[18:33], v[38:41], v[34:37], v[18:33]
	v_mul_u32_u24_e32 v38, 0xc00, v148
	v_mov_b32_e32 v39, v169
	v_lshl_add_u64 v[38:39], s[8:9], 0, v[38:39]
	ds_read_b64_tr_b16 v[42:43], v181 offset:7168
	ds_read_b64_tr_b16 v[44:45], v181 offset:8448
	ds_read_b64_tr_b16 v[48:49], v181 offset:5952
	ds_read_b64_tr_b16 v[46:47], v181 offset:4672
	v_lshl_add_u64 v[152:153], v[38:39], 0, v[168:169]
	v_add_f32_e32 v38, 0, v86
	v_add_f32_e32 v38, v87, v38
	v_add_f32_e32 v38, v88, v38
	v_add_f32_e32 v38, v89, v38
	v_add_f32_e32 v38, v90, v38
	v_add_f32_e32 v38, v91, v38
	s_waitcnt lgkmcnt(0)
	v_mfma_f32_32x32x16_bf16 v[2:17], v[46:49], v[34:37], v[2:17]
	v_add_u32_e32 v34, s10, v213
	ds_read_b64_tr_b16 v[150:151], v181 offset:8512
	ds_read_b64_tr_b16 v[148:149], v181 offset:7232
	v_add_f32_e32 v38, v92, v38
	s_waitcnt vmcnt(15)
	ds_write_b128 v231, v[58:61]
	s_waitcnt vmcnt(14)
	ds_write_b128 v232, v[74:77] offset:4608
	s_waitcnt vmcnt(13)
	ds_write_b128 v231, v[78:81] offset:1152
	s_waitcnt vmcnt(12)
	ds_write_b128 v232, v[82:85] offset:5888
	s_waitcnt vmcnt(11)
	ds_write_b128 v231, v[94:97] offset:2304
	s_waitcnt vmcnt(10)
	ds_write_b128 v232, v[98:101] offset:7168
	s_waitcnt vmcnt(9)
	ds_write_b128 v231, v[102:105] offset:3456
	s_waitcnt vmcnt(8)
	ds_write_b128 v232, v[138:141] offset:8448
	v_med3_i32 v34, v34, 0, v233
	v_add_f32_e32 v161, v93, v38
	v_mul_u32_u24_e32 v38, 0xc00, v34
	ds_read_b128 v[34:37], v177
	v_or_b32_e32 v38, v38, v176
	global_load_dwordx4 v[74:77], v38, s[8:9] offset:1024
	global_load_dwordx4 v[78:81], v38, s[8:9] offset:2048
	v_add_u32_e32 v38, s10, v214
	v_med3_i32 v38, v38, 0, v233
	v_mul_u32_u24_e32 v38, 0xc00, v38
	ds_read_b128 v[58:61], v177 offset:32
	v_mfma_f32_32x32x16_bf16 v[18:33], v[42:45], v[144:147], v[18:33]
	v_or_b32_e32 v86, v38, v176
	global_load_dwordx4 v[82:85], v86, s[8:9] offset:1024
	s_nop 0
	global_load_dwordx4 v[86:89], v86, s[8:9] offset:2048
	v_add_f32_e32 v143, v143, v161
	v_add_f32_e32 v143, v154, v143
	v_add_f32_e32 v143, v155, v143
	v_add_f32_e32 v143, v156, v143
	v_add_f32_e32 v143, v157, v143
	s_waitcnt lgkmcnt(1)
	v_mfma_f32_32x32x16_bf16 v[34:49], v[34:37], v[70:73], 0
	v_add_u32_e32 v70, s10, v215
	v_med3_i32 v70, v70, 0, v233
	v_mul_u32_u24_e32 v70, 0xc00, v70
	v_or_b32_e32 v94, v70, v176
	ds_read_b128 v[138:141], v177 offset:96
	ds_read_b128 v[70:73], v177 offset:64
	global_load_dwordx4 v[90:93], v94, s[8:9] offset:1024
	s_nop 0
	global_load_dwordx4 v[94:97], v94, s[8:9] offset:2048
	v_add_f32_e32 v143, v158, v143
	s_waitcnt lgkmcnt(2)
	v_mfma_f32_32x32x16_bf16 v[34:49], v[58:61], v[62:65], v[34:49]
	v_add_u32_e32 v58, s10, v216
	v_med3_i32 v58, v58, 0, v233
	v_mul_u32_u24_e32 v58, 0xc00, v58
	v_or_b32_e32 v58, v58, v176
	global_load_dwordx4 v[98:101], v58, s[8:9] offset:1024
	global_load_dwordx4 v[102:105], v58, s[8:9] offset:2048
	v_add_f32_e32 v143, v159, v143
	s_waitcnt lgkmcnt(0)
	v_mfma_f32_32x32x16_bf16 v[34:49], v[70:73], v[54:57], v[34:49]
	global_load_dwordx4 v[62:65], v[152:153], off
	global_load_dwordx4 v[58:61], v[152:153], off offset:32
	global_load_dwordx4 v[54:57], v[152:153], off offset:64
	global_load_dwordx4 v[70:73], v[152:153], off offset:96
	v_mfma_f32_32x32x16_bf16 v[34:49], v[138:141], v[66:69], v[34:49]
	v_add_u32_e32 v66, 0x80, v163
	v_cmp_le_u32_e32 vcc, v66, v51
	v_add_u32_e32 v67, 0x82, v163
	v_mfma_f32_32x32x16_bf16 v[2:17], v[148:151], v[144:147], v[2:17]
	s_nop 7
	v_cndmask_b32_e32 v66, v234, v34, vcc
	v_add_u32_e32 v34, 0x81, v163
	v_cmp_le_u32_e32 vcc, v34, v51
	s_nop 1
	v_cndmask_b32_e32 v35, v234, v35, vcc
	v_cmp_le_u32_e32 vcc, v67, v51
	v_add_u32_e32 v67, 0x83, v163
	v_max3_f32 v34, v66, s31, v35
	v_cndmask_b32_e32 v36, v234, v36, vcc
	v_cmp_le_u32_e32 vcc, v67, v51
	v_add_u32_e32 v67, 0x88, v163
	s_nop 0
	v_cndmask_b32_e32 v37, v234, v37, vcc
	v_cmp_le_u32_e32 vcc, v67, v51
	v_add_u32_e32 v67, 0x89, v163
	v_max3_f32 v34, v34, v36, v37
	v_cndmask_b32_e32 v38, v234, v38, vcc
	v_cmp_le_u32_e32 vcc, v67, v51
	v_add_u32_e32 v67, 0x8a, v163
	s_nop 0
	v_cndmask_b32_e32 v39, v234, v39, vcc
	v_cmp_le_u32_e32 vcc, v67, v51
	v_add_u32_e32 v67, 0x8b, v163
	v_max3_f32 v34, v34, v38, v39
	v_cndmask_b32_e32 v40, v234, v40, vcc
	v_cmp_le_u32_e32 vcc, v67, v51
	v_add_u32_e32 v67, 0x90, v163
	s_nop 0
	v_cndmask_b32_e32 v41, v234, v41, vcc
	v_cmp_le_u32_e32 vcc, v67, v51
	v_add_u32_e32 v67, 0x91, v163
	v_max3_f32 v34, v34, v40, v41
	v_cndmask_b32_e32 v42, v234, v42, vcc
	v_cmp_le_u32_e32 vcc, v67, v51
	v_add_u32_e32 v67, 0x92, v163
	s_nop 0
	v_cndmask_b32_e32 v43, v234, v43, vcc
	v_cmp_le_u32_e32 vcc, v67, v51
	v_add_u32_e32 v67, 0x93, v163
	v_max3_f32 v34, v34, v42, v43
	v_cndmask_b32_e32 v44, v234, v44, vcc
	v_cmp_le_u32_e32 vcc, v67, v51
	v_add_u32_e32 v67, 0x98, v163
	s_nop 0
	v_cndmask_b32_e32 v45, v234, v45, vcc
	v_cmp_le_u32_e32 vcc, v67, v51
	v_add_u32_e32 v67, 0x99, v163
	v_max3_f32 v34, v34, v44, v45
	v_cndmask_b32_e32 v46, v234, v46, vcc
	v_cmp_le_u32_e32 vcc, v67, v51
	v_add_u32_e32 v67, 0x9a, v163
	s_nop 0
	v_cndmask_b32_e32 v47, v234, v47, vcc
	v_cmp_le_u32_e32 vcc, v67, v51
	v_add_u32_e32 v67, 0x9b, v163
	v_max3_f32 v34, v34, v46, v47
	v_cndmask_b32_e32 v48, v234, v48, vcc
	v_cmp_le_u32_e32 vcc, v67, v51
	s_nop 1
	v_cndmask_b32_e32 v49, v234, v49, vcc
	v_max3_f32 v51, v34, v48, v49
	v_mov_b32_e32 v67, v51
	s_nop 1
	v_permlane32_swap_b32_e32 v67, v51
	v_add_f32_e32 v34, v160, v143
	v_add_f32_e32 v34, v142, v34
	s_waitcnt lgkmcnt(0)
	v_max_f32_e32 v67, v67, v67
	v_max_f32_e32 v51, v51, v67
	v_cmp_gt_f32_e32 vcc, v51, v164
	s_cbranch_vccz .LBB0_420
; __device__ __forceinline__ unsigned cvt_pk_bf16(float lo, float hi) { unsigned r; asm volatile("v_cvt_pk_bf16_f32 %0, %1, %2" : "=v"(r) : "v"(lo), "v"(hi)); return r; }
; template <int STAGE, int OFF> __device__ __forceinline__ void attn32_unit(const bf16* base, bf16* yrow0, int blk0, int u, LAS unsigned char* xtab, LAS unsigned char* kbuf, LAS unsigned char* vbuf, int lane, ...
;     ...
;         if (__any(mx > m)) {
;             const float mn = fmaxf(m, mx), alpha = __builtin_amdgcn_exp2f(m - mn); m = mn; l *= alpha;
; #pragma unroll
;             for (int i = 0; i < 16; ++i) { o[0][i] *= alpha; o[1][i] *= alpha; }
;         }
;         float ps = 0.f;
; #pragma unroll
;         for (int rg = 0; rg < 16; ++rg) { sc[rg] = __builtin_amdgcn_exp2f(sc[rg] - m); ps += sc[rg]; }
;         l += ps;
;         bf16x8 pb[2];
; #pragma unroll
;         for (int s2 = 0; s2 < 2; ++s2) { v4u w; w.x = pg8::cvt_pk_bf16(sc[8 * s2], sc[8 * s2 + 1]); w.y = pg8::cvt_pk_bf16(sc[8 * s2 + 2], sc[8 * s2 + 3]); w.z = pg8::cvt_pk_bf16(sc[8 * s2 + 4], sc[8 * s2 + 5]); w.w = pg8::cvt_pk_bf16(sc[8 * s2 + 6], sc[8 * s2 + 7]); pb[s2] = __builtin_bit_cast(bf16x8, w); }
; #pragma unroll
;         for (int mb = 0; mb < 2; ++mb)
; #pragma unroll
;             for (int s2 = 0; s2 < 2; ++s2) {
;                 LAS unsigned char* vp = vbuf + tr_off + (16 * s2) * 160 + 64 * mb;
;                 const v4i16 a0 = __builtin_amdgcn_ds_read_tr16_b64_v4i16((LAS v4i16*)vp), a1 = __builtin_amdgcn_ds_read_tr16_b64_v4i16((LAS v4i16*)(vp + 8 * 160));
;                 const bf16x8 va = __builtin_shufflevector(a0, a1, 0, 1, 2, 3, 4, 5, 6, 7);
;                 o[mb] = MFMA32(va, pb[s2], o[mb]);
;             }
;         asm volatile("" ::: "memory");
;     }
;     l += __shfl_xor(l, 32);
;     if (STAGE < 2) {
; #pragma unroll
;         for (int mb = 0; mb < 2; ++mb)
; #pragma unroll
;             for (int gq = 0; gq < 4; ++gq) { v2u w; w.x = pk2(o[mb][4 * gq], o[mb][4 * gq + 1]); w.y = pk2(o[mb][4 * gq + 2], o[mb][4 * gq + 3]); *(LAS v2u*)(xrow + 2 * (32 * mb + 8 * gq + 4 * h)) = w; }
;         if (h == 0) { *(LAS float*)(xrow + 128) = m; *(LAS float*)(xrow + 132) = l; }
;     } else {
;         const float inv = __builtin_amdgcn_rcpf(l);
;         bf16* yo = yrow0 + (size_t)tq * 1024 + 4 * h;
; #pragma unroll
;         for (int mb = 0; mb < 2; ++mb)
; #pragma unroll
	v_max_f32_e32 v51, v51, v51
	v_max_f32_e32 v67, v164, v164
	v_max_f32_e32 v51, v67, v51
	v_sub_f32_e32 v67, v164, v51
	v_exp_f32_e32 v68, v67
	v_mov_b32_e32 v164, v51
	v_pk_mul_f32 v[32:33], v[32:33], v[68:69] op_sel_hi:[1,0]
	v_pk_mul_f32 v[30:31], v[30:31], v[68:69] op_sel_hi:[1,0]
	v_pk_mul_f32 v[28:29], v[28:29], v[68:69] op_sel_hi:[1,0]
	v_pk_mul_f32 v[26:27], v[26:27], v[68:69] op_sel_hi:[1,0]
	v_pk_mul_f32 v[24:25], v[24:25], v[68:69] op_sel_hi:[1,0]
	v_pk_mul_f32 v[22:23], v[22:23], v[68:69] op_sel_hi:[1,0]
	v_pk_mul_f32 v[20:21], v[20:21], v[68:69] op_sel_hi:[1,0]
	v_pk_mul_f32 v[18:19], v[18:19], v[68:69] op_sel_hi:[1,0]
	v_pk_mul_f32 v[16:17], v[16:17], v[68:69] op_sel_hi:[1,0]
	v_pk_mul_f32 v[14:15], v[14:15], v[68:69] op_sel_hi:[1,0]
	v_pk_mul_f32 v[12:13], v[12:13], v[68:69] op_sel_hi:[1,0]
	v_pk_mul_f32 v[10:11], v[10:11], v[68:69] op_sel_hi:[1,0]
	v_pk_mul_f32 v[8:9], v[8:9], v[68:69] op_sel_hi:[1,0]
	v_pk_mul_f32 v[6:7], v[6:7], v[68:69] op_sel_hi:[1,0]
	v_pk_mul_f32 v[4:5], v[4:5], v[68:69] op_sel_hi:[1,0]
	v_pk_mul_f32 v[2:3], v[2:3], v[68:69] op_sel_hi:[1,0]
	v_mul_f32_e32 v34, v34, v68
.LBB0_420:
	v_sub_f32_e32 v36, v36, v164
	v_exp_f32_e32 v142, v36
	v_sub_f32_e32 v36, v37, v164
	v_exp_f32_e32 v143, v36
	v_sub_f32_e32 v36, v38, v164
	v_exp_f32_e32 v144, v36
	v_sub_f32_e32 v36, v39, v164
	v_exp_f32_e32 v145, v36
	v_sub_f32_e32 v36, v40, v164
	v_exp_f32_e32 v146, v36
	v_sub_f32_e32 v36, v41, v164
	v_exp_f32_e32 v147, v36
	v_sub_f32_e32 v36, v42, v164
	v_exp_f32_e32 v148, v36
	v_sub_f32_e32 v36, v43, v164
	v_exp_f32_e32 v149, v36
	v_sub_f32_e32 v36, v44, v164
	v_sub_f32_e32 v51, v66, v164
	v_exp_f32_e32 v150, v36
	v_sub_f32_e32 v36, v45, v164
	v_exp_f32_e32 v51, v51
	v_sub_f32_e32 v35, v35, v164
	v_exp_f32_e32 v151, v36
	v_sub_f32_e32 v36, v46, v164
	v_exp_f32_e32 v35, v35
	v_exp_f32_e32 v152, v36
	v_sub_f32_e32 v36, v47, v164
	v_exp_f32_e32 v153, v36
	v_sub_f32_e32 v36, v48, v164
	v_exp_f32_e32 v48, v36
	v_sub_f32_e32 v36, v49, v164
	v_exp_f32_e32 v49, v36
	v_cvt_pk_bf16_f32 v36, v51, v35
	v_add_f32_e32 v51, 0, v51
	v_add_f32_e32 v35, v35, v51
	v_add_f32_e32 v35, v142, v35
	v_add_f32_e32 v35, v143, v35
	v_add_f32_e32 v35, v144, v35
	v_cvt_pk_bf16_f32 v37, v142, v143
	v_cvt_pk_bf16_f32 v38, v144, v145
	v_cvt_pk_bf16_f32 v39, v146, v147
	v_cvt_pk_bf16_f32 v40, v148, v149
	v_cvt_pk_bf16_f32 v41, v150, v151
	v_cvt_pk_bf16_f32 v42, v152, v153
	v_cvt_pk_bf16_f32 v43, v48, v49
	ds_read_b64_tr_b16 v[44:45], v181 offset:4608
	ds_read_b64_tr_b16 v[46:47], v181 offset:5888
	v_add_f32_e32 v35, v145, v35
	v_add_f32_e32 v35, v146, v35
	v_add_f32_e32 v35, v147, v35
	v_add_f32_e32 v35, v148, v35
	v_add_f32_e32 v35, v149, v35
	s_waitcnt lgkmcnt(0)
	v_mfma_f32_32x32x16_bf16 v[18:33], v[44:47], v[36:39], v[18:33]
	v_add_f32_e32 v35, v150, v35
	v_add_f32_e32 v35, v151, v35
	v_add_f32_e32 v35, v152, v35
	v_add_f32_e32 v35, v153, v35
	v_add_f32_e32 v35, v48, v35
	ds_read_b64_tr_b16 v[66:67], v181 offset:7168
	ds_read_b64_tr_b16 v[68:69], v181 offset:8448
	ds_read_b64_tr_b16 v[140:141], v181 offset:5952
	ds_read_b64_tr_b16 v[138:139], v181 offset:4672
	v_add_f32_e32 v35, v49, v35
	v_add_f32_e32 v34, v34, v35
	v_mov_b32_e32 v35, v34
	s_nop 1
	v_permlane32_swap_b32_e32 v35, v34
	s_waitcnt lgkmcnt(2)
	v_mfma_f32_32x32x16_bf16 v[18:33], v[66:69], v[40:43], v[18:33]
	s_ashr_i32 s13, s12, 31
	s_lshl_b64 s[12:13], s[12:13], 25
	s_add_u32 s0, s18, s12
	s_waitcnt lgkmcnt(0)
	v_add_f32_e32 v34, v34, v35
	v_rcp_f32_e32 v34, v34
	s_addc_u32 s1, s19, s13
	s_add_u32 s12, s0, s39
	v_mfma_f32_32x32x16_bf16 v[2:17], v[138:141], v[36:39], v[2:17]
	s_nop 2
	v_mov_b32_e32 v38, v18
	v_mov_b32_e32 v39, v20
	v_mul_f32_e64 v38, v38, v34
	v_mul_f32_e64 v39, v39, v34
	v_mov_b32_e32 v20, v19
	v_pk_mul_f32 v[18:19], v[20:21], v[34:35] op_sel_hi:[1,0]
	v_and_b32_sdwa v21, v38, v236 dst_sel:DWORD dst_unused:UNUSED_PAD src0_sel:WORD_1 src1_sel:DWORD
	v_mov_b32_e32 v163, v169
	v_add3_u32 v21, v38, v21, s35
	v_and_b32_sdwa v35, v19, v236 dst_sel:DWORD dst_unused:UNUSED_PAD src0_sel:WORD_1 src1_sel:DWORD
	v_and_b32_sdwa v38, v18, v236 dst_sel:DWORD dst_unused:UNUSED_PAD src0_sel:WORD_1 src1_sel:DWORD
	s_addc_u32 s13, s1, 0
	v_lshlrev_b64 v[36:37], 11, v[162:163]
	v_and_b32_sdwa v20, v39, v236 dst_sel:DWORD dst_unused:UNUSED_PAD src0_sel:WORD_1 src1_sel:DWORD
	v_add3_u32 v19, v19, v35, s35
	v_add3_u32 v18, v18, v38, s35
	v_lshl_add_u64 v[36:37], s[12:13], 0, v[36:37]
	v_mov_b32_e32 v171, v169
	v_add3_u32 v20, v39, v20, s35
	v_and_b32_e32 v19, 0xffff0000, v19
	v_and_b32_e32 v18, 0xffff0000, v18
	v_lshl_add_u64 v[36:37], v[36:37], 0, v[170:171]
	v_or_b32_sdwa v19, v19, v20 dst_sel:DWORD dst_unused:UNUSED_PAD src0_sel:DWORD src1_sel:WORD_1
	v_or_b32_sdwa v18, v18, v21 dst_sel:DWORD dst_unused:UNUSED_PAD src0_sel:DWORD src1_sel:WORD_1
	ds_read_b64_tr_b16 v[46:47], v181 offset:8512
	ds_read_b64_tr_b16 v[44:45], v181 offset:7232
	global_store_dwordx2 v[36:37], v[18:19], off
	v_mov_b32_e32 v18, v22
	v_mov_b32_e32 v19, v24
	v_pk_mul_f32 v[18:19], v[18:19], v[34:35] op_sel_hi:[1,0]
	v_mov_b32_e32 v24, v23
	v_pk_mul_f32 v[20:21], v[24:25], v[34:35] op_sel_hi:[1,0]
	v_and_b32_sdwa v22, v19, v236 dst_sel:DWORD dst_unused:UNUSED_PAD src0_sel:WORD_1 src1_sel:DWORD
	v_and_b32_sdwa v23, v18, v236 dst_sel:DWORD dst_unused:UNUSED_PAD src0_sel:WORD_1 src1_sel:DWORD
	v_add3_u32 v18, v18, v23, s35
	v_add3_u32 v19, v19, v22, s35
	v_and_b32_sdwa v22, v21, v236 dst_sel:DWORD dst_unused:UNUSED_PAD src0_sel:WORD_1 src1_sel:DWORD
	v_and_b32_sdwa v23, v20, v236 dst_sel:DWORD dst_unused:UNUSED_PAD src0_sel:WORD_1 src1_sel:DWORD
	v_add3_u32 v21, v21, v22, s35
	v_add3_u32 v20, v20, v23, s35
	v_and_b32_e32 v21, 0xffff0000, v21
	v_and_b32_e32 v20, 0xffff0000, v20
	v_or_b32_sdwa v19, v21, v19 dst_sel:DWORD dst_unused:UNUSED_PAD src0_sel:DWORD src1_sel:WORD_1
	v_or_b32_sdwa v18, v20, v18 dst_sel:DWORD dst_unused:UNUSED_PAD src0_sel:DWORD src1_sel:WORD_1
	global_store_dwordx2 v[36:37], v[18:19], off offset:16
	v_mov_b32_e32 v18, v26
	v_mov_b32_e32 v19, v28
	v_pk_mul_f32 v[18:19], v[18:19], v[34:35] op_sel_hi:[1,0]
	v_mov_b32_e32 v28, v27
	v_pk_mul_f32 v[20:21], v[28:29], v[34:35] op_sel_hi:[1,0]
	v_and_b32_sdwa v22, v19, v236 dst_sel:DWORD dst_unused:UNUSED_PAD src0_sel:WORD_1 src1_sel:DWORD
	v_and_b32_sdwa v23, v18, v236 dst_sel:DWORD dst_unused:UNUSED_PAD src0_sel:WORD_1 src1_sel:DWORD
	v_add3_u32 v18, v18, v23, s35
	v_add3_u32 v19, v19, v22, s35
	v_and_b32_sdwa v22, v21, v236 dst_sel:DWORD dst_unused:UNUSED_PAD src0_sel:WORD_1 src1_sel:DWORD
	v_and_b32_sdwa v23, v20, v236 dst_sel:DWORD dst_unused:UNUSED_PAD src0_sel:WORD_1 src1_sel:DWORD
	v_add3_u32 v21, v21, v22, s35
	v_add3_u32 v20, v20, v23, s35
	v_and_b32_e32 v21, 0xffff0000, v21
	v_and_b32_e32 v20, 0xffff0000, v20
	s_waitcnt lgkmcnt(0)
; __device__ __forceinline__ float bf_lo(unsigned w) { return __uint_as_float(w << 16); }
; __device__ __forceinline__ float bf_hi(unsigned w) { return __uint_as_float(w & 0xffff0000u); }
; #define LAS __attribute__((address_space(3)))
; __device__ __forceinline__ unsigned pk2(float lo, float hi) { return f2bf(lo) | (f2bf(hi) << 16); }
; template <int STAGE, int OFF> __device__ __forceinline__ void attn32_unit(const bf16* base, bf16* yrow0, int blk0, int u, LAS unsigned char* xtab, LAS unsigned char* kbuf, LAS unsigned char* vbuf, int lane, ...
;     ...
;     } else {
; #pragma unroll
;         for (int mb = 0; mb < 2; ++mb)
; #pragma unroll
;             for (int gq = 0; gq < 4; ++gq) { const v2u w = *(const LAS v2u*)(xrow + 2 * (32 * mb + 8 * gq + 4 * h)); o[mb][4 * gq] = bf_lo(w.x); o[mb][4 * gq + 1] = bf_hi(w.x); o[mb][4 * gq + 2] = bf_lo(w.y); o[mb][4 * gq + 3] = bf_hi(w.y); }
;         m = *(const LAS float*)(xrow + 128); l = h == 0 ? *(const LAS float*)(xrow + 132) : 0.f;
;     ...
;         const float inv = __builtin_amdgcn_rcpf(l);
;         bf16* yo = yrow0 + (size_t)tq * 1024 + 4 * h;
; #pragma unroll
;         for (int mb = 0; mb < 2; ++mb)
; #pragma unroll
;             for (int gq = 0; gq < 4; ++gq) { uint2 w; w.x = pk2(o[mb][4 * gq] * inv, o[mb][4 * gq + 1] * inv); w.y = pk2(o[mb][4 * gq + 2] * inv, o[mb][4 * gq + 3] * inv); *(uint2*)(yo + 32 * mb + 8 * gq) = w; }
	v_mfma_f32_32x32x16_bf16 v[2:17], v[44:47], v[40:43], v[2:17]
	v_or_b32_sdwa v19, v21, v19 dst_sel:DWORD dst_unused:UNUSED_PAD src0_sel:DWORD src1_sel:WORD_1
	v_or_b32_sdwa v18, v20, v18 dst_sel:DWORD dst_unused:UNUSED_PAD src0_sel:DWORD src1_sel:WORD_1
	global_store_dwordx2 v[36:37], v[18:19], off offset:32
	v_mov_b32_e32 v18, v30
	v_mov_b32_e32 v19, v32
	v_pk_mul_f32 v[18:19], v[18:19], v[34:35] op_sel_hi:[1,0]
	v_mov_b32_e32 v32, v31
	v_pk_mul_f32 v[20:21], v[32:33], v[34:35] op_sel_hi:[1,0]
	v_and_b32_sdwa v22, v19, v236 dst_sel:DWORD dst_unused:UNUSED_PAD src0_sel:WORD_1 src1_sel:DWORD
	v_and_b32_sdwa v23, v18, v236 dst_sel:DWORD dst_unused:UNUSED_PAD src0_sel:WORD_1 src1_sel:DWORD
	v_add3_u32 v18, v18, v23, s35
	v_add3_u32 v19, v19, v22, s35
	v_and_b32_sdwa v22, v21, v236 dst_sel:DWORD dst_unused:UNUSED_PAD src0_sel:WORD_1 src1_sel:DWORD
	v_and_b32_sdwa v23, v20, v236 dst_sel:DWORD dst_unused:UNUSED_PAD src0_sel:WORD_1 src1_sel:DWORD
	v_add3_u32 v21, v21, v22, s35
	v_add3_u32 v20, v20, v23, s35
	v_and_b32_e32 v21, 0xffff0000, v21
	v_and_b32_e32 v20, 0xffff0000, v20
	v_or_b32_sdwa v19, v21, v19 dst_sel:DWORD dst_unused:UNUSED_PAD src0_sel:DWORD src1_sel:WORD_1
	v_or_b32_sdwa v18, v20, v18 dst_sel:DWORD dst_unused:UNUSED_PAD src0_sel:DWORD src1_sel:WORD_1
	global_store_dwordx2 v[36:37], v[18:19], off offset:48
	v_mov_b32_e32 v18, v2
	v_mov_b32_e32 v19, v4
	v_pk_mul_f32 v[18:19], v[18:19], v[34:35] op_sel_hi:[1,0]
	v_mov_b32_e32 v4, v3
	v_pk_mul_f32 v[2:3], v[4:5], v[34:35] op_sel_hi:[1,0]
	v_and_b32_sdwa v4, v19, v236 dst_sel:DWORD dst_unused:UNUSED_PAD src0_sel:WORD_1 src1_sel:DWORD
	v_and_b32_sdwa v5, v18, v236 dst_sel:DWORD dst_unused:UNUSED_PAD src0_sel:WORD_1 src1_sel:DWORD
	v_add3_u32 v5, v18, v5, s35
	v_add3_u32 v4, v19, v4, s35
	v_and_b32_sdwa v18, v3, v236 dst_sel:DWORD dst_unused:UNUSED_PAD src0_sel:WORD_1 src1_sel:DWORD
	v_and_b32_sdwa v19, v2, v236 dst_sel:DWORD dst_unused:UNUSED_PAD src0_sel:WORD_1 src1_sel:DWORD
	v_add3_u32 v3, v3, v18, s35
	v_add3_u32 v2, v2, v19, s35
	v_and_b32_e32 v3, 0xffff0000, v3
	v_and_b32_e32 v2, 0xffff0000, v2
	v_or_b32_sdwa v3, v3, v4 dst_sel:DWORD dst_unused:UNUSED_PAD src0_sel:DWORD src1_sel:WORD_1
	v_or_b32_sdwa v2, v2, v5 dst_sel:DWORD dst_unused:UNUSED_PAD src0_sel:DWORD src1_sel:WORD_1
	global_store_dwordx2 v[36:37], v[2:3], off offset:64
	v_mov_b32_e32 v2, v6
	v_mov_b32_e32 v3, v8
	v_pk_mul_f32 v[2:3], v[2:3], v[34:35] op_sel_hi:[1,0]
	v_mov_b32_e32 v8, v7
	v_pk_mul_f32 v[4:5], v[8:9], v[34:35] op_sel_hi:[1,0]
	v_and_b32_sdwa v6, v3, v236 dst_sel:DWORD dst_unused:UNUSED_PAD src0_sel:WORD_1 src1_sel:DWORD
	v_and_b32_sdwa v7, v2, v236 dst_sel:DWORD dst_unused:UNUSED_PAD src0_sel:WORD_1 src1_sel:DWORD
	v_add3_u32 v2, v2, v7, s35
	v_add3_u32 v3, v3, v6, s35
	v_and_b32_sdwa v6, v5, v236 dst_sel:DWORD dst_unused:UNUSED_PAD src0_sel:WORD_1 src1_sel:DWORD
	v_and_b32_sdwa v7, v4, v236 dst_sel:DWORD dst_unused:UNUSED_PAD src0_sel:WORD_1 src1_sel:DWORD
	v_add3_u32 v5, v5, v6, s35
	v_add3_u32 v4, v4, v7, s35
	v_and_b32_e32 v5, 0xffff0000, v5
	v_and_b32_e32 v4, 0xffff0000, v4
	v_or_b32_sdwa v3, v5, v3 dst_sel:DWORD dst_unused:UNUSED_PAD src0_sel:DWORD src1_sel:WORD_1
	v_or_b32_sdwa v2, v4, v2 dst_sel:DWORD dst_unused:UNUSED_PAD src0_sel:DWORD src1_sel:WORD_1
	global_store_dwordx2 v[36:37], v[2:3], off offset:80
	v_mov_b32_e32 v2, v10
	v_mov_b32_e32 v3, v12
	v_pk_mul_f32 v[2:3], v[2:3], v[34:35] op_sel_hi:[1,0]
	v_mov_b32_e32 v12, v11
	v_pk_mul_f32 v[4:5], v[12:13], v[34:35] op_sel_hi:[1,0]
	v_and_b32_sdwa v6, v3, v236 dst_sel:DWORD dst_unused:UNUSED_PAD src0_sel:WORD_1 src1_sel:DWORD
	v_and_b32_sdwa v7, v2, v236 dst_sel:DWORD dst_unused:UNUSED_PAD src0_sel:WORD_1 src1_sel:DWORD
	v_add3_u32 v2, v2, v7, s35
	v_add3_u32 v3, v3, v6, s35
	v_and_b32_sdwa v6, v5, v236 dst_sel:DWORD dst_unused:UNUSED_PAD src0_sel:WORD_1 src1_sel:DWORD
	v_and_b32_sdwa v7, v4, v236 dst_sel:DWORD dst_unused:UNUSED_PAD src0_sel:WORD_1 src1_sel:DWORD
	v_add3_u32 v5, v5, v6, s35
	v_add3_u32 v4, v4, v7, s35
	v_and_b32_e32 v5, 0xffff0000, v5
	v_and_b32_e32 v4, 0xffff0000, v4
	v_or_b32_sdwa v3, v5, v3 dst_sel:DWORD dst_unused:UNUSED_PAD src0_sel:DWORD src1_sel:WORD_1
	v_or_b32_sdwa v2, v4, v2 dst_sel:DWORD dst_unused:UNUSED_PAD src0_sel:DWORD src1_sel:WORD_1
	global_store_dwordx2 v[36:37], v[2:3], off offset:96
	v_mov_b32_e32 v2, v14
	v_mov_b32_e32 v3, v16
	v_pk_mul_f32 v[2:3], v[2:3], v[34:35] op_sel_hi:[1,0]
	v_mov_b32_e32 v16, v15
	v_pk_mul_f32 v[4:5], v[16:17], v[34:35] op_sel_hi:[1,0]
	v_and_b32_sdwa v7, v2, v236 dst_sel:DWORD dst_unused:UNUSED_PAD src0_sel:WORD_1 src1_sel:DWORD
	v_and_b32_sdwa v6, v3, v236 dst_sel:DWORD dst_unused:UNUSED_PAD src0_sel:WORD_1 src1_sel:DWORD
	v_add3_u32 v18, v2, v7, s35
	v_and_b32_sdwa v2, v5, v236 dst_sel:DWORD dst_unused:UNUSED_PAD src0_sel:WORD_1 src1_sel:DWORD
	v_add3_u32 v19, v3, v6, s35
	v_and_b32_sdwa v3, v4, v236 dst_sel:DWORD dst_unused:UNUSED_PAD src0_sel:WORD_1 src1_sel:DWORD
	v_add3_u32 v2, v5, v2, s35
	v_add_u32_e32 v14, v229, v166
	v_add3_u32 v20, v4, v3, s35
	v_and_b32_e32 v21, 0xffff0000, v2
	ds_read2_b64 v[10:13], v14 offset1:2
	ds_read2_b64 v[2:5], v14 offset0:4 offset1:6
	ds_read2_b64 v[6:9], v14 offset0:8 offset1:10
	ds_read2_b64 v[14:17], v14 offset0:12 offset1:14
	ds_read_b32 v139, v229 offset:128
	v_and_b32_e32 v20, 0xffff0000, v20
	v_mov_b32_e32 v140, 0
	v_or_b32_sdwa v19, v21, v19 dst_sel:DWORD dst_unused:UNUSED_PAD src0_sel:DWORD src1_sel:WORD_1
	v_or_b32_sdwa v18, v20, v18 dst_sel:DWORD dst_unused:UNUSED_PAD src0_sel:DWORD src1_sel:WORD_1
	global_store_dwordx2 v[36:37], v[18:19], off offset:112
	s_and_saveexec_b64 s[14:15], s[4:5]
	ds_read_b32 v140, v229 offset:132
	s_or_b64 exec, exec, s[14:15]
	s_waitcnt vmcnt(27)
; __device__ __forceinline__ float bf_lo(unsigned w) { return __uint_as_float(w << 16); }
; __device__ __forceinline__ float bf_hi(unsigned w) { return __uint_as_float(w & 0xffff0000u); }
; #define LAS __attribute__((address_space(3)))
; #define MFMA32(a, b, c) __builtin_amdgcn_mfma_f32_32x32x16_bf16((a), (b), (c), 0, 0, 0)
; template <int STAGE, int OFF> __device__ __forceinline__ void attn32_unit(const bf16* base, bf16* yrow0, int blk0, int u, LAS unsigned char* xtab, LAS unsigned char* kbuf, LAS unsigned char* vbuf, int lane, ...
;     ...
;         for (int mb = 0; mb < 2; ++mb)
; #pragma unroll
;             for (int gq = 0; gq < 4; ++gq) { const v2u w = *(const LAS v2u*)(xrow + 2 * (32 * mb + 8 * gq + 4 * h)); o[mb][4 * gq] = bf_lo(w.x); o[mb][4 * gq + 1] = bf_hi(w.x); o[mb][4 * gq + 2] = bf_lo(w.y); o[mb][4 * gq + 3] = bf_hi(w.y); }
;         m = *(const LAS float*)(xrow + 128); l = h == 0 ? *(const LAS float*)(xrow + 132) : 0.f;
;     }
;     const int hi = qi, lo = max(qi - 128, -(t0 >> SH));
;     const unsigned mspan = (unsigned)(hi - lo);
; #pragma unroll
;     for (int pp = 0; pp < 5; ++pp) {
;         constexpr int dummy = 0; (void)dummy;
;         const int set = (pp + OFF) % 2, n0 = -128 + 32 * pp;
; #pragma unroll
;         for (int c = 0; c < 4; ++c) { *(LAS v4u*)(kbuf + (8 * c + lrow) * 144 + lch * 16) = kr[set][c]; *(LAS v4u*)(vbuf + (8 * c + lrow) * 160 + lch * 16) = vr[set][c]; }
;         if (pp + 2 < 5) { ATT32_LOAD(set, pp + 2, t0, SH); }
;         else { const bf16* base_ = base; { const bf16* base = nbase; ATT32_LOAD(set, pp + 2 - 5, nt0, nsh); } (void)base_; }
;         f32x16 sc;
; #pragma unroll
;         for (int i = 0; i < 16; ++i) sc[i] = 0.f;
; #pragma unroll
;         for (int ks = 0; ks < 4; ++ks) { const bf16x8 ka = *(const LAS bf16x8*)(kbuf + qi * 144 + 32 * ks + 16 * h); sc = MFMA32(ka, qb[ks], sc); }
;         if (pp == 4) {
; #pragma unroll
;             for (int ks = 0; ks < 4; ++ks) qb[ks] = *(const bf16x8*)(nbase + (size_t)min(nt0 + (qi << nsh), SEQ - 1) * 1536 + 16 * ks + 8 * h);
;         }
;         const int mbase = n0 + 4 * h - lo; float mx = -INFINITY;
; #pragma unroll
;         for (int rg = 0; rg < 16; ++rg) { sc[rg] = ((unsigned)(mbase + (rg & 3) + 8 * (rg >> 2)) <= mspan) ? sc[rg] : -INFINITY; mx = fmaxf(mx, sc[rg]); }
;         mx = fmaxf(mx, __shfl_xor(mx, 32));
	ds_write_b128 v231, v[106:109]
	s_waitcnt vmcnt(26)
	ds_write_b128 v232, v[110:113] offset:4608
	s_waitcnt vmcnt(25)
	ds_write_b128 v231, v[114:117] offset:1152
	s_waitcnt vmcnt(24)
	ds_write_b128 v232, v[118:121] offset:5888
	s_waitcnt vmcnt(23)
	ds_write_b128 v231, v[122:125] offset:2304
	s_waitcnt vmcnt(22)
	ds_write_b128 v232, v[126:129] offset:7168
	s_waitcnt vmcnt(21)
	ds_write_b128 v231, v[130:133] offset:3456
	s_waitcnt vmcnt(20)
	ds_write_b128 v232, v[134:137] offset:8448
	ds_read_b128 v[34:37], v177
	s_waitcnt lgkmcnt(13)
	v_lshlrev_b32_e32 v22, 16, v12
	v_and_b32_e32 v23, 0xffff0000, v12
	v_add_u32_e32 v12, s10, v218
	v_med3_i32 v12, v12, 0, v233
	v_mul_u32_u24_e32 v12, 0xc00, v12
	v_or_b32_e32 v12, v12, v176
	global_load_dwordx4 v[66:69], v12, s[8:9] offset:1024
	global_load_dwordx4 v[106:109], v12, s[8:9] offset:2048
	ds_read_b128 v[118:121], v177 offset:32
	v_add_u32_e32 v12, s10, v219
	s_waitcnt vmcnt(13) lgkmcnt(1)
	v_mfma_f32_32x32x16_bf16 v[34:49], v[34:37], v[62:65], 0
	v_med3_i32 v12, v12, 0, v233
	v_mul_u32_u24_e32 v12, 0xc00, v12
	v_or_b32_e32 v12, v12, v176
	global_load_dwordx4 v[110:113], v12, s[8:9] offset:1024
	global_load_dwordx4 v[114:117], v12, s[8:9] offset:2048
	v_add_u32_e32 v12, s10, v220
	v_med3_i32 v12, v12, 0, v233
	v_mul_u32_u24_e32 v12, 0xc00, v12
	v_or_b32_e32 v12, v12, v176
	ds_read_b128 v[134:137], v177 offset:96
	ds_read_b128 v[142:145], v177 offset:64
	s_waitcnt vmcnt(14) lgkmcnt(2)
	v_mfma_f32_32x32x16_bf16 v[34:49], v[118:121], v[58:61], v[34:49]
	global_load_dwordx4 v[118:121], v12, s[8:9] offset:1024
	global_load_dwordx4 v[122:125], v12, s[8:9] offset:2048
	v_add_u32_e32 v12, s10, v221
	v_med3_i32 v12, v12, 0, v233
	v_mul_u32_u24_e32 v12, 0xc00, v12
	v_or_b32_e32 v12, v12, v176
	global_load_dwordx4 v[126:129], v12, s[8:9] offset:1024
	global_load_dwordx4 v[130:133], v12, s[8:9] offset:2048
	s_lshr_b32 s0, s10, 4
	s_waitcnt vmcnt(17) lgkmcnt(0)
	v_mfma_f32_32x32x16_bf16 v[34:49], v[142:145], v[54:57], v[34:49]
	s_sub_i32 s0, 0, s0
	v_lshlrev_b32_e32 v18, 16, v10
	v_and_b32_e32 v19, 0xffff0000, v10
	v_lshlrev_b32_e32 v20, 16, v11
	v_and_b32_e32 v21, 0xffff0000, v11
	v_lshlrev_b32_e32 v10, 16, v14
	v_and_b32_e32 v11, 0xffff0000, v14
	s_waitcnt vmcnt(16)
	v_mfma_f32_32x32x16_bf16 v[34:49], v[134:137], v[70:73], v[34:49]
	v_max_i32_e32 v14, s0, v175
	v_sub_u32_e32 v51, v1, v14
	v_sub_u32_e32 v138, v178, v14
	v_cmp_le_u32_e32 vcc, v138, v51
	v_add_u32_e32 v14, 1, v138
	v_lshlrev_b32_e32 v24, 16, v13
	v_and_b32_e32 v25, 0xffff0000, v13
	v_lshlrev_b32_e32 v12, 16, v15
	v_and_b32_e32 v13, 0xffff0000, v15
	s_nop 2
	v_cndmask_b32_e32 v34, v234, v34, vcc
	v_cmp_le_u32_e32 vcc, v14, v51
	v_add_u32_e32 v15, 2, v138
	v_lshlrev_b32_e32 v26, 16, v2
	v_cndmask_b32_e32 v35, v234, v35, vcc
	v_cmp_le_u32_e32 vcc, v15, v51
	v_add_u32_e32 v15, 3, v138
	v_max3_f32 v14, v34, s31, v35
	v_cndmask_b32_e32 v36, v234, v36, vcc
	v_cmp_le_u32_e32 vcc, v15, v51
	v_add_u32_e32 v15, 8, v138
	v_and_b32_e32 v27, 0xffff0000, v2
	v_cndmask_b32_e32 v37, v234, v37, vcc
	v_cmp_le_u32_e32 vcc, v15, v51
	v_add_u32_e32 v15, 9, v138
	v_max3_f32 v14, v14, v36, v37
	v_cndmask_b32_e32 v38, v234, v38, vcc
	v_cmp_le_u32_e32 vcc, v15, v51
	v_add_u32_e32 v15, 10, v138
	v_lshlrev_b32_e32 v28, 16, v3
	v_cndmask_b32_e32 v39, v234, v39, vcc
	v_cmp_le_u32_e32 vcc, v15, v51
	v_add_u32_e32 v15, 11, v138
	v_max3_f32 v14, v14, v38, v39
	v_cndmask_b32_e32 v40, v234, v40, vcc
	v_cmp_le_u32_e32 vcc, v15, v51
	v_add_u32_e32 v15, 16, v138
	v_and_b32_e32 v29, 0xffff0000, v3
	v_cndmask_b32_e32 v41, v234, v41, vcc
	v_cmp_le_u32_e32 vcc, v15, v51
	v_add_u32_e32 v15, 17, v138
	v_max3_f32 v14, v14, v40, v41
	v_cndmask_b32_e32 v42, v234, v42, vcc
	v_cmp_le_u32_e32 vcc, v15, v51
	v_add_u32_e32 v15, 18, v138
	v_lshlrev_b32_e32 v30, 16, v4
	v_cndmask_b32_e32 v43, v234, v43, vcc
	v_cmp_le_u32_e32 vcc, v15, v51
	v_add_u32_e32 v15, 19, v138
	v_max3_f32 v14, v14, v42, v43
	v_cndmask_b32_e32 v44, v234, v44, vcc
	v_cmp_le_u32_e32 vcc, v15, v51
	v_add_u32_e32 v15, 24, v138
	v_and_b32_e32 v31, 0xffff0000, v4
	v_cndmask_b32_e32 v45, v234, v45, vcc
	v_cmp_le_u32_e32 vcc, v15, v51
	v_add_u32_e32 v15, 25, v138
	v_max3_f32 v14, v14, v44, v45
	v_cndmask_b32_e32 v46, v234, v46, vcc
	v_cmp_le_u32_e32 vcc, v15, v51
	v_add_u32_e32 v15, 26, v138
	v_lshlrev_b32_e32 v32, 16, v5
	v_cndmask_b32_e32 v47, v234, v47, vcc
	v_cmp_le_u32_e32 vcc, v15, v51
	v_add_u32_e32 v15, 27, v138
	v_max3_f32 v14, v14, v46, v47
	v_cndmask_b32_e32 v48, v234, v48, vcc
	v_cmp_le_u32_e32 vcc, v15, v51
	v_and_b32_e32 v33, 0xffff0000, v5
	v_lshlrev_b32_e32 v2, 16, v6
	v_cndmask_b32_e32 v49, v234, v49, vcc
	v_max3_f32 v134, v14, v48, v49
	v_mov_b32_e32 v135, v134
	s_nop 1
	v_permlane32_swap_b32_e32 v135, v134
	v_and_b32_e32 v3, 0xffff0000, v6
	v_lshlrev_b32_e32 v4, 16, v7
	v_and_b32_e32 v5, 0xffff0000, v7
	v_lshlrev_b32_e32 v6, 16, v8
	s_waitcnt lgkmcnt(0)
	v_max_f32_e32 v135, v135, v135
	v_max_f32_e32 v134, v134, v135
	v_and_b32_e32 v7, 0xffff0000, v8
	v_lshlrev_b32_e32 v8, 16, v9
	v_and_b32_e32 v9, 0xffff0000, v9
	v_lshlrev_b32_e32 v14, 16, v16
	v_and_b32_e32 v15, 0xffff0000, v16
	v_lshlrev_b32_e32 v16, 16, v17
	v_and_b32_e32 v17, 0xffff0000, v17
	v_cmp_gt_f32_e32 vcc, v134, v139
	s_cbranch_vccz .LBB0_424
	v_max_f32_e32 v134, v134, v134
	v_max_f32_e32 v135, v139, v139
	v_max_f32_e32 v135, v135, v134
	v_sub_f32_e32 v134, v139, v135
	v_exp_f32_e32 v134, v134
	v_mov_b32_e32 v139, v135
	v_pk_mul_f32 v[16:17], v[134:135], v[16:17] op_sel_hi:[0,1]
	v_pk_mul_f32 v[14:15], v[134:135], v[14:15] op_sel_hi:[0,1]
	v_pk_mul_f32 v[12:13], v[134:135], v[12:13] op_sel_hi:[0,1]
	v_pk_mul_f32 v[10:11], v[134:135], v[10:11] op_sel_hi:[0,1]
	v_pk_mul_f32 v[8:9], v[134:135], v[8:9] op_sel_hi:[0,1]
	v_pk_mul_f32 v[6:7], v[134:135], v[6:7] op_sel_hi:[0,1]
	v_pk_mul_f32 v[4:5], v[134:135], v[4:5] op_sel_hi:[0,1]
	v_pk_mul_f32 v[2:3], v[134:135], v[2:3] op_sel_hi:[0,1]
	v_pk_mul_f32 v[32:33], v[134:135], v[32:33] op_sel_hi:[0,1]
	v_pk_mul_f32 v[30:31], v[134:135], v[30:31] op_sel_hi:[0,1]
	v_pk_mul_f32 v[28:29], v[134:135], v[28:29] op_sel_hi:[0,1]
	v_pk_mul_f32 v[26:27], v[134:135], v[26:27] op_sel_hi:[0,1]
	v_pk_mul_f32 v[24:25], v[134:135], v[24:25] op_sel_hi:[0,1]
	v_pk_mul_f32 v[22:23], v[134:135], v[22:23] op_sel_hi:[0,1]
	v_pk_mul_f32 v[20:21], v[134:135], v[20:21] op_sel_hi:[0,1]
	v_pk_mul_f32 v[18:19], v[134:135], v[18:19] op_sel_hi:[0,1]
	v_mul_f32_e32 v140, v140, v134
; #define LAS __attribute__((address_space(3)))
; template <int STAGE, int OFF> __device__ __forceinline__ void attn32_unit(const bf16* base, bf16* yrow0, int blk0, int u, LAS unsigned char* xtab, LAS unsigned char* kbuf, LAS unsigned char* vbuf, int lane, ...
;     ...
;         for (int c = 0; c < 4; ++c) { *(LAS v4u*)(kbuf + (8 * c + lrow) * 144 + lch * 16) = kr[set][c]; *(LAS v4u*)(vbuf + (8 * c + lrow) * 160 + lch * 16) = vr[set][c]; }
;         if (pp + 2 < 5) { ATT32_LOAD(set, pp + 2, t0, SH); }
;         else { const bf16* base_ = base; { const bf16* base = nbase; ATT32_LOAD(set, pp + 2 - 5, nt0, nsh); } (void)base_; }
;         f32x16 sc;
; #pragma unroll
;         for (int i = 0; i < 16; ++i) sc[i] = 0.f;
; #pragma unroll
;         for (int ks = 0; ks < 4; ++ks) { const bf16x8 ka = *(const LAS bf16x8*)(kbuf + qi * 144 + 32 * ks + 16 * h); sc = MFMA32(ka, qb[ks], sc); }
;         if (pp == 4) {
; #pragma unroll
;             for (int ks = 0; ks < 4; ++ks) qb[ks] = *(const bf16x8*)(nbase + (size_t)min(nt0 + (qi << nsh), SEQ - 1) * 1536 + 16 * ks + 8 * h);
;         }
;         const int mbase = n0 + 4 * h - lo; float mx = -INFINITY;
; #pragma unroll
;         for (int rg = 0; rg < 16; ++rg) { sc[rg] = ((unsigned)(mbase + (rg & 3) + 8 * (rg >> 2)) <= mspan) ? sc[rg] : -INFINITY; mx = fmaxf(mx, sc[rg]); }
;         mx = fmaxf(mx, __shfl_xor(mx, 32));
;         if (__any(mx > m)) {
;             const float mn = fmaxf(m, mx), alpha = __builtin_amdgcn_exp2f(m - mn); m = mn; l *= alpha;
; #pragma unroll
;             for (int i = 0; i < 16; ++i) { o[0][i] *= alpha; o[1][i] *= alpha; }
;         }
;         float ps = 0.f;
; #pragma unroll
;         for (int rg = 0; rg < 16; ++rg) { sc[rg] = __builtin_amdgcn_exp2f(sc[rg] - m); ps += sc[rg]; }
;         l += ps;
;         bf16x8 pb[2];
; #pragma unroll
;         for (int s2 = 0; s2 < 2; ++s2) { v4u w; w.x = pg8::cvt_pk_bf16(sc[8 * s2], sc[8 * s2 + 1]); w.y = pg8::cvt_pk_bf16(sc[8 * s2 + 2], sc[8 * s2 + 3]); w.z = pg8::cvt_pk_bf16(sc[8 * s2 + 4], sc[8 * s2 + 5]); w.w = pg8::cvt_pk_bf16(sc[8 * s2 + 6], sc[8 * s2 + 7]); pb[s2] = __builtin_bit_cast(bf16x8, w); }
; #pragma unroll
;         for (int mb = 0; mb < 2; ++mb)
; #pragma unroll
;             for (int s2 = 0; s2 < 2; ++s2) {
;                 LAS unsigned char* vp = vbuf + tr_off + (16 * s2) * 160 + 64 * mb;
.LBB0_424:
	v_sub_f32_e32 v34, v34, v139
	v_exp_f32_e32 v141, v34
	v_sub_f32_e32 v34, v35, v139
	v_exp_f32_e32 v146, v34
	v_sub_f32_e32 v34, v36, v139
	v_exp_f32_e32 v147, v34
	v_sub_f32_e32 v34, v37, v139
	v_exp_f32_e32 v148, v34
	v_sub_f32_e32 v34, v38, v139
	v_exp_f32_e32 v149, v34
	v_sub_f32_e32 v34, v39, v139
	v_exp_f32_e32 v150, v34
	v_sub_f32_e32 v34, v40, v139
	v_exp_f32_e32 v151, v34
	v_sub_f32_e32 v34, v41, v139
	v_exp_f32_e32 v152, v34
	v_sub_f32_e32 v34, v42, v139
	v_exp_f32_e32 v154, v34
	v_sub_f32_e32 v34, v43, v139
	v_exp_f32_e32 v155, v34
	v_sub_f32_e32 v34, v44, v139
	v_exp_f32_e32 v156, v34
	v_sub_f32_e32 v34, v45, v139
	v_exp_f32_e32 v157, v34
	v_sub_f32_e32 v34, v46, v139
	v_exp_f32_e32 v158, v34
	v_sub_f32_e32 v34, v47, v139
	v_exp_f32_e32 v159, v34
	v_sub_f32_e32 v34, v48, v139
	v_exp_f32_e32 v160, v34
	v_sub_f32_e32 v34, v49, v139
	v_exp_f32_e32 v161, v34
	v_cvt_pk_bf16_f32 v34, v141, v146
	v_cvt_pk_bf16_f32 v35, v147, v148
	v_cvt_pk_bf16_f32 v36, v149, v150
	v_cvt_pk_bf16_f32 v37, v151, v152
	v_cvt_pk_bf16_f32 v134, v154, v155
	v_cvt_pk_bf16_f32 v135, v156, v157
	v_cvt_pk_bf16_f32 v136, v158, v159
	v_cvt_pk_bf16_f32 v137, v160, v161
	ds_read_b64_tr_b16 v[38:39], v181 offset:4608
	ds_read_b64_tr_b16 v[40:41], v181 offset:5888
	ds_read_b64_tr_b16 v[44:45], v181 offset:5952
	ds_read_b64_tr_b16 v[42:43], v181 offset:4672
	s_waitcnt lgkmcnt(2)
	v_mfma_f32_32x32x16_bf16 v[18:33], v[38:41], v[34:37], v[18:33]
	ds_read_b64_tr_b16 v[38:39], v181 offset:7168
	ds_read_b64_tr_b16 v[40:41], v181 offset:8448
	v_add_f32_e32 v46, 0, v141
	ds_read_b64_tr_b16 v[144:145], v181 offset:8512
	ds_read_b64_tr_b16 v[142:143], v181 offset:7232
	ds_write_b128 v231, v[74:77]
	ds_write_b128 v232, v[78:81] offset:4608
	ds_write_b128 v231, v[82:85] offset:1152
	ds_write_b128 v232, v[86:89] offset:5888
	ds_write_b128 v231, v[90:93] offset:2304
	ds_write_b128 v232, v[94:97] offset:7168
	ds_write_b128 v231, v[98:101] offset:3456
	ds_write_b128 v232, v[102:105] offset:8448
	v_add_u32_e32 v94, s10, v224
	v_add_u32_e32 v98, s10, v225
	s_waitcnt lgkmcnt(10)
	v_mfma_f32_32x32x16_bf16 v[18:33], v[38:41], v[134:137], v[18:33]
	v_add_f32_e32 v38, v146, v46
	v_add_f32_e32 v38, v147, v38
	v_add_f32_e32 v38, v148, v38
	v_add_f32_e32 v38, v149, v38
	v_add_f32_e32 v38, v150, v38
	v_add_f32_e32 v38, v151, v38
	v_add_f32_e32 v141, v152, v38
	v_mfma_f32_32x32x16_bf16 v[2:17], v[42:45], v[34:37], v[2:17]
	v_add_u32_e32 v34, s10, v222
	v_med3_i32 v34, v34, 0, v233
	v_mul_u32_u24_e32 v38, 0xc00, v34
	ds_read_b128 v[34:37], v177
	v_or_b32_e32 v38, v38, v176
	global_load_dwordx4 v[74:77], v38, s[8:9] offset:1024
	global_load_dwordx4 v[78:81], v38, s[8:9] offset:2048
	v_add_u32_e32 v38, s10, v223
	v_med3_i32 v38, v38, 0, v233
	v_mul_u32_u24_e32 v38, 0xc00, v38
	ds_read_b128 v[90:93], v177 offset:32
	v_or_b32_e32 v86, v38, v176
	s_waitcnt lgkmcnt(1)
	v_mfma_f32_32x32x16_bf16 v[34:49], v[34:37], v[62:65], 0
	v_med3_i32 v94, v94, 0, v233
	v_med3_i32 v98, v98, 0, v233
	v_mul_u32_u24_e32 v94, 0xc00, v94
	v_mul_u32_u24_e32 v98, 0xc00, v98
	v_or_b32_e32 v94, v94, v176
	v_or_b32_e32 v102, v98, v176
	global_load_dwordx4 v[82:85], v86, s[8:9] offset:1024
	s_nop 0
	global_load_dwordx4 v[86:89], v86, s[8:9] offset:2048
	ds_read_b128 v[146:149], v177 offset:96
	ds_read_b128 v[150:153], v177 offset:64
	s_waitcnt lgkmcnt(2)
	v_mfma_f32_32x32x16_bf16 v[34:49], v[90:93], v[58:61], v[34:49]
	global_load_dwordx4 v[90:93], v94, s[8:9] offset:1024
	s_nop 0
	global_load_dwordx4 v[94:97], v94, s[8:9] offset:2048
	s_nop 0
	global_load_dwordx4 v[98:101], v102, s[8:9] offset:1024
	s_nop 0
	global_load_dwordx4 v[102:105], v102, s[8:9] offset:2048
	v_add_f32_e32 v141, v154, v141
	v_add_f32_e32 v141, v155, v141
	v_add_f32_e32 v141, v156, v141
	v_add_f32_e32 v141, v157, v141
	v_add_f32_e32 v141, v158, v141
	s_waitcnt lgkmcnt(0)
	v_mfma_f32_32x32x16_bf16 v[34:49], v[150:153], v[54:57], v[34:49]
	v_add_f32_e32 v141, v159, v141
	v_add_f32_e32 v141, v160, v141
	v_add_f32_e32 v141, v161, v141
	v_mfma_f32_32x32x16_bf16 v[34:49], v[146:149], v[70:73], v[34:49]
	v_add_u32_e32 v146, 32, v138
	v_cmp_le_u32_e32 vcc, v146, v51
	v_add_u32_e32 v146, 33, v138
	v_add_u32_e32 v147, 34, v138
	v_mfma_f32_32x32x16_bf16 v[2:17], v[142:145], v[134:137], v[2:17]
	s_nop 6
	v_cndmask_b32_e32 v34, v234, v34, vcc
	v_cmp_le_u32_e32 vcc, v146, v51
	v_add_f32_e32 v134, v140, v141
	s_nop 0
	v_cndmask_b32_e32 v35, v234, v35, vcc
	v_cmp_le_u32_e32 vcc, v147, v51
	v_add_u32_e32 v147, 35, v138
	v_max3_f32 v146, v34, s31, v35
	v_cndmask_b32_e32 v36, v234, v36, vcc
	v_cmp_le_u32_e32 vcc, v147, v51
	v_add_u32_e32 v147, 40, v138
	s_nop 0
	v_cndmask_b32_e32 v37, v234, v37, vcc
	v_cmp_le_u32_e32 vcc, v147, v51
	v_add_u32_e32 v147, 41, v138
	v_max3_f32 v146, v146, v36, v37
	v_cndmask_b32_e32 v38, v234, v38, vcc
	v_cmp_le_u32_e32 vcc, v147, v51
	v_add_u32_e32 v147, 42, v138
	s_nop 0
	v_cndmask_b32_e32 v39, v234, v39, vcc
	v_cmp_le_u32_e32 vcc, v147, v51
	v_add_u32_e32 v147, 43, v138
	v_max3_f32 v146, v146, v38, v39
	v_cndmask_b32_e32 v40, v234, v40, vcc
	v_cmp_le_u32_e32 vcc, v147, v51
	v_add_u32_e32 v147, 48, v138
	s_nop 0
	v_cndmask_b32_e32 v41, v234, v41, vcc
	v_cmp_le_u32_e32 vcc, v147, v51
	v_add_u32_e32 v147, 49, v138
	v_max3_f32 v146, v146, v40, v41
	v_cndmask_b32_e32 v42, v234, v42, vcc
	v_cmp_le_u32_e32 vcc, v147, v51
	v_add_u32_e32 v147, 50, v138
	s_nop 0
	v_cndmask_b32_e32 v43, v234, v43, vcc
	v_cmp_le_u32_e32 vcc, v147, v51
	v_add_u32_e32 v147, 51, v138
	v_max3_f32 v146, v146, v42, v43
	v_cndmask_b32_e32 v44, v234, v44, vcc
	v_cmp_le_u32_e32 vcc, v147, v51
	v_add_u32_e32 v147, 56, v138
	s_nop 0
	v_cndmask_b32_e32 v45, v234, v45, vcc
	v_cmp_le_u32_e32 vcc, v147, v51
	v_add_u32_e32 v147, 57, v138
	v_max3_f32 v146, v146, v44, v45
	v_cndmask_b32_e32 v46, v234, v46, vcc
	v_cmp_le_u32_e32 vcc, v147, v51
	v_add_u32_e32 v147, 58, v138
	s_nop 0
	v_cndmask_b32_e32 v47, v234, v47, vcc
	v_cmp_le_u32_e32 vcc, v147, v51
	v_add_u32_e32 v147, 59, v138
	v_max3_f32 v146, v146, v46, v47
	v_cndmask_b32_e32 v48, v234, v48, vcc
	v_cmp_le_u32_e32 vcc, v147, v51
	s_nop 1
	v_cndmask_b32_e32 v49, v234, v49, vcc
	v_max3_f32 v146, v146, v48, v49
	v_mov_b32_e32 v147, v146
	s_nop 1
	v_permlane32_swap_b32_e32 v147, v146
	s_waitcnt lgkmcnt(0)
	v_max_f32_e32 v135, v147, v147
	v_max_f32_e32 v135, v146, v135
	v_cmp_gt_f32_e32 vcc, v135, v139
	s_cbranch_vccz .LBB0_426
; #define LAS __attribute__((address_space(3)))
; template <int STAGE, int OFF> __device__ __forceinline__ void attn32_unit(const bf16* base, bf16* yrow0, int blk0, int u, LAS unsigned char* xtab, LAS unsigned char* kbuf, LAS unsigned char* vbuf, int lane, ...
;     ...
;         for (int c = 0; c < 4; ++c) { *(LAS v4u*)(kbuf + (8 * c + lrow) * 144 + lch * 16) = kr[set][c]; *(LAS v4u*)(vbuf + (8 * c + lrow) * 160 + lch * 16) = vr[set][c]; }
;         if (pp + 2 < 5) { ATT32_LOAD(set, pp + 2, t0, SH); }
;         else { const bf16* base_ = base; { const bf16* base = nbase; ATT32_LOAD(set, pp + 2 - 5, nt0, nsh); } (void)base_; }
;         f32x16 sc;
; #pragma unroll
;         for (int i = 0; i < 16; ++i) sc[i] = 0.f;
; #pragma unroll
;         for (int ks = 0; ks < 4; ++ks) { const bf16x8 ka = *(const LAS bf16x8*)(kbuf + qi * 144 + 32 * ks + 16 * h); sc = MFMA32(ka, qb[ks], sc); }
;         if (pp == 4) {
; #pragma unroll
;             for (int ks = 0; ks < 4; ++ks) qb[ks] = *(const bf16x8*)(nbase + (size_t)min(nt0 + (qi << nsh), SEQ - 1) * 1536 + 16 * ks + 8 * h);
;         }
;         const int mbase = n0 + 4 * h - lo; float mx = -INFINITY;
; #pragma unroll
;         for (int rg = 0; rg < 16; ++rg) { sc[rg] = ((unsigned)(mbase + (rg & 3) + 8 * (rg >> 2)) <= mspan) ? sc[rg] : -INFINITY; mx = fmaxf(mx, sc[rg]); }
;         mx = fmaxf(mx, __shfl_xor(mx, 32));
;         if (__any(mx > m)) {
;             const float mn = fmaxf(m, mx), alpha = __builtin_amdgcn_exp2f(m - mn); m = mn; l *= alpha;
; #pragma unroll
;             for (int i = 0; i < 16; ++i) { o[0][i] *= alpha; o[1][i] *= alpha; }
;         }
;         float ps = 0.f;
; #pragma unroll
;         for (int rg = 0; rg < 16; ++rg) { sc[rg] = __builtin_amdgcn_exp2f(sc[rg] - m); ps += sc[rg]; }
;         l += ps;
;         bf16x8 pb[2];
; #pragma unroll
;         for (int s2 = 0; s2 < 2; ++s2) { v4u w; w.x = pg8::cvt_pk_bf16(sc[8 * s2], sc[8 * s2 + 1]); w.y = pg8::cvt_pk_bf16(sc[8 * s2 + 2], sc[8 * s2 + 3]); w.z = pg8::cvt_pk_bf16(sc[8 * s2 + 4], sc[8 * s2 + 5]); w.w = pg8::cvt_pk_bf16(sc[8 * s2 + 6], sc[8 * s2 + 7]); pb[s2] = __builtin_bit_cast(bf16x8, w); }
; #pragma unroll
;         for (int mb = 0; mb < 2; ++mb)
; #pragma unroll
;             for (int s2 = 0; s2 < 2; ++s2) {
;                 LAS unsigned char* vp = vbuf + tr_off + (16 * s2) * 160 + 64 * mb;
	v_max_f32_e32 v135, v135, v135
	v_max_f32_e32 v136, v139, v139
	v_max_f32_e32 v135, v136, v135
	v_sub_f32_e32 v136, v139, v135
	v_exp_f32_e32 v136, v136
	v_mov_b32_e32 v139, v135
	v_pk_mul_f32 v[32:33], v[32:33], v[136:137] op_sel_hi:[1,0]
	v_pk_mul_f32 v[30:31], v[30:31], v[136:137] op_sel_hi:[1,0]
	v_pk_mul_f32 v[28:29], v[28:29], v[136:137] op_sel_hi:[1,0]
	v_pk_mul_f32 v[26:27], v[26:27], v[136:137] op_sel_hi:[1,0]
	v_pk_mul_f32 v[24:25], v[24:25], v[136:137] op_sel_hi:[1,0]
	v_pk_mul_f32 v[22:23], v[22:23], v[136:137] op_sel_hi:[1,0]
	v_pk_mul_f32 v[20:21], v[20:21], v[136:137] op_sel_hi:[1,0]
	v_pk_mul_f32 v[18:19], v[18:19], v[136:137] op_sel_hi:[1,0]
	v_pk_mul_f32 v[16:17], v[16:17], v[136:137] op_sel_hi:[1,0]
	v_pk_mul_f32 v[14:15], v[14:15], v[136:137] op_sel_hi:[1,0]
	v_pk_mul_f32 v[12:13], v[12:13], v[136:137] op_sel_hi:[1,0]
	v_pk_mul_f32 v[10:11], v[10:11], v[136:137] op_sel_hi:[1,0]
	v_pk_mul_f32 v[8:9], v[8:9], v[136:137] op_sel_hi:[1,0]
	v_pk_mul_f32 v[6:7], v[6:7], v[136:137] op_sel_hi:[1,0]
	v_pk_mul_f32 v[4:5], v[4:5], v[136:137] op_sel_hi:[1,0]
	v_pk_mul_f32 v[2:3], v[2:3], v[136:137] op_sel_hi:[1,0]
	v_mul_f32_e32 v134, v134, v136
.LBB0_426:
	v_sub_f32_e32 v34, v34, v139
	v_exp_f32_e32 v135, v34
	v_sub_f32_e32 v34, v35, v139
	v_exp_f32_e32 v136, v34
	v_sub_f32_e32 v34, v36, v139
	v_exp_f32_e32 v137, v34
	v_sub_f32_e32 v34, v37, v139
	v_exp_f32_e32 v148, v34
	v_sub_f32_e32 v34, v38, v139
	v_exp_f32_e32 v149, v34
	v_sub_f32_e32 v34, v39, v139
	v_exp_f32_e32 v150, v34
	v_sub_f32_e32 v34, v40, v139
	v_exp_f32_e32 v151, v34
	v_sub_f32_e32 v34, v41, v139
	v_exp_f32_e32 v152, v34
	v_sub_f32_e32 v34, v42, v139
	v_exp_f32_e32 v156, v34
	v_sub_f32_e32 v34, v43, v139
	v_exp_f32_e32 v157, v34
	v_sub_f32_e32 v34, v44, v139
	v_exp_f32_e32 v158, v34
	v_sub_f32_e32 v34, v45, v139
	v_exp_f32_e32 v159, v34
	v_sub_f32_e32 v34, v46, v139
	v_exp_f32_e32 v160, v34
	v_sub_f32_e32 v34, v47, v139
	v_exp_f32_e32 v161, v34
	v_sub_f32_e32 v34, v48, v139
	v_exp_f32_e32 v162, v34
	v_sub_f32_e32 v34, v49, v139
	v_exp_f32_e32 v163, v34
	v_cvt_pk_bf16_f32 v34, v135, v136
	v_cvt_pk_bf16_f32 v35, v137, v148
	v_cvt_pk_bf16_f32 v36, v149, v150
	v_cvt_pk_bf16_f32 v37, v151, v152
	v_cvt_pk_bf16_f32 v140, v156, v157
	v_cvt_pk_bf16_f32 v141, v158, v159
	v_cvt_pk_bf16_f32 v142, v160, v161
	v_cvt_pk_bf16_f32 v143, v162, v163
	ds_read_b64_tr_b16 v[38:39], v181 offset:4608
	ds_read_b64_tr_b16 v[40:41], v181 offset:5888
	ds_read_b64_tr_b16 v[44:45], v181 offset:5952
	ds_read_b64_tr_b16 v[42:43], v181 offset:4672
	s_waitcnt lgkmcnt(2)
	v_mfma_f32_32x32x16_bf16 v[18:33], v[38:41], v[34:37], v[18:33]
	ds_read_b64_tr_b16 v[38:39], v181 offset:7168
	ds_read_b64_tr_b16 v[40:41], v181 offset:8448
	v_add_f32_e32 v46, 0, v135
	ds_read_b64_tr_b16 v[146:147], v181 offset:8512
	ds_read_b64_tr_b16 v[144:145], v181 offset:7232
	s_waitcnt vmcnt(15)
	ds_write_b128 v231, v[66:69]
	s_waitcnt vmcnt(14)
	ds_write_b128 v232, v[106:109] offset:4608
	s_waitcnt vmcnt(13)
	ds_write_b128 v231, v[110:113] offset:1152
	s_waitcnt vmcnt(12)
	ds_write_b128 v232, v[114:117] offset:5888
	s_waitcnt vmcnt(11)
	ds_write_b128 v231, v[118:121] offset:2304
	s_waitcnt vmcnt(10)
	ds_write_b128 v232, v[122:125] offset:7168
	s_waitcnt vmcnt(9)
	ds_write_b128 v231, v[126:129] offset:3456
	s_waitcnt vmcnt(8)
	ds_write_b128 v232, v[130:133] offset:8448
	v_add_u32_e32 v122, s10, v227
	v_add_u32_e32 v126, s10, v228
	s_waitcnt lgkmcnt(10)
	v_mfma_f32_32x32x16_bf16 v[18:33], v[38:41], v[140:143], v[18:33]
	v_add_f32_e32 v38, v136, v46
	v_add_f32_e32 v38, v137, v38
	v_add_f32_e32 v38, v148, v38
	v_add_f32_e32 v38, v149, v38
	v_add_f32_e32 v38, v150, v38
	v_add_f32_e32 v38, v151, v38
	v_add_f32_e32 v135, v152, v38
	v_mfma_f32_32x32x16_bf16 v[2:17], v[42:45], v[34:37], v[2:17]
	v_add_u32_e32 v34, s10, v207
	v_min_u32_e32 v34, 0x3fff, v34
	v_mul_u32_u24_e32 v38, 0xc00, v34
	ds_read_b128 v[34:37], v177
	v_or_b32_e32 v38, v38, v176
	global_load_dwordx4 v[66:69], v38, s[8:9] offset:1024
	global_load_dwordx4 v[106:109], v38, s[8:9] offset:2048
	v_add_u32_e32 v38, s10, v226
	v_min_u32_e32 v38, 0x3fff, v38
	v_mul_u32_u24_e32 v38, 0xc00, v38
	ds_read_b128 v[118:121], v177 offset:32
	v_or_b32_e32 v114, v38, v176
	s_waitcnt lgkmcnt(1)
	v_mfma_f32_32x32x16_bf16 v[34:49], v[34:37], v[62:65], 0
	v_min_u32_e32 v122, 0x3fff, v122
	v_min_u32_e32 v126, 0x3fff, v126
	v_mul_u32_u24_e32 v122, 0xc00, v122
	v_mul_u32_u24_e32 v126, 0xc00, v126
	v_or_b32_e32 v122, v122, v176
	v_or_b32_e32 v130, v126, v176
	global_load_dwordx4 v[110:113], v114, s[8:9] offset:1024
	s_nop 0
	global_load_dwordx4 v[114:117], v114, s[8:9] offset:2048
	ds_read_b128 v[148:151], v177 offset:96
	ds_read_b128 v[152:155], v177 offset:64
	s_waitcnt lgkmcnt(2)
	v_mfma_f32_32x32x16_bf16 v[34:49], v[118:121], v[58:61], v[34:49]
	global_load_dwordx4 v[118:121], v122, s[8:9] offset:1024
	s_nop 0
	global_load_dwordx4 v[122:125], v122, s[8:9] offset:2048
	s_nop 0
	global_load_dwordx4 v[126:129], v130, s[8:9] offset:1024
	s_nop 0
	global_load_dwordx4 v[130:133], v130, s[8:9] offset:2048
	v_add_u32_e32 v136, 64, v138
	v_cmp_le_u32_e32 vcc, v136, v51
	v_add_u32_e32 v136, 0x41, v138
	v_add_u32_e32 v137, 0x42, v138
	v_add_f32_e32 v135, v156, v135
	s_waitcnt lgkmcnt(0)
; #define LAS __attribute__((address_space(3)))
; template <int STAGE, int OFF> __device__ __forceinline__ void attn32_unit(const bf16* base, bf16* yrow0, int blk0, int u, LAS unsigned char* xtab, LAS unsigned char* kbuf, LAS unsigned char* vbuf, int lane, ...
;     ...
;         for (int c = 0; c < 4; ++c) { *(LAS v4u*)(kbuf + (8 * c + lrow) * 144 + lch * 16) = kr[set][c]; *(LAS v4u*)(vbuf + (8 * c + lrow) * 160 + lch * 16) = vr[set][c]; }
;         if (pp + 2 < 5) { ATT32_LOAD(set, pp + 2, t0, SH); }
;         else { const bf16* base_ = base; { const bf16* base = nbase; ATT32_LOAD(set, pp + 2 - 5, nt0, nsh); } (void)base_; }
;         f32x16 sc;
; #pragma unroll
;         for (int i = 0; i < 16; ++i) sc[i] = 0.f;
; #pragma unroll
;         for (int ks = 0; ks < 4; ++ks) { const bf16x8 ka = *(const LAS bf16x8*)(kbuf + qi * 144 + 32 * ks + 16 * h); sc = MFMA32(ka, qb[ks], sc); }
;         if (pp == 4) {
; #pragma unroll
;             for (int ks = 0; ks < 4; ++ks) qb[ks] = *(const bf16x8*)(nbase + (size_t)min(nt0 + (qi << nsh), SEQ - 1) * 1536 + 16 * ks + 8 * h);
;         }
;         const int mbase = n0 + 4 * h - lo; float mx = -INFINITY;
; #pragma unroll
;         for (int rg = 0; rg < 16; ++rg) { sc[rg] = ((unsigned)(mbase + (rg & 3) + 8 * (rg >> 2)) <= mspan) ? sc[rg] : -INFINITY; mx = fmaxf(mx, sc[rg]); }
;         mx = fmaxf(mx, __shfl_xor(mx, 32));
;         if (__any(mx > m)) {
;             const float mn = fmaxf(m, mx), alpha = __builtin_amdgcn_exp2f(m - mn); m = mn; l *= alpha;
; #pragma unroll
;             for (int i = 0; i < 16; ++i) { o[0][i] *= alpha; o[1][i] *= alpha; }
;         }
;         float ps = 0.f;
; #pragma unroll
;         for (int rg = 0; rg < 16; ++rg) { sc[rg] = __builtin_amdgcn_exp2f(sc[rg] - m); ps += sc[rg]; }
;         l += ps;
;         bf16x8 pb[2];
; #pragma unroll
;         for (int s2 = 0; s2 < 2; ++s2) { v4u w; w.x = pg8::cvt_pk_bf16(sc[8 * s2], sc[8 * s2 + 1]); w.y = pg8::cvt_pk_bf16(sc[8 * s2 + 2], sc[8 * s2 + 3]); w.z = pg8::cvt_pk_bf16(sc[8 * s2 + 4], sc[8 * s2 + 5]); w.w = pg8::cvt_pk_bf16(sc[8 * s2 + 6], sc[8 * s2 + 7]); pb[s2] = __builtin_bit_cast(bf16x8, w); }
; #pragma unroll
;         for (int mb = 0; mb < 2; ++mb)
; #pragma unroll
;             for (int s2 = 0; s2 < 2; ++s2) {
;                 LAS unsigned char* vp = vbuf + tr_off + (16 * s2) * 160 + 64 * mb;
	v_mfma_f32_32x32x16_bf16 v[34:49], v[152:155], v[54:57], v[34:49]
	v_add_f32_e32 v135, v157, v135
	v_add_f32_e32 v135, v158, v135
	v_add_f32_e32 v135, v159, v135
	v_add_f32_e32 v135, v160, v135
	v_add_f32_e32 v135, v161, v135
	v_add_f32_e32 v135, v162, v135
	v_add_f32_e32 v135, v163, v135
	v_mfma_f32_32x32x16_bf16 v[34:49], v[148:151], v[70:73], v[34:49]
	v_add_f32_e32 v135, v134, v135
	v_mfma_f32_32x32x16_bf16 v[2:17], v[144:147], v[140:143], v[2:17]
	s_nop 9
	v_cndmask_b32_e32 v34, v234, v34, vcc
	v_cmp_le_u32_e32 vcc, v136, v51
	s_nop 1
	v_cndmask_b32_e32 v35, v234, v35, vcc
	v_cmp_le_u32_e32 vcc, v137, v51
	v_add_u32_e32 v137, 0x43, v138
	v_max3_f32 v136, v34, s31, v35
	v_cndmask_b32_e32 v36, v234, v36, vcc
	v_cmp_le_u32_e32 vcc, v137, v51
	v_add_u32_e32 v137, 0x48, v138
	s_nop 0
	v_cndmask_b32_e32 v37, v234, v37, vcc
	v_cmp_le_u32_e32 vcc, v137, v51
	v_add_u32_e32 v137, 0x49, v138
	v_max3_f32 v136, v136, v36, v37
	v_cndmask_b32_e32 v38, v234, v38, vcc
	v_cmp_le_u32_e32 vcc, v137, v51
	v_add_u32_e32 v137, 0x4a, v138
	s_nop 0
	v_cndmask_b32_e32 v39, v234, v39, vcc
	v_cmp_le_u32_e32 vcc, v137, v51
	v_add_u32_e32 v137, 0x4b, v138
	v_max3_f32 v136, v136, v38, v39
	v_cndmask_b32_e32 v40, v234, v40, vcc
	v_cmp_le_u32_e32 vcc, v137, v51
	v_add_u32_e32 v137, 0x50, v138
	s_nop 0
	v_cndmask_b32_e32 v41, v234, v41, vcc
	v_cmp_le_u32_e32 vcc, v137, v51
	v_add_u32_e32 v137, 0x51, v138
	v_max3_f32 v136, v136, v40, v41
	v_cndmask_b32_e32 v42, v234, v42, vcc
	v_cmp_le_u32_e32 vcc, v137, v51
	v_add_u32_e32 v137, 0x52, v138
	s_nop 0
	v_cndmask_b32_e32 v43, v234, v43, vcc
	v_cmp_le_u32_e32 vcc, v137, v51
	v_add_u32_e32 v137, 0x53, v138
	v_max3_f32 v136, v136, v42, v43
	v_cndmask_b32_e32 v44, v234, v44, vcc
	v_cmp_le_u32_e32 vcc, v137, v51
	v_add_u32_e32 v137, 0x58, v138
	s_nop 0
	v_cndmask_b32_e32 v45, v234, v45, vcc
	v_cmp_le_u32_e32 vcc, v137, v51
	v_add_u32_e32 v137, 0x59, v138
	v_max3_f32 v136, v136, v44, v45
	v_cndmask_b32_e32 v46, v234, v46, vcc
	v_cmp_le_u32_e32 vcc, v137, v51
	v_add_u32_e32 v137, 0x5a, v138
	s_nop 0
	v_cndmask_b32_e32 v47, v234, v47, vcc
	v_cmp_le_u32_e32 vcc, v137, v51
	v_add_u32_e32 v137, 0x5b, v138
	v_max3_f32 v136, v136, v46, v47
	v_cndmask_b32_e32 v48, v234, v48, vcc
	v_cmp_le_u32_e32 vcc, v137, v51
	s_nop 1
	v_cndmask_b32_e32 v49, v234, v49, vcc
	v_max3_f32 v136, v136, v48, v49
	v_mov_b32_e32 v137, v136
	s_nop 1
	v_permlane32_swap_b32_e32 v137, v136
	s_waitcnt lgkmcnt(0)
	v_max_f32_e32 v134, v137, v137
	v_max_f32_e32 v134, v136, v134
	v_cmp_gt_f32_e32 vcc, v134, v139
	s_cbranch_vccz .LBB0_428
	v_max_f32_e32 v134, v134, v134
	v_max_f32_e32 v136, v139, v139
	v_max_f32_e32 v136, v136, v134
	v_sub_f32_e32 v134, v139, v136
	v_exp_f32_e32 v134, v134
	v_mov_b32_e32 v139, v136
	v_pk_mul_f32 v[32:33], v[32:33], v[134:135] op_sel_hi:[1,0]
	v_pk_mul_f32 v[30:31], v[30:31], v[134:135] op_sel_hi:[1,0]
	v_pk_mul_f32 v[28:29], v[28:29], v[134:135] op_sel_hi:[1,0]
	v_pk_mul_f32 v[26:27], v[26:27], v[134:135] op_sel_hi:[1,0]
	v_pk_mul_f32 v[24:25], v[24:25], v[134:135] op_sel_hi:[1,0]
	v_pk_mul_f32 v[22:23], v[22:23], v[134:135] op_sel_hi:[1,0]
	v_pk_mul_f32 v[20:21], v[20:21], v[134:135] op_sel_hi:[1,0]
	v_pk_mul_f32 v[18:19], v[18:19], v[134:135] op_sel_hi:[1,0]
	v_pk_mul_f32 v[16:17], v[16:17], v[134:135] op_sel_hi:[1,0]
	v_pk_mul_f32 v[14:15], v[14:15], v[134:135] op_sel_hi:[1,0]
	v_pk_mul_f32 v[12:13], v[12:13], v[134:135] op_sel_hi:[1,0]
	v_pk_mul_f32 v[10:11], v[10:11], v[134:135] op_sel_hi:[1,0]
	v_pk_mul_f32 v[8:9], v[8:9], v[134:135] op_sel_hi:[1,0]
	v_pk_mul_f32 v[6:7], v[6:7], v[134:135] op_sel_hi:[1,0]
	v_pk_mul_f32 v[4:5], v[4:5], v[134:135] op_sel_hi:[1,0]
	v_pk_mul_f32 v[2:3], v[2:3], v[134:135] op_sel_hi:[1,0]
	v_mul_f32_e32 v135, v135, v134
.LBB0_428:
	v_sub_f32_e32 v34, v34, v139
	v_exp_f32_e32 v136, v34
	v_sub_f32_e32 v34, v35, v139
	v_exp_f32_e32 v137, v34
	v_sub_f32_e32 v34, v36, v139
	v_exp_f32_e32 v148, v34
	v_sub_f32_e32 v34, v37, v139
	v_exp_f32_e32 v149, v34
	v_sub_f32_e32 v34, v38, v139
	v_exp_f32_e32 v150, v34
	v_sub_f32_e32 v34, v39, v139
	v_exp_f32_e32 v151, v34
	v_sub_f32_e32 v34, v40, v139
	v_exp_f32_e32 v152, v34
	v_sub_f32_e32 v34, v41, v139
	v_exp_f32_e32 v153, v34
	v_sub_f32_e32 v34, v42, v139
	v_exp_f32_e32 v156, v34
	v_sub_f32_e32 v34, v43, v139
	v_exp_f32_e32 v157, v34
	v_sub_f32_e32 v34, v44, v139
	v_exp_f32_e32 v158, v34
	v_sub_f32_e32 v34, v45, v139
	v_exp_f32_e32 v159, v34
	v_sub_f32_e32 v34, v46, v139
	v_exp_f32_e32 v160, v34
	v_sub_f32_e32 v34, v47, v139
	v_exp_f32_e32 v161, v34
	v_sub_f32_e32 v34, v48, v139
	v_exp_f32_e32 v162, v34
	v_sub_f32_e32 v34, v49, v139
	v_exp_f32_e32 v163, v34
	v_cvt_pk_bf16_f32 v34, v136, v137
	v_cvt_pk_bf16_f32 v35, v148, v149
	v_cvt_pk_bf16_f32 v36, v150, v151
	v_cvt_pk_bf16_f32 v37, v152, v153
	v_cvt_pk_bf16_f32 v140, v156, v157
	v_cvt_pk_bf16_f32 v141, v158, v159
	v_cvt_pk_bf16_f32 v142, v160, v161
	v_cvt_pk_bf16_f32 v143, v162, v163
	ds_read_b64_tr_b16 v[38:39], v181 offset:4608
	ds_read_b64_tr_b16 v[40:41], v181 offset:5888
	ds_read_b64_tr_b16 v[42:43], v181 offset:7168
	ds_read_b64_tr_b16 v[44:45], v181 offset:8448
	ds_read_b64_tr_b16 v[48:49], v181 offset:5952
	ds_read_b64_tr_b16 v[46:47], v181 offset:4672
	s_waitcnt lgkmcnt(4)
	v_mfma_f32_32x32x16_bf16 v[18:33], v[38:41], v[34:37], v[18:33]
	v_add_f32_e32 v38, 0, v136
	s_lshl_b32 s0, s38, 9
	v_add_f32_e32 v38, v137, v38
	s_and_b32 s10, s0, 0x3e00
	v_add_f32_e32 v38, v148, v38
	s_add_i32 s10, s10, s23
	v_add_f32_e32 v38, v149, v38
	v_add_u32_e32 v134, s10, v180
	v_add_f32_e32 v38, v150, v38
	v_add_f32_e32 v38, v151, v38
	s_waitcnt lgkmcnt(0)
; #define LAS __attribute__((address_space(3)))
; template <int STAGE, int OFF> __device__ __forceinline__ void attn32_unit(const bf16* base, bf16* yrow0, int blk0, int u, LAS unsigned char* xtab, LAS unsigned char* kbuf, LAS unsigned char* vbuf, int lane, ...
;     ...
;         for (int c = 0; c < 4; ++c) { *(LAS v4u*)(kbuf + (8 * c + lrow) * 144 + lch * 16) = kr[set][c]; *(LAS v4u*)(vbuf + (8 * c + lrow) * 160 + lch * 16) = vr[set][c]; }
;         if (pp + 2 < 5) { ATT32_LOAD(set, pp + 2, t0, SH); }
;         else { const bf16* base_ = base; { const bf16* base = nbase; ATT32_LOAD(set, pp + 2 - 5, nt0, nsh); } (void)base_; }
;         f32x16 sc;
; #pragma unroll
;         for (int i = 0; i < 16; ++i) sc[i] = 0.f;
; #pragma unroll
;         for (int ks = 0; ks < 4; ++ks) { const bf16x8 ka = *(const LAS bf16x8*)(kbuf + qi * 144 + 32 * ks + 16 * h); sc = MFMA32(ka, qb[ks], sc); }
;         if (pp == 4) {
; #pragma unroll
;             for (int ks = 0; ks < 4; ++ks) qb[ks] = *(const bf16x8*)(nbase + (size_t)min(nt0 + (qi << nsh), SEQ - 1) * 1536 + 16 * ks + 8 * h);
;         }
;         const int mbase = n0 + 4 * h - lo; float mx = -INFINITY;
; #pragma unroll
;         for (int rg = 0; rg < 16; ++rg) { sc[rg] = ((unsigned)(mbase + (rg & 3) + 8 * (rg >> 2)) <= mspan) ? sc[rg] : -INFINITY; mx = fmaxf(mx, sc[rg]); }
;         mx = fmaxf(mx, __shfl_xor(mx, 32));
;         if (__any(mx > m)) {
;             const float mn = fmaxf(m, mx), alpha = __builtin_amdgcn_exp2f(m - mn); m = mn; l *= alpha;
; #pragma unroll
;             for (int i = 0; i < 16; ++i) { o[0][i] *= alpha; o[1][i] *= alpha; }
;         }
;         float ps = 0.f;
; #pragma unroll
;         for (int rg = 0; rg < 16; ++rg) { sc[rg] = __builtin_amdgcn_exp2f(sc[rg] - m); ps += sc[rg]; }
;         l += ps;
;         bf16x8 pb[2];
; #pragma unroll
;         for (int s2 = 0; s2 < 2; ++s2) { v4u w; w.x = pg8::cvt_pk_bf16(sc[8 * s2], sc[8 * s2 + 1]); w.y = pg8::cvt_pk_bf16(sc[8 * s2 + 2], sc[8 * s2 + 3]); w.z = pg8::cvt_pk_bf16(sc[8 * s2 + 4], sc[8 * s2 + 5]); w.w = pg8::cvt_pk_bf16(sc[8 * s2 + 6], sc[8 * s2 + 7]); pb[s2] = __builtin_bit_cast(bf16x8, w); }
; #pragma unroll
;         for (int mb = 0; mb < 2; ++mb)
; #pragma unroll
;             for (int s2 = 0; s2 < 2; ++s2) {
;                 LAS unsigned char* vp = vbuf + tr_off + (16 * s2) * 160 + 64 * mb;
	v_mfma_f32_32x32x16_bf16 v[2:17], v[46:49], v[34:37], v[2:17]
	v_add_u32_e32 v34, 0x60, v134
	s_ashr_i32 s0, s38, 8
	ds_read_b64_tr_b16 v[146:147], v181 offset:8512
	ds_read_b64_tr_b16 v[144:145], v181 offset:7232
	v_add_f32_e32 v38, v152, v38
	s_waitcnt vmcnt(15)
	ds_write_b128 v231, v[74:77]
	s_waitcnt vmcnt(14)
	ds_write_b128 v232, v[78:81] offset:4608
	s_waitcnt vmcnt(13)
	ds_write_b128 v231, v[82:85] offset:1152
	s_waitcnt vmcnt(12)
	ds_write_b128 v232, v[86:89] offset:5888
	s_waitcnt vmcnt(11)
	ds_write_b128 v231, v[90:93] offset:2304
	s_waitcnt vmcnt(10)
	ds_write_b128 v232, v[94:97] offset:7168
	s_waitcnt vmcnt(9)
	ds_write_b128 v231, v[98:101] offset:3456
	s_waitcnt vmcnt(8)
	ds_write_b128 v232, v[102:105] offset:8448
	v_med3_i32 v34, v34, 0, v233
	s_mul_hi_i32 s1, s0, 0x3000000
	s_mul_i32 s0, s0, 0x3000000
	v_add_f32_e32 v136, v153, v38
	v_mul_u32_u24_e32 v38, 0xc00, v34
	ds_read_b128 v[34:37], v177
	s_add_u32 s0, s16, s0
	s_addc_u32 s1, s17, s1
	s_lshl_b32 s8, s38, 2
	s_and_b32 s8, s8, 0x380
	s_add_u32 s8, s0, s8
	s_addc_u32 s9, s1, 0
	v_or_b32_e32 v38, v38, v176
	global_load_dwordx4 v[74:77], v38, s[8:9] offset:1024
	global_load_dwordx4 v[82:85], v38, s[8:9] offset:2048
	v_add_u32_e32 v38, 0x68, v134
	v_med3_i32 v38, v38, 0, v233
	v_mul_u32_u24_e32 v38, 0xc00, v38
	ds_read_b128 v[86:89], v177 offset:32
	v_mfma_f32_32x32x16_bf16 v[18:33], v[42:45], v[140:143], v[18:33]
	v_or_b32_e32 v90, v38, v176
	global_load_dwordx4 v[78:81], v90, s[8:9] offset:1024
	global_load_dwordx4 v[94:97], v90, s[8:9] offset:2048
	v_add_u32_e32 v90, 0x70, v134
	v_med3_i32 v90, v90, 0, v233
	v_mul_u32_u24_e32 v90, 0xc00, v90
	v_or_b32_e32 v90, v90, v176
	ds_read_b128 v[148:151], v177 offset:96
	ds_read_b128 v[152:155], v177 offset:64
	s_waitcnt lgkmcnt(3)
	v_mfma_f32_32x32x16_bf16 v[34:49], v[34:37], v[62:65], 0
	v_add_u32_e32 v137, 0x60, v138
	v_cmp_le_u32_e32 vcc, v137, v51
	v_add_u32_e32 v137, 0x61, v138
	v_add_f32_e32 v136, v156, v136
	v_add_f32_e32 v136, v157, v136
	v_add_f32_e32 v136, v158, v136
	v_add_f32_e32 v136, v159, v136
	s_waitcnt lgkmcnt(2)
	v_mfma_f32_32x32x16_bf16 v[34:49], v[86:89], v[58:61], v[34:49]
	global_load_dwordx4 v[86:89], v90, s[8:9] offset:1024
	global_load_dwordx4 v[98:101], v90, s[8:9] offset:2048
	v_add_u32_e32 v90, 0x78, v134
	v_med3_i32 v90, v90, 0, v233
	v_mul_u32_u24_e32 v90, 0xc00, v90
	v_or_b32_e32 v102, v90, v176
	global_load_dwordx4 v[90:93], v102, s[8:9] offset:1024
	s_nop 0
	global_load_dwordx4 v[102:105], v102, s[8:9] offset:2048
	v_add_f32_e32 v136, v160, v136
	s_waitcnt lgkmcnt(0)
	v_mfma_f32_32x32x16_bf16 v[34:49], v[152:155], v[54:57], v[34:49]
	v_add_f32_e32 v136, v161, v136
	v_add_f32_e32 v136, v162, v136
	v_add_f32_e32 v136, v163, v136
	v_mfma_f32_32x32x16_bf16 v[34:49], v[148:151], v[70:73], v[34:49]
	v_add_u32_e32 v148, 0x62, v138
	v_mfma_f32_32x32x16_bf16 v[2:17], v[144:147], v[140:143], v[2:17]
	s_nop 9
	v_cndmask_b32_e32 v34, v234, v34, vcc
	v_cmp_le_u32_e32 vcc, v137, v51
	v_add_f32_e32 v140, v135, v136
	s_nop 0
	v_cndmask_b32_e32 v35, v234, v35, vcc
	v_cmp_le_u32_e32 vcc, v148, v51
	v_add_u32_e32 v148, 0x63, v138
	v_max3_f32 v137, v34, s31, v35
	v_cndmask_b32_e32 v36, v234, v36, vcc
	v_cmp_le_u32_e32 vcc, v148, v51
	v_add_u32_e32 v148, 0x68, v138
	s_nop 0
	v_cndmask_b32_e32 v37, v234, v37, vcc
	v_cmp_le_u32_e32 vcc, v148, v51
	v_add_u32_e32 v148, 0x69, v138
	v_max3_f32 v137, v137, v36, v37
	v_cndmask_b32_e32 v38, v234, v38, vcc
	v_cmp_le_u32_e32 vcc, v148, v51
	v_add_u32_e32 v148, 0x6a, v138
	s_nop 0
	v_cndmask_b32_e32 v39, v234, v39, vcc
	v_cmp_le_u32_e32 vcc, v148, v51
	v_add_u32_e32 v148, 0x6b, v138
	v_max3_f32 v137, v137, v38, v39
	v_cndmask_b32_e32 v40, v234, v40, vcc
	v_cmp_le_u32_e32 vcc, v148, v51
	v_add_u32_e32 v148, 0x70, v138
	s_nop 0
	v_cndmask_b32_e32 v41, v234, v41, vcc
	v_cmp_le_u32_e32 vcc, v148, v51
	v_add_u32_e32 v148, 0x71, v138
	v_max3_f32 v137, v137, v40, v41
	v_cndmask_b32_e32 v42, v234, v42, vcc
	v_cmp_le_u32_e32 vcc, v148, v51
	v_add_u32_e32 v148, 0x72, v138
	s_nop 0
	v_cndmask_b32_e32 v43, v234, v43, vcc
	v_cmp_le_u32_e32 vcc, v148, v51
	v_add_u32_e32 v148, 0x73, v138
	v_max3_f32 v137, v137, v42, v43
	v_cndmask_b32_e32 v44, v234, v44, vcc
	v_cmp_le_u32_e32 vcc, v148, v51
	v_add_u32_e32 v148, 0x78, v138
	s_nop 0
	v_cndmask_b32_e32 v45, v234, v45, vcc
	v_cmp_le_u32_e32 vcc, v148, v51
	v_add_u32_e32 v148, 0x79, v138
	v_max3_f32 v137, v137, v44, v45
	v_cndmask_b32_e32 v46, v234, v46, vcc
	v_cmp_le_u32_e32 vcc, v148, v51
	v_add_u32_e32 v148, 0x7a, v138
	s_nop 0
	v_cndmask_b32_e32 v47, v234, v47, vcc
	v_cmp_le_u32_e32 vcc, v148, v51
	v_add_u32_e32 v148, 0x7b, v138
	v_max3_f32 v137, v137, v46, v47
	v_cndmask_b32_e32 v48, v234, v48, vcc
	v_cmp_le_u32_e32 vcc, v148, v51
	s_nop 1
	v_cndmask_b32_e32 v49, v234, v49, vcc
	v_max3_f32 v137, v137, v48, v49
	v_mov_b32_e32 v148, v137
	s_nop 1
	v_permlane32_swap_b32_e32 v148, v137
	s_waitcnt lgkmcnt(0)
	v_max_f32_e32 v135, v148, v148
	v_max_f32_e32 v135, v137, v135
	v_cmp_gt_f32_e32 vcc, v135, v139
	s_cbranch_vccz .LBB0_430
	v_max_f32_e32 v135, v135, v135
	v_max_f32_e32 v136, v139, v139
	v_max_f32_e32 v135, v136, v135
	v_sub_f32_e32 v136, v139, v135
	v_exp_f32_e32 v136, v136
	v_mov_b32_e32 v139, v135
	v_pk_mul_f32 v[32:33], v[32:33], v[136:137] op_sel_hi:[1,0]
	v_pk_mul_f32 v[30:31], v[30:31], v[136:137] op_sel_hi:[1,0]
	v_pk_mul_f32 v[28:29], v[28:29], v[136:137] op_sel_hi:[1,0]
	v_pk_mul_f32 v[26:27], v[26:27], v[136:137] op_sel_hi:[1,0]
	v_pk_mul_f32 v[24:25], v[24:25], v[136:137] op_sel_hi:[1,0]
	v_pk_mul_f32 v[22:23], v[22:23], v[136:137] op_sel_hi:[1,0]
	v_pk_mul_f32 v[20:21], v[20:21], v[136:137] op_sel_hi:[1,0]
	v_pk_mul_f32 v[18:19], v[18:19], v[136:137] op_sel_hi:[1,0]
	v_pk_mul_f32 v[16:17], v[16:17], v[136:137] op_sel_hi:[1,0]
	v_pk_mul_f32 v[14:15], v[14:15], v[136:137] op_sel_hi:[1,0]
	v_pk_mul_f32 v[12:13], v[12:13], v[136:137] op_sel_hi:[1,0]
	v_pk_mul_f32 v[10:11], v[10:11], v[136:137] op_sel_hi:[1,0]
	v_pk_mul_f32 v[8:9], v[8:9], v[136:137] op_sel_hi:[1,0]
	v_pk_mul_f32 v[6:7], v[6:7], v[136:137] op_sel_hi:[1,0]
	v_pk_mul_f32 v[4:5], v[4:5], v[136:137] op_sel_hi:[1,0]
	v_pk_mul_f32 v[2:3], v[2:3], v[136:137] op_sel_hi:[1,0]
	v_mul_f32_e32 v140, v140, v136
; #define LAS __attribute__((address_space(3)))
; template <int STAGE, int OFF> __device__ __forceinline__ void attn32_unit(const bf16* base, bf16* yrow0, int blk0, int u, LAS unsigned char* xtab, LAS unsigned char* kbuf, LAS unsigned char* vbuf, int lane, ...
;     ...
;         for (int c = 0; c < 4; ++c) { *(LAS v4u*)(kbuf + (8 * c + lrow) * 144 + lch * 16) = kr[set][c]; *(LAS v4u*)(vbuf + (8 * c + lrow) * 160 + lch * 16) = vr[set][c]; }
;         if (pp + 2 < 5) { ATT32_LOAD(set, pp + 2, t0, SH); }
;         else { const bf16* base_ = base; { const bf16* base = nbase; ATT32_LOAD(set, pp + 2 - 5, nt0, nsh); } (void)base_; }
;         f32x16 sc;
; #pragma unroll
;         for (int i = 0; i < 16; ++i) sc[i] = 0.f;
; #pragma unroll
;         for (int ks = 0; ks < 4; ++ks) { const bf16x8 ka = *(const LAS bf16x8*)(kbuf + qi * 144 + 32 * ks + 16 * h); sc = MFMA32(ka, qb[ks], sc); }
;         if (pp == 4) {
; #pragma unroll
;             for (int ks = 0; ks < 4; ++ks) qb[ks] = *(const bf16x8*)(nbase + (size_t)min(nt0 + (qi << nsh), SEQ - 1) * 1536 + 16 * ks + 8 * h);
;         }
;         const int mbase = n0 + 4 * h - lo; float mx = -INFINITY;
; #pragma unroll
;         for (int rg = 0; rg < 16; ++rg) { sc[rg] = ((unsigned)(mbase + (rg & 3) + 8 * (rg >> 2)) <= mspan) ? sc[rg] : -INFINITY; mx = fmaxf(mx, sc[rg]); }
;         mx = fmaxf(mx, __shfl_xor(mx, 32));
;         if (__any(mx > m)) {
;             const float mn = fmaxf(m, mx), alpha = __builtin_amdgcn_exp2f(m - mn); m = mn; l *= alpha;
; #pragma unroll
;             for (int i = 0; i < 16; ++i) { o[0][i] *= alpha; o[1][i] *= alpha; }
;         }
;         float ps = 0.f;
; #pragma unroll
;         for (int rg = 0; rg < 16; ++rg) { sc[rg] = __builtin_amdgcn_exp2f(sc[rg] - m); ps += sc[rg]; }
;         l += ps;
;         bf16x8 pb[2];
; #pragma unroll
;         for (int s2 = 0; s2 < 2; ++s2) { v4u w; w.x = pg8::cvt_pk_bf16(sc[8 * s2], sc[8 * s2 + 1]); w.y = pg8::cvt_pk_bf16(sc[8 * s2 + 2], sc[8 * s2 + 3]); w.z = pg8::cvt_pk_bf16(sc[8 * s2 + 4], sc[8 * s2 + 5]); w.w = pg8::cvt_pk_bf16(sc[8 * s2 + 6], sc[8 * s2 + 7]); pb[s2] = __builtin_bit_cast(bf16x8, w); }
; #pragma unroll
;         for (int mb = 0; mb < 2; ++mb)
; #pragma unroll
;             for (int s2 = 0; s2 < 2; ++s2) {
;                 LAS unsigned char* vp = vbuf + tr_off + (16 * s2) * 160 + 64 * mb;
.LBB0_430:
	v_sub_f32_e32 v34, v34, v139
	v_exp_f32_e32 v135, v34
	v_sub_f32_e32 v34, v35, v139
	v_exp_f32_e32 v136, v34
	v_sub_f32_e32 v34, v36, v139
	v_exp_f32_e32 v137, v34
	v_sub_f32_e32 v34, v37, v139
	v_exp_f32_e32 v141, v34
	v_sub_f32_e32 v34, v38, v139
	v_exp_f32_e32 v150, v34
	v_sub_f32_e32 v34, v39, v139
	v_exp_f32_e32 v151, v34
	v_sub_f32_e32 v34, v40, v139
	v_exp_f32_e32 v152, v34
	v_sub_f32_e32 v34, v41, v139
	v_exp_f32_e32 v153, v34
	v_sub_f32_e32 v34, v42, v139
	v_exp_f32_e32 v156, v34
	v_sub_f32_e32 v34, v43, v139
	v_exp_f32_e32 v157, v34
	v_sub_f32_e32 v34, v44, v139
	v_exp_f32_e32 v158, v34
	v_sub_f32_e32 v34, v45, v139
	v_exp_f32_e32 v159, v34
	v_sub_f32_e32 v34, v46, v139
	v_exp_f32_e32 v160, v34
	v_sub_f32_e32 v34, v47, v139
	v_exp_f32_e32 v161, v34
	v_sub_f32_e32 v34, v48, v139
	v_exp_f32_e32 v162, v34
	v_sub_f32_e32 v34, v49, v139
	v_exp_f32_e32 v163, v34
	v_cvt_pk_bf16_f32 v34, v135, v136
	v_cvt_pk_bf16_f32 v35, v137, v141
	v_cvt_pk_bf16_f32 v36, v150, v151
	v_cvt_pk_bf16_f32 v37, v152, v153
	v_cvt_pk_bf16_f32 v142, v156, v157
	v_cvt_pk_bf16_f32 v143, v158, v159
	v_cvt_pk_bf16_f32 v144, v160, v161
	v_cvt_pk_bf16_f32 v145, v162, v163
	ds_read_b64_tr_b16 v[38:39], v181 offset:4608
	ds_read_b64_tr_b16 v[40:41], v181 offset:5888
	v_or_b32_e32 v42, s10, v1
	v_min_i32_e32 v146, 0x3fff, v42
	s_waitcnt lgkmcnt(0)
	v_mfma_f32_32x32x16_bf16 v[18:33], v[38:41], v[34:37], v[18:33]
	v_mov_b64_e32 v[38:39], s[8:9]
	v_mad_i64_i32 v[38:39], s[10:11], v146, s30, v[38:39]
	ds_read_b64_tr_b16 v[42:43], v181 offset:7168
	ds_read_b64_tr_b16 v[44:45], v181 offset:8448
	ds_read_b64_tr_b16 v[48:49], v181 offset:5952
	ds_read_b64_tr_b16 v[46:47], v181 offset:4672
	v_lshl_add_u64 v[154:155], v[38:39], 0, v[168:169]
	v_add_f32_e32 v38, 0, v135
	v_add_f32_e32 v38, v136, v38
	v_add_f32_e32 v38, v137, v38
	v_add_f32_e32 v38, v141, v38
	v_add_f32_e32 v38, v150, v38
	v_add_f32_e32 v38, v151, v38
	s_waitcnt lgkmcnt(0)
	v_mfma_f32_32x32x16_bf16 v[2:17], v[46:49], v[34:37], v[2:17]
	v_add_u32_e32 v34, 0x80, v134
	ds_read_b64_tr_b16 v[148:149], v181 offset:8512
	ds_read_b64_tr_b16 v[146:147], v181 offset:7232
	v_add_f32_e32 v38, v152, v38
	s_waitcnt vmcnt(15)
	ds_write_b128 v231, v[66:69]
	s_waitcnt vmcnt(14)
	ds_write_b128 v232, v[106:109] offset:4608
	s_waitcnt vmcnt(13)
	ds_write_b128 v231, v[110:113] offset:1152
	s_waitcnt vmcnt(12)
	ds_write_b128 v232, v[114:117] offset:5888
	s_waitcnt vmcnt(11)
	ds_write_b128 v231, v[118:121] offset:2304
	s_waitcnt vmcnt(10)
	ds_write_b128 v232, v[122:125] offset:7168
	s_waitcnt vmcnt(9)
	ds_write_b128 v231, v[126:129] offset:3456
	s_waitcnt vmcnt(8)
	ds_write_b128 v232, v[130:133] offset:8448
	v_med3_i32 v34, v34, 0, v233
	v_add_f32_e32 v141, v153, v38
	v_mul_u32_u24_e32 v38, 0xc00, v34
	ds_read_b128 v[34:37], v177
	v_or_b32_e32 v38, v38, v176
	global_load_dwordx4 v[106:109], v38, s[8:9] offset:1024
	global_load_dwordx4 v[122:125], v38, s[8:9] offset:2048
	v_add_u32_e32 v38, 0x88, v134
	v_med3_i32 v38, v38, 0, v233
	v_mul_u32_u24_e32 v38, 0xc00, v38
	ds_read_b128 v[66:69], v177 offset:32
	v_mfma_f32_32x32x16_bf16 v[18:33], v[42:45], v[142:145], v[18:33]
	v_or_b32_e32 v114, v38, v176
	global_load_dwordx4 v[110:113], v114, s[8:9] offset:1024
	global_load_dwordx4 v[126:129], v114, s[8:9] offset:2048
	v_add_f32_e32 v141, v156, v141
	v_add_f32_e32 v141, v157, v141
	v_add_f32_e32 v141, v158, v141
	v_add_f32_e32 v141, v159, v141
	v_add_f32_e32 v141, v160, v141
	s_waitcnt lgkmcnt(1)
	v_mfma_f32_32x32x16_bf16 v[34:49], v[34:37], v[62:65], 0
	v_add_u32_e32 v62, 0x90, v134
	v_med3_i32 v62, v62, 0, v233
	v_mul_u32_u24_e32 v62, 0xc00, v62
	v_or_b32_e32 v118, v62, v176
	ds_read_b128 v[150:153], v177 offset:96
	ds_read_b128 v[62:65], v177 offset:64
	global_load_dwordx4 v[114:117], v118, s[8:9] offset:1024
	global_load_dwordx4 v[130:133], v118, s[8:9] offset:2048
	v_add_f32_e32 v141, v161, v141
	s_waitcnt lgkmcnt(2)
	v_mfma_f32_32x32x16_bf16 v[34:49], v[66:69], v[58:61], v[34:49]
	v_add_u32_e32 v58, 0x98, v134
	v_med3_i32 v58, v58, 0, v233
	v_mul_u32_u24_e32 v58, 0xc00, v58
	v_or_b32_e32 v58, v58, v176
	global_load_dwordx4 v[118:121], v58, s[8:9] offset:1024
	global_load_dwordx4 v[134:137], v58, s[8:9] offset:2048
	v_add_f32_e32 v141, v162, v141
	s_waitcnt lgkmcnt(0)
	v_mfma_f32_32x32x16_bf16 v[34:49], v[62:65], v[54:57], v[34:49]
	global_load_dwordx4 v[66:69], v[154:155], off
	global_load_dwordx4 v[62:65], v[154:155], off offset:32
	global_load_dwordx4 v[58:61], v[154:155], off offset:64
	global_load_dwordx4 v[54:57], v[154:155], off offset:96
	v_mfma_f32_32x32x16_bf16 v[34:49], v[150:153], v[70:73], v[34:49]
	v_add_u32_e32 v70, 0x80, v138
	v_cmp_le_u32_e32 vcc, v70, v51
	v_add_u32_e32 v71, 0x82, v138
	v_mfma_f32_32x32x16_bf16 v[2:17], v[146:149], v[142:145], v[2:17]
	s_nop 7
	v_cndmask_b32_e32 v70, v234, v34, vcc
	v_add_u32_e32 v34, 0x81, v138
	v_cmp_le_u32_e32 vcc, v34, v51
	s_nop 1
	v_cndmask_b32_e32 v35, v234, v35, vcc
	v_cmp_le_u32_e32 vcc, v71, v51
	v_add_u32_e32 v71, 0x83, v138
	v_max3_f32 v34, v70, s31, v35
	v_cndmask_b32_e32 v36, v234, v36, vcc
	v_cmp_le_u32_e32 vcc, v71, v51
	v_add_u32_e32 v71, 0x88, v138
	s_nop 0
	v_cndmask_b32_e32 v37, v234, v37, vcc
	v_cmp_le_u32_e32 vcc, v71, v51
	v_add_u32_e32 v71, 0x89, v138
	v_max3_f32 v34, v34, v36, v37
	v_cndmask_b32_e32 v38, v234, v38, vcc
	v_cmp_le_u32_e32 vcc, v71, v51
	v_add_u32_e32 v71, 0x8a, v138
	s_nop 0
	v_cndmask_b32_e32 v39, v234, v39, vcc
	v_cmp_le_u32_e32 vcc, v71, v51
	v_add_u32_e32 v71, 0x8b, v138
	v_max3_f32 v34, v34, v38, v39
	v_cndmask_b32_e32 v40, v234, v40, vcc
	v_cmp_le_u32_e32 vcc, v71, v51
	v_add_u32_e32 v71, 0x90, v138
	s_nop 0
	v_cndmask_b32_e32 v41, v234, v41, vcc
	v_cmp_le_u32_e32 vcc, v71, v51
	v_add_u32_e32 v71, 0x91, v138
	v_max3_f32 v34, v34, v40, v41
	v_cndmask_b32_e32 v42, v234, v42, vcc
	v_cmp_le_u32_e32 vcc, v71, v51
	v_add_u32_e32 v71, 0x92, v138
	s_nop 0
	v_cndmask_b32_e32 v43, v234, v43, vcc
	v_cmp_le_u32_e32 vcc, v71, v51
	v_add_u32_e32 v71, 0x93, v138
	v_max3_f32 v34, v34, v42, v43
	v_cndmask_b32_e32 v44, v234, v44, vcc
	v_cmp_le_u32_e32 vcc, v71, v51
	v_add_u32_e32 v71, 0x98, v138
	s_nop 0
	v_cndmask_b32_e32 v45, v234, v45, vcc
	v_cmp_le_u32_e32 vcc, v71, v51
	v_add_u32_e32 v71, 0x99, v138
	v_max3_f32 v34, v34, v44, v45
	v_cndmask_b32_e32 v46, v234, v46, vcc
	v_cmp_le_u32_e32 vcc, v71, v51
	v_add_u32_e32 v71, 0x9a, v138
	s_nop 0
	v_cndmask_b32_e32 v47, v234, v47, vcc
	v_cmp_le_u32_e32 vcc, v71, v51
	v_add_u32_e32 v71, 0x9b, v138
	v_max3_f32 v34, v34, v46, v47
	v_cndmask_b32_e32 v48, v234, v48, vcc
	v_cmp_le_u32_e32 vcc, v71, v51
	s_nop 1
	v_cndmask_b32_e32 v49, v234, v49, vcc
	v_max3_f32 v51, v34, v48, v49
	v_mov_b32_e32 v71, v51
	s_nop 1
	v_permlane32_swap_b32_e32 v71, v51
	v_add_f32_e32 v34, v163, v141
	v_add_f32_e32 v34, v140, v34
	s_waitcnt lgkmcnt(0)
	v_max_f32_e32 v71, v71, v71
	v_max_f32_e32 v51, v51, v71
	v_cmp_gt_f32_e32 vcc, v51, v139
	s_cbranch_vccz .LBB0_355
; template <int STAGE, int OFF> __device__ __forceinline__ void attn32_unit(const bf16* base, bf16* yrow0, int blk0, int u, LAS unsigned char* xtab, LAS unsigned char* kbuf, LAS unsigned char* vbuf, int lane, ...
;     ...
;         if (__any(mx > m)) {
;             const float mn = fmaxf(m, mx), alpha = __builtin_amdgcn_exp2f(m - mn); m = mn; l *= alpha;
; #pragma unroll
;             for (int i = 0; i < 16; ++i) { o[0][i] *= alpha; o[1][i] *= alpha; }
;         }
	v_max_f32_e32 v51, v51, v51
	v_max_f32_e32 v71, v139, v139
	v_max_f32_e32 v51, v71, v51
	v_sub_f32_e32 v71, v139, v51
	v_exp_f32_e32 v72, v71
	v_mov_b32_e32 v139, v51
	v_pk_mul_f32 v[32:33], v[32:33], v[72:73] op_sel_hi:[1,0]
	v_pk_mul_f32 v[30:31], v[30:31], v[72:73] op_sel_hi:[1,0]
	v_pk_mul_f32 v[28:29], v[28:29], v[72:73] op_sel_hi:[1,0]
	v_pk_mul_f32 v[26:27], v[26:27], v[72:73] op_sel_hi:[1,0]
	v_pk_mul_f32 v[24:25], v[24:25], v[72:73] op_sel_hi:[1,0]
	v_pk_mul_f32 v[22:23], v[22:23], v[72:73] op_sel_hi:[1,0]
	v_pk_mul_f32 v[20:21], v[20:21], v[72:73] op_sel_hi:[1,0]
	v_pk_mul_f32 v[18:19], v[18:19], v[72:73] op_sel_hi:[1,0]
	v_pk_mul_f32 v[16:17], v[16:17], v[72:73] op_sel_hi:[1,0]
	v_pk_mul_f32 v[14:15], v[14:15], v[72:73] op_sel_hi:[1,0]
	v_pk_mul_f32 v[12:13], v[12:13], v[72:73] op_sel_hi:[1,0]
	v_pk_mul_f32 v[10:11], v[10:11], v[72:73] op_sel_hi:[1,0]
	v_pk_mul_f32 v[8:9], v[8:9], v[72:73] op_sel_hi:[1,0]
	v_pk_mul_f32 v[6:7], v[6:7], v[72:73] op_sel_hi:[1,0]
	v_pk_mul_f32 v[4:5], v[4:5], v[72:73] op_sel_hi:[1,0]
	v_pk_mul_f32 v[2:3], v[2:3], v[72:73] op_sel_hi:[1,0]
	v_mul_f32_e32 v34, v34, v72
	s_branch .LBB0_355
